# v72 + sc0 scope bit on the weight-fragment (B operand) global loads of all GEMM loops (264 loads)
# baseline (speedup 1.0000x reference)
.LBB0_349:
	s_or_b64 exec, exec, s[0:1]
	s_ashr_i32 s47, s46, 31
	v_mov_b32_e32 v12, v0
	s_waitcnt lgkmcnt(0)
	s_barrier
	s_lshl_b64 s[0:1], s[46:47], 11
	s_add_u32 s0, s6, s0
	v_ashrrev_i32_e32 v4, 4, v12
	v_lshlrev_b32_e32 v5, 3, v12
	v_and_b32_e32 v154, 0x78, v5
	v_ashrrev_i32_e32 v5, 31, v4
	s_addc_u32 s1, s7, s1
	v_lshlrev_b64 v[6:7], 11, v[4:5]
	v_lshl_add_u64 v[132:133], s[0:1], 0, v[6:7]
	s_mov_b64 s[0:1], 0x10000
	v_lshl_add_u64 v[134:135], v[132:133], 0, s[0:1]
	s_mov_b64 s[0:1], 0x20000
	v_readlane_b32 s12, v247, 9
	v_lshl_add_u64 v[136:137], v[132:133], 0, s[0:1]
	s_mov_b64 s[0:1], 0x30000
	v_or_b32_e32 v8, s12, v154
	v_lshl_add_u64 v[138:139], v[132:133], 0, s[0:1]
	v_readfirstlane_b32 s0, v12
	v_lshlrev_b32_e32 v6, 1, v8
	v_mov_b32_e32 v7, v2
	s_ashr_i32 s12, s0, 6
	v_lshl_add_u64 v[8:9], v[132:133], 0, v[6:7]
	s_cmp_lt_i32 s12, 8
	v_lshl_add_u64 v[10:11], v[134:135], 0, v[6:7]
	global_load_dwordx4 v[52:55], v[8:9], off
	global_load_dwordx4 v[56:59], v[10:11], off
	v_lshl_add_u64 v[8:9], v[136:137], 0, v[6:7]
	v_readlane_b32 s0, v247, 10
	s_cselect_b64 s[48:49], -1, 0
	v_lshl_add_u64 v[6:7], v[138:139], 0, v[6:7]
	global_load_dwordx4 v[60:63], v[8:9], off
	global_load_dwordx4 v[64:67], v[6:7], off
	v_or_b32_e32 v8, s0, v154
	s_and_b64 s[0:1], s[48:49], exec
	s_cselect_b32 s0, s12, 7
	s_ashr_i32 s1, s0, 31
	s_lshl_b64 s[0:1], s[0:1], 16
	v_readlane_b32 s18, v248, 21
	v_and_b32_e32 v6, 63, v12
	v_lshlrev_b32_e32 v7, 8, v4
	v_xor_b32_e32 v4, v4, v12
	s_add_u32 s0, s87, s0
	v_readlane_b32 s20, v248, 48
	v_mov_b32_e32 v21, v2
	v_readlane_b32 s19, v248, 22
	v_bfe_u32 v156, v12, 4, 2
	v_lshlrev_b32_e32 v20, 4, v6
	v_lshlrev_b32_e32 v4, 4, v4
	s_addc_u32 s1, s20, s1
	v_mov_b32_e32 v5, v2
	s_mov_b32 s19, s21
	v_bitop3_b32 v6, v156, v12, 15 bitop3:0x78
	v_and_or_b32 v9, v4, s84, v7
	v_lshlrev_b32_e32 v4, 1, v8
	v_lshl_add_u64 v[140:141], s[0:1], 0, v[20:21]
	v_lshlrev_b32_e32 v70, 4, v6
	v_lshl_add_u64 v[6:7], v[132:133], 0, v[4:5]
	v_add_u32_e32 v157, 0, v9
	v_lshl_add_u64 v[8:9], v[134:135], 0, v[4:5]
	v_lshl_add_u64 v[10:11], v[136:137], 0, v[4:5]
	v_lshl_add_u64 v[4:5], v[138:139], 0, v[4:5]
	v_lshl_add_u64 v[32:33], v[140:141], 0, s[18:19]
	v_and_b32_e32 v155, 15, v12
	global_load_dwordx4 v[16:19], v[6:7], off
	global_load_dwordx4 v[12:15], v[8:9], off
	s_nop 0
	global_load_dwordx4 v[8:11], v[10:11], off
	s_nop 0
	global_load_dwordx4 v[4:7], v[4:5], off sc0
	s_nop 0
	global_load_dwordx4 v[36:39], v[32:33], off sc0
	global_load_dwordx4 v[28:31], v[32:33], off offset:1024 sc0
	global_load_dwordx4 v[24:27], v[32:33], off offset:2048 sc0
	global_load_dwordx4 v[20:23], v[32:33], off offset:3072 sc0
	v_add_co_u32_e32 v32, vcc, s14, v32
	s_cmp_gt_i32 s12, 3
	s_nop 0
	v_addc_co_u32_e32 v33, vcc, 0, v33, vcc
	global_load_dwordx4 v[48:51], v[32:33], off sc0
	global_load_dwordx4 v[44:47], v[32:33], off offset:1024 sc0
	global_load_dwordx4 v[40:43], v[32:33], off offset:2048 sc0
	s_nop 0
	global_load_dwordx4 v[32:35], v[32:33], off offset:3072 sc0
	s_mov_b32 s0, s18
	v_writelane_b32 v248, s0, 21
	s_cselect_b64 s[50:51], -1, 0
	s_cmp_eq_u32 s12, 4
	v_writelane_b32 v248, s1, 22
	s_cselect_b64 s[52:53], -1, 0
	s_lshl_b32 s0, s12, 5
	s_ashr_i32 s1, s0, 31
	s_lshl_b32 s38, s12, 9
	s_lshl_b32 s20, s12, 13
	s_lshl_b32 s12, s12, 2
	s_and_b32 s39, s20, 0xffff8000
	s_and_b32 s20, s12, 12
	s_add_i32 s76, s0, 0xfffffe00
	s_lshl_b64 s[0:1], s[0:1], 1
	v_readlane_b32 s18, v247, 7
	s_waitcnt vmcnt(15)
	ds_write_b128 v157, v[52:55]
	s_waitcnt vmcnt(14)
	ds_write_b128 v157, v[56:59] offset:8192
	s_waitcnt vmcnt(13)
	ds_write_b128 v157, v[60:63] offset:16384
	s_waitcnt vmcnt(12)
	ds_write_b128 v157, v[64:67] offset:24576
	v_bitop3_b32 v52, v156, v155, 4 bitop3:0x36
	v_bitop3_b32 v53, v156, v155, 8 bitop3:0x36
	v_bitop3_b32 v54, v156, v155, 12 bitop3:0x36
	v_readlane_b32 s19, v247, 8
	s_add_u32 s54, s18, s0
	v_lshl_add_u32 v69, v155, 8, 0
	v_lshlrev_b32_e32 v52, 4, v52
	v_lshlrev_b32_e32 v53, 4, v53
	v_lshlrev_b32_e32 v54, 4, v54
	s_addc_u32 s55, s19, s1
	s_add_i32 s77, s38, 0
	s_add_i32 s89, s39, 0
	v_mov_b32_e32 v68, 0
	s_mov_b32 s58, 1
	s_mov_b32 s59, 0
	s_mov_b32 s66, 2
	s_or_b32 s47, s46, 16
	s_or_b32 s70, s46, 32
	s_or_b32 s71, s46, 48
	s_or_b32 s72, s46, 64
	s_or_b32 s73, s46, 0x50
	s_or_b32 s74, s46, 0x60
	s_or_b32 s75, s46, 0x70
	s_add_i32 s77, s77, 0x20000
	s_add_i32 s78, s89, 0x10000
	s_add_i32 s79, s89, 0x11000
	s_add_i32 s82, s89, 0x12000
	s_add_i32 s83, s89, 0x13000
	s_add_i32 s84, s89, 0x14000
	s_add_i32 s85, s89, 0x15000
	s_add_i32 s88, s89, 0x16000
	s_add_i32 s89, s89, 0x17000
	v_add_u32_e32 v158, v69, v70
	v_add_u32_e32 v159, v69, v52
	v_add_u32_e32 v160, v69, v53
	v_add_u32_e32 v161, v69, v54
	s_mov_b64 s[56:57], s[42:43]
	s_mov_b32 s90, 0
	s_mov_b32 s38, 0
	s_mov_b32 s91, 0
	v_mov_b32_e32 v69, v68
	v_mov_b32_e32 v70, v68
	v_mov_b32_e32 v71, v68
	v_mov_b32_e32 v72, v68
	v_mov_b32_e32 v73, v68
	v_mov_b32_e32 v74, v68
	v_mov_b32_e32 v75, v68
	v_mov_b32_e32 v76, v68
	v_mov_b32_e32 v77, v68
	v_mov_b32_e32 v78, v68
	v_mov_b32_e32 v79, v68
	v_mov_b32_e32 v84, v68
	v_mov_b32_e32 v85, v68
	v_mov_b32_e32 v86, v68
	v_mov_b32_e32 v87, v68
	v_mov_b32_e32 v88, v68
	v_mov_b32_e32 v89, v68
	v_mov_b32_e32 v90, v68
	v_mov_b32_e32 v91, v68
	v_mov_b32_e32 v92, v68
	v_mov_b32_e32 v93, v68
	v_mov_b32_e32 v94, v68
	v_mov_b32_e32 v95, v68
	v_mov_b32_e32 v96, v68
	v_mov_b32_e32 v97, v68
	v_mov_b32_e32 v98, v68
	v_mov_b32_e32 v99, v68
	v_mov_b32_e32 v100, v68
	v_mov_b32_e32 v101, v68
	v_mov_b32_e32 v102, v68
	v_mov_b32_e32 v103, v68
	v_mov_b32_e32 v52, v68
	v_mov_b32_e32 v53, v68
	v_mov_b32_e32 v54, v68
	v_mov_b32_e32 v55, v68
	v_mov_b32_e32 v56, v68
	v_mov_b32_e32 v57, v68
	v_mov_b32_e32 v58, v68
	v_mov_b32_e32 v59, v68
	v_mov_b32_e32 v104, v68
	v_mov_b32_e32 v105, v68
	v_mov_b32_e32 v106, v68
	v_mov_b32_e32 v107, v68
	v_mov_b32_e32 v108, v68
	v_mov_b32_e32 v109, v68
	v_mov_b32_e32 v110, v68
	v_mov_b32_e32 v111, v68
	v_mov_b32_e32 v112, v68
	v_mov_b32_e32 v113, v68
	v_mov_b32_e32 v114, v68
	v_mov_b32_e32 v115, v68
	v_mov_b32_e32 v116, v68
	v_mov_b32_e32 v117, v68
	v_mov_b32_e32 v118, v68
	v_mov_b32_e32 v119, v68
	v_mov_b32_e32 v120, v68
	v_mov_b32_e32 v121, v68
	v_mov_b32_e32 v122, v68
	v_mov_b32_e32 v123, v68
	v_mov_b32_e32 v124, v68
	v_mov_b32_e32 v125, v68
	v_mov_b32_e32 v126, v68
	v_mov_b32_e32 v127, v68
	s_waitcnt lgkmcnt(0)
	s_barrier
	s_branch .LBB0_354

.LBB0_358:
	s_add_i32 s0, s66, s81
	s_lshl_b32 s1, s0, 7
	s_add_i32 s12, s1, 0xfffffc00
	s_cmp_gt_i32 s0, 7
	s_cselect_b32 s0, s12, s1
	v_or_b32_e32 v60, s0, v154
	s_add_i32 s0, s59, s23
	s_add_i32 s1, s0, -4
	s_cmp_gt_i32 s0, 3
	s_cselect_b32 s0, s1, s0
	s_add_i32 s12, s58, s81
	s_lshl_b32 s39, s12, 2
	ds_read_b128 v[80:83], v158
	ds_read_b128 v[128:131], v158 offset:4096
	ds_read_b128 v[142:145], v158 offset:8192
	ds_read_b128 v[146:149], v158 offset:12288
	ds_read_b128 v[150:153], v158 offset:16384
	ds_read_b128 v[162:165], v158 offset:20480
	ds_read_b128 v[166:169], v158 offset:24576
	ds_read_b128 v[170:173], v158 offset:28672
	s_ashr_i32 s1, s0, 31
	s_sub_i32 s58, s39, 32
	s_cmp_gt_i32 s12, 7
	s_cselect_b32 s58, s58, s39
	s_ashr_i32 s59, s58, 31
	s_lshl_b64 s[0:1], s[0:1], 19
	v_ashrrev_i32_e32 v61, 31, v60
	v_lshl_add_u64 v[62:63], v[140:141], 0, s[0:1]
	s_lshl_b64 s[0:1], s[58:59], 10
	v_lshlrev_b64 v[60:61], 1, v[60:61]
	v_lshl_add_u64 v[186:187], v[62:63], 0, s[0:1]
	v_lshl_add_u64 v[182:183], v[136:137], 0, v[60:61]
	v_lshl_add_u64 v[184:185], v[138:139], 0, v[60:61]
	v_lshl_add_u64 v[62:63], v[132:133], 0, v[60:61]
	v_lshl_add_u64 v[60:61], v[134:135], 0, v[60:61]
	global_load_dwordx4 v[64:67], v[62:63], off
	s_nop 0
	global_load_dwordx4 v[60:63], v[60:61], off
	s_waitcnt vmcnt(9) lgkmcnt(7)
	v_mfma_f32_16x16x32_bf16 v[124:127], v[36:39], v[80:83], v[124:127]
	s_waitcnt vmcnt(5)
	v_mfma_f32_16x16x32_bf16 v[80:83], v[48:51], v[80:83], v[120:123]
	s_waitcnt lgkmcnt(6)
	v_mfma_f32_16x16x32_bf16 v[116:119], v[36:39], v[128:131], v[116:119]
	v_mfma_f32_16x16x32_bf16 v[112:115], v[48:51], v[128:131], v[112:115]
	s_waitcnt lgkmcnt(5)
	v_mfma_f32_16x16x32_bf16 v[108:111], v[36:39], v[142:145], v[108:111]
	v_mfma_f32_16x16x32_bf16 v[104:107], v[48:51], v[142:145], v[104:107]
	s_waitcnt lgkmcnt(4)
	v_mfma_f32_16x16x32_bf16 v[120:123], v[36:39], v[146:149], v[56:59]
	v_mfma_f32_16x16x32_bf16 v[128:131], v[48:51], v[146:149], v[52:55]
	ds_read_b128 v[142:145], v159
	ds_read_b128 v[146:149], v159 offset:4096
	ds_read_b128 v[174:177], v159 offset:8192
	ds_read_b128 v[178:181], v159 offset:12288
	global_load_dwordx4 v[56:59], v[182:183], off sc0
	global_load_dwordx4 v[52:55], v[184:185], off
	s_waitcnt lgkmcnt(7)
	v_mfma_f32_16x16x32_bf16 v[100:103], v[36:39], v[150:153], v[100:103]
	v_mfma_f32_16x16x32_bf16 v[96:99], v[48:51], v[150:153], v[96:99]
	s_waitcnt lgkmcnt(6)
	v_mfma_f32_16x16x32_bf16 v[92:95], v[36:39], v[162:165], v[92:95]
	v_mfma_f32_16x16x32_bf16 v[88:91], v[48:51], v[162:165], v[88:91]
	s_waitcnt lgkmcnt(5)
	v_mfma_f32_16x16x32_bf16 v[84:87], v[36:39], v[166:169], v[84:87]
	s_waitcnt lgkmcnt(4)
	v_mfma_f32_16x16x32_bf16 v[72:75], v[36:39], v[170:173], v[72:75]
	v_mfma_f32_16x16x32_bf16 v[68:71], v[48:51], v[170:173], v[68:71]
	v_mfma_f32_16x16x32_bf16 v[150:153], v[48:51], v[166:169], v[76:79]
	ds_read_b128 v[162:165], v159 offset:16384
	ds_read_b128 v[166:169], v159 offset:20480
	ds_read_b128 v[170:173], v159 offset:24576
	ds_read_b128 v[182:185], v159 offset:28672
	v_add_co_u32_e32 v188, vcc, s14, v186
	s_nop 1
	v_addc_co_u32_e32 v189, vcc, 0, v187, vcc
	global_load_dwordx4 v[36:39], v[186:187], off sc0
	global_load_dwordx4 v[48:51], v[188:189], off sc0
	ds_write_b128 v157, v[16:19] offset:32768
	s_waitcnt lgkmcnt(8)
	v_mfma_f32_16x16x32_bf16 v[16:19], v[28:31], v[142:145], v[124:127]
	s_waitcnt vmcnt(8)
	v_mfma_f32_16x16x32_bf16 v[80:83], v[44:47], v[142:145], v[80:83]
	s_waitcnt lgkmcnt(7)
	v_mfma_f32_16x16x32_bf16 v[116:119], v[28:31], v[146:149], v[116:119]
	v_mfma_f32_16x16x32_bf16 v[112:115], v[44:47], v[146:149], v[112:115]
	s_waitcnt lgkmcnt(6)
	v_mfma_f32_16x16x32_bf16 v[108:111], v[28:31], v[174:177], v[108:111]
	v_mfma_f32_16x16x32_bf16 v[104:107], v[44:47], v[174:177], v[104:107]
	s_waitcnt lgkmcnt(5)
	v_mfma_f32_16x16x32_bf16 v[120:123], v[28:31], v[178:181], v[120:123]
	v_mfma_f32_16x16x32_bf16 v[124:127], v[44:47], v[178:181], v[128:131]
	s_nop 2
	ds_read_b128 v[128:131], v160
	ds_read_b128 v[142:145], v160 offset:4096
	ds_read_b128 v[146:149], v160 offset:8192
	ds_read_b128 v[174:177], v160 offset:12288
	global_load_dwordx4 v[76:79], v[186:187], off offset:1024 sc0
	ds_write_b128 v157, v[12:15] offset:40960
	s_waitcnt lgkmcnt(9)
	v_mfma_f32_16x16x32_bf16 v[12:15], v[28:31], v[162:165], v[100:103]
	v_mfma_f32_16x16x32_bf16 v[96:99], v[44:47], v[162:165], v[96:99]
	s_waitcnt lgkmcnt(8)
	v_mfma_f32_16x16x32_bf16 v[92:95], v[28:31], v[166:169], v[92:95]
	v_mfma_f32_16x16x32_bf16 v[88:91], v[44:47], v[166:169], v[88:91]
	s_waitcnt lgkmcnt(7)
	v_mfma_f32_16x16x32_bf16 v[84:87], v[28:31], v[170:173], v[84:87]
	v_mfma_f32_16x16x32_bf16 v[100:103], v[44:47], v[170:173], v[150:153]
	s_waitcnt lgkmcnt(6)
	v_mfma_f32_16x16x32_bf16 v[28:31], v[28:31], v[182:185], v[72:75]
	v_mfma_f32_16x16x32_bf16 v[150:153], v[44:47], v[182:185], v[68:71]
	ds_read_b128 v[162:165], v160 offset:16384
	ds_read_b128 v[166:169], v160 offset:20480
	ds_read_b128 v[170:173], v160 offset:24576
	ds_read_b128 v[178:181], v160 offset:28672
	global_load_dwordx4 v[72:75], v[186:187], off offset:2048 sc0
	global_load_dwordx4 v[44:47], v[188:189], off offset:1024 sc0
	ds_write_b128 v157, v[8:11] offset:49152
	s_waitcnt lgkmcnt(9)
	v_mfma_f32_16x16x32_bf16 v[8:11], v[24:27], v[128:131], v[16:19]
	s_waitcnt vmcnt(10)
	v_mfma_f32_16x16x32_bf16 v[16:19], v[40:43], v[128:131], v[80:83]
	s_waitcnt lgkmcnt(8)
	v_mfma_f32_16x16x32_bf16 v[80:83], v[24:27], v[142:145], v[116:119]
	v_mfma_f32_16x16x32_bf16 v[112:115], v[40:43], v[142:145], v[112:115]
	s_waitcnt lgkmcnt(7)
	v_mfma_f32_16x16x32_bf16 v[108:111], v[24:27], v[146:149], v[108:111]
	v_mfma_f32_16x16x32_bf16 v[104:107], v[40:43], v[146:149], v[104:107]
	s_waitcnt lgkmcnt(6)
	v_mfma_f32_16x16x32_bf16 v[128:131], v[24:27], v[174:177], v[120:123]
	v_mfma_f32_16x16x32_bf16 v[142:145], v[40:43], v[174:177], v[124:127]
	ds_read_b128 v[116:119], v161
	ds_read_b128 v[146:149], v161 offset:4096
	ds_read_b128 v[174:177], v161 offset:8192
	ds_read_b128 v[182:185], v161 offset:12288
	global_load_dwordx4 v[68:71], v[186:187], off offset:3072 sc0
	ds_write_b128 v157, v[4:7] offset:57344
	s_waitcnt lgkmcnt(9)
	v_mfma_f32_16x16x32_bf16 v[12:15], v[24:27], v[162:165], v[12:15]
	v_mfma_f32_16x16x32_bf16 v[96:99], v[40:43], v[162:165], v[96:99]
	s_waitcnt lgkmcnt(8)
	v_mfma_f32_16x16x32_bf16 v[92:95], v[24:27], v[166:169], v[92:95]
	v_mfma_f32_16x16x32_bf16 v[88:91], v[40:43], v[166:169], v[88:91]
	s_waitcnt lgkmcnt(7)
	v_mfma_f32_16x16x32_bf16 v[84:87], v[24:27], v[170:173], v[84:87]
	s_waitcnt lgkmcnt(6)
	v_mfma_f32_16x16x32_bf16 v[24:27], v[24:27], v[178:181], v[28:31]
	v_mfma_f32_16x16x32_bf16 v[162:165], v[40:43], v[170:173], v[100:103]
	v_mfma_f32_16x16x32_bf16 v[150:153], v[40:43], v[178:181], v[150:153]
	s_nop 0
	ds_read_b128 v[28:31], v161 offset:16384
	ds_read_b128 v[166:169], v161 offset:20480
	ds_read_b128 v[170:173], v161 offset:24576
	ds_read_b128 v[178:181], v161 offset:28672
	global_load_dwordx4 v[40:43], v[188:189], off offset:2048 sc0
	s_waitcnt lgkmcnt(8)
	v_mfma_f32_16x16x32_bf16 v[120:123], v[20:23], v[116:119], v[8:11]
	s_waitcnt vmcnt(11)
	v_mfma_f32_16x16x32_bf16 v[124:127], v[32:35], v[116:119], v[16:19]
	s_waitcnt lgkmcnt(7)
	v_mfma_f32_16x16x32_bf16 v[116:119], v[20:23], v[146:149], v[80:83]
	v_mfma_f32_16x16x32_bf16 v[112:115], v[32:35], v[146:149], v[112:115]
	s_waitcnt lgkmcnt(6)
	v_mfma_f32_16x16x32_bf16 v[108:111], v[20:23], v[174:177], v[108:111]
	v_mfma_f32_16x16x32_bf16 v[104:107], v[32:35], v[174:177], v[104:107]
	s_waitcnt lgkmcnt(5)
	v_mfma_f32_16x16x32_bf16 v[8:11], v[20:23], v[182:185], v[128:131]
	v_mfma_f32_16x16x32_bf16 v[4:7], v[32:35], v[182:185], v[142:145]
	global_load_dwordx4 v[80:83], v[188:189], off offset:3072 sc0
	s_waitcnt lgkmcnt(3)
	v_mfma_f32_16x16x32_bf16 v[100:103], v[20:23], v[28:31], v[12:15]
	v_mfma_f32_16x16x32_bf16 v[96:99], v[32:35], v[28:31], v[96:99]
	s_waitcnt lgkmcnt(2)
	v_mfma_f32_16x16x32_bf16 v[92:95], v[20:23], v[166:169], v[92:95]
	v_mfma_f32_16x16x32_bf16 v[88:91], v[32:35], v[166:169], v[88:91]
	s_waitcnt lgkmcnt(1)
	v_mfma_f32_16x16x32_bf16 v[84:87], v[20:23], v[170:173], v[84:87]
	v_mfma_f32_16x16x32_bf16 v[28:31], v[32:35], v[170:173], v[162:165]
	s_waitcnt lgkmcnt(0)
	v_mfma_f32_16x16x32_bf16 v[24:27], v[20:23], v[178:181], v[24:27]
	v_mfma_f32_16x16x32_bf16 v[20:23], v[32:35], v[178:181], v[150:153]
	s_cmp_eq_u32 s38, -1
	s_cselect_b64 s[0:1], -1, 0
	s_and_b64 s[0:1], s[0:1], s[48:49]
	s_andn2_b64 vcc, exec, s[0:1]
	s_cbranch_vccnz .LBB0_360
	v_mov_b32_e32 v12, v156
	v_mov_b32_e32 v13, v155

.LBB0_376:
	v_lshl_add_u32 v12, v162, 2, 0
	v_add_u32_e32 v12, 0x20000, v12
	ds_read2_b32 v[148:149], v12 offset1:16
	ds_read2_b32 v[146:147], v12 offset0:32 offset1:48
	ds_read2_b32 v[144:145], v12 offset0:64 offset1:80
	ds_read2_b32 v[142:143], v12 offset0:96 offset1:112
	s_add_i32 s12, s90, s23
	s_add_i32 s38, s12, -4
	s_cmp_gt_i32 s12, 3
	s_cselect_b32 s62, s38, s12
	s_mov_b64 s[58:59], -1
	s_mov_b64 s[56:57], 0
	s_cmp_lt_i32 s62, 1
	s_mov_b64 s[38:39], 0
	s_cbranch_scc1 .LBB0_390
	s_cmp_eq_u32 s62, 1
	s_mov_b64 s[38:39], -1
	s_cbranch_scc0 .LBB0_387
	s_and_b64 vcc, exec, s[50:51]
	s_cbranch_vccz .LBB0_382
	s_andn2_b64 vcc, exec, s[52:53]
	s_cbranch_vccnz .LBB0_381
	v_add_u32_e32 v180, s46, v162
	v_lshlrev_b32_e32 v152, 2, v163
	v_ashrrev_i32_e32 v181, 31, v180
	v_ashrrev_i32_e32 v153, 31, v152
	v_lshlrev_b64 v[12:13], 7, v[180:181]
	v_lshl_add_u64 v[12:13], s[4:5], 0, v[12:13]
	v_lshlrev_b64 v[150:151], 2, v[152:153]
	v_lshl_add_u64 v[12:13], v[12:13], 0, v[150:151]
	global_load_dwordx4 v[164:167], v[12:13], off
	global_load_dwordx4 v[168:171], v[12:13], off offset:64
	v_add_u32_e32 v12, 16, v180
	v_ashrrev_i32_e32 v13, 31, v12
	v_lshlrev_b64 v[12:13], 7, v[12:13]
	v_lshl_add_u64 v[12:13], s[4:5], 0, v[12:13]
	v_lshl_add_u64 v[12:13], v[12:13], 0, v[150:151]
	global_load_dwordx4 v[172:175], v[12:13], off
	global_load_dwordx4 v[176:179], v[12:13], off offset:64
	v_add_u32_e32 v12, 32, v180
	v_ashrrev_i32_e32 v13, 31, v12
	v_lshlrev_b64 v[12:13], 7, v[12:13]
	v_lshl_add_u64 v[12:13], s[4:5], 0, v[12:13]
	v_lshl_add_u64 v[12:13], v[12:13], 0, v[150:151]
	global_load_dwordx4 v[32:35], v[12:13], off
	global_load_dwordx4 v[128:131], v[12:13], off offset:64
	v_add_u32_e32 v12, 48, v180
	v_ashrrev_i32_e32 v13, 31, v12
	v_lshlrev_b64 v[12:13], 7, v[12:13]
	v_lshl_add_u64 v[12:13], s[4:5], 0, v[12:13]
	v_lshl_add_u64 v[16:17], v[12:13], 0, v[150:151]
	global_load_dwordx4 v[12:15], v[16:17], off sc0
	s_nop 0
	global_load_dwordx4 v[16:19], v[16:17], off offset:64 sc0
	s_waitcnt lgkmcnt(3)
	v_pk_mul_f32 v[184:185], v[122:123], v[148:149] op_sel_hi:[1,0]
	v_pk_mul_f32 v[186:187], v[120:121], v[148:149] op_sel_hi:[1,0]
	v_pk_mul_f32 v[188:189], v[126:127], v[148:149] op_sel_hi:[1,0]
	v_pk_mul_f32 v[190:191], v[124:125], v[148:149] op_sel_hi:[1,0]
	v_ashrrev_i32_e32 v182, 11, v180
	v_ashrrev_i32_e32 v183, 31, v182
	v_readlane_b32 s18, v251, 55
	v_readlane_b32 s19, v251, 56
	v_lshlrev_b64 v[152:153], 1, v[152:153]
	s_waitcnt vmcnt(6)
	v_pk_mul_f32 v[192:193], v[188:189], v[170:171]
	v_pk_mul_f32 v[194:195], v[190:191], v[168:169]
	v_pk_mul_f32 v[170:171], v[184:185], v[170:171]
	v_pk_mul_f32 v[168:169], v[186:187], v[168:169]
	v_pk_fma_f32 v[192:193], v[184:185], v[166:167], v[192:193] neg_lo:[0,0,1] neg_hi:[0,0,1]
	v_pk_fma_f32 v[194:195], v[186:187], v[164:165], v[194:195] neg_lo:[0,0,1] neg_hi:[0,0,1]
	v_pk_fma_f32 v[166:167], v[188:189], v[166:167], v[170:171]
	v_pk_fma_f32 v[164:165], v[190:191], v[164:165], v[168:169]
	v_lshlrev_b32_e32 v168, 6, v180
	v_cvt_pk_bf16_f32 v164, v164, v165
	v_cvt_pk_bf16_f32 v165, v166, v167
	v_lshlrev_b64 v[166:167], 17, v[182:183]
	v_lshl_add_u64 v[166:167], s[18:19], 0, v[166:167]
	v_and_b32_e32 v168, 0x1ffc0, v168
	v_mov_b32_e32 v169, v2
	v_lshl_add_u64 v[166:167], v[166:167], 0, v[168:169]
	v_cvt_pk_bf16_f32 v194, v194, v195
	v_cvt_pk_bf16_f32 v195, v192, v193
	v_lshl_add_u64 v[166:167], v[166:167], 0, v[152:153]
	global_store_dwordx2 v[166:167], v[194:195], off
	global_store_dwordx2 v[166:167], v[164:165], off offset:32
	v_mov_b32_e32 v166, v149
	v_pk_mul_f32 v[168:169], v[118:119], v[166:167] op_sel_hi:[1,0]
	v_pk_mul_f32 v[170:171], v[116:117], v[166:167] op_sel_hi:[1,0]
	v_pk_mul_f32 v[180:181], v[114:115], v[166:167] op_sel_hi:[1,0]
	v_pk_mul_f32 v[166:167], v[112:113], v[166:167] op_sel_hi:[1,0]
	v_add_u32_e32 v186, s47, v162
	s_waitcnt vmcnt(6)
	v_pk_mul_f32 v[182:183], v[180:181], v[178:179]
	v_pk_mul_f32 v[184:185], v[166:167], v[176:177]
	v_ashrrev_i32_e32 v164, 11, v186
	v_pk_fma_f32 v[182:183], v[168:169], v[174:175], v[182:183] neg_lo:[0,0,1] neg_hi:[0,0,1]
	v_pk_fma_f32 v[184:185], v[170:171], v[172:173], v[184:185] neg_lo:[0,0,1] neg_hi:[0,0,1]
	v_pk_mul_f32 v[168:169], v[168:169], v[178:179]
	v_pk_mul_f32 v[170:171], v[170:171], v[176:177]
	v_pk_fma_f32 v[168:169], v[180:181], v[174:175], v[168:169]
	v_pk_fma_f32 v[166:167], v[166:167], v[172:173], v[170:171]
	v_ashrrev_i32_e32 v165, 31, v164
	v_cvt_pk_bf16_f32 v166, v166, v167
	v_cvt_pk_bf16_f32 v167, v168, v169
	v_lshlrev_b64 v[164:165], 17, v[164:165]
	v_lshlrev_b32_e32 v168, 6, v186
	v_lshl_add_u64 v[164:165], s[18:19], 0, v[164:165]
	v_and_b32_e32 v168, 0x1ffc0, v168
	v_mov_b32_e32 v169, v2
	v_lshl_add_u64 v[164:165], v[164:165], 0, v[168:169]
	v_cvt_pk_bf16_f32 v184, v184, v185
	v_cvt_pk_bf16_f32 v185, v182, v183
	v_lshl_add_u64 v[164:165], v[164:165], 0, v[152:153]
	global_store_dwordx2 v[164:165], v[184:185], off
	global_store_dwordx2 v[164:165], v[166:167], off offset:32
	v_add_u32_e32 v178, s70, v162
	s_waitcnt lgkmcnt(2)
	v_pk_mul_f32 v[166:167], v[110:111], v[146:147] op_sel_hi:[1,0]
	v_pk_mul_f32 v[168:169], v[108:109], v[146:147] op_sel_hi:[1,0]
	v_pk_mul_f32 v[170:171], v[106:107], v[146:147] op_sel_hi:[1,0]
	v_pk_mul_f32 v[172:173], v[104:105], v[146:147] op_sel_hi:[1,0]
	v_ashrrev_i32_e32 v164, 11, v178
	s_waitcnt vmcnt(6)
	v_pk_mul_f32 v[174:175], v[170:171], v[130:131]
	v_pk_mul_f32 v[176:177], v[172:173], v[128:129]
	v_pk_mul_f32 v[130:131], v[166:167], v[130:131]
	v_pk_mul_f32 v[128:129], v[168:169], v[128:129]
	v_pk_fma_f32 v[174:175], v[166:167], v[34:35], v[174:175] neg_lo:[0,0,1] neg_hi:[0,0,1]
	v_pk_fma_f32 v[176:177], v[168:169], v[32:33], v[176:177] neg_lo:[0,0,1] neg_hi:[0,0,1]
	v_pk_fma_f32 v[34:35], v[170:171], v[34:35], v[130:131]
	v_pk_fma_f32 v[32:33], v[172:173], v[32:33], v[128:129]
	v_ashrrev_i32_e32 v165, 31, v164
	v_cvt_pk_bf16_f32 v32, v32, v33
	v_cvt_pk_bf16_f32 v33, v34, v35
	v_lshlrev_b64 v[34:35], 17, v[164:165]
	v_lshlrev_b32_e32 v128, 6, v178
	v_lshl_add_u64 v[34:35], s[18:19], 0, v[34:35]
	v_and_b32_e32 v128, 0x1ffc0, v128
	v_mov_b32_e32 v129, v2
	v_lshl_add_u64 v[34:35], v[34:35], 0, v[128:129]
	v_cvt_pk_bf16_f32 v176, v176, v177
	v_cvt_pk_bf16_f32 v177, v174, v175
	v_lshl_add_u64 v[34:35], v[34:35], 0, v[152:153]
	global_store_dwordx2 v[34:35], v[176:177], off
	global_store_dwordx2 v[34:35], v[32:33], off offset:32
	v_mov_b32_e32 v34, v147
	v_add_u32_e32 v170, s71, v162
	v_pk_mul_f32 v[128:129], v[10:11], v[34:35] op_sel_hi:[1,0]
	v_pk_mul_f32 v[130:131], v[8:9], v[34:35] op_sel_hi:[1,0]
	v_pk_mul_f32 v[164:165], v[6:7], v[34:35] op_sel_hi:[1,0]
	v_pk_mul_f32 v[34:35], v[4:5], v[34:35] op_sel_hi:[1,0]
	v_ashrrev_i32_e32 v32, 11, v170
	s_waitcnt vmcnt(6)
	v_pk_mul_f32 v[166:167], v[164:165], v[18:19]
	v_pk_mul_f32 v[168:169], v[34:35], v[16:17]
	v_pk_mul_f32 v[18:19], v[128:129], v[18:19]
	v_pk_mul_f32 v[16:17], v[130:131], v[16:17]
	v_pk_fma_f32 v[166:167], v[128:129], v[14:15], v[166:167] neg_lo:[0,0,1] neg_hi:[0,0,1]
	v_pk_fma_f32 v[168:169], v[130:131], v[12:13], v[168:169] neg_lo:[0,0,1] neg_hi:[0,0,1]
	v_pk_fma_f32 v[14:15], v[164:165], v[14:15], v[18:19]
	v_pk_fma_f32 v[12:13], v[34:35], v[12:13], v[16:17]
	v_ashrrev_i32_e32 v33, 31, v32
	v_cvt_pk_bf16_f32 v12, v12, v13
	v_cvt_pk_bf16_f32 v13, v14, v15
	v_lshlrev_b64 v[14:15], 17, v[32:33]
	v_lshlrev_b32_e32 v16, 6, v170
	v_lshl_add_u64 v[14:15], s[18:19], 0, v[14:15]
	v_and_b32_e32 v16, 0x1ffc0, v16
	v_mov_b32_e32 v17, v2
	v_lshl_add_u64 v[14:15], v[14:15], 0, v[16:17]
	v_add_u32_e32 v180, s72, v162
	v_cvt_pk_bf16_f32 v168, v168, v169
	v_cvt_pk_bf16_f32 v169, v166, v167
	v_lshl_add_u64 v[14:15], v[14:15], 0, v[152:153]
	v_ashrrev_i32_e32 v181, 31, v180
	global_store_dwordx2 v[14:15], v[168:169], off
	global_store_dwordx2 v[14:15], v[12:13], off offset:32
	v_lshlrev_b64 v[12:13], 7, v[180:181]
	v_lshl_add_u64 v[12:13], s[4:5], 0, v[12:13]
	v_lshl_add_u64 v[16:17], v[12:13], 0, v[150:151]
	global_load_dwordx4 v[12:15], v[16:17], off sc0
	s_nop 0
	global_load_dwordx4 v[16:19], v[16:17], off offset:64 sc0
	v_add_u32_e32 v32, 16, v180
	v_ashrrev_i32_e32 v33, 31, v32
	v_lshlrev_b64 v[32:33], 7, v[32:33]
	v_lshl_add_u64 v[32:33], s[4:5], 0, v[32:33]
	v_lshl_add_u64 v[128:129], v[32:33], 0, v[150:151]
	global_load_dwordx4 v[32:35], v[128:129], off
	s_nop 0
	global_load_dwordx4 v[128:131], v[128:129], off offset:64
	v_add_u32_e32 v164, 32, v180
	v_ashrrev_i32_e32 v165, 31, v164
	v_lshlrev_b64 v[164:165], 7, v[164:165]
	v_lshl_add_u64 v[164:165], s[4:5], 0, v[164:165]
	v_lshl_add_u64 v[168:169], v[164:165], 0, v[150:151]
	global_load_dwordx4 v[164:167], v[168:169], off
	s_nop 0
	global_load_dwordx4 v[168:171], v[168:169], off offset:64
	v_add_u32_e32 v172, 48, v180
	v_ashrrev_i32_e32 v173, 31, v172
	v_lshlrev_b64 v[172:173], 7, v[172:173]
	v_lshl_add_u64 v[172:173], s[4:5], 0, v[172:173]
	v_lshl_add_u64 v[150:151], v[172:173], 0, v[150:151]
	global_load_dwordx4 v[172:175], v[150:151], off
	global_load_dwordx4 v[176:179], v[150:151], off offset:64
	s_waitcnt lgkmcnt(1)
	v_pk_mul_f32 v[182:183], v[102:103], v[144:145] op_sel_hi:[1,0]
	v_pk_mul_f32 v[184:185], v[100:101], v[144:145] op_sel_hi:[1,0]
	v_pk_mul_f32 v[186:187], v[98:99], v[144:145] op_sel_hi:[1,0]
	v_pk_mul_f32 v[188:189], v[96:97], v[144:145] op_sel_hi:[1,0]
	v_ashrrev_i32_e32 v150, 11, v180
	v_ashrrev_i32_e32 v151, 31, v150
	s_waitcnt vmcnt(6)
	v_pk_mul_f32 v[190:191], v[186:187], v[18:19]
	v_pk_mul_f32 v[192:193], v[188:189], v[16:17]
	v_pk_mul_f32 v[18:19], v[182:183], v[18:19]
	v_pk_mul_f32 v[16:17], v[184:185], v[16:17]
	v_pk_fma_f32 v[190:191], v[182:183], v[14:15], v[190:191] neg_lo:[0,0,1] neg_hi:[0,0,1]
	v_pk_fma_f32 v[192:193], v[184:185], v[12:13], v[192:193] neg_lo:[0,0,1] neg_hi:[0,0,1]
	v_pk_fma_f32 v[14:15], v[186:187], v[14:15], v[18:19]
	v_pk_fma_f32 v[12:13], v[188:189], v[12:13], v[16:17]
	v_lshlrev_b32_e32 v16, 6, v180
	v_cvt_pk_bf16_f32 v12, v12, v13
	v_cvt_pk_bf16_f32 v13, v14, v15
	v_lshlrev_b64 v[14:15], 17, v[150:151]
	v_lshl_add_u64 v[14:15], s[18:19], 0, v[14:15]
	v_and_b32_e32 v16, 0x1ffc0, v16
	v_mov_b32_e32 v17, v2
	v_lshl_add_u64 v[14:15], v[14:15], 0, v[16:17]
	v_cvt_pk_bf16_f32 v192, v192, v193
	v_cvt_pk_bf16_f32 v193, v190, v191
	v_lshl_add_u64 v[14:15], v[14:15], 0, v[152:153]
	global_store_dwordx2 v[14:15], v[192:193], off
	global_store_dwordx2 v[14:15], v[12:13], off offset:32
	v_mov_b32_e32 v14, v145
	v_pk_mul_f32 v[16:17], v[94:95], v[14:15] op_sel_hi:[1,0]
	v_pk_mul_f32 v[18:19], v[92:93], v[14:15] op_sel_hi:[1,0]
	v_pk_mul_f32 v[150:151], v[90:91], v[14:15] op_sel_hi:[1,0]
	v_pk_mul_f32 v[14:15], v[88:89], v[14:15] op_sel_hi:[1,0]
	v_add_u32_e32 v184, s73, v162
	s_waitcnt vmcnt(6)
	v_pk_mul_f32 v[180:181], v[150:151], v[130:131]
	v_pk_mul_f32 v[182:183], v[14:15], v[128:129]
	v_ashrrev_i32_e32 v12, 11, v184
	v_pk_fma_f32 v[180:181], v[16:17], v[34:35], v[180:181] neg_lo:[0,0,1] neg_hi:[0,0,1]
	v_pk_fma_f32 v[182:183], v[18:19], v[32:33], v[182:183] neg_lo:[0,0,1] neg_hi:[0,0,1]
	v_pk_mul_f32 v[16:17], v[16:17], v[130:131]
	v_pk_mul_f32 v[18:19], v[18:19], v[128:129]
	v_pk_fma_f32 v[16:17], v[150:151], v[34:35], v[16:17]
	v_pk_fma_f32 v[14:15], v[14:15], v[32:33], v[18:19]
	v_ashrrev_i32_e32 v13, 31, v12
	v_cvt_pk_bf16_f32 v14, v14, v15
	v_cvt_pk_bf16_f32 v15, v16, v17
	v_lshlrev_b64 v[12:13], 17, v[12:13]
	v_lshlrev_b32_e32 v16, 6, v184
	v_lshl_add_u64 v[12:13], s[18:19], 0, v[12:13]
	v_and_b32_e32 v16, 0x1ffc0, v16
	v_mov_b32_e32 v17, v2
	v_lshl_add_u64 v[12:13], v[12:13], 0, v[16:17]
	v_cvt_pk_bf16_f32 v182, v182, v183
	v_cvt_pk_bf16_f32 v183, v180, v181
	v_lshl_add_u64 v[12:13], v[12:13], 0, v[152:153]
	s_waitcnt lgkmcnt(0)
	v_pk_mul_f32 v[18:19], v[30:31], v[142:143] op_sel_hi:[1,0]
	v_pk_mul_f32 v[32:33], v[28:29], v[142:143] op_sel_hi:[1,0]
	global_store_dwordx2 v[12:13], v[182:183], off
	global_store_dwordx2 v[12:13], v[14:15], off offset:32
	v_add_u32_e32 v130, s74, v162
	v_pk_mul_f32 v[14:15], v[86:87], v[142:143] op_sel_hi:[1,0]
	v_pk_mul_f32 v[16:17], v[84:85], v[142:143] op_sel_hi:[1,0]
	s_waitcnt vmcnt(6)
	v_pk_mul_f32 v[34:35], v[18:19], v[170:171]
	v_pk_mul_f32 v[128:129], v[32:33], v[168:169]
	v_ashrrev_i32_e32 v12, 11, v130
	v_pk_fma_f32 v[34:35], v[14:15], v[166:167], v[34:35] neg_lo:[0,0,1] neg_hi:[0,0,1]
	v_pk_fma_f32 v[128:129], v[16:17], v[164:165], v[128:129] neg_lo:[0,0,1] neg_hi:[0,0,1]
	v_pk_mul_f32 v[14:15], v[14:15], v[170:171]
	v_pk_mul_f32 v[16:17], v[16:17], v[168:169]
	v_pk_fma_f32 v[14:15], v[18:19], v[166:167], v[14:15]
	v_pk_fma_f32 v[16:17], v[32:33], v[164:165], v[16:17]
	v_ashrrev_i32_e32 v13, 31, v12
	v_cvt_pk_bf16_f32 v16, v16, v17
	v_cvt_pk_bf16_f32 v17, v14, v15
	v_lshlrev_b64 v[12:13], 17, v[12:13]
	v_lshlrev_b32_e32 v14, 6, v130
	v_lshl_add_u64 v[12:13], s[18:19], 0, v[12:13]
	v_and_b32_e32 v14, 0x1ffc0, v14
	v_mov_b32_e32 v15, v2
	v_lshl_add_u64 v[12:13], v[12:13], 0, v[14:15]
	v_cvt_pk_bf16_f32 v128, v128, v129
	v_cvt_pk_bf16_f32 v129, v34, v35
	v_lshl_add_u64 v[12:13], v[12:13], 0, v[152:153]
	v_mov_b32_e32 v14, v143
	global_store_dwordx2 v[12:13], v[128:129], off
	global_store_dwordx2 v[12:13], v[16:17], off offset:32
	v_pk_mul_f32 v[16:17], v[26:27], v[14:15] op_sel_hi:[1,0]
	v_pk_mul_f32 v[18:19], v[24:25], v[14:15] op_sel_hi:[1,0]
	v_pk_mul_f32 v[32:33], v[22:23], v[14:15] op_sel_hi:[1,0]
	v_pk_mul_f32 v[14:15], v[20:21], v[14:15] op_sel_hi:[1,0]
	v_add_u32_e32 v130, s75, v162
	s_waitcnt vmcnt(6)
	v_pk_mul_f32 v[34:35], v[32:33], v[178:179]
	v_pk_mul_f32 v[128:129], v[14:15], v[176:177]
	v_ashrrev_i32_e32 v12, 11, v130
	v_pk_fma_f32 v[34:35], v[16:17], v[174:175], v[34:35] neg_lo:[0,0,1] neg_hi:[0,0,1]
	v_pk_fma_f32 v[128:129], v[18:19], v[172:173], v[128:129] neg_lo:[0,0,1] neg_hi:[0,0,1]
	v_pk_mul_f32 v[16:17], v[16:17], v[178:179]
	v_pk_mul_f32 v[18:19], v[18:19], v[176:177]
	v_pk_fma_f32 v[16:17], v[32:33], v[174:175], v[16:17]
	v_pk_fma_f32 v[14:15], v[14:15], v[172:173], v[18:19]
	v_ashrrev_i32_e32 v13, 31, v12
	v_cvt_pk_bf16_f32 v14, v14, v15
	v_cvt_pk_bf16_f32 v15, v16, v17
	v_lshlrev_b64 v[12:13], 17, v[12:13]
	v_lshlrev_b32_e32 v16, 6, v130
	v_lshl_add_u64 v[12:13], s[18:19], 0, v[12:13]
	v_and_b32_e32 v16, 0x1ffc0, v16
	v_mov_b32_e32 v17, v2
	v_lshl_add_u64 v[12:13], v[12:13], 0, v[16:17]
	v_cvt_pk_bf16_f32 v128, v128, v129
	v_cvt_pk_bf16_f32 v129, v34, v35
	v_lshl_add_u64 v[12:13], v[12:13], 0, v[152:153]
	global_store_dwordx2 v[12:13], v[128:129], off
	global_store_dwordx2 v[12:13], v[14:15], off offset:32

.LBB0_402:
	s_add_i32 s12, s66, 1
	s_cmp_lg_u32 s12, 8
	s_cselect_b32 s66, s12, 0
	s_add_i32 s12, s66, s81
	s_lshl_b32 s38, s12, 7
	s_add_i32 s39, s38, 0xfffffc00
	s_cmp_gt_i32 s12, 7
	s_cselect_b32 s12, s39, s38
	v_or_b32_e32 v12, s12, v154
	s_add_i32 s12, s61, s23
	s_add_i32 s38, s12, -4
	s_cmp_gt_i32 s12, 3
	s_cselect_b32 s38, s38, s12
	s_add_i32 s12, s67, s81
	s_lshl_b32 s61, s12, 2
	ds_read_b128 v[32:35], v158 offset:32768
	ds_read_b128 v[128:131], v158 offset:36864
	ds_read_b128 v[142:145], v158 offset:40960
	ds_read_b128 v[146:149], v158 offset:45056
	ds_read_b128 v[150:153], v158 offset:49152
	ds_read_b128 v[162:165], v158 offset:53248
	ds_read_b128 v[166:169], v158 offset:57344
	ds_read_b128 v[170:173], v158 offset:61440
	s_ashr_i32 s39, s38, 31
	s_sub_i32 s67, s61, 32
	s_cmp_gt_i32 s12, 7
	s_cselect_b32 s96, s67, s61
	s_ashr_i32 s97, s96, 31
	s_lshl_b64 s[38:39], s[38:39], 19
	v_ashrrev_i32_e32 v13, 31, v12
	v_lshl_add_u64 v[14:15], v[140:141], 0, s[38:39]
	s_lshl_b64 s[38:39], s[96:97], 10
	v_lshlrev_b64 v[12:13], 1, v[12:13]
	v_lshl_add_u64 v[186:187], v[14:15], 0, s[38:39]
	v_lshl_add_u64 v[182:183], v[136:137], 0, v[12:13]
	v_lshl_add_u64 v[184:185], v[138:139], 0, v[12:13]
	v_lshl_add_u64 v[14:15], v[132:133], 0, v[12:13]
	v_lshl_add_u64 v[12:13], v[134:135], 0, v[12:13]
	global_load_dwordx4 v[16:19], v[14:15], off
	s_nop 0
	global_load_dwordx4 v[12:15], v[12:13], off
	s_waitcnt vmcnt(9) lgkmcnt(7)
	v_mfma_f32_16x16x32_bf16 v[120:123], v[36:39], v[32:35], v[120:123]
	s_waitcnt vmcnt(8)
	v_mfma_f32_16x16x32_bf16 v[32:35], v[48:51], v[32:35], v[124:127]
	s_waitcnt lgkmcnt(6)
	v_mfma_f32_16x16x32_bf16 v[116:119], v[36:39], v[128:131], v[116:119]
	v_mfma_f32_16x16x32_bf16 v[112:115], v[48:51], v[128:131], v[112:115]
	s_waitcnt lgkmcnt(5)
	v_mfma_f32_16x16x32_bf16 v[108:111], v[36:39], v[142:145], v[108:111]
	v_mfma_f32_16x16x32_bf16 v[104:107], v[48:51], v[142:145], v[104:107]
	s_waitcnt lgkmcnt(4)
	v_mfma_f32_16x16x32_bf16 v[124:127], v[36:39], v[146:149], v[8:11]
	v_mfma_f32_16x16x32_bf16 v[128:131], v[48:51], v[146:149], v[4:7]
	ds_read_b128 v[142:145], v159 offset:32768
	ds_read_b128 v[146:149], v159 offset:36864
	ds_read_b128 v[174:177], v159 offset:40960
	ds_read_b128 v[178:181], v159 offset:45056
	global_load_dwordx4 v[8:11], v[182:183], off sc0
	global_load_dwordx4 v[4:7], v[184:185], off
	s_waitcnt lgkmcnt(7)
	v_mfma_f32_16x16x32_bf16 v[100:103], v[36:39], v[150:153], v[100:103]
	v_mfma_f32_16x16x32_bf16 v[96:99], v[48:51], v[150:153], v[96:99]
	s_waitcnt lgkmcnt(6)
	v_mfma_f32_16x16x32_bf16 v[92:95], v[36:39], v[162:165], v[92:95]
	v_mfma_f32_16x16x32_bf16 v[88:91], v[48:51], v[162:165], v[88:91]
	s_waitcnt lgkmcnt(5)
	v_mfma_f32_16x16x32_bf16 v[84:87], v[36:39], v[166:169], v[84:87]
	s_waitcnt lgkmcnt(4)
	v_mfma_f32_16x16x32_bf16 v[24:27], v[36:39], v[170:173], v[24:27]
	v_mfma_f32_16x16x32_bf16 v[20:23], v[48:51], v[170:173], v[20:23]
	v_mfma_f32_16x16x32_bf16 v[150:153], v[48:51], v[166:169], v[28:31]
	ds_read_b128 v[162:165], v159 offset:49152
	ds_read_b128 v[166:169], v159 offset:53248
	ds_read_b128 v[170:173], v159 offset:57344
	ds_read_b128 v[182:185], v159 offset:61440
	v_add_co_u32_e32 v188, vcc, s14, v186
	s_nop 1
	v_addc_co_u32_e32 v189, vcc, 0, v187, vcc
	global_load_dwordx4 v[36:39], v[186:187], off sc0
	global_load_dwordx4 v[48:51], v[188:189], off sc0
	ds_write_b128 v157, v[64:67]
	s_waitcnt vmcnt(11) lgkmcnt(8)
	v_mfma_f32_16x16x32_bf16 v[64:67], v[76:79], v[142:145], v[120:123]
	s_waitcnt vmcnt(9)
	v_mfma_f32_16x16x32_bf16 v[32:35], v[44:47], v[142:145], v[32:35]
	s_waitcnt lgkmcnt(7)
	v_mfma_f32_16x16x32_bf16 v[116:119], v[76:79], v[146:149], v[116:119]
	v_mfma_f32_16x16x32_bf16 v[112:115], v[44:47], v[146:149], v[112:115]
	s_waitcnt lgkmcnt(6)
	v_mfma_f32_16x16x32_bf16 v[108:111], v[76:79], v[174:177], v[108:111]
	v_mfma_f32_16x16x32_bf16 v[104:107], v[44:47], v[174:177], v[104:107]
	s_waitcnt lgkmcnt(5)
	v_mfma_f32_16x16x32_bf16 v[120:123], v[76:79], v[178:181], v[124:127]
	v_mfma_f32_16x16x32_bf16 v[124:127], v[44:47], v[178:181], v[128:131]
	s_nop 2
	ds_read_b128 v[128:131], v160 offset:32768
	ds_read_b128 v[142:145], v160 offset:36864
	ds_read_b128 v[146:149], v160 offset:40960
	ds_read_b128 v[174:177], v160 offset:45056
	global_load_dwordx4 v[28:31], v[186:187], off offset:1024 sc0
	ds_write_b128 v157, v[60:63] offset:8192
	s_waitcnt lgkmcnt(9)
	v_mfma_f32_16x16x32_bf16 v[60:63], v[76:79], v[162:165], v[100:103]
	v_mfma_f32_16x16x32_bf16 v[96:99], v[44:47], v[162:165], v[96:99]
	s_waitcnt lgkmcnt(8)
	v_mfma_f32_16x16x32_bf16 v[92:95], v[76:79], v[166:169], v[92:95]
	v_mfma_f32_16x16x32_bf16 v[88:91], v[44:47], v[166:169], v[88:91]
	s_waitcnt lgkmcnt(7)
	v_mfma_f32_16x16x32_bf16 v[84:87], v[76:79], v[170:173], v[84:87]
	v_mfma_f32_16x16x32_bf16 v[100:103], v[44:47], v[170:173], v[150:153]
	s_waitcnt lgkmcnt(6)
	v_mfma_f32_16x16x32_bf16 v[76:79], v[76:79], v[182:185], v[24:27]
	v_mfma_f32_16x16x32_bf16 v[150:153], v[44:47], v[182:185], v[20:23]
	ds_read_b128 v[162:165], v160 offset:49152
	ds_read_b128 v[166:169], v160 offset:53248
	ds_read_b128 v[170:173], v160 offset:57344
	ds_read_b128 v[178:181], v160 offset:61440
	global_load_dwordx4 v[24:27], v[186:187], off offset:2048 sc0
	global_load_dwordx4 v[44:47], v[188:189], off offset:1024 sc0
	ds_write_b128 v157, v[56:59] offset:16384
	s_waitcnt lgkmcnt(9)
	v_mfma_f32_16x16x32_bf16 v[56:59], v[72:75], v[128:131], v[64:67]
	s_waitcnt vmcnt(10)
	v_mfma_f32_16x16x32_bf16 v[32:35], v[40:43], v[128:131], v[32:35]
	s_waitcnt lgkmcnt(8)
	v_mfma_f32_16x16x32_bf16 v[112:115], v[40:43], v[142:145], v[112:115]
	s_waitcnt lgkmcnt(7)
	v_mfma_f32_16x16x32_bf16 v[108:111], v[72:75], v[146:149], v[108:111]
	v_mfma_f32_16x16x32_bf16 v[104:107], v[40:43], v[146:149], v[104:107]
	v_mfma_f32_16x16x32_bf16 v[64:67], v[72:75], v[142:145], v[116:119]
	s_waitcnt lgkmcnt(6)
	v_mfma_f32_16x16x32_bf16 v[128:131], v[72:75], v[174:177], v[120:123]
	v_mfma_f32_16x16x32_bf16 v[142:145], v[40:43], v[174:177], v[124:127]
	ds_read_b128 v[116:119], v161 offset:32768
	ds_read_b128 v[146:149], v161 offset:36864
	ds_read_b128 v[174:177], v161 offset:40960
	ds_read_b128 v[182:185], v161 offset:45056
	global_load_dwordx4 v[20:23], v[186:187], off offset:3072 sc0
	ds_write_b128 v157, v[52:55] offset:24576
	s_waitcnt lgkmcnt(9)
	v_mfma_f32_16x16x32_bf16 v[60:63], v[72:75], v[162:165], v[60:63]
	v_mfma_f32_16x16x32_bf16 v[96:99], v[40:43], v[162:165], v[96:99]
	s_waitcnt lgkmcnt(8)
	v_mfma_f32_16x16x32_bf16 v[92:95], v[72:75], v[166:169], v[92:95]
	v_mfma_f32_16x16x32_bf16 v[88:91], v[40:43], v[166:169], v[88:91]
	s_waitcnt lgkmcnt(7)
	v_mfma_f32_16x16x32_bf16 v[84:87], v[72:75], v[170:173], v[84:87]
	s_waitcnt lgkmcnt(6)
	v_mfma_f32_16x16x32_bf16 v[72:75], v[72:75], v[178:181], v[76:79]
	v_mfma_f32_16x16x32_bf16 v[162:165], v[40:43], v[170:173], v[100:103]
	v_mfma_f32_16x16x32_bf16 v[150:153], v[40:43], v[178:181], v[150:153]
	s_nop 0
	ds_read_b128 v[76:79], v161 offset:49152
	ds_read_b128 v[166:169], v161 offset:53248
	ds_read_b128 v[170:173], v161 offset:57344
	ds_read_b128 v[178:181], v161 offset:61440
	global_load_dwordx4 v[40:43], v[188:189], off offset:2048 sc0
	s_waitcnt lgkmcnt(8)
	v_mfma_f32_16x16x32_bf16 v[124:127], v[68:71], v[116:119], v[56:59]
	s_waitcnt vmcnt(11)
	v_mfma_f32_16x16x32_bf16 v[120:123], v[80:83], v[116:119], v[32:35]
	s_waitcnt lgkmcnt(7)
	v_mfma_f32_16x16x32_bf16 v[116:119], v[68:71], v[146:149], v[64:67]
	v_mfma_f32_16x16x32_bf16 v[112:115], v[80:83], v[146:149], v[112:115]
	s_waitcnt lgkmcnt(6)
	v_mfma_f32_16x16x32_bf16 v[108:111], v[68:71], v[174:177], v[108:111]
	v_mfma_f32_16x16x32_bf16 v[104:107], v[80:83], v[174:177], v[104:107]
	s_waitcnt lgkmcnt(5)
	v_mfma_f32_16x16x32_bf16 v[56:59], v[68:71], v[182:185], v[128:131]
	v_mfma_f32_16x16x32_bf16 v[52:55], v[80:83], v[182:185], v[142:145]
	global_load_dwordx4 v[32:35], v[188:189], off offset:3072 sc0
	s_waitcnt lgkmcnt(3)
	v_mfma_f32_16x16x32_bf16 v[100:103], v[68:71], v[76:79], v[60:63]
	v_mfma_f32_16x16x32_bf16 v[96:99], v[80:83], v[76:79], v[96:99]
	s_waitcnt lgkmcnt(2)
	v_mfma_f32_16x16x32_bf16 v[92:95], v[68:71], v[166:169], v[92:95]
	v_mfma_f32_16x16x32_bf16 v[88:91], v[80:83], v[166:169], v[88:91]
	s_waitcnt lgkmcnt(1)
	v_mfma_f32_16x16x32_bf16 v[84:87], v[68:71], v[170:173], v[84:87]
	v_mfma_f32_16x16x32_bf16 v[76:79], v[80:83], v[170:173], v[162:165]
	s_waitcnt lgkmcnt(0)
	v_mfma_f32_16x16x32_bf16 v[72:75], v[68:71], v[178:181], v[72:75]
	v_mfma_f32_16x16x32_bf16 v[68:71], v[80:83], v[178:181], v[150:153]
	s_cmp_eq_u32 s62, -1
	s_cselect_b64 s[38:39], -1, 0
	s_and_b64 s[38:39], s[38:39], s[48:49]
	s_andn2_b64 vcc, exec, s[38:39]
	s_cbranch_vccnz .LBB0_404
	v_mov_b32_e32 v60, v155
	v_mov_b32_e32 v61, v156

.LBB0_441:
	s_or_b64 exec, exec, s[38:39]
	s_waitcnt vmcnt(7)
	v_mov_b32_e32 v36, v0
	s_waitcnt lgkmcnt(0)
	s_barrier
	v_readlane_b32 s18, v248, 23
	v_readfirstlane_b32 s0, v36
	s_ashr_i32 s50, s0, 6
	s_cmp_lt_i32 s50, 8
	s_cselect_b64 s[0:1], -1, 0
	s_and_b64 s[38:39], s[0:1], exec
	s_cselect_b32 s38, s50, 7
	s_ashr_i32 s39, s38, 31
	s_lshl_b64 s[38:39], s[38:39], 14
	v_and_b32_e32 v3, 63, v36
	s_add_u32 s38, s26, s38
	s_addc_u32 s39, s27, s39
	v_lshlrev_b32_e32 v4, 4, v3
	v_mov_b32_e32 v5, v2
	v_readlane_b32 s19, v248, 24
	v_lshl_add_u64 v[124:125], s[38:39], 0, v[4:5]
	s_mov_b32 s19, s21
	v_lshl_add_u64 v[16:17], v[124:125], 0, s[18:19]
	global_load_dwordx4 v[20:23], v[16:17], off sc0
	global_load_dwordx4 v[12:15], v[16:17], off offset:1024 sc0
	global_load_dwordx4 v[8:11], v[16:17], off offset:2048 sc0
	global_load_dwordx4 v[4:7], v[16:17], off offset:3072 sc0
	v_add_co_u32_e32 v16, vcc, s94, v16
	v_bfe_u32 v127, v36, 4, 2
	s_nop 0
	v_addc_co_u32_e32 v17, vcc, 0, v17, vcc
	global_load_dwordx4 v[32:35], v[16:17], off sc0
	global_load_dwordx4 v[28:31], v[16:17], off offset:1024 sc0
	global_load_dwordx4 v[24:27], v[16:17], off offset:2048 sc0
	s_nop 0
	global_load_dwordx4 v[16:19], v[16:17], off offset:3072 sc0
	s_mov_b32 s12, s18
	v_and_b32_e32 v3, 15, v36
	v_bitop3_b32 v36, v127, v36, 15 bitop3:0x78
	v_writelane_b32 v248, s12, 23
	v_lshlrev_b32_e32 v133, 4, v36
	v_bitop3_b32 v36, v127, v3, 4 bitop3:0x36
	v_writelane_b32 v248, s13, 24
	v_lshlrev_b32_e32 v143, 4, v36
	v_bitop3_b32 v36, v127, v3, 8 bitop3:0x36
	v_lshlrev_b32_e32 v37, 8, v3
	s_add_i32 s20, 0, 0x10000
	v_readlane_b32 s18, v248, 8
	v_lshlrev_b32_e32 v147, 4, v36
	v_bitop3_b32 v36, v127, v3, 12 bitop3:0x36
	s_mov_b32 s38, 1
	s_mov_b32 s12, 0
	v_add_u32_e32 v129, s20, v37
	v_add_u32_e32 v139, s18, v37
	v_lshlrev_b32_e32 v151, 4, v36
	v_readlane_b32 s51, v249, 61
	s_mov_b32 s52, 0
	s_movk_i32 s84, 0xf0
	s_barrier
	s_branch .LBB0_443

.LBB0_443:
	s_add_i32 s20, s12, s33
	s_add_i32 s39, s20, -3
	s_cmp_gt_i32 s20, 2
	s_cselect_b32 s40, s39, s20
	s_ashr_i32 s41, s40, 31
	s_lshl_b32 s20, s38, 2
	s_lshl_b64 s[40:41], s[40:41], 17
	s_lshl_b64 s[48:49], s[20:21], 10
	v_add_u32_e32 v64, v129, v133
	v_lshl_add_u64 v[52:53], v[124:125], 0, s[40:41]
	s_cmp_lt_i32 s12, 2
	ds_read_b128 v[36:39], v64
	s_waitcnt vmcnt(9)
	ds_read_b128 v[40:43], v64 offset:4096
	ds_read_b128 v[44:47], v64 offset:8192
	ds_read_b128 v[48:51], v64 offset:12288
	v_lshl_add_u64 v[130:131], v[52:53], 0, s[48:49]
	ds_read_b128 v[52:55], v64 offset:16384
	ds_read_b128 v[56:59], v64 offset:20480
	ds_read_b128 v[60:63], v64 offset:24576
	ds_read_b128 v[64:67], v64 offset:28672
	s_cselect_b64 s[54:55], -1, 0
	s_and_b64 s[56:57], s[54:55], exec
	s_cselect_b32 s20, 0, s38
	s_cmp_gt_i32 s38, 0
	s_cselect_b64 s[38:39], -1, 0
	s_and_b64 s[40:41], s[38:39], exec
	s_cselect_b32 s53, s20, 1
	s_and_b64 s[38:39], s[38:39], s[54:55]
	s_waitcnt vmcnt(7) lgkmcnt(7)
	v_mfma_f32_16x16x32_bf16 v[68:71], v[20:23], v[36:39], 0
	s_waitcnt vmcnt(3)
	v_mfma_f32_16x16x32_bf16 v[36:39], v[32:35], v[36:39], 0
	s_waitcnt lgkmcnt(6)
	v_mfma_f32_16x16x32_bf16 v[72:75], v[20:23], v[40:43], 0
	v_mfma_f32_16x16x32_bf16 v[40:43], v[32:35], v[40:43], 0
	s_waitcnt lgkmcnt(5)
	v_mfma_f32_16x16x32_bf16 v[76:79], v[20:23], v[44:47], 0
	v_mfma_f32_16x16x32_bf16 v[44:47], v[32:35], v[44:47], 0
	s_waitcnt lgkmcnt(4)
	v_mfma_f32_16x16x32_bf16 v[80:83], v[20:23], v[48:51], 0
	v_mfma_f32_16x16x32_bf16 v[48:51], v[32:35], v[48:51], 0
	v_add_u32_e32 v120, v129, v143
	ds_read_b128 v[84:87], v120
	ds_read_b128 v[88:91], v120 offset:4096
	ds_read_b128 v[92:95], v120 offset:8192
	ds_read_b128 v[96:99], v120 offset:12288
	s_waitcnt lgkmcnt(7)
	v_mfma_f32_16x16x32_bf16 v[100:103], v[20:23], v[52:55], 0
	v_mfma_f32_16x16x32_bf16 v[52:55], v[32:35], v[52:55], 0
	s_waitcnt lgkmcnt(6)
	v_mfma_f32_16x16x32_bf16 v[104:107], v[20:23], v[56:59], 0
	v_mfma_f32_16x16x32_bf16 v[56:59], v[32:35], v[56:59], 0
	s_waitcnt lgkmcnt(5)
	v_mfma_f32_16x16x32_bf16 v[108:111], v[20:23], v[60:63], 0
	v_mfma_f32_16x16x32_bf16 v[60:63], v[32:35], v[60:63], 0
	s_waitcnt lgkmcnt(4)
	v_mfma_f32_16x16x32_bf16 v[20:23], v[20:23], v[64:67], 0
	v_mfma_f32_16x16x32_bf16 v[32:35], v[32:35], v[64:67], 0
	ds_read_b128 v[64:67], v120 offset:16384
	ds_read_b128 v[112:115], v120 offset:20480
	ds_read_b128 v[116:119], v120 offset:24576
	ds_read_b128 v[120:123], v120 offset:28672
	s_movk_i32 s18, 0x2000
	v_add_co_u32_e32 v140, vcc, s18, v130
	s_nop 1
	v_addc_co_u32_e32 v141, vcc, 0, v131, vcc
	global_load_dwordx4 v[134:137], v[130:131], off sc0
	global_load_dwordx4 v[152:155], v[140:141], off sc0
	s_waitcnt lgkmcnt(7)
	v_mfma_f32_16x16x32_bf16 v[68:71], v[12:15], v[84:87], v[68:71]
	s_waitcnt vmcnt(4)
	v_mfma_f32_16x16x32_bf16 v[36:39], v[28:31], v[84:87], v[36:39]
	s_waitcnt lgkmcnt(6)
	v_mfma_f32_16x16x32_bf16 v[72:75], v[12:15], v[88:91], v[72:75]
	v_mfma_f32_16x16x32_bf16 v[40:43], v[28:31], v[88:91], v[40:43]
	s_waitcnt lgkmcnt(5)
	v_mfma_f32_16x16x32_bf16 v[76:79], v[12:15], v[92:95], v[76:79]
	v_mfma_f32_16x16x32_bf16 v[44:47], v[28:31], v[92:95], v[44:47]
	s_waitcnt lgkmcnt(4)
	v_mfma_f32_16x16x32_bf16 v[80:83], v[12:15], v[96:99], v[80:83]
	v_mfma_f32_16x16x32_bf16 v[48:51], v[28:31], v[96:99], v[48:51]
	v_add_u32_e32 v126, v129, v147
	ds_read_b128 v[84:87], v126
	ds_read_b128 v[88:91], v126 offset:4096
	ds_read_b128 v[92:95], v126 offset:8192
	ds_read_b128 v[96:99], v126 offset:12288
	global_load_dwordx4 v[156:159], v[130:131], off offset:1024 sc0
	s_waitcnt lgkmcnt(7)
	v_mfma_f32_16x16x32_bf16 v[100:103], v[12:15], v[64:67], v[100:103]
	v_mfma_f32_16x16x32_bf16 v[52:55], v[28:31], v[64:67], v[52:55]
	s_waitcnt lgkmcnt(6)
	v_mfma_f32_16x16x32_bf16 v[64:67], v[12:15], v[112:115], v[104:107]
	v_mfma_f32_16x16x32_bf16 v[56:59], v[28:31], v[112:115], v[56:59]
	s_waitcnt lgkmcnt(5)
	v_mfma_f32_16x16x32_bf16 v[104:107], v[12:15], v[116:119], v[108:111]
	v_mfma_f32_16x16x32_bf16 v[60:63], v[28:31], v[116:119], v[60:63]
	s_waitcnt lgkmcnt(4)
	v_mfma_f32_16x16x32_bf16 v[12:15], v[12:15], v[120:123], v[20:23]
	v_mfma_f32_16x16x32_bf16 v[20:23], v[28:31], v[120:123], v[32:35]
	ds_read_b128 v[28:31], v126 offset:16384
	s_nop 1
	ds_read_b128 v[32:35], v126 offset:20480
	ds_read_b128 v[108:111], v126 offset:24576
	ds_read_b128 v[112:115], v126 offset:28672
	global_load_dwordx4 v[116:119], v[130:131], off offset:2048 sc0
	global_load_dwordx4 v[120:123], v[140:141], off offset:1024 sc0
	s_waitcnt lgkmcnt(7)
	v_mfma_f32_16x16x32_bf16 v[68:71], v[8:11], v[84:87], v[68:71]
	s_waitcnt vmcnt(6)
	v_mfma_f32_16x16x32_bf16 v[36:39], v[24:27], v[84:87], v[36:39]
	s_waitcnt lgkmcnt(6)
	v_mfma_f32_16x16x32_bf16 v[72:75], v[8:11], v[88:91], v[72:75]
	v_mfma_f32_16x16x32_bf16 v[40:43], v[24:27], v[88:91], v[40:43]
	s_waitcnt lgkmcnt(5)
	v_mfma_f32_16x16x32_bf16 v[76:79], v[8:11], v[92:95], v[76:79]
	v_mfma_f32_16x16x32_bf16 v[44:47], v[24:27], v[92:95], v[44:47]
	s_waitcnt lgkmcnt(4)
	v_mfma_f32_16x16x32_bf16 v[80:83], v[8:11], v[96:99], v[80:83]
	v_mfma_f32_16x16x32_bf16 v[48:51], v[24:27], v[96:99], v[48:51]
	v_add_u32_e32 v126, v129, v151
	ds_read_b128 v[84:87], v126
	ds_read_b128 v[88:91], v126 offset:4096
	ds_read_b128 v[92:95], v126 offset:8192
	ds_read_b128 v[96:99], v126 offset:12288
	global_load_dwordx4 v[160:163], v[130:131], off offset:3072 sc0
	s_waitcnt lgkmcnt(7)
	v_mfma_f32_16x16x32_bf16 v[100:103], v[8:11], v[28:31], v[100:103]
	v_mfma_f32_16x16x32_bf16 v[28:31], v[24:27], v[28:31], v[52:55]
	s_waitcnt lgkmcnt(6)
	v_mfma_f32_16x16x32_bf16 v[52:55], v[8:11], v[32:35], v[64:67]
	v_mfma_f32_16x16x32_bf16 v[32:35], v[24:27], v[32:35], v[56:59]
	s_waitcnt lgkmcnt(5)
	v_mfma_f32_16x16x32_bf16 v[56:59], v[8:11], v[108:111], v[104:107]
	v_mfma_f32_16x16x32_bf16 v[60:63], v[24:27], v[108:111], v[60:63]
	s_waitcnt lgkmcnt(4)
	v_mfma_f32_16x16x32_bf16 v[8:11], v[8:11], v[112:115], v[12:15]
	v_mfma_f32_16x16x32_bf16 v[12:15], v[24:27], v[112:115], v[20:23]
	s_nop 2
	ds_read_b128 v[20:23], v126 offset:16384
	ds_read_b128 v[24:27], v126 offset:20480
	ds_read_b128 v[64:67], v126 offset:24576
	ds_read_b128 v[104:107], v126 offset:28672
	global_load_dwordx4 v[108:111], v[140:141], off offset:2048 sc0
	s_waitcnt lgkmcnt(7)
	v_mfma_f32_16x16x32_bf16 v[68:71], v[4:7], v[84:87], v[68:71]
	s_waitcnt vmcnt(7)
	v_mfma_f32_16x16x32_bf16 v[36:39], v[16:19], v[84:87], v[36:39]
	s_waitcnt lgkmcnt(6)
	v_mfma_f32_16x16x32_bf16 v[72:75], v[4:7], v[88:91], v[72:75]
	v_mfma_f32_16x16x32_bf16 v[40:43], v[16:19], v[88:91], v[40:43]
	s_waitcnt lgkmcnt(5)
	v_mfma_f32_16x16x32_bf16 v[76:79], v[4:7], v[92:95], v[76:79]
	v_mfma_f32_16x16x32_bf16 v[44:47], v[16:19], v[92:95], v[44:47]
	s_waitcnt lgkmcnt(4)
	v_mfma_f32_16x16x32_bf16 v[80:83], v[4:7], v[96:99], v[80:83]
	v_mfma_f32_16x16x32_bf16 v[48:51], v[16:19], v[96:99], v[48:51]
	global_load_dwordx4 v[112:115], v[140:141], off offset:3072 sc0
	s_waitcnt lgkmcnt(3)
	v_mfma_f32_16x16x32_bf16 v[84:87], v[4:7], v[20:23], v[100:103]
	v_mfma_f32_16x16x32_bf16 v[20:23], v[16:19], v[20:23], v[28:31]
	s_waitcnt lgkmcnt(2)
	v_mfma_f32_16x16x32_bf16 v[28:31], v[4:7], v[24:27], v[52:55]
	v_mfma_f32_16x16x32_bf16 v[24:27], v[16:19], v[24:27], v[32:35]
	s_waitcnt lgkmcnt(1)
	v_mfma_f32_16x16x32_bf16 v[32:35], v[4:7], v[64:67], v[56:59]
	v_mfma_f32_16x16x32_bf16 v[52:55], v[16:19], v[64:67], v[60:63]
	s_waitcnt lgkmcnt(0)
	v_mfma_f32_16x16x32_bf16 v[4:7], v[4:7], v[104:107], v[8:11]
	v_mfma_f32_16x16x32_bf16 v[8:11], v[16:19], v[104:107], v[12:15]
	s_cmp_lg_u64 s[38:39], 0
	s_addc_u32 s54, s12, 0
	s_cmp_lg_u64 s[38:39], 0
	s_addc_u32 s12, s33, s12
	s_add_i32 s20, s12, -3
	s_cmp_gt_i32 s12, 2
	s_cselect_b32 s38, s20, s12
	s_ashr_i32 s39, s38, 31
	s_lshl_b32 s20, s53, 2
	s_lshl_b64 s[38:39], s[38:39], 17
	s_lshl_b64 s[40:41], s[20:21], 10
	v_add_u32_e32 v96, v139, v133
	v_lshl_add_u64 v[64:65], v[124:125], 0, s[38:39]
	s_barrier
	ds_read_b128 v[12:15], v96
	ds_read_b128 v[16:19], v96 offset:4096
	ds_read_b128 v[56:59], v96 offset:8192
	ds_read_b128 v[60:63], v96 offset:12288
	v_lshl_add_u64 v[130:131], v[64:65], 0, s[40:41]
	ds_read_b128 v[64:67], v96 offset:16384
	ds_read_b128 v[88:91], v96 offset:20480
	ds_read_b128 v[92:95], v96 offset:24576
	ds_read_b128 v[96:99], v96 offset:28672
	s_waitcnt vmcnt(7) lgkmcnt(7)
	v_mfma_f32_16x16x32_bf16 v[68:71], v[134:137], v[12:15], v[68:71]
	s_waitcnt vmcnt(6)
	v_mfma_f32_16x16x32_bf16 v[12:15], v[152:155], v[12:15], v[36:39]
	s_waitcnt lgkmcnt(6)
	v_mfma_f32_16x16x32_bf16 v[36:39], v[134:137], v[16:19], v[72:75]
	v_mfma_f32_16x16x32_bf16 v[16:19], v[152:155], v[16:19], v[40:43]
	s_waitcnt lgkmcnt(5)
	v_mfma_f32_16x16x32_bf16 v[40:43], v[134:137], v[56:59], v[76:79]
	v_mfma_f32_16x16x32_bf16 v[44:47], v[152:155], v[56:59], v[44:47]
	s_waitcnt lgkmcnt(4)
	v_mfma_f32_16x16x32_bf16 v[56:59], v[134:137], v[60:63], v[80:83]
	v_mfma_f32_16x16x32_bf16 v[48:51], v[152:155], v[60:63], v[48:51]
	v_add_u32_e32 v104, v139, v143
	ds_read_b128 v[60:63], v104
	ds_read_b128 v[72:75], v104 offset:4096
	ds_read_b128 v[76:79], v104 offset:8192
	ds_read_b128 v[80:83], v104 offset:12288
	s_waitcnt lgkmcnt(7)
	v_mfma_f32_16x16x32_bf16 v[84:87], v[134:137], v[64:67], v[84:87]
	v_mfma_f32_16x16x32_bf16 v[64:67], v[152:155], v[64:67], v[20:23]
	s_waitcnt lgkmcnt(6)
	v_mfma_f32_16x16x32_bf16 v[28:31], v[134:137], v[88:91], v[28:31]
	v_mfma_f32_16x16x32_bf16 v[24:27], v[152:155], v[88:91], v[24:27]
	s_waitcnt lgkmcnt(5)
	v_mfma_f32_16x16x32_bf16 v[88:91], v[134:137], v[92:95], v[32:35]
	v_mfma_f32_16x16x32_bf16 v[52:55], v[152:155], v[92:95], v[52:55]
	s_waitcnt lgkmcnt(4)
	v_mfma_f32_16x16x32_bf16 v[4:7], v[134:137], v[96:99], v[4:7]
	v_mfma_f32_16x16x32_bf16 v[8:11], v[152:155], v[96:99], v[8:11]
	ds_read_b128 v[92:95], v104 offset:16384
	ds_read_b128 v[96:99], v104 offset:20480
	ds_read_b128 v[100:103], v104 offset:24576
	ds_read_b128 v[104:107], v104 offset:28672
	v_add_co_u32_e32 v140, vcc, s18, v130
	s_movk_i32 s94, 0x2000
	s_nop 0
	v_addc_co_u32_e32 v141, vcc, 0, v131, vcc
	global_load_dwordx4 v[20:23], v[130:131], off sc0
	global_load_dwordx4 v[32:35], v[140:141], off sc0
	s_waitcnt vmcnt(7) lgkmcnt(7)
	v_mfma_f32_16x16x32_bf16 v[68:71], v[156:159], v[60:63], v[68:71]
	s_waitcnt vmcnt(5)
	v_mfma_f32_16x16x32_bf16 v[60:63], v[120:123], v[60:63], v[12:15]
	s_waitcnt lgkmcnt(6)
	v_mfma_f32_16x16x32_bf16 v[36:39], v[156:159], v[72:75], v[36:39]
	v_mfma_f32_16x16x32_bf16 v[16:19], v[120:123], v[72:75], v[16:19]
	s_waitcnt lgkmcnt(5)
	v_mfma_f32_16x16x32_bf16 v[40:43], v[156:159], v[76:79], v[40:43]
	v_mfma_f32_16x16x32_bf16 v[44:47], v[120:123], v[76:79], v[44:47]
	s_waitcnt lgkmcnt(4)
	v_mfma_f32_16x16x32_bf16 v[56:59], v[156:159], v[80:83], v[56:59]
	v_mfma_f32_16x16x32_bf16 v[48:51], v[120:123], v[80:83], v[48:51]
	v_add_u32_e32 v126, v139, v147
	ds_read_b128 v[72:75], v126
	ds_read_b128 v[76:79], v126 offset:4096
	ds_read_b128 v[80:83], v126 offset:8192
	ds_read_b128 v[134:137], v126 offset:12288
	global_load_dwordx4 v[12:15], v[130:131], off offset:1024 sc0
	s_waitcnt lgkmcnt(7)
	v_mfma_f32_16x16x32_bf16 v[84:87], v[156:159], v[92:95], v[84:87]
	v_mfma_f32_16x16x32_bf16 v[64:67], v[120:123], v[92:95], v[64:67]
	s_waitcnt lgkmcnt(6)
	v_mfma_f32_16x16x32_bf16 v[92:95], v[156:159], v[96:99], v[28:31]
	v_mfma_f32_16x16x32_bf16 v[24:27], v[120:123], v[96:99], v[24:27]
	s_waitcnt lgkmcnt(5)
	v_mfma_f32_16x16x32_bf16 v[88:91], v[156:159], v[100:103], v[88:91]
	v_mfma_f32_16x16x32_bf16 v[52:55], v[120:123], v[100:103], v[52:55]
	s_waitcnt lgkmcnt(4)
	v_mfma_f32_16x16x32_bf16 v[96:99], v[156:159], v[104:107], v[4:7]
	v_mfma_f32_16x16x32_bf16 v[100:103], v[120:123], v[104:107], v[8:11]
	ds_read_b128 v[104:107], v126 offset:16384
	ds_read_b128 v[120:123], v126 offset:20480
	ds_read_b128 v[152:155], v126 offset:24576
	ds_read_b128 v[156:159], v126 offset:28672
	global_load_dwordx4 v[8:11], v[130:131], off offset:2048 sc0
	global_load_dwordx4 v[28:31], v[140:141], off offset:1024 sc0
	s_waitcnt lgkmcnt(7)
	v_mfma_f32_16x16x32_bf16 v[68:71], v[116:119], v[72:75], v[68:71]
	s_waitcnt vmcnt(6)
	v_mfma_f32_16x16x32_bf16 v[60:63], v[108:111], v[72:75], v[60:63]
	s_waitcnt lgkmcnt(6)
	v_mfma_f32_16x16x32_bf16 v[36:39], v[116:119], v[76:79], v[36:39]
	v_mfma_f32_16x16x32_bf16 v[16:19], v[108:111], v[76:79], v[16:19]
	s_waitcnt lgkmcnt(5)
	v_mfma_f32_16x16x32_bf16 v[40:43], v[116:119], v[80:83], v[40:43]
	v_mfma_f32_16x16x32_bf16 v[44:47], v[108:111], v[80:83], v[44:47]
	s_waitcnt lgkmcnt(4)
	v_mfma_f32_16x16x32_bf16 v[56:59], v[116:119], v[134:137], v[56:59]
	v_mfma_f32_16x16x32_bf16 v[48:51], v[108:111], v[134:137], v[48:51]
	v_add_u32_e32 v80, v139, v151
	ds_read_b128 v[72:75], v80
	ds_read_b128 v[76:79], v80 offset:4096
	ds_read_b128 v[134:137], v80 offset:8192
	ds_read_b128 v[164:167], v80 offset:12288
	global_load_dwordx4 v[4:7], v[130:131], off offset:3072 sc0
	s_waitcnt lgkmcnt(7)
	v_mfma_f32_16x16x32_bf16 v[168:171], v[116:119], v[104:107], v[84:87]
	v_mfma_f32_16x16x32_bf16 v[104:107], v[108:111], v[104:107], v[64:67]
	s_waitcnt lgkmcnt(6)
	v_mfma_f32_16x16x32_bf16 v[172:175], v[116:119], v[120:123], v[92:95]
	v_mfma_f32_16x16x32_bf16 v[120:123], v[108:111], v[120:123], v[24:27]
	s_waitcnt lgkmcnt(5)
	v_mfma_f32_16x16x32_bf16 v[176:179], v[116:119], v[152:155], v[88:91]
	v_mfma_f32_16x16x32_bf16 v[152:155], v[108:111], v[152:155], v[52:55]
	s_waitcnt lgkmcnt(4)
	v_mfma_f32_16x16x32_bf16 v[116:119], v[116:119], v[156:159], v[96:99]
	v_mfma_f32_16x16x32_bf16 v[100:103], v[108:111], v[156:159], v[100:103]
	ds_read_b128 v[52:55], v80 offset:16384
	ds_read_b128 v[108:111], v80 offset:20480
	ds_read_b128 v[156:159], v80 offset:24576
	ds_read_b128 v[180:183], v80 offset:28672
	global_load_dwordx4 v[24:27], v[140:141], off offset:2048 sc0
	s_waitcnt lgkmcnt(7)
	v_mfma_f32_16x16x32_bf16 v[96:99], v[160:163], v[72:75], v[68:71]
	s_waitcnt vmcnt(7)
	v_mfma_f32_16x16x32_bf16 v[92:95], v[112:115], v[72:75], v[60:63]
	s_waitcnt lgkmcnt(6)
	v_mfma_f32_16x16x32_bf16 v[88:91], v[160:163], v[76:79], v[36:39]
	v_mfma_f32_16x16x32_bf16 v[84:87], v[112:115], v[76:79], v[16:19]
	s_waitcnt lgkmcnt(5)
	v_mfma_f32_16x16x32_bf16 v[80:83], v[160:163], v[134:137], v[40:43]
	v_mfma_f32_16x16x32_bf16 v[76:79], v[112:115], v[134:137], v[44:47]
	s_waitcnt lgkmcnt(4)
	v_mfma_f32_16x16x32_bf16 v[72:75], v[160:163], v[164:167], v[56:59]
	v_mfma_f32_16x16x32_bf16 v[68:71], v[112:115], v[164:167], v[48:51]
	global_load_dwordx4 v[16:19], v[140:141], off offset:3072 sc0
	s_waitcnt lgkmcnt(3)
	v_mfma_f32_16x16x32_bf16 v[64:67], v[160:163], v[52:55], v[168:171]
	v_mfma_f32_16x16x32_bf16 v[60:63], v[112:115], v[52:55], v[104:107]
	s_waitcnt lgkmcnt(2)
	v_mfma_f32_16x16x32_bf16 v[56:59], v[160:163], v[108:111], v[172:175]
	v_mfma_f32_16x16x32_bf16 v[52:55], v[112:115], v[108:111], v[120:123]
	s_waitcnt lgkmcnt(1)
	v_mfma_f32_16x16x32_bf16 v[48:51], v[160:163], v[156:159], v[176:179]
	v_mfma_f32_16x16x32_bf16 v[44:47], v[112:115], v[156:159], v[152:155]
	s_waitcnt lgkmcnt(0)
	v_mfma_f32_16x16x32_bf16 v[40:43], v[160:163], v[180:183], v[116:119]
	v_mfma_f32_16x16x32_bf16 v[36:39], v[112:115], v[180:183], v[100:103]
	s_andn2_b64 vcc, exec, s[0:1]
	s_cbranch_vccnz .LBB0_442
	v_mov_b32_e32 v169, v127
	v_mov_b32_e32 v106, v3
	s_add_i32 s12, s33, s52
	v_lshl_add_u32 v100, v106, 2, 0
	v_add_u32_e32 v107, 0x20200, v100
	ds_read2_b32 v[100:101], v107 offset1:16
	s_sub_i32 s20, s51, 24
	s_cmp_gt_u32 s12, 2
	s_cselect_b32 s12, s20, s51
	s_add_i32 s12, s12, s50
	s_mul_hi_i32 s20, s12, 0x55555556
	ds_read2_b32 v[102:103], v107 offset0:32 offset1:48
	s_waitcnt lgkmcnt(1)
	v_mul_f32_e32 v154, 0x3e16c740, v100
	ds_read2_b32 v[104:105], v107 offset0:64 offset1:80
	v_mul_f32_e32 v150, 0x3e16c740, v101
	ds_read2_b32 v[100:101], v107 offset0:96 offset1:112
	s_lshr_b32 s38, s20, 31
	s_add_i32 s40, s20, s38
	s_mul_i32 s20, s40, -3
	s_add_i32 s20, s20, s12
	v_add_u32_e32 v156, s46, v106
	v_add_u32_e32 v168, s47, v106
	v_add_u32_e32 v167, s70, v106
	v_add_u32_e32 v166, s71, v106
	v_add_u32_e32 v136, s72, v106
	v_add_u32_e32 v165, s73, v106
	v_add_u32_e32 v164, s74, v106
	s_waitcnt lgkmcnt(2)
	v_mul_f32_e32 v146, 0x3e16c740, v102
	v_mul_f32_e32 v142, 0x3e16c740, v103
	s_waitcnt lgkmcnt(1)
	v_mul_f32_e32 v138, 0x3e16c740, v104
	v_mul_f32_e32 v132, 0x3e16c740, v105
	s_waitcnt lgkmcnt(0)
	v_mul_f32_e32 v128, 0x3e16c740, v100
	v_mul_f32_e32 v126, 0x3e16c740, v101
	s_mov_b64 s[38:39], -1
	s_cmp_lt_i32 s20, 2
	v_ashrrev_i32_e32 v158, 11, v156
	v_ashrrev_i32_e32 v152, 11, v168
	v_ashrrev_i32_e32 v148, 11, v167
	v_ashrrev_i32_e32 v144, 11, v166
	v_ashrrev_i32_e32 v140, 11, v136
	v_ashrrev_i32_e32 v134, 11, v165
	v_ashrrev_i32_e32 v130, 11, v164
	v_add_u32_e32 v155, s75, v106
	s_cbranch_scc1 .LBB0_446
	v_lshlrev_b32_e32 v160, 2, v169
	v_ashrrev_i32_e32 v157, 31, v156
	v_ashrrev_i32_e32 v161, 31, v160
	v_lshlrev_b64 v[100:101], 7, v[156:157]
	v_lshl_add_u64 v[100:101], s[4:5], 0, v[100:101]
	v_lshlrev_b64 v[162:163], 2, v[160:161]
	v_lshl_add_u64 v[100:101], v[100:101], 0, v[162:163]
	global_load_dwordx4 v[170:173], v[100:101], off
	global_load_dwordx4 v[174:177], v[100:101], off offset:64
	v_add_u32_e32 v100, 16, v156
	v_ashrrev_i32_e32 v101, 31, v100
	v_lshlrev_b64 v[100:101], 7, v[100:101]
	v_lshl_add_u64 v[100:101], s[4:5], 0, v[100:101]
	v_lshl_add_u64 v[100:101], v[100:101], 0, v[162:163]
	global_load_dwordx4 v[116:119], v[100:101], off
	global_load_dwordx4 v[120:123], v[100:101], off offset:64
	v_add_u32_e32 v100, 32, v156
	v_ashrrev_i32_e32 v101, 31, v100
	v_lshlrev_b64 v[100:101], 7, v[100:101]
	v_lshl_add_u64 v[100:101], s[4:5], 0, v[100:101]
	v_lshl_add_u64 v[100:101], v[100:101], 0, v[162:163]
	global_load_dwordx4 v[108:111], v[100:101], off
	global_load_dwordx4 v[112:115], v[100:101], off offset:64
	v_add_u32_e32 v100, 48, v156
	v_ashrrev_i32_e32 v101, 31, v100
	v_lshlrev_b64 v[100:101], 7, v[100:101]
	v_lshl_add_u64 v[100:101], s[4:5], 0, v[100:101]
	v_lshl_add_u64 v[104:105], v[100:101], 0, v[162:163]
	global_load_dwordx4 v[100:103], v[104:105], off
	s_nop 0
	global_load_dwordx4 v[104:107], v[104:105], off offset:64
	s_ashr_i32 s41, s40, 31
	v_ashrrev_i32_e32 v159, 31, v158
	s_lshl_b64 s[48:49], s[40:41], 11
	v_lshlrev_b64 v[178:179], 14, v[158:159]
	v_lshl_add_u64 v[178:179], v[178:179], 0, s[48:49]
	v_and_or_b32 v178, v156, s17, v178
	v_pk_mul_f32 v[180:181], v[98:99], v[154:155] op_sel_hi:[1,0]
	v_pk_mul_f32 v[182:183], v[96:97], v[154:155] op_sel_hi:[1,0]
	v_pk_mul_f32 v[184:185], v[94:95], v[154:155] op_sel_hi:[1,0]
	v_pk_mul_f32 v[186:187], v[92:93], v[154:155] op_sel_hi:[1,0]
	v_lshlrev_b64 v[178:179], 6, v[178:179]
	v_lshl_add_u64 v[178:179], s[28:29], 0, v[178:179]
	v_lshlrev_b64 v[160:161], 1, v[160:161]
	v_lshl_add_u64 v[178:179], v[178:179], 0, v[160:161]
	v_ashrrev_i32_e32 v153, 31, v152
	v_ashrrev_i32_e32 v149, 31, v148
	v_ashrrev_i32_e32 v145, 31, v144
	v_ashrrev_i32_e32 v137, 31, v136
	v_ashrrev_i32_e32 v141, 31, v140
	v_ashrrev_i32_e32 v135, 31, v134
	v_ashrrev_i32_e32 v131, 31, v130
	s_mov_b64 s[38:39], 0
	s_waitcnt vmcnt(6)
	v_pk_mul_f32 v[188:189], v[184:185], v[176:177]
	v_pk_mul_f32 v[190:191], v[186:187], v[174:175]
	v_pk_mul_f32 v[176:177], v[180:181], v[176:177]
	v_pk_mul_f32 v[174:175], v[182:183], v[174:175]
	v_pk_fma_f32 v[188:189], v[180:181], v[172:173], v[188:189] neg_lo:[0,0,1] neg_hi:[0,0,1]
	v_pk_fma_f32 v[190:191], v[182:183], v[170:171], v[190:191] neg_lo:[0,0,1] neg_hi:[0,0,1]
	v_pk_fma_f32 v[172:173], v[184:185], v[172:173], v[176:177]
	v_pk_fma_f32 v[170:171], v[186:187], v[170:171], v[174:175]
	v_cvt_pk_bf16_f32 v190, v190, v191
	v_cvt_pk_bf16_f32 v170, v170, v171
	v_cvt_pk_bf16_f32 v171, v172, v173
	global_store_dwordx2 v[178:179], v[170:171], off offset:32
	v_lshlrev_b64 v[170:171], 14, v[152:153]
	v_cvt_pk_bf16_f32 v191, v188, v189
	v_lshl_add_u64 v[170:171], v[170:171], 0, s[48:49]
	global_store_dwordx2 v[178:179], v[190:191], off
	v_and_or_b32 v170, v168, s17, v170
	v_pk_mul_f32 v[172:173], v[90:91], v[150:151] op_sel_hi:[1,0]
	v_pk_mul_f32 v[174:175], v[88:89], v[150:151] op_sel_hi:[1,0]
	v_pk_mul_f32 v[176:177], v[86:87], v[150:151] op_sel_hi:[1,0]
	v_pk_mul_f32 v[178:179], v[84:85], v[150:151] op_sel_hi:[1,0]
	v_lshlrev_b64 v[170:171], 6, v[170:171]
	s_waitcnt vmcnt(6)
	v_pk_mul_f32 v[180:181], v[176:177], v[122:123]
	v_pk_mul_f32 v[182:183], v[178:179], v[120:121]
	v_pk_mul_f32 v[122:123], v[172:173], v[122:123]
	v_pk_mul_f32 v[120:121], v[174:175], v[120:121]
	v_lshl_add_u64 v[170:171], s[28:29], 0, v[170:171]
	v_pk_fma_f32 v[180:181], v[172:173], v[118:119], v[180:181] neg_lo:[0,0,1] neg_hi:[0,0,1]
	v_pk_fma_f32 v[182:183], v[174:175], v[116:117], v[182:183] neg_lo:[0,0,1] neg_hi:[0,0,1]
	v_pk_fma_f32 v[118:119], v[176:177], v[118:119], v[122:123]
	v_pk_fma_f32 v[116:117], v[178:179], v[116:117], v[120:121]
	v_lshl_add_u64 v[170:171], v[170:171], 0, v[160:161]
	v_cvt_pk_bf16_f32 v116, v116, v117
	v_cvt_pk_bf16_f32 v117, v118, v119
	global_store_dwordx2 v[170:171], v[116:117], off offset:32
	v_lshlrev_b64 v[116:117], 14, v[148:149]
	v_cvt_pk_bf16_f32 v182, v182, v183
	v_cvt_pk_bf16_f32 v183, v180, v181
	v_lshl_add_u64 v[116:117], v[116:117], 0, s[48:49]
	global_store_dwordx2 v[170:171], v[182:183], off
	v_and_or_b32 v116, v167, s17, v116
	v_pk_mul_f32 v[118:119], v[82:83], v[146:147] op_sel_hi:[1,0]
	v_pk_mul_f32 v[120:121], v[80:81], v[146:147] op_sel_hi:[1,0]
	v_pk_mul_f32 v[122:123], v[78:79], v[146:147] op_sel_hi:[1,0]
	v_pk_mul_f32 v[170:171], v[76:77], v[146:147] op_sel_hi:[1,0]
	v_lshlrev_b64 v[116:117], 6, v[116:117]
	s_waitcnt vmcnt(6)
	v_pk_mul_f32 v[172:173], v[122:123], v[114:115]
	v_pk_mul_f32 v[174:175], v[170:171], v[112:113]
	v_pk_mul_f32 v[114:115], v[118:119], v[114:115]
	v_pk_mul_f32 v[112:113], v[120:121], v[112:113]
	v_lshl_add_u64 v[116:117], s[28:29], 0, v[116:117]
	v_pk_fma_f32 v[172:173], v[118:119], v[110:111], v[172:173] neg_lo:[0,0,1] neg_hi:[0,0,1]
	v_pk_fma_f32 v[174:175], v[120:121], v[108:109], v[174:175] neg_lo:[0,0,1] neg_hi:[0,0,1]
	v_pk_fma_f32 v[110:111], v[122:123], v[110:111], v[114:115]
	v_pk_fma_f32 v[108:109], v[170:171], v[108:109], v[112:113]
	v_lshl_add_u64 v[116:117], v[116:117], 0, v[160:161]
	v_cvt_pk_bf16_f32 v108, v108, v109
	v_cvt_pk_bf16_f32 v109, v110, v111
	global_store_dwordx2 v[116:117], v[108:109], off offset:32
	v_lshlrev_b64 v[108:109], 14, v[144:145]
	v_cvt_pk_bf16_f32 v174, v174, v175
	v_cvt_pk_bf16_f32 v175, v172, v173
	v_lshl_add_u64 v[108:109], v[108:109], 0, s[48:49]
	global_store_dwordx2 v[116:117], v[174:175], off
	v_and_or_b32 v108, v166, s17, v108
	v_pk_mul_f32 v[110:111], v[74:75], v[142:143] op_sel_hi:[1,0]
	v_pk_mul_f32 v[112:113], v[72:73], v[142:143] op_sel_hi:[1,0]
	v_pk_mul_f32 v[114:115], v[70:71], v[142:143] op_sel_hi:[1,0]
	v_pk_mul_f32 v[116:117], v[68:69], v[142:143] op_sel_hi:[1,0]
	v_lshlrev_b64 v[108:109], 6, v[108:109]
	s_waitcnt vmcnt(6)
	v_pk_mul_f32 v[118:119], v[114:115], v[106:107]
	v_pk_mul_f32 v[120:121], v[116:117], v[104:105]
	v_pk_mul_f32 v[106:107], v[110:111], v[106:107]
	v_pk_mul_f32 v[104:105], v[112:113], v[104:105]
	v_lshl_add_u64 v[108:109], s[28:29], 0, v[108:109]
	v_pk_fma_f32 v[118:119], v[110:111], v[102:103], v[118:119] neg_lo:[0,0,1] neg_hi:[0,0,1]
	v_pk_fma_f32 v[120:121], v[112:113], v[100:101], v[120:121] neg_lo:[0,0,1] neg_hi:[0,0,1]
	v_pk_fma_f32 v[102:103], v[114:115], v[102:103], v[106:107]
	v_pk_fma_f32 v[100:101], v[116:117], v[100:101], v[104:105]
	v_lshl_add_u64 v[108:109], v[108:109], 0, v[160:161]
	v_cvt_pk_bf16_f32 v100, v100, v101
	v_cvt_pk_bf16_f32 v101, v102, v103
	global_store_dwordx2 v[108:109], v[100:101], off offset:32
	v_lshlrev_b64 v[100:101], 7, v[136:137]
	v_cvt_pk_bf16_f32 v120, v120, v121
	v_cvt_pk_bf16_f32 v121, v118, v119
	v_lshl_add_u64 v[100:101], s[4:5], 0, v[100:101]
	global_store_dwordx2 v[108:109], v[120:121], off
	v_lshl_add_u64 v[104:105], v[100:101], 0, v[162:163]
	global_load_dwordx4 v[100:103], v[104:105], off
	s_nop 0
	global_load_dwordx4 v[104:107], v[104:105], off offset:64
	v_add_u32_e32 v108, 16, v136
	v_ashrrev_i32_e32 v109, 31, v108
	v_lshlrev_b64 v[108:109], 7, v[108:109]
	v_lshl_add_u64 v[108:109], s[4:5], 0, v[108:109]
	v_lshl_add_u64 v[112:113], v[108:109], 0, v[162:163]
	global_load_dwordx4 v[108:111], v[112:113], off
	s_nop 0
	global_load_dwordx4 v[112:115], v[112:113], off offset:64
	v_add_u32_e32 v116, 32, v136
	v_ashrrev_i32_e32 v117, 31, v116
	v_lshlrev_b64 v[116:117], 7, v[116:117]
	v_lshl_add_u64 v[116:117], s[4:5], 0, v[116:117]
	v_lshl_add_u64 v[120:121], v[116:117], 0, v[162:163]
	global_load_dwordx4 v[116:119], v[120:121], off
	s_nop 0
	global_load_dwordx4 v[120:123], v[120:121], off offset:64
	v_add_u32_e32 v170, 48, v136
	v_ashrrev_i32_e32 v171, 31, v170
	v_lshlrev_b64 v[170:171], 7, v[170:171]
	v_lshl_add_u64 v[170:171], s[4:5], 0, v[170:171]
	v_lshl_add_u64 v[162:163], v[170:171], 0, v[162:163]
	global_load_dwordx4 v[170:173], v[162:163], off
	global_load_dwordx4 v[174:177], v[162:163], off offset:64
	v_lshlrev_b64 v[162:163], 14, v[140:141]
	v_lshl_add_u64 v[162:163], v[162:163], 0, s[48:49]
	v_and_or_b32 v162, v136, s17, v162
	v_pk_mul_f32 v[178:179], v[66:67], v[138:139] op_sel_hi:[1,0]
	v_pk_mul_f32 v[180:181], v[64:65], v[138:139] op_sel_hi:[1,0]
	v_pk_mul_f32 v[182:183], v[62:63], v[138:139] op_sel_hi:[1,0]
	v_pk_mul_f32 v[184:185], v[60:61], v[138:139] op_sel_hi:[1,0]
	v_lshlrev_b64 v[162:163], 6, v[162:163]
	v_lshl_add_u64 v[162:163], s[28:29], 0, v[162:163]
	v_lshl_add_u64 v[162:163], v[162:163], 0, v[160:161]
	s_waitcnt vmcnt(6)
	v_pk_mul_f32 v[186:187], v[182:183], v[106:107]
	v_pk_mul_f32 v[188:189], v[184:185], v[104:105]
	v_pk_mul_f32 v[106:107], v[178:179], v[106:107]
	v_pk_mul_f32 v[104:105], v[180:181], v[104:105]
	v_pk_fma_f32 v[186:187], v[178:179], v[102:103], v[186:187] neg_lo:[0,0,1] neg_hi:[0,0,1]
	v_pk_fma_f32 v[188:189], v[180:181], v[100:101], v[188:189] neg_lo:[0,0,1] neg_hi:[0,0,1]
	v_pk_fma_f32 v[102:103], v[182:183], v[102:103], v[106:107]
	v_pk_fma_f32 v[100:101], v[184:185], v[100:101], v[104:105]
	v_cvt_pk_bf16_f32 v188, v188, v189
	v_cvt_pk_bf16_f32 v100, v100, v101
	v_cvt_pk_bf16_f32 v101, v102, v103
	v_cvt_pk_bf16_f32 v189, v186, v187
	global_store_dwordx2 v[162:163], v[100:101], off offset:32
	v_lshlrev_b64 v[100:101], 14, v[134:135]
	global_store_dwordx2 v[162:163], v[188:189], off
	v_lshl_add_u64 v[100:101], v[100:101], 0, s[48:49]
	v_pk_mul_f32 v[106:107], v[54:55], v[132:133] op_sel_hi:[1,0]
	v_pk_mul_f32 v[162:163], v[52:53], v[132:133] op_sel_hi:[1,0]
	v_and_or_b32 v100, v165, s17, v100
	v_pk_mul_f32 v[102:103], v[58:59], v[132:133] op_sel_hi:[1,0]
	v_pk_mul_f32 v[104:105], v[56:57], v[132:133] op_sel_hi:[1,0]
	s_waitcnt vmcnt(6)
	v_pk_mul_f32 v[178:179], v[106:107], v[114:115]
	v_pk_mul_f32 v[180:181], v[162:163], v[112:113]
	v_lshlrev_b64 v[100:101], 6, v[100:101]
	v_pk_fma_f32 v[178:179], v[102:103], v[110:111], v[178:179] neg_lo:[0,0,1] neg_hi:[0,0,1]
	v_pk_fma_f32 v[180:181], v[104:105], v[108:109], v[180:181] neg_lo:[0,0,1] neg_hi:[0,0,1]
	v_pk_mul_f32 v[102:103], v[102:103], v[114:115]
	v_pk_mul_f32 v[104:105], v[104:105], v[112:113]
	v_lshl_add_u64 v[100:101], s[28:29], 0, v[100:101]
	v_pk_fma_f32 v[102:103], v[106:107], v[110:111], v[102:103]
	v_pk_fma_f32 v[104:105], v[162:163], v[108:109], v[104:105]
	v_lshl_add_u64 v[100:101], v[100:101], 0, v[160:161]
	v_cvt_pk_bf16_f32 v180, v180, v181
	v_cvt_pk_bf16_f32 v181, v178, v179
	v_cvt_pk_bf16_f32 v104, v104, v105
	v_cvt_pk_bf16_f32 v105, v102, v103
	global_store_dwordx2 v[100:101], v[180:181], off
	global_store_dwordx2 v[100:101], v[104:105], off offset:32
	v_lshlrev_b64 v[100:101], 14, v[130:131]
	v_lshl_add_u64 v[100:101], v[100:101], 0, s[48:49]
	v_pk_mul_f32 v[106:107], v[46:47], v[128:129] op_sel_hi:[1,0]
	v_pk_mul_f32 v[108:109], v[44:45], v[128:129] op_sel_hi:[1,0]
	v_and_or_b32 v100, v164, s17, v100
	v_pk_mul_f32 v[102:103], v[50:51], v[128:129] op_sel_hi:[1,0]
	v_pk_mul_f32 v[104:105], v[48:49], v[128:129] op_sel_hi:[1,0]
	s_waitcnt vmcnt(6)
	v_pk_mul_f32 v[110:111], v[106:107], v[122:123]
	v_pk_mul_f32 v[112:113], v[108:109], v[120:121]
	v_lshlrev_b64 v[100:101], 6, v[100:101]
	v_pk_fma_f32 v[110:111], v[102:103], v[118:119], v[110:111] neg_lo:[0,0,1] neg_hi:[0,0,1]
	v_pk_fma_f32 v[112:113], v[104:105], v[116:117], v[112:113] neg_lo:[0,0,1] neg_hi:[0,0,1]
	v_pk_mul_f32 v[102:103], v[102:103], v[122:123]
	v_pk_mul_f32 v[104:105], v[104:105], v[120:121]
	v_lshl_add_u64 v[100:101], s[28:29], 0, v[100:101]
	v_pk_fma_f32 v[102:103], v[106:107], v[118:119], v[102:103]
	v_pk_fma_f32 v[104:105], v[108:109], v[116:117], v[104:105]
	v_lshl_add_u64 v[100:101], v[100:101], 0, v[160:161]
	v_cvt_pk_bf16_f32 v112, v112, v113
	v_cvt_pk_bf16_f32 v113, v110, v111
	v_cvt_pk_bf16_f32 v104, v104, v105
	v_cvt_pk_bf16_f32 v105, v102, v103
	global_store_dwordx2 v[100:101], v[112:113], off
	global_store_dwordx2 v[100:101], v[104:105], off offset:32
	v_ashrrev_i32_e32 v100, 11, v155
	v_ashrrev_i32_e32 v101, 31, v100
	v_lshlrev_b64 v[100:101], 14, v[100:101]
	v_lshl_add_u64 v[100:101], v[100:101], 0, s[48:49]
	v_pk_mul_f32 v[106:107], v[38:39], v[126:127] op_sel_hi:[1,0]
	v_pk_mul_f32 v[108:109], v[36:37], v[126:127] op_sel_hi:[1,0]
	v_and_or_b32 v100, v155, s17, v100
	v_pk_mul_f32 v[102:103], v[42:43], v[126:127] op_sel_hi:[1,0]
	v_pk_mul_f32 v[104:105], v[40:41], v[126:127] op_sel_hi:[1,0]
	s_waitcnt vmcnt(6)
	v_pk_mul_f32 v[110:111], v[106:107], v[176:177]
	v_pk_mul_f32 v[112:113], v[108:109], v[174:175]
	v_lshlrev_b64 v[100:101], 6, v[100:101]
	v_pk_fma_f32 v[110:111], v[102:103], v[172:173], v[110:111] neg_lo:[0,0,1] neg_hi:[0,0,1]
	v_pk_fma_f32 v[112:113], v[104:105], v[170:171], v[112:113] neg_lo:[0,0,1] neg_hi:[0,0,1]
	v_pk_mul_f32 v[102:103], v[102:103], v[176:177]
	v_pk_mul_f32 v[104:105], v[104:105], v[174:175]
	v_lshl_add_u64 v[100:101], s[28:29], 0, v[100:101]
	v_pk_fma_f32 v[102:103], v[106:107], v[172:173], v[102:103]
	v_pk_fma_f32 v[104:105], v[108:109], v[170:171], v[104:105]
	v_lshl_add_u64 v[100:101], v[100:101], 0, v[160:161]
	v_cvt_pk_bf16_f32 v112, v112, v113
	v_cvt_pk_bf16_f32 v113, v110, v111
	v_cvt_pk_bf16_f32 v104, v104, v105
	v_cvt_pk_bf16_f32 v105, v102, v103
	global_store_dwordx2 v[100:101], v[112:113], off
	global_store_dwordx2 v[100:101], v[104:105], off offset:32

.LBB0_448:
	s_waitcnt vmcnt(5)
	v_mov_b32_e32 v12, v0
	s_waitcnt vmcnt(0)
	s_barrier
	v_readlane_b32 s18, v247, 7
	s_waitcnt vmcnt(2)
	v_ashrrev_i32_e32 v4, 4, v12
	v_readfirstlane_b32 s0, v12
	v_xor_b32_e32 v7, v4, v12
	s_ashr_i32 s12, s0, 6
	v_and_b32_e32 v5, 63, v12
	v_lshlrev_b32_e32 v6, 8, v4
	v_lshlrev_b32_e32 v7, 4, v7
	s_cmp_lt_i32 s12, 8
	v_and_or_b32 v13, v7, s84, v6
	v_lshlrev_b32_e32 v6, 4, v5
	v_ashrrev_i32_e32 v5, 31, v4
	s_cselect_b64 s[40:41], -1, 0
	v_lshlrev_b64 v[4:5], 8, v[4:5]
	v_readlane_b32 s19, v247, 8
	v_lshlrev_b32_e32 v8, 4, v12
	s_and_b64 s[0:1], s[40:41], exec
	v_lshl_add_u64 v[4:5], s[18:19], 0, v[4:5]
	v_and_b32_e32 v8, 0xf0, v8
	v_mov_b32_e32 v9, v2
	s_cselect_b32 s0, s12, 7
	v_lshl_add_u64 v[8:9], v[4:5], 0, v[8:9]
	s_ashr_i32 s1, s0, 31
	v_add_co_u32_e32 v10, vcc, s94, v8
	s_lshl_b64 s[0:1], s[0:1], 13
	s_nop 0
	v_addc_co_u32_e32 v11, vcc, 0, v9, vcc
	s_add_u32 s48, s63, s0
	v_add_co_u32_e32 v136, vcc, s16, v8
	s_addc_u32 s49, s64, s1
	global_load_dwordx4 v[28:31], v[8:9], off
	global_load_dwordx4 v[24:27], v[10:11], off
	v_addc_co_u32_e32 v137, vcc, 0, v9, vcc
	s_movk_i32 s1, 0x6000
	v_add_co_u32_e32 v138, vcc, s1, v8
	global_load_dwordx4 v[20:23], v[136:137], off
	s_nop 0
	v_addc_co_u32_e32 v139, vcc, 0, v9, vcc
	v_readlane_b32 s0, v247, 13
	global_load_dwordx4 v[32:35], v[138:139], off
	s_lshl_b32 s20, s0, 1
	v_readlane_b32 s0, v247, 14
	v_mov_b32_e32 v7, v2
	s_lshl_b32 s0, s0, 1
	s_lshl_b32 s38, s12, 5
	v_lshl_add_u64 v[6:7], s[48:49], 0, v[6:7]
	s_cmp_gt_i32 s12, 7
	v_lshl_add_u64 v[4:5], v[6:7], 0, s[20:21]
	s_movk_i32 s12, 0x1000
	global_load_dwordx4 v[36:39], v[4:5], off sc0
	global_load_dwordx4 v[44:47], v[4:5], off offset:1024 sc0
	global_load_dwordx4 v[48:51], v[4:5], off offset:2048 sc0
	global_load_dwordx4 v[52:55], v[4:5], off offset:3072 sc0
	v_add_co_u32_e32 v4, vcc, s12, v4
	v_bfe_u32 v120, v12, 4, 2
	s_nop 0
	v_addc_co_u32_e32 v5, vcc, 0, v5, vcc
	global_load_dwordx4 v[40:43], v[4:5], off sc0
	global_load_dwordx4 v[64:67], v[4:5], off offset:1024 sc0
	global_load_dwordx4 v[60:63], v[4:5], off offset:2048 sc0
	global_load_dwordx4 v[56:59], v[4:5], off offset:3072 sc0
	v_and_b32_e32 v3, 15, v12
	v_bitop3_b32 v4, v120, v12, 15 bitop3:0x78
	v_lshl_add_u32 v172, v3, 8, 0
	v_lshlrev_b32_e32 v4, 4, v4
	v_add_u32_e32 v121, 0, v13
	s_mov_b32 s1, s21
	v_add_u32_e32 v122, v172, v4
	v_lshl_add_u64 v[174:175], v[6:7], 0, s[0:1]
	s_waitcnt vmcnt(11)
	ds_write_b128 v121, v[28:31]
	s_waitcnt vmcnt(10)
	ds_write_b128 v121, v[24:27] offset:8192
	s_waitcnt vmcnt(9)
	ds_write_b128 v121, v[20:23] offset:16384
	s_waitcnt vmcnt(8)
	ds_write_b128 v121, v[32:35] offset:24576
	s_waitcnt lgkmcnt(0)
	s_barrier
	ds_read_b128 v[4:7], v122
	ds_read_b128 v[12:15], v122 offset:4096
	ds_read_b128 v[68:71], v122 offset:8192
	ds_read_b128 v[72:75], v122 offset:12288
	ds_read_b128 v[76:79], v122 offset:16384
	ds_read_b128 v[80:83], v122 offset:20480
	ds_read_b128 v[84:87], v122 offset:24576
	ds_read_b128 v[88:91], v122 offset:28672
	global_load_dwordx4 v[16:19], v[8:9], off
	s_nop 0
	global_load_dwordx4 v[8:11], v[10:11], off
	s_waitcnt vmcnt(9) lgkmcnt(7)
	v_mfma_f32_16x16x32_bf16 v[92:95], v[36:39], v[4:7], 0
	s_waitcnt vmcnt(5)
	v_mfma_f32_16x16x32_bf16 v[96:99], v[40:43], v[4:7], 0
	s_waitcnt lgkmcnt(6)
	v_mfma_f32_16x16x32_bf16 v[100:103], v[36:39], v[12:15], 0
	v_mfma_f32_16x16x32_bf16 v[104:107], v[40:43], v[12:15], 0
	s_waitcnt lgkmcnt(5)
	v_mfma_f32_16x16x32_bf16 v[108:111], v[36:39], v[68:71], 0
	v_mfma_f32_16x16x32_bf16 v[68:71], v[40:43], v[68:71], 0
	s_waitcnt lgkmcnt(4)
	v_mfma_f32_16x16x32_bf16 v[112:115], v[36:39], v[72:75], 0
	v_mfma_f32_16x16x32_bf16 v[72:75], v[40:43], v[72:75], 0
	v_bitop3_b32 v4, v120, v3, 4 bitop3:0x36
	v_lshlrev_b32_e32 v4, 4, v4
	v_add_u32_e32 v123, v172, v4
	ds_read_b128 v[116:119], v123
	ds_read_b128 v[124:127], v123 offset:4096
	ds_read_b128 v[128:131], v123 offset:8192
	ds_read_b128 v[132:135], v123 offset:12288
	global_load_dwordx4 v[12:15], v[136:137], off
	global_load_dwordx4 v[4:7], v[138:139], off
	s_waitcnt lgkmcnt(7)
	v_mfma_f32_16x16x32_bf16 v[136:139], v[36:39], v[76:79], 0
	v_mfma_f32_16x16x32_bf16 v[76:79], v[40:43], v[76:79], 0
	s_waitcnt lgkmcnt(6)
	v_mfma_f32_16x16x32_bf16 v[140:143], v[36:39], v[80:83], 0
	v_mfma_f32_16x16x32_bf16 v[80:83], v[40:43], v[80:83], 0
	s_waitcnt lgkmcnt(5)
	v_mfma_f32_16x16x32_bf16 v[144:147], v[36:39], v[84:87], 0
	v_mfma_f32_16x16x32_bf16 v[84:87], v[40:43], v[84:87], 0
	s_waitcnt lgkmcnt(4)
	v_mfma_f32_16x16x32_bf16 v[148:151], v[36:39], v[88:91], 0
	v_mfma_f32_16x16x32_bf16 v[88:91], v[40:43], v[88:91], 0
	ds_read_b128 v[152:155], v123 offset:16384
	ds_read_b128 v[156:159], v123 offset:20480
	ds_read_b128 v[160:163], v123 offset:24576
	ds_read_b128 v[164:167], v123 offset:28672
	v_add_co_u32_e32 v182, vcc, s12, v174
	s_nop 1
	v_addc_co_u32_e32 v183, vcc, 0, v175, vcc
	global_load_dwordx4 v[36:39], v[174:175], off sc0
	global_load_dwordx4 v[40:43], v[182:183], off sc0
	ds_write_b128 v121, v[28:31] offset:32768
	s_waitcnt lgkmcnt(8)
	v_mfma_f32_16x16x32_bf16 v[92:95], v[44:47], v[116:119], v[92:95]
	s_waitcnt vmcnt(8)
	v_mfma_f32_16x16x32_bf16 v[96:99], v[64:67], v[116:119], v[96:99]
	s_waitcnt lgkmcnt(7)
	v_mfma_f32_16x16x32_bf16 v[100:103], v[44:47], v[124:127], v[100:103]
	v_mfma_f32_16x16x32_bf16 v[104:107], v[64:67], v[124:127], v[104:107]
	s_waitcnt lgkmcnt(6)
	v_mfma_f32_16x16x32_bf16 v[108:111], v[44:47], v[128:131], v[108:111]
	v_mfma_f32_16x16x32_bf16 v[68:71], v[64:67], v[128:131], v[68:71]
	s_waitcnt lgkmcnt(5)
	v_mfma_f32_16x16x32_bf16 v[112:115], v[44:47], v[132:135], v[112:115]
	v_mfma_f32_16x16x32_bf16 v[72:75], v[64:67], v[132:135], v[72:75]
	v_bitop3_b32 v28, v120, v3, 8 bitop3:0x36
	v_lshlrev_b32_e32 v28, 4, v28
	v_add_u32_e32 v124, v172, v28
	ds_read_b128 v[116:119], v124
	ds_read_b128 v[126:129], v124 offset:4096
	ds_read_b128 v[130:133], v124 offset:8192
	ds_read_b128 v[168:171], v124 offset:12288
	global_load_dwordx4 v[28:31], v[174:175], off offset:1024 sc0
	ds_write_b128 v121, v[24:27] offset:40960
	s_waitcnt lgkmcnt(9)
	v_mfma_f32_16x16x32_bf16 v[76:79], v[64:67], v[152:155], v[76:79]
	s_waitcnt lgkmcnt(8)
	v_mfma_f32_16x16x32_bf16 v[80:83], v[64:67], v[156:159], v[80:83]
	s_waitcnt lgkmcnt(7)
	v_mfma_f32_16x16x32_bf16 v[84:87], v[64:67], v[160:163], v[84:87]
	s_waitcnt lgkmcnt(6)
	v_mfma_f32_16x16x32_bf16 v[64:67], v[64:67], v[164:167], v[88:91]
	v_mfma_f32_16x16x32_bf16 v[134:137], v[44:47], v[152:155], v[136:139]
	v_mfma_f32_16x16x32_bf16 v[138:141], v[44:47], v[156:159], v[140:143]
	v_mfma_f32_16x16x32_bf16 v[142:145], v[44:47], v[160:163], v[144:147]
	v_mfma_f32_16x16x32_bf16 v[146:149], v[44:47], v[164:167], v[148:151]
	ds_read_b128 v[88:91], v124 offset:16384
	s_nop 1
	ds_read_b128 v[150:153], v124 offset:20480
	ds_read_b128 v[154:157], v124 offset:24576
	ds_read_b128 v[158:161], v124 offset:28672
	global_load_dwordx4 v[24:27], v[174:175], off offset:2048 sc0
	global_load_dwordx4 v[44:47], v[182:183], off offset:1024 sc0
	ds_write_b128 v121, v[20:23] offset:49152
	s_waitcnt lgkmcnt(9)
	v_mfma_f32_16x16x32_bf16 v[92:95], v[48:51], v[116:119], v[92:95]
	s_waitcnt vmcnt(10)
	v_mfma_f32_16x16x32_bf16 v[96:99], v[60:63], v[116:119], v[96:99]
	s_waitcnt lgkmcnt(8)
	v_mfma_f32_16x16x32_bf16 v[100:103], v[48:51], v[126:129], v[100:103]
	v_mfma_f32_16x16x32_bf16 v[104:107], v[60:63], v[126:129], v[104:107]
	s_waitcnt lgkmcnt(7)
	v_mfma_f32_16x16x32_bf16 v[68:71], v[60:63], v[130:133], v[68:71]
	s_waitcnt lgkmcnt(6)
	v_mfma_f32_16x16x32_bf16 v[72:75], v[60:63], v[168:171], v[72:75]
	v_mfma_f32_16x16x32_bf16 v[126:129], v[48:51], v[130:133], v[108:111]
	v_mfma_f32_16x16x32_bf16 v[130:133], v[48:51], v[168:171], v[112:115]
	v_bitop3_b32 v20, v120, v3, 12 bitop3:0x36
	v_lshlrev_b32_e32 v20, 4, v20
	v_add_u32_e32 v125, v172, v20
	ds_read_b128 v[108:111], v125
	ds_read_b128 v[162:165], v125 offset:4096
	ds_read_b128 v[166:169], v125 offset:8192
	ds_read_b128 v[170:173], v125 offset:12288
	global_load_dwordx4 v[20:23], v[174:175], off offset:3072 sc0
	ds_write_b128 v121, v[32:35] offset:57344
	s_waitcnt lgkmcnt(9)
	v_mfma_f32_16x16x32_bf16 v[76:79], v[60:63], v[88:91], v[76:79]
	v_mfma_f32_16x16x32_bf16 v[134:137], v[48:51], v[88:91], v[134:137]
	s_waitcnt lgkmcnt(8)
	v_mfma_f32_16x16x32_bf16 v[138:141], v[48:51], v[150:153], v[138:141]
	v_mfma_f32_16x16x32_bf16 v[150:153], v[60:63], v[150:153], v[80:83]
	s_waitcnt lgkmcnt(7)
	v_mfma_f32_16x16x32_bf16 v[142:145], v[48:51], v[154:157], v[142:145]
	v_mfma_f32_16x16x32_bf16 v[154:157], v[60:63], v[154:157], v[84:87]
	s_waitcnt lgkmcnt(6)
	v_mfma_f32_16x16x32_bf16 v[146:149], v[48:51], v[158:161], v[146:149]
	v_mfma_f32_16x16x32_bf16 v[158:161], v[60:63], v[158:161], v[64:67]
	ds_read_b128 v[60:63], v125 offset:16384
	s_nop 1
	ds_read_b128 v[64:67], v125 offset:20480
	ds_read_b128 v[174:177], v125 offset:24576
	ds_read_b128 v[178:181], v125 offset:28672
	global_load_dwordx4 v[48:51], v[182:183], off offset:2048 sc0
	s_waitcnt lgkmcnt(8)
	v_mfma_f32_16x16x32_bf16 v[116:119], v[52:55], v[108:111], v[92:95]
	s_waitcnt vmcnt(11)
	v_mfma_f32_16x16x32_bf16 v[112:115], v[56:59], v[108:111], v[96:99]
	s_waitcnt lgkmcnt(7)
	v_mfma_f32_16x16x32_bf16 v[108:111], v[52:55], v[162:165], v[100:103]
	v_mfma_f32_16x16x32_bf16 v[104:107], v[56:59], v[162:165], v[104:107]
	s_waitcnt lgkmcnt(6)
	v_mfma_f32_16x16x32_bf16 v[100:103], v[52:55], v[166:169], v[126:129]
	v_mfma_f32_16x16x32_bf16 v[96:99], v[56:59], v[166:169], v[68:71]
	s_waitcnt lgkmcnt(5)
	v_mfma_f32_16x16x32_bf16 v[92:95], v[52:55], v[170:173], v[130:133]
	v_mfma_f32_16x16x32_bf16 v[88:91], v[56:59], v[170:173], v[72:75]
	global_load_dwordx4 v[32:35], v[182:183], off offset:3072 sc0
	s_waitcnt lgkmcnt(3)
	v_mfma_f32_16x16x32_bf16 v[84:87], v[52:55], v[60:63], v[134:137]
	v_mfma_f32_16x16x32_bf16 v[80:83], v[56:59], v[60:63], v[76:79]
	s_waitcnt lgkmcnt(2)
	v_mfma_f32_16x16x32_bf16 v[76:79], v[52:55], v[64:67], v[138:141]
	v_mfma_f32_16x16x32_bf16 v[72:75], v[56:59], v[64:67], v[150:153]
	s_waitcnt lgkmcnt(1)
	v_mfma_f32_16x16x32_bf16 v[68:71], v[52:55], v[174:177], v[142:145]
	v_mfma_f32_16x16x32_bf16 v[64:67], v[56:59], v[174:177], v[154:157]
	s_waitcnt lgkmcnt(0)
	v_mfma_f32_16x16x32_bf16 v[60:63], v[52:55], v[178:181], v[146:149]
	v_mfma_f32_16x16x32_bf16 v[52:55], v[56:59], v[178:181], v[158:161]
	s_cbranch_scc1 .LBB0_450
	v_readlane_b32 s1, v247, 15
	v_mov_b32_e32 v126, v3
	v_mov_b32_e32 v56, v120
	s_add_i32 s1, s38, s1
	v_readlane_b32 s18, v251, 51
	v_lshl_add_u32 v57, v56, 3, s1
	v_ashrrev_i32_e32 v56, 6, v57
	v_and_b32_e32 v130, 56, v57
	v_lshl_add_u32 v57, v126, 2, 0
	v_add_u32_e32 v131, 0x20400, v57
	ds_read2_b32 v[58:59], v131 offset1:16
	v_add_u32_e32 v132, s46, v126
	v_ashrrev_i32_e32 v126, 11, v132
	v_ashrrev_i32_e32 v57, 31, v56
	v_ashrrev_i32_e32 v127, 31, v126
	s_waitcnt lgkmcnt(0)
	v_pk_mul_f32 v[116:117], v[116:117], v[58:59] op_sel_hi:[1,0]
	v_lshlrev_b64 v[56:57], 11, v[56:57]
	v_pk_mul_f32 v[128:129], v[114:115], v[58:59] op_sel_hi:[1,0]
	v_pk_mul_f32 v[114:115], v[112:113], v[58:59] op_sel_hi:[1,0]
	v_cvt_pk_bf16_f32 v112, v116, v117
	v_lshlrev_b64 v[116:117], 14, v[126:127]
	v_lshl_add_u64 v[116:117], v[56:57], 0, v[116:117]
	v_and_or_b32 v116, v132, s17, v116
	v_pk_mul_f32 v[118:119], v[118:119], v[58:59] op_sel_hi:[1,0]
	v_lshlrev_b64 v[116:117], 7, v[116:117]
	v_readlane_b32 s19, v251, 52
	v_cvt_pk_bf16_f32 v113, v118, v119
	v_lshlrev_b32_e32 v118, 1, v130
	v_lshl_add_u64 v[116:117], s[18:19], 0, v[116:117]
	v_mov_b32_e32 v119, v2
	v_cvt_pk_bf16_f32 v114, v114, v115
	v_cvt_pk_bf16_f32 v115, v128, v129
	v_lshl_add_u64 v[116:117], v[116:117], 0, v[118:119]
	global_store_dwordx4 v[116:117], v[112:115], off
	s_nop 1
	v_add_u32_e32 v113, 16, v132
	v_ashrrev_i32_e32 v58, 11, v113
	v_mov_b32_e32 v112, v59
	v_ashrrev_i32_e32 v59, 31, v58
	v_lshlrev_b64 v[58:59], 14, v[58:59]
	v_lshl_add_u64 v[58:59], v[58:59], 0, v[56:57]
	v_and_or_b32 v58, v113, s17, v58
	v_lshlrev_b64 v[58:59], 7, v[58:59]
	v_pk_mul_f32 v[110:111], v[110:111], v[112:113] op_sel_hi:[1,0]
	v_pk_mul_f32 v[108:109], v[108:109], v[112:113] op_sel_hi:[1,0]
	v_pk_mul_f32 v[114:115], v[106:107], v[112:113] op_sel_hi:[1,0]
	v_pk_mul_f32 v[106:107], v[104:105], v[112:113] op_sel_hi:[1,0]
	v_lshl_add_u64 v[58:59], s[18:19], 0, v[58:59]
	v_cvt_pk_bf16_f32 v104, v108, v109
	v_cvt_pk_bf16_f32 v105, v110, v111
	v_cvt_pk_bf16_f32 v106, v106, v107
	v_cvt_pk_bf16_f32 v107, v114, v115
	v_lshl_add_u64 v[58:59], v[58:59], 0, v[118:119]
	global_store_dwordx4 v[58:59], v[104:107], off
	ds_read2_b32 v[108:109], v131 offset0:32 offset1:48
	s_waitcnt lgkmcnt(0)
	v_pk_mul_f32 v[102:103], v[102:103], v[108:109] op_sel_hi:[1,0]
	v_add_u32_e32 v106, 32, v132
	v_ashrrev_i32_e32 v58, 11, v106
	v_ashrrev_i32_e32 v59, 31, v58
	v_lshlrev_b64 v[58:59], 14, v[58:59]
	v_lshl_add_u64 v[58:59], v[58:59], 0, v[56:57]
	v_and_or_b32 v58, v106, s17, v58
	v_lshlrev_b64 v[58:59], 7, v[58:59]
	v_pk_mul_f32 v[100:101], v[100:101], v[108:109] op_sel_hi:[1,0]
	v_pk_mul_f32 v[104:105], v[98:99], v[108:109] op_sel_hi:[1,0]
	v_pk_mul_f32 v[98:99], v[96:97], v[108:109] op_sel_hi:[1,0]
	v_lshl_add_u64 v[58:59], s[18:19], 0, v[58:59]
	v_cvt_pk_bf16_f32 v96, v100, v101
	v_cvt_pk_bf16_f32 v97, v102, v103
	v_cvt_pk_bf16_f32 v98, v98, v99
	v_cvt_pk_bf16_f32 v99, v104, v105
	v_lshl_add_u64 v[58:59], v[58:59], 0, v[118:119]
	global_store_dwordx4 v[58:59], v[96:99], off
	s_nop 1
	v_add_u32_e32 v97, 48, v132
	v_ashrrev_i32_e32 v58, 11, v97
	v_ashrrev_i32_e32 v59, 31, v58
	v_lshlrev_b64 v[58:59], 14, v[58:59]
	v_lshl_add_u64 v[58:59], v[58:59], 0, v[56:57]
	v_and_or_b32 v58, v97, s17, v58
	v_mov_b32_e32 v96, v109
	v_lshlrev_b64 v[58:59], 7, v[58:59]
	v_pk_mul_f32 v[94:95], v[94:95], v[96:97] op_sel_hi:[1,0]
	v_pk_mul_f32 v[92:93], v[92:93], v[96:97] op_sel_hi:[1,0]
	v_pk_mul_f32 v[98:99], v[90:91], v[96:97] op_sel_hi:[1,0]
	v_pk_mul_f32 v[90:91], v[88:89], v[96:97] op_sel_hi:[1,0]
	v_lshl_add_u64 v[58:59], s[18:19], 0, v[58:59]
	v_cvt_pk_bf16_f32 v88, v92, v93
	v_cvt_pk_bf16_f32 v89, v94, v95
	v_cvt_pk_bf16_f32 v90, v90, v91
	v_cvt_pk_bf16_f32 v91, v98, v99
	v_lshl_add_u64 v[58:59], v[58:59], 0, v[118:119]
	global_store_dwordx4 v[58:59], v[88:91], off
	ds_read2_b32 v[92:93], v131 offset0:64 offset1:80
	s_waitcnt lgkmcnt(0)
	v_pk_mul_f32 v[86:87], v[86:87], v[92:93] op_sel_hi:[1,0]
	v_add_u32_e32 v90, 64, v132
	v_ashrrev_i32_e32 v58, 11, v90
	v_ashrrev_i32_e32 v59, 31, v58
	v_lshlrev_b64 v[58:59], 14, v[58:59]
	v_lshl_add_u64 v[58:59], v[58:59], 0, v[56:57]
	v_and_or_b32 v58, v90, s17, v58
	v_lshlrev_b64 v[58:59], 7, v[58:59]
	v_pk_mul_f32 v[84:85], v[84:85], v[92:93] op_sel_hi:[1,0]
	v_pk_mul_f32 v[88:89], v[82:83], v[92:93] op_sel_hi:[1,0]
	v_pk_mul_f32 v[82:83], v[80:81], v[92:93] op_sel_hi:[1,0]
	v_lshl_add_u64 v[58:59], s[18:19], 0, v[58:59]
	v_cvt_pk_bf16_f32 v80, v84, v85
	v_cvt_pk_bf16_f32 v81, v86, v87
	v_cvt_pk_bf16_f32 v82, v82, v83
	v_cvt_pk_bf16_f32 v83, v88, v89
	v_lshl_add_u64 v[58:59], v[58:59], 0, v[118:119]
	global_store_dwordx4 v[58:59], v[80:83], off
	s_nop 1
	v_add_u32_e32 v81, 0x50, v132
	v_ashrrev_i32_e32 v58, 11, v81
	v_ashrrev_i32_e32 v59, 31, v58
	v_lshlrev_b64 v[58:59], 14, v[58:59]
	v_lshl_add_u64 v[58:59], v[58:59], 0, v[56:57]
	v_and_or_b32 v58, v81, s17, v58
	v_mov_b32_e32 v80, v93
	v_lshlrev_b64 v[58:59], 7, v[58:59]
	v_pk_mul_f32 v[78:79], v[78:79], v[80:81] op_sel_hi:[1,0]
	v_pk_mul_f32 v[76:77], v[76:77], v[80:81] op_sel_hi:[1,0]
	v_pk_mul_f32 v[82:83], v[74:75], v[80:81] op_sel_hi:[1,0]
	v_pk_mul_f32 v[74:75], v[72:73], v[80:81] op_sel_hi:[1,0]
	v_lshl_add_u64 v[58:59], s[18:19], 0, v[58:59]
	v_cvt_pk_bf16_f32 v72, v76, v77
	v_cvt_pk_bf16_f32 v73, v78, v79
	v_cvt_pk_bf16_f32 v74, v74, v75
	v_cvt_pk_bf16_f32 v75, v82, v83
	v_lshl_add_u64 v[58:59], v[58:59], 0, v[118:119]
	global_store_dwordx4 v[58:59], v[72:75], off
	ds_read2_b32 v[76:77], v131 offset0:96 offset1:112
	s_waitcnt lgkmcnt(0)
	v_pk_mul_f32 v[70:71], v[70:71], v[76:77] op_sel_hi:[1,0]
	v_add_u32_e32 v74, 0x60, v132
	v_ashrrev_i32_e32 v58, 11, v74
	v_ashrrev_i32_e32 v59, 31, v58
	v_lshlrev_b64 v[58:59], 14, v[58:59]
	v_lshl_add_u64 v[58:59], v[58:59], 0, v[56:57]
	v_and_or_b32 v58, v74, s17, v58
	v_lshlrev_b64 v[58:59], 7, v[58:59]
	v_pk_mul_f32 v[68:69], v[68:69], v[76:77] op_sel_hi:[1,0]
	v_pk_mul_f32 v[72:73], v[66:67], v[76:77] op_sel_hi:[1,0]
	v_pk_mul_f32 v[66:67], v[64:65], v[76:77] op_sel_hi:[1,0]
	v_lshl_add_u64 v[58:59], s[18:19], 0, v[58:59]
	v_cvt_pk_bf16_f32 v64, v68, v69
	v_cvt_pk_bf16_f32 v65, v70, v71
	v_cvt_pk_bf16_f32 v66, v66, v67
	v_cvt_pk_bf16_f32 v67, v72, v73
	v_lshl_add_u64 v[58:59], v[58:59], 0, v[118:119]
	global_store_dwordx4 v[58:59], v[64:67], off
	s_nop 1
	v_add_u32_e32 v65, 0x70, v132
	v_ashrrev_i32_e32 v58, 11, v65
	v_ashrrev_i32_e32 v59, 31, v58
	v_lshlrev_b64 v[58:59], 14, v[58:59]
	v_lshl_add_u64 v[56:57], v[58:59], 0, v[56:57]
	v_and_or_b32 v56, v65, s17, v56
	v_mov_b32_e32 v64, v77
	v_lshlrev_b64 v[56:57], 7, v[56:57]
	v_pk_mul_f32 v[62:63], v[62:63], v[64:65] op_sel_hi:[1,0]
	v_pk_mul_f32 v[60:61], v[60:61], v[64:65] op_sel_hi:[1,0]
	v_pk_mul_f32 v[66:67], v[54:55], v[64:65] op_sel_hi:[1,0]
	v_pk_mul_f32 v[54:55], v[52:53], v[64:65] op_sel_hi:[1,0]
	v_lshl_add_u64 v[56:57], s[18:19], 0, v[56:57]
	v_cvt_pk_bf16_f32 v52, v60, v61
	v_cvt_pk_bf16_f32 v53, v62, v63
	v_cvt_pk_bf16_f32 v54, v54, v55
	v_cvt_pk_bf16_f32 v55, v66, v67
	v_lshl_add_u64 v[56:57], v[56:57], 0, v[118:119]
	global_store_dwordx4 v[56:57], v[52:55], off

.LBB0_452:
	s_nop 2
	v_mov_b32_e32 v12, v0
	s_barrier
	v_readlane_b32 s18, v247, 7
	v_readfirstlane_b32 s1, v12
	v_ashrrev_i32_e32 v4, 4, v12
	s_ashr_i32 s1, s1, 6
	v_xor_b32_e32 v7, v4, v12
	s_cmp_lt_i32 s1, 8
	v_and_b32_e32 v5, 63, v12
	v_lshlrev_b32_e32 v6, 8, v4
	v_lshlrev_b32_e32 v7, 4, v7
	s_cselect_b64 s[40:41], -1, 0
	v_and_or_b32 v13, v7, s84, v6
	v_lshlrev_b32_e32 v6, 4, v5
	v_ashrrev_i32_e32 v5, 31, v4
	s_and_b64 s[38:39], s[40:41], exec
	v_lshlrev_b64 v[4:5], 8, v[4:5]
	v_readlane_b32 s19, v247, 8
	v_lshlrev_b32_e32 v8, 4, v12
	s_cselect_b32 s38, s1, 7
	v_lshl_add_u64 v[4:5], s[18:19], 0, v[4:5]
	v_and_b32_e32 v8, 0xf0, v8
	v_mov_b32_e32 v9, v2
	s_ashr_i32 s39, s38, 31
	v_lshl_add_u64 v[8:9], v[4:5], 0, v[8:9]
	s_lshl_b64 s[38:39], s[38:39], 13
	v_add_co_u32_e32 v10, vcc, s94, v8
	s_add_u32 s48, s65, s38
	s_nop 0
	v_addc_co_u32_e32 v11, vcc, 0, v9, vcc
	s_addc_u32 s49, s68, s39
	s_lshl_b32 s38, s1, 5
	v_add_co_u32_e32 v140, vcc, s16, v8
	s_cmp_gt_i32 s1, 7
	global_load_dwordx4 v[24:27], v[8:9], off
	global_load_dwordx4 v[44:47], v[10:11], off
	v_addc_co_u32_e32 v141, vcc, 0, v9, vcc
	s_movk_i32 s1, 0x6000
	v_add_co_u32_e32 v142, vcc, s1, v8
	global_load_dwordx4 v[20:23], v[140:141], off sc0
	s_nop 0
	v_addc_co_u32_e32 v143, vcc, 0, v9, vcc
	global_load_dwordx4 v[32:35], v[142:143], off
	v_mov_b32_e32 v7, v2
	v_lshl_add_u64 v[6:7], s[48:49], 0, v[6:7]
	v_lshl_add_u64 v[4:5], v[6:7], 0, s[20:21]
	global_load_dwordx4 v[28:31], v[4:5], off sc0
	global_load_dwordx4 v[60:63], v[4:5], off offset:1024 sc0
	global_load_dwordx4 v[48:51], v[4:5], off offset:2048 sc0
	global_load_dwordx4 v[52:55], v[4:5], off offset:3072 sc0
	v_add_co_u32_e32 v4, vcc, s12, v4
	v_bfe_u32 v120, v12, 4, 2
	s_nop 0
	v_addc_co_u32_e32 v5, vcc, 0, v5, vcc
	global_load_dwordx4 v[36:39], v[4:5], off sc0
	global_load_dwordx4 v[64:67], v[4:5], off offset:1024 sc0
	global_load_dwordx4 v[56:59], v[4:5], off offset:2048 sc0
	global_load_dwordx4 v[76:79], v[4:5], off offset:3072 sc0
	v_and_b32_e32 v3, 15, v12
	v_bitop3_b32 v4, v120, v12, 15 bitop3:0x78
	v_lshl_add_u32 v178, v3, 8, 0
	v_lshlrev_b32_e32 v4, 4, v4
	v_add_u32_e32 v121, 0, v13
	s_mov_b32 s1, s21
	v_add_u32_e32 v122, v178, v4
	v_lshl_add_u64 v[176:177], v[6:7], 0, s[0:1]
	s_waitcnt vmcnt(11)
	ds_write_b128 v121, v[24:27]
	s_waitcnt vmcnt(10)
	ds_write_b128 v121, v[44:47] offset:8192
	s_waitcnt vmcnt(9)
	ds_write_b128 v121, v[20:23] offset:16384
	s_waitcnt vmcnt(8)
	ds_write_b128 v121, v[32:35] offset:24576
	s_waitcnt lgkmcnt(0)
	s_barrier
	ds_read_b128 v[4:7], v122
	ds_read_b128 v[12:15], v122 offset:4096
	ds_read_b128 v[40:43], v122 offset:8192
	ds_read_b128 v[68:71], v122 offset:12288
	ds_read_b128 v[72:75], v122 offset:16384
	ds_read_b128 v[80:83], v122 offset:20480
	ds_read_b128 v[84:87], v122 offset:24576
	ds_read_b128 v[88:91], v122 offset:28672
	global_load_dwordx4 v[16:19], v[8:9], off
	s_nop 0
	global_load_dwordx4 v[8:11], v[10:11], off
	s_waitcnt vmcnt(9) lgkmcnt(7)
	v_mfma_f32_16x16x32_bf16 v[92:95], v[4:7], v[28:31], 0
	s_waitcnt vmcnt(5)
	v_mfma_f32_16x16x32_bf16 v[96:99], v[4:7], v[36:39], 0
	s_waitcnt lgkmcnt(6)
	v_mfma_f32_16x16x32_bf16 v[100:103], v[12:15], v[28:31], 0
	v_mfma_f32_16x16x32_bf16 v[104:107], v[12:15], v[36:39], 0
	s_waitcnt lgkmcnt(5)
	v_mfma_f32_16x16x32_bf16 v[108:111], v[40:43], v[28:31], 0
	v_mfma_f32_16x16x32_bf16 v[112:115], v[40:43], v[36:39], 0
	s_waitcnt lgkmcnt(4)
	v_mfma_f32_16x16x32_bf16 v[116:119], v[68:71], v[28:31], 0
	v_mfma_f32_16x16x32_bf16 v[68:71], v[68:71], v[36:39], 0
	v_bitop3_b32 v4, v120, v3, 4 bitop3:0x36
	v_lshlrev_b32_e32 v4, 4, v4
	v_add_u32_e32 v123, v178, v4
	ds_read_b128 v[124:127], v123
	ds_read_b128 v[128:131], v123 offset:4096
	ds_read_b128 v[132:135], v123 offset:8192
	ds_read_b128 v[136:139], v123 offset:12288
	global_load_dwordx4 v[12:15], v[140:141], off sc0
	global_load_dwordx4 v[4:7], v[142:143], off
	s_waitcnt lgkmcnt(7)
	v_mfma_f32_16x16x32_bf16 v[140:143], v[72:75], v[28:31], 0
	v_mfma_f32_16x16x32_bf16 v[72:75], v[72:75], v[36:39], 0
	s_waitcnt lgkmcnt(6)
	v_mfma_f32_16x16x32_bf16 v[144:147], v[80:83], v[28:31], 0
	v_mfma_f32_16x16x32_bf16 v[80:83], v[80:83], v[36:39], 0
	s_waitcnt lgkmcnt(5)
	v_mfma_f32_16x16x32_bf16 v[148:151], v[84:87], v[28:31], 0
	v_mfma_f32_16x16x32_bf16 v[84:87], v[84:87], v[36:39], 0
	s_waitcnt lgkmcnt(4)
	v_mfma_f32_16x16x32_bf16 v[152:155], v[88:91], v[28:31], 0
	v_mfma_f32_16x16x32_bf16 v[88:91], v[88:91], v[36:39], 0
	ds_read_b128 v[156:159], v123 offset:16384
	ds_read_b128 v[160:163], v123 offset:20480
	ds_read_b128 v[164:167], v123 offset:24576
	ds_read_b128 v[168:171], v123 offset:28672
	v_add_co_u32_e32 v186, vcc, s12, v176
	s_nop 1
	v_addc_co_u32_e32 v187, vcc, 0, v177, vcc
	global_load_dwordx4 v[36:39], v[176:177], off sc0
	global_load_dwordx4 v[40:43], v[186:187], off sc0
	ds_write_b128 v121, v[24:27] offset:32768
	s_waitcnt lgkmcnt(8)
	v_mfma_f32_16x16x32_bf16 v[92:95], v[124:127], v[60:63], v[92:95]
	s_waitcnt vmcnt(8)
	v_mfma_f32_16x16x32_bf16 v[96:99], v[124:127], v[64:67], v[96:99]
	s_waitcnt lgkmcnt(7)
	v_mfma_f32_16x16x32_bf16 v[100:103], v[128:131], v[60:63], v[100:103]
	v_mfma_f32_16x16x32_bf16 v[104:107], v[128:131], v[64:67], v[104:107]
	s_waitcnt lgkmcnt(6)
	v_mfma_f32_16x16x32_bf16 v[108:111], v[132:135], v[60:63], v[108:111]
	v_mfma_f32_16x16x32_bf16 v[112:115], v[132:135], v[64:67], v[112:115]
	s_waitcnt lgkmcnt(5)
	v_mfma_f32_16x16x32_bf16 v[116:119], v[136:139], v[60:63], v[116:119]
	v_mfma_f32_16x16x32_bf16 v[68:71], v[136:139], v[64:67], v[68:71]
	v_bitop3_b32 v24, v120, v3, 8 bitop3:0x36
	v_lshlrev_b32_e32 v24, 4, v24
	v_add_u32_e32 v124, v178, v24
	ds_read_b128 v[126:129], v124
	ds_read_b128 v[130:133], v124 offset:4096
	ds_read_b128 v[134:137], v124 offset:8192
	ds_read_b128 v[172:175], v124 offset:12288
	global_load_dwordx4 v[28:31], v[176:177], off offset:1024 sc0
	ds_write_b128 v121, v[44:47] offset:40960
	s_waitcnt lgkmcnt(9)
	v_mfma_f32_16x16x32_bf16 v[138:141], v[156:159], v[60:63], v[140:143]
	v_mfma_f32_16x16x32_bf16 v[72:75], v[156:159], v[64:67], v[72:75]
	s_waitcnt lgkmcnt(8)
	v_mfma_f32_16x16x32_bf16 v[142:145], v[160:163], v[60:63], v[144:147]
	v_mfma_f32_16x16x32_bf16 v[80:83], v[160:163], v[64:67], v[80:83]
	s_waitcnt lgkmcnt(7)
	v_mfma_f32_16x16x32_bf16 v[146:149], v[164:167], v[60:63], v[148:151]
	v_mfma_f32_16x16x32_bf16 v[84:87], v[164:167], v[64:67], v[84:87]
	s_waitcnt lgkmcnt(6)
	v_mfma_f32_16x16x32_bf16 v[60:63], v[168:171], v[60:63], v[152:155]
	v_mfma_f32_16x16x32_bf16 v[64:67], v[168:171], v[64:67], v[88:91]
	s_nop 2
	ds_read_b128 v[88:91], v124 offset:16384
	ds_read_b128 v[150:153], v124 offset:20480
	ds_read_b128 v[154:157], v124 offset:24576
	ds_read_b128 v[158:161], v124 offset:28672
	global_load_dwordx4 v[24:27], v[176:177], off offset:2048 sc0
	global_load_dwordx4 v[44:47], v[186:187], off offset:1024 sc0
	ds_write_b128 v121, v[20:23] offset:49152
	s_waitcnt lgkmcnt(9)
	v_mfma_f32_16x16x32_bf16 v[92:95], v[126:129], v[48:51], v[92:95]
	s_waitcnt vmcnt(10)
	v_mfma_f32_16x16x32_bf16 v[96:99], v[126:129], v[56:59], v[96:99]
	s_waitcnt lgkmcnt(8)
	v_mfma_f32_16x16x32_bf16 v[100:103], v[130:133], v[48:51], v[100:103]
	v_mfma_f32_16x16x32_bf16 v[104:107], v[130:133], v[56:59], v[104:107]
	s_waitcnt lgkmcnt(6)
	v_mfma_f32_16x16x32_bf16 v[68:71], v[172:175], v[56:59], v[68:71]
	v_mfma_f32_16x16x32_bf16 v[126:129], v[134:137], v[48:51], v[108:111]
	v_mfma_f32_16x16x32_bf16 v[130:133], v[134:137], v[56:59], v[112:115]
	v_mfma_f32_16x16x32_bf16 v[134:137], v[172:175], v[48:51], v[116:119]
	v_bitop3_b32 v20, v120, v3, 12 bitop3:0x36
	v_lshlrev_b32_e32 v20, 4, v20
	v_add_u32_e32 v125, v178, v20
	ds_read_b128 v[108:111], v125
	ds_read_b128 v[162:165], v125 offset:4096
	ds_read_b128 v[166:169], v125 offset:8192
	ds_read_b128 v[170:173], v125 offset:12288
	global_load_dwordx4 v[20:23], v[176:177], off offset:3072 sc0
	ds_write_b128 v121, v[32:35] offset:57344
	s_waitcnt lgkmcnt(9)
	v_mfma_f32_16x16x32_bf16 v[72:75], v[88:91], v[56:59], v[72:75]
	v_mfma_f32_16x16x32_bf16 v[138:141], v[88:91], v[48:51], v[138:141]
	s_waitcnt lgkmcnt(8)
	v_mfma_f32_16x16x32_bf16 v[142:145], v[150:153], v[48:51], v[142:145]
	v_mfma_f32_16x16x32_bf16 v[150:153], v[150:153], v[56:59], v[80:83]
	s_waitcnt lgkmcnt(7)
	v_mfma_f32_16x16x32_bf16 v[146:149], v[154:157], v[48:51], v[146:149]
	v_mfma_f32_16x16x32_bf16 v[154:157], v[154:157], v[56:59], v[84:87]
	s_waitcnt lgkmcnt(6)
	v_mfma_f32_16x16x32_bf16 v[174:177], v[158:161], v[48:51], v[60:63]
	v_mfma_f32_16x16x32_bf16 v[158:161], v[158:161], v[56:59], v[64:67]
	ds_read_b128 v[56:59], v125 offset:16384
	s_nop 0
	ds_read_b128 v[60:63], v125 offset:20480
	ds_read_b128 v[178:181], v125 offset:24576
	ds_read_b128 v[182:185], v125 offset:28672
	global_load_dwordx4 v[48:51], v[186:187], off offset:2048 sc0
	s_waitcnt lgkmcnt(8)
	v_mfma_f32_16x16x32_bf16 v[116:119], v[108:111], v[52:55], v[92:95]
	s_waitcnt vmcnt(11)
	v_mfma_f32_16x16x32_bf16 v[112:115], v[108:111], v[76:79], v[96:99]
	s_waitcnt lgkmcnt(7)
	v_mfma_f32_16x16x32_bf16 v[108:111], v[162:165], v[52:55], v[100:103]
	v_mfma_f32_16x16x32_bf16 v[104:107], v[162:165], v[76:79], v[104:107]
	s_waitcnt lgkmcnt(6)
	v_mfma_f32_16x16x32_bf16 v[100:103], v[166:169], v[52:55], v[126:129]
	v_mfma_f32_16x16x32_bf16 v[96:99], v[166:169], v[76:79], v[130:133]
	s_waitcnt lgkmcnt(5)
	v_mfma_f32_16x16x32_bf16 v[92:95], v[170:173], v[52:55], v[134:137]
	v_mfma_f32_16x16x32_bf16 v[88:91], v[170:173], v[76:79], v[68:71]
	global_load_dwordx4 v[32:35], v[186:187], off offset:3072 sc0
	s_waitcnt lgkmcnt(3)
	v_mfma_f32_16x16x32_bf16 v[84:87], v[56:59], v[52:55], v[138:141]
	v_mfma_f32_16x16x32_bf16 v[80:83], v[56:59], v[76:79], v[72:75]
	s_waitcnt lgkmcnt(2)
	v_mfma_f32_16x16x32_bf16 v[72:75], v[60:63], v[52:55], v[142:145]
	v_mfma_f32_16x16x32_bf16 v[68:71], v[60:63], v[76:79], v[150:153]
	s_waitcnt lgkmcnt(1)
	v_mfma_f32_16x16x32_bf16 v[64:67], v[178:181], v[52:55], v[146:149]
	v_mfma_f32_16x16x32_bf16 v[60:63], v[178:181], v[76:79], v[154:157]
	s_waitcnt lgkmcnt(0)
	v_mfma_f32_16x16x32_bf16 v[56:59], v[182:185], v[52:55], v[174:177]
	v_mfma_f32_16x16x32_bf16 v[52:55], v[182:185], v[76:79], v[158:161]
	s_cbranch_scc1 .LBB0_454
	v_mov_b32_e32 v128, v120
	v_mov_b32_e32 v76, v3
	v_readlane_b32 s0, v247, 15
	v_and_b32_e32 v130, 1, v128
	s_add_i32 s0, s38, s0
	v_lshlrev_b32_e32 v77, 4, v130
	v_add3_u32 v131, s0, v76, v77
	v_lshl_add_u32 v76, v128, 4, 0
	v_add_u32_e32 v132, 0x20400, v76
	ds_read_b128 v[76:79], v132
	v_lshl_add_u32 v133, v128, 2, s46
	v_ashrrev_i32_e32 v128, 11, v133
	v_ashrrev_i32_e32 v126, 6, v131
	v_ashrrev_i32_e32 v129, 31, v128
	v_readlane_b32 s0, v251, 53
	v_ashrrev_i32_e32 v127, 31, v126
	s_waitcnt lgkmcnt(0)
	v_pk_mul_f32 v[118:119], v[118:119], v[78:79]
	v_pk_mul_f32 v[116:117], v[116:117], v[76:77]
	v_pk_mul_f32 v[78:79], v[114:115], v[78:79]
	v_pk_mul_f32 v[76:77], v[112:113], v[76:77]
	v_lshlrev_b64 v[112:113], 21, v[128:129]
	v_readlane_b32 s1, v251, 54
	v_cvt_pk_bf16_f32 v116, v116, v117
	v_cvt_pk_bf16_f32 v117, v118, v119
	v_cvt_pk_bf16_f32 v118, v76, v77
	v_cvt_pk_bf16_f32 v119, v78, v79
	v_lshlrev_b64 v[76:77], 18, v[126:127]
	v_lshlrev_b32_e32 v78, 12, v131
	v_lshl_add_u64 v[112:113], s[0:1], 0, v[112:113]
	v_and_b32_e32 v134, 0x7fc, v133
	v_and_b32_e32 v78, 0x3f000, v78
	v_mov_b32_e32 v79, v2
	v_lshl_add_u64 v[112:113], v[112:113], 0, v[76:77]
	v_lshl_add_u64 v[112:113], v[112:113], 0, v[78:79]
	v_lshlrev_b32_e32 v114, 1, v134
	v_mov_b32_e32 v115, v2
	v_lshl_add_u64 v[112:113], v[112:113], 0, v[114:115]
	v_lshlrev_b32_e32 v128, 3, v130
	v_sub_co_u32_e32 v126, vcc, v112, v128
	s_nop 1
	v_permlane16_swap_b32 v116, v118
	v_permlane16_swap_b32 v117, v119
	s_nop 1
	v_subbrev_co_u32_e32 v127, vcc, 0, v113, vcc
	ds_read_b128 v[112:115], v132 offset:64
	global_store_dwordx4 v[126:127], v[116:119], off
	s_waitcnt lgkmcnt(0)
	v_pk_mul_f32 v[110:111], v[110:111], v[114:115]
	v_add_u32_e32 v117, 16, v133
	v_ashrrev_i32_e32 v116, 11, v117
	v_and_b32_e32 v118, 0x7fc, v117
	v_pk_mul_f32 v[108:109], v[108:109], v[112:113]
	v_pk_mul_f32 v[104:105], v[104:105], v[112:113]
	v_ashrrev_i32_e32 v117, 31, v116
	v_cvt_pk_bf16_f32 v108, v108, v109
	v_cvt_pk_bf16_f32 v109, v110, v111
	v_cvt_pk_bf16_f32 v110, v104, v105
	v_lshlrev_b64 v[104:105], 21, v[116:117]
	v_lshl_add_u64 v[104:105], s[0:1], 0, v[104:105]
	v_pk_mul_f32 v[106:107], v[106:107], v[114:115]
	v_lshl_add_u64 v[104:105], v[104:105], 0, v[76:77]
	v_cvt_pk_bf16_f32 v111, v106, v107
	v_lshl_add_u64 v[104:105], v[104:105], 0, v[78:79]
	v_lshlrev_b32_e32 v106, 1, v118
	v_mov_b32_e32 v107, v2
	v_lshl_add_u64 v[104:105], v[104:105], 0, v[106:107]
	v_sub_co_u32_e32 v112, vcc, v104, v128
	s_nop 1
	v_permlane16_swap_b32 v108, v110
	v_permlane16_swap_b32 v109, v111
	s_nop 1
	v_subbrev_co_u32_e32 v113, vcc, 0, v105, vcc
	ds_read_b128 v[104:107], v132 offset:128
	global_store_dwordx4 v[112:113], v[108:111], off
	s_waitcnt lgkmcnt(0)
	v_pk_mul_f32 v[102:103], v[102:103], v[106:107]
	v_add_u32_e32 v109, 32, v133
	v_ashrrev_i32_e32 v108, 11, v109
	v_and_b32_e32 v110, 0x7fc, v109
	v_pk_mul_f32 v[100:101], v[100:101], v[104:105]
	v_pk_mul_f32 v[96:97], v[96:97], v[104:105]
	v_ashrrev_i32_e32 v109, 31, v108
	v_cvt_pk_bf16_f32 v100, v100, v101
	v_cvt_pk_bf16_f32 v101, v102, v103
	v_cvt_pk_bf16_f32 v102, v96, v97
	v_lshlrev_b64 v[96:97], 21, v[108:109]
	v_lshl_add_u64 v[96:97], s[0:1], 0, v[96:97]
	v_pk_mul_f32 v[98:99], v[98:99], v[106:107]
	v_lshl_add_u64 v[96:97], v[96:97], 0, v[76:77]
	v_cvt_pk_bf16_f32 v103, v98, v99
	v_lshl_add_u64 v[96:97], v[96:97], 0, v[78:79]
	v_lshlrev_b32_e32 v98, 1, v110
	v_mov_b32_e32 v99, v2
	v_lshl_add_u64 v[96:97], v[96:97], 0, v[98:99]
	v_sub_co_u32_e32 v104, vcc, v96, v128
	s_nop 1
	v_permlane16_swap_b32 v100, v102
	v_permlane16_swap_b32 v101, v103
	s_nop 1
	v_subbrev_co_u32_e32 v105, vcc, 0, v97, vcc
	ds_read_b128 v[96:99], v132 offset:192
	global_store_dwordx4 v[104:105], v[100:103], off
	s_waitcnt lgkmcnt(0)
	v_pk_mul_f32 v[94:95], v[94:95], v[98:99]
	v_add_u32_e32 v101, 48, v133
	v_ashrrev_i32_e32 v100, 11, v101
	v_and_b32_e32 v102, 0x7fc, v101
	v_pk_mul_f32 v[92:93], v[92:93], v[96:97]
	v_pk_mul_f32 v[88:89], v[88:89], v[96:97]
	v_ashrrev_i32_e32 v101, 31, v100
	v_cvt_pk_bf16_f32 v92, v92, v93
	v_cvt_pk_bf16_f32 v93, v94, v95
	v_cvt_pk_bf16_f32 v94, v88, v89
	v_lshlrev_b64 v[88:89], 21, v[100:101]
	v_lshl_add_u64 v[88:89], s[0:1], 0, v[88:89]
	v_pk_mul_f32 v[90:91], v[90:91], v[98:99]
	v_lshl_add_u64 v[88:89], v[88:89], 0, v[76:77]
	v_cvt_pk_bf16_f32 v95, v90, v91
	v_lshl_add_u64 v[88:89], v[88:89], 0, v[78:79]
	v_lshlrev_b32_e32 v90, 1, v102
	v_mov_b32_e32 v91, v2
	v_lshl_add_u64 v[88:89], v[88:89], 0, v[90:91]
	v_sub_co_u32_e32 v96, vcc, v88, v128
	s_nop 1
	v_permlane16_swap_b32 v92, v94
	v_permlane16_swap_b32 v93, v95
	s_nop 1
	v_subbrev_co_u32_e32 v97, vcc, 0, v89, vcc
	ds_read_b128 v[88:91], v132 offset:256
	global_store_dwordx4 v[96:97], v[92:95], off
	s_waitcnt lgkmcnt(0)
	v_pk_mul_f32 v[86:87], v[86:87], v[90:91]
	v_add_u32_e32 v93, 64, v133
	v_ashrrev_i32_e32 v92, 11, v93
	v_and_b32_e32 v94, 0x7fc, v93
	v_pk_mul_f32 v[84:85], v[84:85], v[88:89]
	v_pk_mul_f32 v[80:81], v[80:81], v[88:89]
	v_ashrrev_i32_e32 v93, 31, v92
	v_cvt_pk_bf16_f32 v84, v84, v85
	v_cvt_pk_bf16_f32 v85, v86, v87
	v_cvt_pk_bf16_f32 v86, v80, v81
	v_lshlrev_b64 v[80:81], 21, v[92:93]
	v_lshl_add_u64 v[80:81], s[0:1], 0, v[80:81]
	v_pk_mul_f32 v[82:83], v[82:83], v[90:91]
	v_lshl_add_u64 v[80:81], v[80:81], 0, v[76:77]
	v_cvt_pk_bf16_f32 v87, v82, v83
	v_lshl_add_u64 v[80:81], v[80:81], 0, v[78:79]
	v_lshlrev_b32_e32 v82, 1, v94
	v_mov_b32_e32 v83, v2
	v_lshl_add_u64 v[80:81], v[80:81], 0, v[82:83]
	v_sub_co_u32_e32 v88, vcc, v80, v128
	s_nop 1
	v_permlane16_swap_b32 v84, v86
	v_permlane16_swap_b32 v85, v87
	s_nop 1
	v_subbrev_co_u32_e32 v89, vcc, 0, v81, vcc
	ds_read_b128 v[80:83], v132 offset:320
	global_store_dwordx4 v[88:89], v[84:87], off
	s_waitcnt lgkmcnt(0)
	v_pk_mul_f32 v[74:75], v[74:75], v[82:83]
	v_add_u32_e32 v85, 0x50, v133
	v_ashrrev_i32_e32 v84, 11, v85
	v_and_b32_e32 v86, 0x7fc, v85
	v_pk_mul_f32 v[72:73], v[72:73], v[80:81]
	v_pk_mul_f32 v[68:69], v[68:69], v[80:81]
	v_ashrrev_i32_e32 v85, 31, v84
	v_cvt_pk_bf16_f32 v72, v72, v73
	v_cvt_pk_bf16_f32 v73, v74, v75
	v_cvt_pk_bf16_f32 v74, v68, v69
	v_lshlrev_b64 v[68:69], 21, v[84:85]
	v_lshl_add_u64 v[68:69], s[0:1], 0, v[68:69]
	v_pk_mul_f32 v[70:71], v[70:71], v[82:83]
	v_lshl_add_u64 v[68:69], v[68:69], 0, v[76:77]
	v_cvt_pk_bf16_f32 v75, v70, v71
	v_lshl_add_u64 v[68:69], v[68:69], 0, v[78:79]
	v_lshlrev_b32_e32 v70, 1, v86
	v_mov_b32_e32 v71, v2
	v_lshl_add_u64 v[68:69], v[68:69], 0, v[70:71]
	v_sub_co_u32_e32 v80, vcc, v68, v128
	s_nop 1
	v_permlane16_swap_b32 v72, v74
	v_permlane16_swap_b32 v73, v75
	s_nop 1
	v_subbrev_co_u32_e32 v81, vcc, 0, v69, vcc
	ds_read_b128 v[68:71], v132 offset:384
	global_store_dwordx4 v[80:81], v[72:75], off
	s_waitcnt lgkmcnt(0)
	v_pk_mul_f32 v[66:67], v[66:67], v[70:71]
	v_add_u32_e32 v73, 0x60, v133
	v_ashrrev_i32_e32 v72, 11, v73
	v_and_b32_e32 v74, 0x7fc, v73
	v_pk_mul_f32 v[64:65], v[64:65], v[68:69]
	v_pk_mul_f32 v[60:61], v[60:61], v[68:69]
	v_ashrrev_i32_e32 v73, 31, v72
	v_cvt_pk_bf16_f32 v64, v64, v65
	v_cvt_pk_bf16_f32 v65, v66, v67
	v_cvt_pk_bf16_f32 v66, v60, v61
	v_lshlrev_b64 v[60:61], 21, v[72:73]
	v_lshl_add_u64 v[60:61], s[0:1], 0, v[60:61]
	v_pk_mul_f32 v[62:63], v[62:63], v[70:71]
	v_lshl_add_u64 v[60:61], v[60:61], 0, v[76:77]
	v_cvt_pk_bf16_f32 v67, v62, v63
	v_lshl_add_u64 v[60:61], v[60:61], 0, v[78:79]
	v_lshlrev_b32_e32 v62, 1, v74
	v_mov_b32_e32 v63, v2
	v_lshl_add_u64 v[60:61], v[60:61], 0, v[62:63]
	v_sub_co_u32_e32 v68, vcc, v60, v128
	s_nop 1
	v_permlane16_swap_b32 v64, v66
	v_permlane16_swap_b32 v65, v67
	s_nop 1
	v_subbrev_co_u32_e32 v69, vcc, 0, v61, vcc
	ds_read_b128 v[60:63], v132 offset:448
	global_store_dwordx4 v[68:69], v[64:67], off
	s_waitcnt lgkmcnt(0)
	v_pk_mul_f32 v[58:59], v[58:59], v[62:63]
	v_add_u32_e32 v65, 0x70, v133
	v_ashrrev_i32_e32 v64, 11, v65
	v_and_b32_e32 v66, 0x7fc, v65
	v_pk_mul_f32 v[56:57], v[56:57], v[60:61]
	v_pk_mul_f32 v[52:53], v[52:53], v[60:61]
	v_ashrrev_i32_e32 v65, 31, v64
	v_cvt_pk_bf16_f32 v56, v56, v57
	v_cvt_pk_bf16_f32 v57, v58, v59
	v_cvt_pk_bf16_f32 v58, v52, v53
	v_lshlrev_b64 v[52:53], 21, v[64:65]
	v_lshl_add_u64 v[52:53], s[0:1], 0, v[52:53]
	v_pk_mul_f32 v[54:55], v[54:55], v[62:63]
	v_lshl_add_u64 v[52:53], v[52:53], 0, v[76:77]
	v_cvt_pk_bf16_f32 v59, v54, v55
	v_lshl_add_u64 v[52:53], v[52:53], 0, v[78:79]
	v_lshlrev_b32_e32 v54, 1, v66
	v_mov_b32_e32 v55, v2
	v_lshl_add_u64 v[52:53], v[52:53], 0, v[54:55]
	v_sub_co_u32_e32 v52, vcc, v52, v128
	s_nop 1
	v_permlane16_swap_b32 v56, v58
	v_permlane16_swap_b32 v57, v59
	s_nop 1
	v_subbrev_co_u32_e32 v53, vcc, 0, v53, vcc
	global_store_dwordx4 v[52:53], v[56:59], off

.LBB0_781:
	s_ashr_i32 s40, s52, 5
	s_and_b32 s53, s52, 31
	s_lshl_b32 s1, s40, 7
	s_lshl_b32 s0, s53, 11
	s_ashr_i32 s12, s1, 31
	s_add_u32 s0, s0, s1
	s_addc_u32 s1, 0, s12
	s_lshl_b64 s[0:1], s[0:1], 9
	s_add_u32 s0, s8, s0
	s_waitcnt vmcnt(8)
	v_mov_b32_e32 v36, v0
	s_addc_u32 s1, s9, s1
	s_lshl_b32 s12, s53, 16
	v_mov_b32_e32 v56, v0
	s_barrier
	s_add_u32 s12, s48, s12
	s_addc_u32 s39, s49, 0
	v_readfirstlane_b32 s38, v56
	s_ashr_i32 s41, s38, 6
	s_cmp_lt_i32 s41, 8
	s_cselect_b32 s42, s41, 7
	s_ashr_i32 s43, s42, 31
	s_waitcnt vmcnt(8)
	v_ashrrev_i32_e32 v4, 4, v56
	s_lshl_b64 s[42:43], s[42:43], 13
	v_lshlrev_b32_e32 v6, 3, v56
	v_xor_b32_e32 v7, v4, v56
	s_add_u32 s42, s12, s42
	v_and_b32_e32 v5, 63, v56
	v_and_b32_e32 v22, 0x78, v6
	v_lshlrev_b32_e32 v6, 8, v4
	v_lshlrev_b32_e32 v7, 4, v7
	s_addc_u32 s43, s39, s43
	v_and_or_b32 v57, v7, s84, v6
	v_lshlrev_b32_e32 v6, 4, v5
	v_mov_b32_e32 v7, v2
	v_readlane_b32 s12, v249, 38
	v_ashrrev_i32_e32 v5, 31, v4
	v_lshl_add_u64 v[54:55], s[42:43], 0, v[6:7]
	v_or_b32_e32 v6, s12, v22
	v_lshlrev_b64 v[4:5], 9, v[4:5]
	v_lshl_add_u64 v[20:21], s[0:1], 0, v[4:5]
	v_lshlrev_b32_e32 v16, 1, v6
	v_mov_b32_e32 v17, v2
	s_mov_b64 s[42:43], 0x4000
	v_lshl_add_u64 v[70:71], v[20:21], 0, v[16:17]
	v_lshl_add_u64 v[24:25], v[20:21], 0, s[42:43]
	s_mov_b64 s[42:43], 0x8000
	global_load_dwordx4 v[4:7], v[70:71], off
	v_lshl_add_u64 v[74:75], v[24:25], 0, v[16:17]
	v_lshl_add_u64 v[28:29], v[20:21], 0, s[42:43]
	s_mov_b64 s[42:43], 0xc000
	global_load_dwordx4 v[8:11], v[74:75], off
	v_lshl_add_u64 v[94:95], v[28:29], 0, v[16:17]
	v_lshl_add_u64 v[32:33], v[20:21], 0, s[42:43]
	global_load_dwordx4 v[12:15], v[94:95], off
	v_lshl_add_u64 v[98:99], v[32:33], 0, v[16:17]
	global_load_dwordx4 v[16:19], v[98:99], off
	v_readlane_b32 s12, v249, 39
	v_readlane_b32 s18, v248, 11
	v_readlane_b32 s19, v248, 12
	v_or_b32_e32 v22, s12, v22
	v_lshlrev_b32_e32 v34, 1, v22
	v_mov_b32_e32 v35, v2
	s_mov_b32 s19, s21
	v_lshl_add_u64 v[20:21], v[20:21], 0, v[34:35]
	v_lshl_add_u64 v[24:25], v[24:25], 0, v[34:35]
	v_lshl_add_u64 v[28:29], v[28:29], 0, v[34:35]
	v_lshl_add_u64 v[32:33], v[32:33], 0, v[34:35]
	v_lshl_add_u64 v[50:51], v[54:55], 0, s[18:19]
	global_load_dwordx4 v[20:23], v[20:21], off
	s_mov_b32 s12, s18
	global_load_dwordx4 v[24:27], v[24:25], off
	v_writelane_b32 v248, s12, 11
	global_load_dwordx4 v[28:31], v[28:29], off
	v_and_b32_e32 v3, 15, v56
	global_load_dwordx4 v[32:35], v[32:33], off
	s_nop 0
	global_load_dwordx4 v[38:41], v[50:51], off sc0
	global_load_dwordx4 v[42:45], v[50:51], off offset:1024 sc0
	global_load_dwordx4 v[46:49], v[50:51], off offset:2048 sc0
	s_nop 0
	global_load_dwordx4 v[50:53], v[50:51], off offset:3072 sc0
	v_writelane_b32 v248, s13, 12
	v_bfe_u32 v37, v56, 4, 2
	v_add_u32_e32 v120, 0, v57
	v_readlane_b32 s18, v248, 13
	v_readlane_b32 s19, v248, 14
	v_lshl_add_u32 v121, v3, 8, 0
	s_mov_b32 s19, s21
	v_lshl_add_u64 v[118:119], v[54:55], 0, s[18:19]
	s_mov_b32 s12, s18
	v_writelane_b32 v248, s12, 13
	s_cmp_gt_i32 s41, 7
	s_waitcnt vmcnt(11)
	ds_write_b128 v120, v[4:7]
	s_waitcnt vmcnt(10)
	ds_write_b128 v120, v[8:11] offset:8192
	s_waitcnt vmcnt(9)
	ds_write_b128 v120, v[12:15] offset:16384
	s_waitcnt vmcnt(8)
	ds_write_b128 v120, v[16:19] offset:24576
	v_bitop3_b32 v4, v37, v56, 15 bitop3:0x78
	v_lshl_add_u32 v122, v4, 4, v121
	s_waitcnt lgkmcnt(0)
	s_barrier
	ds_read_b128 v[4:7], v122
	ds_read_b128 v[8:11], v122 offset:4096
	ds_read_b128 v[12:15], v122 offset:8192
	ds_read_b128 v[16:19], v122 offset:12288
	ds_read_b128 v[54:57], v122 offset:16384
	ds_read_b128 v[58:61], v122 offset:20480
	ds_read_b128 v[62:65], v122 offset:24576
	ds_read_b128 v[66:69], v122 offset:28672
	v_writelane_b32 v248, s13, 14
	global_load_dwordx4 v[70:73], v[70:71], off
	s_nop 0
	global_load_dwordx4 v[74:77], v[74:75], off
	s_waitcnt vmcnt(5) lgkmcnt(7)
	v_mfma_f32_16x16x32_bf16 v[4:7], v[38:41], v[4:7], 0
	s_waitcnt lgkmcnt(6)
	v_mfma_f32_16x16x32_bf16 v[8:11], v[38:41], v[8:11], 0
	s_waitcnt lgkmcnt(5)
	v_mfma_f32_16x16x32_bf16 v[12:15], v[38:41], v[12:15], 0
	s_waitcnt lgkmcnt(4)
	v_mfma_f32_16x16x32_bf16 v[16:19], v[38:41], v[16:19], 0
	v_bitop3_b32 v78, v37, v3, 4 bitop3:0x36
	v_lshl_add_u32 v123, v78, 4, v121
	ds_read_b128 v[78:81], v123
	ds_read_b128 v[82:85], v123 offset:4096
	ds_read_b128 v[86:89], v123 offset:8192
	ds_read_b128 v[90:93], v123 offset:12288
	global_load_dwordx4 v[94:97], v[94:95], off
	s_nop 0
	global_load_dwordx4 v[98:101], v[98:99], off
	s_waitcnt lgkmcnt(7)
	v_mfma_f32_16x16x32_bf16 v[54:57], v[38:41], v[54:57], 0
	s_waitcnt lgkmcnt(6)
	v_mfma_f32_16x16x32_bf16 v[58:61], v[38:41], v[58:61], 0
	s_waitcnt lgkmcnt(5)
	v_mfma_f32_16x16x32_bf16 v[62:65], v[38:41], v[62:65], 0
	s_waitcnt lgkmcnt(4)
	v_mfma_f32_16x16x32_bf16 v[38:41], v[38:41], v[66:69], 0
	ds_read_b128 v[66:69], v123 offset:16384
	ds_read_b128 v[102:105], v123 offset:20480
	ds_read_b128 v[106:109], v123 offset:24576
	ds_read_b128 v[110:113], v123 offset:28672
	global_load_dwordx4 v[114:117], v[118:119], off sc0
	ds_write_b128 v120, v[20:23] offset:32768
	s_waitcnt vmcnt(7) lgkmcnt(8)
	v_mfma_f32_16x16x32_bf16 v[4:7], v[42:45], v[78:81], v[4:7]
	s_waitcnt lgkmcnt(7)
	v_mfma_f32_16x16x32_bf16 v[8:11], v[42:45], v[82:85], v[8:11]
	s_waitcnt lgkmcnt(6)
	v_mfma_f32_16x16x32_bf16 v[12:15], v[42:45], v[86:89], v[12:15]
	s_waitcnt lgkmcnt(5)
	v_mfma_f32_16x16x32_bf16 v[16:19], v[42:45], v[90:93], v[16:19]
	v_bitop3_b32 v20, v37, v3, 8 bitop3:0x36
	v_lshl_add_u32 v124, v20, 4, v121
	ds_read_b128 v[20:23], v124
	ds_read_b128 v[78:81], v124 offset:4096
	ds_read_b128 v[82:85], v124 offset:8192
	ds_read_b128 v[86:89], v124 offset:12288
	global_load_dwordx4 v[90:93], v[118:119], off offset:1024 sc0
	ds_write_b128 v120, v[24:27] offset:40960
	s_waitcnt lgkmcnt(9)
	v_mfma_f32_16x16x32_bf16 v[24:27], v[42:45], v[66:69], v[54:57]
	s_waitcnt lgkmcnt(8)
	v_mfma_f32_16x16x32_bf16 v[54:57], v[42:45], v[102:105], v[58:61]
	s_waitcnt lgkmcnt(7)
	v_mfma_f32_16x16x32_bf16 v[58:61], v[42:45], v[106:109], v[62:65]
	s_waitcnt lgkmcnt(6)
	v_mfma_f32_16x16x32_bf16 v[38:41], v[42:45], v[110:113], v[38:41]
	ds_read_b128 v[42:45], v124 offset:16384
	ds_read_b128 v[62:65], v124 offset:20480
	ds_read_b128 v[66:69], v124 offset:24576
	ds_read_b128 v[102:105], v124 offset:28672
	global_load_dwordx4 v[106:109], v[118:119], off offset:2048 sc0
	ds_write_b128 v120, v[28:31] offset:49152
	s_waitcnt vmcnt(8) lgkmcnt(9)
	v_mfma_f32_16x16x32_bf16 v[4:7], v[46:49], v[20:23], v[4:7]
	s_waitcnt lgkmcnt(8)
	v_mfma_f32_16x16x32_bf16 v[8:11], v[46:49], v[78:81], v[8:11]
	s_waitcnt lgkmcnt(7)
	v_mfma_f32_16x16x32_bf16 v[12:15], v[46:49], v[82:85], v[12:15]
	s_waitcnt lgkmcnt(6)
	v_mfma_f32_16x16x32_bf16 v[16:19], v[46:49], v[86:89], v[16:19]
	v_bitop3_b32 v20, v37, v3, 12 bitop3:0x36
	v_lshl_add_u32 v110, v20, 4, v121
	ds_read_b128 v[20:23], v110
	ds_read_b128 v[28:31], v110 offset:4096
	ds_read_b128 v[78:81], v110 offset:8192
	ds_read_b128 v[82:85], v110 offset:12288
	global_load_dwordx4 v[86:89], v[118:119], off offset:3072 sc0
	ds_write_b128 v120, v[32:35] offset:57344
	s_waitcnt lgkmcnt(9)
	v_mfma_f32_16x16x32_bf16 v[24:27], v[46:49], v[42:45], v[24:27]
	s_waitcnt lgkmcnt(8)
	v_mfma_f32_16x16x32_bf16 v[32:35], v[46:49], v[62:65], v[54:57]
	s_waitcnt lgkmcnt(7)
	v_mfma_f32_16x16x32_bf16 v[42:45], v[46:49], v[66:69], v[58:61]
	s_waitcnt lgkmcnt(6)
	v_mfma_f32_16x16x32_bf16 v[38:41], v[46:49], v[102:105], v[38:41]
	ds_read_b128 v[46:49], v110 offset:16384
	ds_read_b128 v[54:57], v110 offset:20480
	ds_read_b128 v[58:61], v110 offset:24576
	ds_read_b128 v[62:65], v110 offset:28672
	s_waitcnt vmcnt(8) lgkmcnt(8)
	v_mfma_f32_16x16x32_bf16 v[4:7], v[50:53], v[20:23], v[4:7]
	s_waitcnt lgkmcnt(7)
	v_mfma_f32_16x16x32_bf16 v[8:11], v[50:53], v[28:31], v[8:11]
	s_waitcnt lgkmcnt(6)
	v_mfma_f32_16x16x32_bf16 v[12:15], v[50:53], v[78:81], v[12:15]
	s_waitcnt lgkmcnt(5)
	v_mfma_f32_16x16x32_bf16 v[16:19], v[50:53], v[82:85], v[16:19]
	s_waitcnt lgkmcnt(3)
	v_mfma_f32_16x16x32_bf16 v[20:23], v[50:53], v[46:49], v[24:27]
	s_waitcnt lgkmcnt(2)
	v_mfma_f32_16x16x32_bf16 v[24:27], v[50:53], v[54:57], v[32:35]
	s_waitcnt lgkmcnt(1)
	v_mfma_f32_16x16x32_bf16 v[28:31], v[50:53], v[58:61], v[42:45]
	s_waitcnt lgkmcnt(0)
	v_mfma_f32_16x16x32_bf16 v[32:35], v[50:53], v[62:65], v[38:41]
	s_barrier
	s_nop 1
	ds_read_b128 v[38:41], v122 offset:32768
	ds_read_b128 v[42:45], v122 offset:36864
	ds_read_b128 v[46:49], v122 offset:40960
	ds_read_b128 v[50:53], v122 offset:45056
	ds_read_b128 v[54:57], v122 offset:49152
	ds_read_b128 v[58:61], v122 offset:53248
	ds_read_b128 v[62:65], v122 offset:57344
	ds_read_b128 v[66:69], v122 offset:61440
	s_waitcnt vmcnt(3) lgkmcnt(7)
	v_mfma_f32_16x16x32_bf16 v[4:7], v[114:117], v[38:41], v[4:7]
	s_waitcnt lgkmcnt(6)
	v_mfma_f32_16x16x32_bf16 v[8:11], v[114:117], v[42:45], v[8:11]
	s_waitcnt lgkmcnt(5)
	v_mfma_f32_16x16x32_bf16 v[12:15], v[114:117], v[46:49], v[12:15]
	s_waitcnt lgkmcnt(4)
	v_mfma_f32_16x16x32_bf16 v[16:19], v[114:117], v[50:53], v[16:19]
	ds_read_b128 v[38:41], v123 offset:32768
	ds_read_b128 v[42:45], v123 offset:36864
	ds_read_b128 v[46:49], v123 offset:40960
	ds_read_b128 v[50:53], v123 offset:45056
	s_waitcnt lgkmcnt(7)
	v_mfma_f32_16x16x32_bf16 v[20:23], v[114:117], v[54:57], v[20:23]
	s_waitcnt lgkmcnt(6)
	v_mfma_f32_16x16x32_bf16 v[24:27], v[114:117], v[58:61], v[24:27]
	s_waitcnt lgkmcnt(5)
	v_mfma_f32_16x16x32_bf16 v[28:31], v[114:117], v[62:65], v[28:31]
	s_waitcnt lgkmcnt(4)
	v_mfma_f32_16x16x32_bf16 v[32:35], v[114:117], v[66:69], v[32:35]
	ds_read_b128 v[54:57], v123 offset:49152
	ds_read_b128 v[58:61], v123 offset:53248
	ds_read_b128 v[62:65], v123 offset:57344
	ds_read_b128 v[66:69], v123 offset:61440
	ds_write_b128 v120, v[70:73]
	s_waitcnt vmcnt(2) lgkmcnt(8)
	v_mfma_f32_16x16x32_bf16 v[4:7], v[90:93], v[38:41], v[4:7]
	s_waitcnt lgkmcnt(7)
	v_mfma_f32_16x16x32_bf16 v[8:11], v[90:93], v[42:45], v[8:11]
	s_waitcnt lgkmcnt(6)
	v_mfma_f32_16x16x32_bf16 v[12:15], v[90:93], v[46:49], v[12:15]
	s_waitcnt lgkmcnt(5)
	v_mfma_f32_16x16x32_bf16 v[16:19], v[90:93], v[50:53], v[16:19]
	ds_read_b128 v[38:41], v124 offset:32768
	ds_read_b128 v[42:45], v124 offset:36864
	ds_read_b128 v[46:49], v124 offset:40960
	ds_read_b128 v[50:53], v124 offset:45056
	ds_write_b128 v120, v[74:77] offset:8192
	s_waitcnt lgkmcnt(9)
	v_mfma_f32_16x16x32_bf16 v[20:23], v[90:93], v[54:57], v[20:23]
	s_waitcnt lgkmcnt(8)
	v_mfma_f32_16x16x32_bf16 v[24:27], v[90:93], v[58:61], v[24:27]
	s_waitcnt lgkmcnt(7)
	v_mfma_f32_16x16x32_bf16 v[28:31], v[90:93], v[62:65], v[28:31]
	s_waitcnt lgkmcnt(6)
	v_mfma_f32_16x16x32_bf16 v[32:35], v[90:93], v[66:69], v[32:35]
	ds_read_b128 v[54:57], v124 offset:49152
	ds_read_b128 v[58:61], v124 offset:53248
	ds_read_b128 v[62:65], v124 offset:57344
	ds_read_b128 v[66:69], v124 offset:61440
	ds_write_b128 v120, v[94:97] offset:16384
	s_waitcnt vmcnt(1) lgkmcnt(9)
	v_mfma_f32_16x16x32_bf16 v[4:7], v[106:109], v[38:41], v[4:7]
	s_waitcnt lgkmcnt(8)
	v_mfma_f32_16x16x32_bf16 v[8:11], v[106:109], v[42:45], v[8:11]
	s_waitcnt lgkmcnt(7)
	v_mfma_f32_16x16x32_bf16 v[12:15], v[106:109], v[46:49], v[12:15]
	s_waitcnt lgkmcnt(6)
	v_mfma_f32_16x16x32_bf16 v[16:19], v[106:109], v[50:53], v[16:19]
	ds_read_b128 v[38:41], v110 offset:32768
	ds_read_b128 v[42:45], v110 offset:36864
	ds_read_b128 v[46:49], v110 offset:40960
	ds_read_b128 v[50:53], v110 offset:45056
	ds_write_b128 v120, v[98:101] offset:24576
	s_waitcnt lgkmcnt(9)
	v_mfma_f32_16x16x32_bf16 v[20:23], v[106:109], v[54:57], v[20:23]
	s_waitcnt lgkmcnt(8)
	v_mfma_f32_16x16x32_bf16 v[54:57], v[106:109], v[58:61], v[24:27]
	s_waitcnt lgkmcnt(7)
	v_mfma_f32_16x16x32_bf16 v[58:61], v[106:109], v[62:65], v[28:31]
	s_waitcnt lgkmcnt(6)
	v_mfma_f32_16x16x32_bf16 v[62:65], v[106:109], v[66:69], v[32:35]
	ds_read_b128 v[66:69], v110 offset:49152
	ds_read_b128 v[70:73], v110 offset:53248
	ds_read_b128 v[74:77], v110 offset:57344
	ds_read_b128 v[78:81], v110 offset:61440
	s_waitcnt vmcnt(0) lgkmcnt(8)
	v_mfma_f32_16x16x32_bf16 v[32:35], v[86:89], v[38:41], v[4:7]
	s_waitcnt lgkmcnt(7)
	v_mfma_f32_16x16x32_bf16 v[28:31], v[86:89], v[42:45], v[8:11]
	s_waitcnt lgkmcnt(6)
	v_mfma_f32_16x16x32_bf16 v[24:27], v[86:89], v[46:49], v[12:15]
	s_waitcnt lgkmcnt(5)
	v_mfma_f32_16x16x32_bf16 v[16:19], v[86:89], v[50:53], v[16:19]
	s_waitcnt lgkmcnt(3)
	v_mfma_f32_16x16x32_bf16 v[20:23], v[86:89], v[66:69], v[20:23]
	s_waitcnt lgkmcnt(2)
	v_mfma_f32_16x16x32_bf16 v[12:15], v[86:89], v[70:73], v[54:57]
	s_waitcnt lgkmcnt(1)
	v_mfma_f32_16x16x32_bf16 v[8:11], v[86:89], v[74:77], v[58:61]
	s_waitcnt lgkmcnt(0)
	v_mfma_f32_16x16x32_bf16 v[4:7], v[86:89], v[78:81], v[62:65]
	s_cbranch_scc1 .LBB0_783
	s_andn2_b32 s38, s38, 63
	s_add_i32 s12, s38, 0
	v_lshlrev_b32_e32 v3, 9, v3
	v_lshlrev_b32_e32 v37, 4, v37
	s_add_i32 s38, s12, 0x10000
	v_add3_u32 v38, s38, v3, v37
	s_add_i32 s38, s12, 0x12000
	ds_write_b128 v38, v[32:35]
	v_add3_u32 v32, s38, v3, v37
	s_add_i32 s38, s12, 0x14000
	ds_write_b128 v32, v[28:31]
	v_add3_u32 v28, s38, v3, v37
	s_add_i32 s38, s12, 0x16000
	ds_write_b128 v28, v[24:27]
	v_add3_u32 v24, s38, v3, v37
	s_add_i32 s38, s12, 0x18000
	ds_write_b128 v24, v[16:19]
	v_add3_u32 v16, s38, v3, v37
	s_add_i32 s38, s12, 0x1a000
	ds_write_b128 v16, v[20:23]
	v_add3_u32 v16, s38, v3, v37
	s_add_i32 s38, s12, 0x1c000
	s_add_i32 s12, s12, 0x1e000
	ds_write_b128 v16, v[12:15]
	v_add3_u32 v12, s38, v3, v37
	v_add3_u32 v3, s12, v3, v37
	ds_write_b128 v12, v[8:11]
	ds_write_b128 v3, v[4:7]

.LBB0_819:
	s_mul_i32 s0, s53, 0x30000
	s_add_u32 s38, s50, s0
	s_addc_u32 s39, s51, 0
	s_ashr_i32 s41, s12, 6
	s_min_i32 s0, s41, 7
	s_mul_i32 s0, s0, 24
	s_ashr_i32 s1, s0, 31
	s_lshl_b64 s[0:1], s[0:1], 10
	v_and_b32_e32 v3, 63, v58
	s_add_u32 s0, s38, s0
	s_addc_u32 s1, s39, s1
	v_lshlrev_b32_e32 v36, 4, v3
	v_mov_b32_e32 v37, v2
	v_lshl_add_u64 v[176:177], s[0:1], 0, v[36:37]
	v_readlane_b32 s0, v248, 15
	v_readlane_b32 s1, v248, 16
	v_mov_b32_e32 v33, v2
	s_mov_b32 s1, s21
	v_lshl_add_u64 v[32:33], v[32:33], 1, v[34:35]
	s_mov_b32 s12, s0
	v_lshl_add_u64 v[40:41], v[176:177], 0, s[0:1]
	s_movk_i32 s0, 0x3000
	global_load_dwordx4 v[52:55], v[32:33], off
	s_nop 0
	global_load_dwordx4 v[32:35], v[40:41], off sc0
	global_load_dwordx4 v[44:47], v[40:41], off offset:1024 sc0
	global_load_dwordx4 v[60:63], v[40:41], off offset:2048 sc0
	global_load_dwordx4 v[36:39], v[40:41], off offset:3072 sc0
	v_add_co_u32_e32 v40, vcc, s0, v40
	v_lshlrev_b32_e32 v57, 8, v56
	s_nop 0
	v_addc_co_u32_e32 v41, vcc, 0, v41, vcc
	global_load_dwordx4 v[48:51], v[40:41], off sc0
	global_load_dwordx4 v[68:71], v[40:41], off offset:1024 sc0
	global_load_dwordx4 v[64:67], v[40:41], off offset:2048 sc0
	s_nop 0
	global_load_dwordx4 v[40:43], v[40:41], off offset:3072 sc0
	v_xor_b32_e32 v56, v56, v58
	v_lshlrev_b32_e32 v56, 4, v56
	v_and_or_b32 v56, v56, s84, v57
	v_bfe_u32 v3, v58, 4, 2
	v_add_u32_e32 v181, 0, v56
	v_and_b32_e32 v180, 15, v58
	s_waitcnt vmcnt(15)
	ds_write_b128 v181, v[4:7]
	s_waitcnt vmcnt(14)
	ds_write_b128 v181, v[8:11] offset:8192
	s_waitcnt vmcnt(13)
	ds_write_b128 v181, v[12:15] offset:16384
	s_waitcnt vmcnt(12)
	ds_write_b128 v181, v[16:19] offset:24576
	v_bitop3_b32 v4, v3, v58, 15 bitop3:0x78
	v_lshl_add_u32 v134, v180, 8, 0
	v_lshlrev_b32_e32 v4, 4, v4
	v_add_u32_e32 v182, v134, v4
	s_waitcnt lgkmcnt(0)
	s_barrier
	ds_read_b128 v[88:91], v182
	ds_read_b128 v[96:99], v182 offset:4096
	ds_read_b128 v[16:19], v182 offset:8192
	ds_read_b128 v[12:15], v182 offset:12288
	ds_read_b128 v[80:83], v182 offset:16384
	ds_read_b128 v[76:79], v182 offset:20480
	ds_read_b128 v[72:75], v182 offset:24576
	ds_read_b128 v[56:59], v182 offset:28672
	v_readlane_b32 s0, v249, 46
	v_writelane_b32 v248, s12, 15
	s_nop 0
	v_or_b32_e32 v132, s0, v84
	v_ashrrev_i32_e32 v133, 31, v132
	v_writelane_b32 v248, s13, 16
	s_movk_i32 s0, 0xff
	v_cmp_lt_i32_e32 vcc, s0, v132
	s_and_saveexec_b64 s[0:1], vcc
	s_xor_b64 s[0:1], exec, s[0:1]
	s_movk_i32 s18, 0xfe00
	v_lshl_add_u64 v[4:5], v[132:133], 1, v[160:161]
	s_mov_b32 s19, -1
	v_lshl_add_u64 v[4:5], v[4:5], 0, s[18:19]
	s_andn2_saveexec_b64 s[0:1], s[0:1]
	v_lshl_add_u64 v[4:5], v[132:133], 1, v[162:163]
	s_or_b64 exec, exec, s[0:1]
	global_load_dwordx4 v[4:7], v[4:5], off
	s_and_saveexec_b64 s[0:1], vcc
	s_xor_b64 s[0:1], exec, s[0:1]
	s_movk_i32 s18, 0xfe00
	v_lshl_add_u64 v[8:9], v[132:133], 1, v[166:167]
	s_mov_b32 s19, -1
	v_lshl_add_u64 v[8:9], v[8:9], 0, s[18:19]
	s_andn2_saveexec_b64 s[0:1], s[0:1]
	v_lshl_add_u64 v[8:9], v[132:133], 1, v[170:171]
	s_or_b64 exec, exec, s[0:1]
	global_load_dwordx4 v[8:11], v[8:9], off
	s_waitcnt vmcnt(9) lgkmcnt(7)
	v_mfma_f32_16x16x32_bf16 v[84:87], v[32:35], v[88:91], 0
	s_waitcnt vmcnt(5)
	v_mfma_f32_16x16x32_bf16 v[88:91], v[48:51], v[88:91], 0
	s_waitcnt lgkmcnt(6)
	v_mfma_f32_16x16x32_bf16 v[92:95], v[32:35], v[96:99], 0
	v_mfma_f32_16x16x32_bf16 v[96:99], v[48:51], v[96:99], 0
	s_waitcnt lgkmcnt(5)
	v_mfma_f32_16x16x32_bf16 v[100:103], v[32:35], v[16:19], 0
	v_mfma_f32_16x16x32_bf16 v[104:107], v[48:51], v[16:19], 0
	s_waitcnt lgkmcnt(4)
	v_mfma_f32_16x16x32_bf16 v[108:111], v[32:35], v[12:15], 0
	v_mfma_f32_16x16x32_bf16 v[112:115], v[48:51], v[12:15], 0
	v_bitop3_b32 v12, v3, v180, 4 bitop3:0x36
	v_lshlrev_b32_e32 v12, 4, v12
	v_add_u32_e32 v183, v134, v12
	ds_read_b128 v[128:131], v183
	ds_read_b128 v[124:127], v183 offset:4096
	ds_read_b128 v[120:123], v183 offset:8192
	ds_read_b128 v[116:119], v183 offset:12288
	s_and_saveexec_b64 s[0:1], vcc
	s_xor_b64 s[0:1], exec, s[0:1]
	s_movk_i32 s18, 0xfe00
	v_lshl_add_u64 v[12:13], v[132:133], 1, v[164:165]
	s_mov_b32 s19, -1
	v_lshl_add_u64 v[12:13], v[12:13], 0, s[18:19]
	s_andn2_saveexec_b64 s[0:1], s[0:1]
	v_lshl_add_u64 v[12:13], v[132:133], 1, v[168:169]
	s_or_b64 exec, exec, s[0:1]
	global_load_dwordx4 v[12:15], v[12:13], off
	s_and_saveexec_b64 s[0:1], vcc
	s_xor_b64 s[0:1], exec, s[0:1]
	s_movk_i32 s18, 0xfe00
	v_lshl_add_u64 v[16:17], v[132:133], 1, v[172:173]
	s_mov_b32 s19, -1
	v_lshl_add_u64 v[16:17], v[16:17], 0, s[18:19]
	s_andn2_saveexec_b64 s[0:1], s[0:1]
	v_lshl_add_u64 v[16:17], v[132:133], 1, v[174:175]
	s_or_b64 exec, exec, s[0:1]
	global_load_dwordx4 v[16:19], v[16:17], off
	v_readlane_b32 s0, v249, 49
	v_readlane_b32 s1, v249, 50
	s_nop 1
	v_lshl_add_u64 v[198:199], v[176:177], 0, s[0:1]
	s_waitcnt lgkmcnt(7)
	v_mfma_f32_16x16x32_bf16 v[136:139], v[32:35], v[80:83], 0
	v_mfma_f32_16x16x32_bf16 v[80:83], v[48:51], v[80:83], 0
	s_waitcnt lgkmcnt(6)
	v_mfma_f32_16x16x32_bf16 v[140:143], v[32:35], v[76:79], 0
	v_mfma_f32_16x16x32_bf16 v[76:79], v[48:51], v[76:79], 0
	s_waitcnt lgkmcnt(5)
	v_mfma_f32_16x16x32_bf16 v[144:147], v[32:35], v[72:75], 0
	v_mfma_f32_16x16x32_bf16 v[72:75], v[48:51], v[72:75], 0
	s_waitcnt lgkmcnt(4)
	v_mfma_f32_16x16x32_bf16 v[148:151], v[32:35], v[56:59], 0
	v_mfma_f32_16x16x32_bf16 v[152:155], v[48:51], v[56:59], 0
	ds_read_b128 v[156:159], v183 offset:16384
	ds_read_b128 v[186:189], v183 offset:20480
	ds_read_b128 v[190:193], v183 offset:24576
	ds_read_b128 v[194:197], v183 offset:28672
	s_movk_i32 s0, 0x3000
	v_add_co_u32_e32 v214, vcc, s0, v198
	s_nop 1
	v_addc_co_u32_e32 v215, vcc, 0, v199, vcc
	global_load_dwordx4 v[48:51], v[198:199], off sc0
	global_load_dwordx4 v[56:59], v[214:215], off sc0
	ds_write_b128 v181, v[20:23] offset:32768
	s_waitcnt lgkmcnt(8)
	v_mfma_f32_16x16x32_bf16 v[20:23], v[44:47], v[128:131], v[84:87]
	s_waitcnt vmcnt(8)
	v_mfma_f32_16x16x32_bf16 v[84:87], v[68:71], v[128:131], v[88:91]
	s_waitcnt lgkmcnt(7)
	v_mfma_f32_16x16x32_bf16 v[88:91], v[44:47], v[124:127], v[92:95]
	v_mfma_f32_16x16x32_bf16 v[92:95], v[68:71], v[124:127], v[96:99]
	s_waitcnt lgkmcnt(6)
	v_mfma_f32_16x16x32_bf16 v[96:99], v[44:47], v[120:123], v[100:103]
	v_mfma_f32_16x16x32_bf16 v[100:103], v[68:71], v[120:123], v[104:107]
	s_waitcnt lgkmcnt(5)
	v_mfma_f32_16x16x32_bf16 v[104:107], v[44:47], v[116:119], v[108:111]
	v_mfma_f32_16x16x32_bf16 v[108:111], v[68:71], v[116:119], v[112:115]
	v_bitop3_b32 v32, v3, v180, 8 bitop3:0x36
	v_lshlrev_b32_e32 v32, 4, v32
	v_add_u32_e32 v184, v134, v32
	ds_read_b128 v[112:115], v184
	ds_read_b128 v[116:119], v184 offset:4096
	ds_read_b128 v[120:123], v184 offset:8192
	ds_read_b128 v[124:127], v184 offset:12288
	global_load_dwordx4 v[32:35], v[198:199], off offset:1024 sc0
	ds_write_b128 v181, v[24:27] offset:40960
	s_waitcnt lgkmcnt(9)
	v_mfma_f32_16x16x32_bf16 v[128:131], v[44:47], v[156:159], v[136:139]
	v_mfma_f32_16x16x32_bf16 v[80:83], v[68:71], v[156:159], v[80:83]
	s_waitcnt lgkmcnt(8)
	v_mfma_f32_16x16x32_bf16 v[136:139], v[44:47], v[186:189], v[140:143]
	v_mfma_f32_16x16x32_bf16 v[76:79], v[68:71], v[186:189], v[76:79]
	s_waitcnt lgkmcnt(7)
	v_mfma_f32_16x16x32_bf16 v[140:143], v[44:47], v[190:193], v[144:147]
	v_mfma_f32_16x16x32_bf16 v[72:75], v[68:71], v[190:193], v[72:75]
	s_waitcnt lgkmcnt(6)
	v_mfma_f32_16x16x32_bf16 v[144:147], v[44:47], v[194:197], v[148:151]
	v_mfma_f32_16x16x32_bf16 v[68:71], v[68:71], v[194:197], v[152:155]
	s_nop 1
	ds_read_b128 v[148:151], v184 offset:16384
	ds_read_b128 v[152:155], v184 offset:20480
	ds_read_b128 v[156:159], v184 offset:24576
	ds_read_b128 v[186:189], v184 offset:28672
	global_load_dwordx4 v[24:27], v[198:199], off offset:2048 sc0
	global_load_dwordx4 v[44:47], v[214:215], off offset:1024 sc0
	ds_write_b128 v181, v[28:31] offset:49152
	s_waitcnt lgkmcnt(9)
	v_mfma_f32_16x16x32_bf16 v[28:31], v[60:63], v[112:115], v[20:23]
	s_waitcnt vmcnt(10)
	v_mfma_f32_16x16x32_bf16 v[84:87], v[64:67], v[112:115], v[84:87]
	s_waitcnt lgkmcnt(8)
	v_mfma_f32_16x16x32_bf16 v[88:91], v[60:63], v[116:119], v[88:91]
	v_mfma_f32_16x16x32_bf16 v[92:95], v[64:67], v[116:119], v[92:95]
	s_waitcnt lgkmcnt(7)
	v_mfma_f32_16x16x32_bf16 v[96:99], v[60:63], v[120:123], v[96:99]
	v_mfma_f32_16x16x32_bf16 v[100:103], v[64:67], v[120:123], v[100:103]
	s_waitcnt lgkmcnt(6)
	v_mfma_f32_16x16x32_bf16 v[104:107], v[60:63], v[124:127], v[104:107]
	v_mfma_f32_16x16x32_bf16 v[108:111], v[64:67], v[124:127], v[108:111]
	v_bitop3_b32 v20, v3, v180, 12 bitop3:0x36
	v_lshlrev_b32_e32 v20, 4, v20
	v_add_u32_e32 v185, v134, v20
	ds_read_b128 v[112:115], v185
	ds_read_b128 v[124:127], v185 offset:4096
	ds_read_b128 v[132:135], v185 offset:8192
	ds_read_b128 v[190:193], v185 offset:12288
	global_load_dwordx4 v[20:23], v[198:199], off offset:3072 sc0
	ds_write_b128 v181, v[52:55] offset:57344
	s_waitcnt lgkmcnt(9)
	v_mfma_f32_16x16x32_bf16 v[194:197], v[60:63], v[148:151], v[128:131]
	v_mfma_f32_16x16x32_bf16 v[80:83], v[64:67], v[148:151], v[80:83]
	s_waitcnt lgkmcnt(8)
	v_mfma_f32_16x16x32_bf16 v[148:151], v[60:63], v[152:155], v[136:139]
	v_mfma_f32_16x16x32_bf16 v[76:79], v[64:67], v[152:155], v[76:79]
	s_waitcnt lgkmcnt(7)
	v_mfma_f32_16x16x32_bf16 v[152:155], v[60:63], v[156:159], v[140:143]
	v_mfma_f32_16x16x32_bf16 v[156:159], v[64:67], v[156:159], v[72:75]
	s_waitcnt lgkmcnt(6)
	v_mfma_f32_16x16x32_bf16 v[144:147], v[60:63], v[186:189], v[144:147]
	v_mfma_f32_16x16x32_bf16 v[186:189], v[64:67], v[186:189], v[68:71]
	s_nop 2
	ds_read_b128 v[68:71], v185 offset:16384
	ds_read_b128 v[198:201], v185 offset:20480
	ds_read_b128 v[202:205], v185 offset:24576
	ds_read_b128 v[224:227], v185 offset:28672
	global_load_dwordx4 v[52:55], v[214:215], off offset:2048 sc0
	s_waitcnt lgkmcnt(8)
	v_mfma_f32_16x16x32_bf16 v[60:63], v[36:39], v[112:115], v[28:31]
	s_waitcnt vmcnt(11)
	v_mfma_f32_16x16x32_bf16 v[116:119], v[40:43], v[112:115], v[84:87]
	s_waitcnt lgkmcnt(7)
	v_mfma_f32_16x16x32_bf16 v[120:123], v[36:39], v[124:127], v[88:91]
	v_mfma_f32_16x16x32_bf16 v[124:127], v[40:43], v[124:127], v[92:95]
	s_waitcnt lgkmcnt(6)
	v_mfma_f32_16x16x32_bf16 v[128:131], v[36:39], v[132:135], v[96:99]
	v_mfma_f32_16x16x32_bf16 v[132:135], v[40:43], v[132:135], v[100:103]
	s_waitcnt lgkmcnt(5)
	v_mfma_f32_16x16x32_bf16 v[136:139], v[36:39], v[190:193], v[104:107]
	v_mfma_f32_16x16x32_bf16 v[140:143], v[40:43], v[190:193], v[108:111]
	global_load_dwordx4 v[28:31], v[214:215], off offset:3072 sc0
	s_waitcnt lgkmcnt(3)
	v_mfma_f32_16x16x32_bf16 v[64:67], v[36:39], v[68:71], v[194:197]
	v_mfma_f32_16x16x32_bf16 v[68:71], v[40:43], v[68:71], v[80:83]
	s_waitcnt lgkmcnt(2)
	v_mfma_f32_16x16x32_bf16 v[72:75], v[36:39], v[198:201], v[148:151]
	v_mfma_f32_16x16x32_bf16 v[76:79], v[40:43], v[198:201], v[76:79]
	s_waitcnt lgkmcnt(1)
	v_mfma_f32_16x16x32_bf16 v[80:83], v[36:39], v[202:205], v[152:155]
	v_mfma_f32_16x16x32_bf16 v[84:87], v[40:43], v[202:205], v[156:159]
	s_waitcnt lgkmcnt(0)
	v_mfma_f32_16x16x32_bf16 v[88:91], v[36:39], v[224:227], v[144:147]
	v_mfma_f32_16x16x32_bf16 v[92:95], v[40:43], v[224:227], v[186:189]
	s_barrier
	ds_read_b128 v[156:159], v182 offset:32768
	ds_read_b128 v[152:155], v182 offset:36864
	ds_read_b128 v[148:151], v182 offset:40960
	ds_read_b128 v[144:147], v182 offset:45056
	ds_read_b128 v[108:111], v182 offset:49152
	ds_read_b128 v[104:107], v182 offset:53248
	ds_read_b128 v[100:103], v182 offset:57344
	ds_read_b128 v[96:99], v182 offset:61440
	v_readlane_b32 s18, v249, 40
	v_readlane_b32 s19, v249, 41
	s_mov_b64 s[0:1], -1
	s_and_b64 vcc, exec, s[18:19]
	v_lshlrev_b32_e32 v178, 1, v178
	s_cbranch_vccz .LBB0_837
	v_mov_b32_e32 v179, v2
	s_movk_i32 s0, 0xfe00
	v_lshl_add_u64 v[36:37], v[160:161], 0, v[178:179]
	s_mov_b32 s1, -1
	v_lshl_add_u64 v[36:37], v[36:37], 0, s[0:1]
	s_mov_b64 s[0:1], 0

.LBB0_843:
	global_load_dwordx4 v[40:43], v[40:41], off sc0
	s_waitcnt vmcnt(9) lgkmcnt(7)
	v_mfma_f32_16x16x32_bf16 v[112:115], v[48:51], v[156:159], v[60:63]
	s_waitcnt vmcnt(8)
	v_mfma_f32_16x16x32_bf16 v[116:119], v[56:59], v[156:159], v[116:119]
	s_waitcnt lgkmcnt(6)
	v_mfma_f32_16x16x32_bf16 v[120:123], v[48:51], v[152:155], v[120:123]
	v_mfma_f32_16x16x32_bf16 v[124:127], v[56:59], v[152:155], v[124:127]
	s_waitcnt lgkmcnt(5)
	v_mfma_f32_16x16x32_bf16 v[128:131], v[48:51], v[148:151], v[128:131]
	v_mfma_f32_16x16x32_bf16 v[132:135], v[56:59], v[148:151], v[132:135]
	s_waitcnt lgkmcnt(4)
	v_mfma_f32_16x16x32_bf16 v[136:139], v[48:51], v[144:147], v[136:139]
	v_mfma_f32_16x16x32_bf16 v[140:143], v[56:59], v[144:147], v[140:143]
	ds_read_b128 v[156:159], v183 offset:32768
	ds_read_b128 v[152:155], v183 offset:36864
	ds_read_b128 v[148:151], v183 offset:40960
	ds_read_b128 v[144:147], v183 offset:45056
	v_readlane_b32 s18, v249, 40
	v_readlane_b32 s19, v249, 41
	s_andn2_b64 vcc, exec, s[18:19]
	s_mov_b64 s[38:39], -1
	v_cndmask_b32_e64 v60, 0, 1, s[18:19]
	v_cmp_ne_u32_e64 s[0:1], 1, v60
	s_cbranch_vccnz .LBB0_845
	v_mov_b32_e32 v179, v2
	s_movk_i32 s18, 0xfe00
	v_lshl_add_u64 v[60:61], v[164:165], 0, v[178:179]
	s_mov_b32 s19, -1
	v_lshl_add_u64 v[60:61], v[60:61], 0, s[18:19]
	s_cbranch_execnz .LBB0_847
	s_branch .LBB0_846

.LBB0_851:
	global_load_dwordx4 v[160:163], v[160:161], off
	v_readlane_b32 s0, v249, 47
	v_readlane_b32 s1, v249, 48
	s_cmp_gt_i32 s41, 7
	s_nop 0
	v_lshl_add_u64 v[164:165], v[176:177], 0, s[0:1]
	s_waitcnt lgkmcnt(7)
	v_mfma_f32_16x16x32_bf16 v[64:67], v[48:51], v[108:111], v[64:67]
	v_mfma_f32_16x16x32_bf16 v[68:71], v[56:59], v[108:111], v[68:71]
	s_waitcnt lgkmcnt(6)
	v_mfma_f32_16x16x32_bf16 v[72:75], v[48:51], v[104:107], v[72:75]
	v_mfma_f32_16x16x32_bf16 v[76:79], v[56:59], v[104:107], v[76:79]
	s_waitcnt lgkmcnt(5)
	v_mfma_f32_16x16x32_bf16 v[80:83], v[48:51], v[100:103], v[80:83]
	v_mfma_f32_16x16x32_bf16 v[84:87], v[56:59], v[100:103], v[84:87]
	s_waitcnt lgkmcnt(4)
	v_mfma_f32_16x16x32_bf16 v[48:51], v[48:51], v[96:99], v[88:91]
	v_mfma_f32_16x16x32_bf16 v[56:59], v[56:59], v[96:99], v[92:95]
	s_nop 1
	ds_read_b128 v[88:91], v183 offset:49152
	ds_read_b128 v[92:95], v183 offset:53248
	ds_read_b128 v[96:99], v183 offset:57344
	ds_read_b128 v[100:103], v183 offset:61440
	s_movk_i32 s0, 0x3000
	v_add_co_u32_e32 v166, vcc, s0, v164
	s_nop 1
	v_addc_co_u32_e32 v167, vcc, 0, v165, vcc
	global_load_dwordx4 v[104:107], v[164:165], off sc0
	global_load_dwordx4 v[108:111], v[166:167], off sc0
	ds_write_b128 v181, v[4:7]
	s_waitcnt vmcnt(11) lgkmcnt(8)
	v_mfma_f32_16x16x32_bf16 v[4:7], v[32:35], v[156:159], v[112:115]
	s_waitcnt vmcnt(9)
	v_mfma_f32_16x16x32_bf16 v[112:115], v[44:47], v[156:159], v[116:119]
	s_waitcnt lgkmcnt(7)
	v_mfma_f32_16x16x32_bf16 v[116:119], v[32:35], v[152:155], v[120:123]
	v_mfma_f32_16x16x32_bf16 v[120:123], v[44:47], v[152:155], v[124:127]
	s_waitcnt lgkmcnt(6)
	v_mfma_f32_16x16x32_bf16 v[124:127], v[32:35], v[148:151], v[128:131]
	v_mfma_f32_16x16x32_bf16 v[128:131], v[44:47], v[148:151], v[132:135]
	s_waitcnt lgkmcnt(5)
	v_mfma_f32_16x16x32_bf16 v[132:135], v[32:35], v[144:147], v[136:139]
	v_mfma_f32_16x16x32_bf16 v[136:139], v[44:47], v[144:147], v[140:143]
	s_nop 2
	ds_read_b128 v[140:143], v184 offset:32768
	ds_read_b128 v[144:147], v184 offset:36864
	ds_read_b128 v[148:151], v184 offset:40960
	ds_read_b128 v[152:155], v184 offset:45056
	global_load_dwordx4 v[156:159], v[164:165], off offset:1024 sc0
	ds_write_b128 v181, v[8:11] offset:8192
	s_waitcnt lgkmcnt(9)
	v_mfma_f32_16x16x32_bf16 v[8:11], v[32:35], v[88:91], v[64:67]
	v_mfma_f32_16x16x32_bf16 v[64:67], v[44:47], v[88:91], v[68:71]
	s_waitcnt lgkmcnt(8)
	v_mfma_f32_16x16x32_bf16 v[68:71], v[32:35], v[92:95], v[72:75]
	v_mfma_f32_16x16x32_bf16 v[72:75], v[44:47], v[92:95], v[76:79]
	s_waitcnt lgkmcnt(7)
	v_mfma_f32_16x16x32_bf16 v[76:79], v[32:35], v[96:99], v[80:83]
	v_mfma_f32_16x16x32_bf16 v[80:83], v[44:47], v[96:99], v[84:87]
	s_waitcnt lgkmcnt(6)
	v_mfma_f32_16x16x32_bf16 v[32:35], v[32:35], v[100:103], v[48:51]
	v_mfma_f32_16x16x32_bf16 v[44:47], v[44:47], v[100:103], v[56:59]
	s_nop 1
	ds_read_b128 v[48:51], v184 offset:49152
	ds_read_b128 v[56:59], v184 offset:53248
	ds_read_b128 v[84:87], v184 offset:57344
	ds_read_b128 v[88:91], v184 offset:61440
	global_load_dwordx4 v[92:95], v[164:165], off offset:2048 sc0
	global_load_dwordx4 v[96:99], v[166:167], off offset:1024 sc0
	ds_write_b128 v181, v[12:15] offset:16384
	s_waitcnt lgkmcnt(9)
	v_mfma_f32_16x16x32_bf16 v[4:7], v[24:27], v[140:143], v[4:7]
	s_waitcnt vmcnt(10)
	v_mfma_f32_16x16x32_bf16 v[12:15], v[52:55], v[140:143], v[112:115]
	s_waitcnt lgkmcnt(8)
	v_mfma_f32_16x16x32_bf16 v[100:103], v[24:27], v[144:147], v[116:119]
	v_mfma_f32_16x16x32_bf16 v[112:115], v[52:55], v[144:147], v[120:123]
	s_waitcnt lgkmcnt(7)
	v_mfma_f32_16x16x32_bf16 v[116:119], v[24:27], v[148:151], v[124:127]
	v_mfma_f32_16x16x32_bf16 v[120:123], v[52:55], v[148:151], v[128:131]
	s_waitcnt lgkmcnt(6)
	v_mfma_f32_16x16x32_bf16 v[124:127], v[24:27], v[152:155], v[132:135]
	v_mfma_f32_16x16x32_bf16 v[128:131], v[52:55], v[152:155], v[136:139]
	s_nop 1
	ds_read_b128 v[132:135], v185 offset:32768
	ds_read_b128 v[136:139], v185 offset:36864
	ds_read_b128 v[140:143], v185 offset:40960
	ds_read_b128 v[144:147], v185 offset:45056
	global_load_dwordx4 v[148:151], v[164:165], off offset:3072 sc0
	ds_write_b128 v181, v[16:19] offset:24576
	s_waitcnt lgkmcnt(9)
	v_mfma_f32_16x16x32_bf16 v[8:11], v[24:27], v[48:51], v[8:11]
	v_mfma_f32_16x16x32_bf16 v[16:19], v[52:55], v[48:51], v[64:67]
	s_waitcnt lgkmcnt(8)
	v_mfma_f32_16x16x32_bf16 v[48:51], v[24:27], v[56:59], v[68:71]
	v_mfma_f32_16x16x32_bf16 v[56:59], v[52:55], v[56:59], v[72:75]
	s_waitcnt lgkmcnt(7)
	v_mfma_f32_16x16x32_bf16 v[64:67], v[24:27], v[84:87], v[76:79]
	s_waitcnt lgkmcnt(6)
	v_mfma_f32_16x16x32_bf16 v[24:27], v[24:27], v[88:91], v[32:35]
	v_mfma_f32_16x16x32_bf16 v[32:35], v[52:55], v[88:91], v[44:47]
	v_mfma_f32_16x16x32_bf16 v[68:71], v[52:55], v[84:87], v[80:83]
	s_nop 1
	ds_read_b128 v[44:47], v185 offset:49152
	ds_read_b128 v[52:55], v185 offset:53248
	ds_read_b128 v[72:75], v185 offset:57344
	ds_read_b128 v[76:79], v185 offset:61440
	global_load_dwordx4 v[80:83], v[166:167], off offset:2048 sc0
	s_waitcnt lgkmcnt(8)
	v_mfma_f32_16x16x32_bf16 v[4:7], v[20:23], v[132:135], v[4:7]
	s_waitcnt vmcnt(11)
	v_mfma_f32_16x16x32_bf16 v[12:15], v[28:31], v[132:135], v[12:15]
	s_waitcnt lgkmcnt(7)
	v_mfma_f32_16x16x32_bf16 v[84:87], v[20:23], v[136:139], v[100:103]
	v_mfma_f32_16x16x32_bf16 v[88:91], v[28:31], v[136:139], v[112:115]
	s_waitcnt lgkmcnt(6)
	v_mfma_f32_16x16x32_bf16 v[100:103], v[20:23], v[140:143], v[116:119]
	v_mfma_f32_16x16x32_bf16 v[112:115], v[28:31], v[140:143], v[120:123]
	s_waitcnt lgkmcnt(5)
	v_mfma_f32_16x16x32_bf16 v[116:119], v[20:23], v[144:147], v[124:127]
	v_mfma_f32_16x16x32_bf16 v[120:123], v[28:31], v[144:147], v[128:131]
	s_nop 1
	global_load_dwordx4 v[124:127], v[166:167], off offset:3072 sc0
	s_waitcnt lgkmcnt(3)
	v_mfma_f32_16x16x32_bf16 v[8:11], v[20:23], v[44:47], v[8:11]
	v_mfma_f32_16x16x32_bf16 v[16:19], v[28:31], v[44:47], v[16:19]
	s_waitcnt lgkmcnt(2)
	v_mfma_f32_16x16x32_bf16 v[44:47], v[20:23], v[52:55], v[48:51]
	v_mfma_f32_16x16x32_bf16 v[48:51], v[28:31], v[52:55], v[56:59]
	s_waitcnt lgkmcnt(1)
	v_mfma_f32_16x16x32_bf16 v[52:55], v[20:23], v[72:75], v[64:67]
	v_mfma_f32_16x16x32_bf16 v[56:59], v[28:31], v[72:75], v[68:71]
	s_waitcnt lgkmcnt(0)
	v_mfma_f32_16x16x32_bf16 v[20:23], v[20:23], v[76:79], v[24:27]
	v_mfma_f32_16x16x32_bf16 v[24:27], v[28:31], v[76:79], v[32:35]
	s_barrier
	ds_read_b128 v[28:31], v182
	s_nop 0
	ds_read_b128 v[32:35], v182 offset:4096
	ds_read_b128 v[64:67], v182 offset:8192
	ds_read_b128 v[68:71], v182 offset:12288
	ds_read_b128 v[72:75], v182 offset:16384
	ds_read_b128 v[76:79], v182 offset:20480
	ds_read_b128 v[128:131], v182 offset:24576
	ds_read_b128 v[132:135], v182 offset:28672
	s_waitcnt vmcnt(7) lgkmcnt(7)
	v_mfma_f32_16x16x32_bf16 v[4:7], v[104:107], v[28:31], v[4:7]
	s_waitcnt vmcnt(6)
	v_mfma_f32_16x16x32_bf16 v[12:15], v[108:111], v[28:31], v[12:15]
	s_waitcnt lgkmcnt(6)
	v_mfma_f32_16x16x32_bf16 v[28:31], v[104:107], v[32:35], v[84:87]
	v_mfma_f32_16x16x32_bf16 v[32:35], v[108:111], v[32:35], v[88:91]
	s_waitcnt lgkmcnt(5)
	v_mfma_f32_16x16x32_bf16 v[84:87], v[104:107], v[64:67], v[100:103]
	v_mfma_f32_16x16x32_bf16 v[64:67], v[108:111], v[64:67], v[112:115]
	s_waitcnt lgkmcnt(4)
	v_mfma_f32_16x16x32_bf16 v[88:91], v[104:107], v[68:71], v[116:119]
	v_mfma_f32_16x16x32_bf16 v[68:71], v[108:111], v[68:71], v[120:123]
	ds_read_b128 v[100:103], v183
	ds_read_b128 v[112:115], v183 offset:4096
	ds_read_b128 v[116:119], v183 offset:8192
	ds_read_b128 v[120:123], v183 offset:12288
	s_waitcnt lgkmcnt(7)
	v_mfma_f32_16x16x32_bf16 v[8:11], v[104:107], v[72:75], v[8:11]
	v_mfma_f32_16x16x32_bf16 v[16:19], v[108:111], v[72:75], v[16:19]
	s_waitcnt lgkmcnt(6)
	v_mfma_f32_16x16x32_bf16 v[44:47], v[104:107], v[76:79], v[44:47]
	v_mfma_f32_16x16x32_bf16 v[48:51], v[108:111], v[76:79], v[48:51]
	s_waitcnt lgkmcnt(5)
	v_mfma_f32_16x16x32_bf16 v[52:55], v[104:107], v[128:131], v[52:55]
	v_mfma_f32_16x16x32_bf16 v[56:59], v[108:111], v[128:131], v[56:59]
	s_waitcnt lgkmcnt(4)
	v_mfma_f32_16x16x32_bf16 v[20:23], v[104:107], v[132:135], v[20:23]
	v_mfma_f32_16x16x32_bf16 v[24:27], v[108:111], v[132:135], v[24:27]
	ds_read_b128 v[72:75], v183 offset:16384
	ds_read_b128 v[76:79], v183 offset:20480
	ds_read_b128 v[104:107], v183 offset:24576
	ds_read_b128 v[108:111], v183 offset:28672
	ds_write_b128 v181, v[36:39] offset:32768
	s_waitcnt vmcnt(5) lgkmcnt(8)
	v_mfma_f32_16x16x32_bf16 v[4:7], v[156:159], v[100:103], v[4:7]
	s_waitcnt vmcnt(3)
	v_mfma_f32_16x16x32_bf16 v[12:15], v[96:99], v[100:103], v[12:15]
	s_waitcnt lgkmcnt(7)
	v_mfma_f32_16x16x32_bf16 v[28:31], v[156:159], v[112:115], v[28:31]
	v_mfma_f32_16x16x32_bf16 v[32:35], v[96:99], v[112:115], v[32:35]
	s_waitcnt lgkmcnt(6)
	v_mfma_f32_16x16x32_bf16 v[36:39], v[156:159], v[116:119], v[84:87]
	v_mfma_f32_16x16x32_bf16 v[64:67], v[96:99], v[116:119], v[64:67]
	s_waitcnt lgkmcnt(5)
	v_mfma_f32_16x16x32_bf16 v[84:87], v[156:159], v[120:123], v[88:91]
	v_mfma_f32_16x16x32_bf16 v[68:71], v[96:99], v[120:123], v[68:71]
	s_nop 1
	ds_read_b128 v[88:91], v184
	ds_read_b128 v[100:103], v184 offset:4096
	ds_read_b128 v[112:115], v184 offset:8192
	ds_read_b128 v[116:119], v184 offset:12288
	ds_write_b128 v181, v[40:43] offset:40960
	s_waitcnt lgkmcnt(9)
	v_mfma_f32_16x16x32_bf16 v[8:11], v[156:159], v[72:75], v[8:11]
	v_mfma_f32_16x16x32_bf16 v[16:19], v[96:99], v[72:75], v[16:19]
	s_waitcnt lgkmcnt(8)
	v_mfma_f32_16x16x32_bf16 v[40:43], v[156:159], v[76:79], v[44:47]
	v_mfma_f32_16x16x32_bf16 v[44:47], v[96:99], v[76:79], v[48:51]
	s_waitcnt lgkmcnt(7)
	v_mfma_f32_16x16x32_bf16 v[48:51], v[156:159], v[104:107], v[52:55]
	v_mfma_f32_16x16x32_bf16 v[52:55], v[96:99], v[104:107], v[56:59]
	s_waitcnt lgkmcnt(6)
	v_mfma_f32_16x16x32_bf16 v[20:23], v[156:159], v[108:111], v[20:23]
	v_mfma_f32_16x16x32_bf16 v[24:27], v[96:99], v[108:111], v[24:27]
	ds_read_b128 v[56:59], v184 offset:16384
	ds_read_b128 v[72:75], v184 offset:20480
	ds_read_b128 v[76:79], v184 offset:24576
	ds_read_b128 v[96:99], v184 offset:28672
	ds_write_b128 v181, v[60:63] offset:49152
	s_waitcnt lgkmcnt(9)
	v_mfma_f32_16x16x32_bf16 v[4:7], v[92:95], v[88:91], v[4:7]
	s_waitcnt vmcnt(1)
	v_mfma_f32_16x16x32_bf16 v[12:15], v[80:83], v[88:91], v[12:15]
	s_waitcnt lgkmcnt(8)
	v_mfma_f32_16x16x32_bf16 v[28:31], v[92:95], v[100:103], v[28:31]
	v_mfma_f32_16x16x32_bf16 v[32:35], v[80:83], v[100:103], v[32:35]
	s_waitcnt lgkmcnt(7)
	v_mfma_f32_16x16x32_bf16 v[36:39], v[92:95], v[112:115], v[36:39]
	v_mfma_f32_16x16x32_bf16 v[88:91], v[80:83], v[112:115], v[64:67]
	s_waitcnt lgkmcnt(6)
	v_mfma_f32_16x16x32_bf16 v[84:87], v[92:95], v[116:119], v[84:87]
	v_mfma_f32_16x16x32_bf16 v[68:71], v[80:83], v[116:119], v[68:71]
	ds_read_b128 v[60:63], v185
	ds_read_b128 v[100:103], v185 offset:4096
	ds_read_b128 v[104:107], v185 offset:8192
	ds_read_b128 v[108:111], v185 offset:12288
	ds_write_b128 v181, v[160:163] offset:57344
	s_waitcnt lgkmcnt(9)
	v_mfma_f32_16x16x32_bf16 v[8:11], v[92:95], v[56:59], v[8:11]
	v_mfma_f32_16x16x32_bf16 v[16:19], v[80:83], v[56:59], v[16:19]
	s_waitcnt lgkmcnt(8)
	v_mfma_f32_16x16x32_bf16 v[112:115], v[92:95], v[72:75], v[40:43]
	v_mfma_f32_16x16x32_bf16 v[72:75], v[80:83], v[72:75], v[44:47]
	s_waitcnt lgkmcnt(7)
	v_mfma_f32_16x16x32_bf16 v[116:119], v[92:95], v[76:79], v[48:51]
	v_mfma_f32_16x16x32_bf16 v[76:79], v[80:83], v[76:79], v[52:55]
	s_waitcnt lgkmcnt(6)
	v_mfma_f32_16x16x32_bf16 v[92:95], v[92:95], v[96:99], v[20:23]
	v_mfma_f32_16x16x32_bf16 v[80:83], v[80:83], v[96:99], v[24:27]
	s_nop 1
	ds_read_b128 v[20:23], v185 offset:16384
	ds_read_b128 v[96:99], v185 offset:20480
	ds_read_b128 v[120:123], v185 offset:24576
	ds_read_b128 v[128:131], v185 offset:28672
	s_waitcnt lgkmcnt(8)
	v_mfma_f32_16x16x32_bf16 v[64:67], v[148:151], v[60:63], v[4:7]
	s_waitcnt vmcnt(0)
	v_mfma_f32_16x16x32_bf16 v[60:63], v[124:127], v[60:63], v[12:15]
	s_waitcnt lgkmcnt(7)
	v_mfma_f32_16x16x32_bf16 v[56:59], v[148:151], v[100:103], v[28:31]
	v_mfma_f32_16x16x32_bf16 v[52:55], v[124:127], v[100:103], v[32:35]
	s_waitcnt lgkmcnt(6)
	v_mfma_f32_16x16x32_bf16 v[48:51], v[148:151], v[104:107], v[36:39]
	v_mfma_f32_16x16x32_bf16 v[44:47], v[124:127], v[104:107], v[88:91]
	s_waitcnt lgkmcnt(5)
	v_mfma_f32_16x16x32_bf16 v[40:43], v[148:151], v[108:111], v[84:87]
	v_mfma_f32_16x16x32_bf16 v[36:39], v[124:127], v[108:111], v[68:71]
	s_waitcnt lgkmcnt(3)
	v_mfma_f32_16x16x32_bf16 v[32:35], v[148:151], v[20:23], v[8:11]
	v_mfma_f32_16x16x32_bf16 v[28:31], v[124:127], v[20:23], v[16:19]
	s_waitcnt lgkmcnt(2)
	v_mfma_f32_16x16x32_bf16 v[24:27], v[148:151], v[96:99], v[112:115]
	v_mfma_f32_16x16x32_bf16 v[20:23], v[124:127], v[96:99], v[72:75]
	s_waitcnt lgkmcnt(1)
	v_mfma_f32_16x16x32_bf16 v[16:19], v[148:151], v[120:123], v[116:119]
	v_mfma_f32_16x16x32_bf16 v[12:15], v[124:127], v[120:123], v[76:79]
	s_waitcnt lgkmcnt(0)
	v_mfma_f32_16x16x32_bf16 v[8:11], v[148:151], v[128:131], v[92:95]
	v_mfma_f32_16x16x32_bf16 v[4:7], v[124:127], v[128:131], v[80:83]
	s_cbranch_scc1 .LBB0_780
	v_mul_f32_e32 v73, 0x3d372713, v60
	v_mul_f32_e32 v73, v60, v73
	v_fma_f32 v73, v60, v73, v60
	v_mul_f32_e32 v73, 0x3f4c422a, v73
	v_mul_f32_e32 v73, 0xc038aa3b, v73
	v_exp_f32_e32 v73, v73
	v_mul_f32_e32 v72, 0x3d372713, v64
	v_mul_f32_e32 v72, v64, v72
	v_fma_f32 v72, v64, v72, v64
	v_add_f32_e32 v73, 1.0, v73
	v_rcp_f32_e32 v74, v73
	v_mul_f32_e32 v73, 0x3d372713, v65
	v_mul_f32_e32 v73, v65, v73
	v_fma_f32 v73, v65, v73, v65
	v_mul_f32_e32 v72, 0x3f4c422a, v72
	v_mul_f32_e32 v73, 0x3f4c422a, v73
	v_mul_f32_e32 v72, 0xc038aa3b, v72
	v_mul_f32_e32 v73, 0xc038aa3b, v73
	v_exp_f32_e32 v72, v72
	v_exp_f32_e32 v73, v73
	s_lshl_b32 s0, s41, 5
	v_add_f32_e32 v72, 1.0, v72
	v_add_f32_e32 v73, 1.0, v73
	v_rcp_f32_e32 v72, v72
	v_rcp_f32_e32 v73, v73
	v_lshl_add_u32 v68, v3, 3, s0
	s_ashr_i32 s41, s40, 31
	s_lshl_b32 s0, s53, 20
	v_pk_mul_f32 v[64:65], v[64:65], v[72:73]
	v_mul_f32_e32 v72, 0x3d372713, v61
	v_mul_f32_e32 v72, v61, v72
	v_fma_f32 v72, v61, v72, v61
	v_mul_f32_e32 v72, 0x3f4c422a, v72
	v_mul_f32_e32 v72, 0xc038aa3b, v72
	v_mul_f32_e32 v73, 0x3d372713, v62
	v_exp_f32_e32 v72, v72
	v_mul_f32_e32 v73, v62, v73
	v_fma_f32 v73, v62, v73, v62
	v_mul_f32_e32 v73, 0x3f4c422a, v73
	v_mul_f32_e32 v73, 0xc038aa3b, v73
	v_add_f32_e32 v72, 1.0, v72
	v_exp_f32_e32 v73, v73
	v_rcp_f32_e32 v75, v72
	v_mul_f32_e32 v72, 0x3d372713, v66
	v_mul_f32_e32 v72, v66, v72
	v_add_f32_e32 v73, 1.0, v73
	v_pk_mul_f32 v[60:61], v[60:61], v[74:75]
	v_rcp_f32_e32 v74, v73
	v_mul_f32_e32 v73, 0x3d372713, v67
	v_mul_f32_e32 v73, v67, v73
	v_fma_f32 v72, v66, v72, v66
	v_fma_f32 v73, v67, v73, v67
	v_mul_f32_e32 v72, 0x3f4c422a, v72
	v_mul_f32_e32 v73, 0x3f4c422a, v73
	v_mul_f32_e32 v72, 0xc038aa3b, v72
	v_mul_f32_e32 v73, 0xc038aa3b, v73
	v_exp_f32_e32 v72, v72
	v_exp_f32_e32 v73, v73
	v_readlane_b32 s18, v251, 57
	v_ashrrev_i32_e32 v68, 4, v68
	v_add_f32_e32 v72, 1.0, v72
	v_add_f32_e32 v73, 1.0, v73
	v_rcp_f32_e32 v72, v72
	v_rcp_f32_e32 v73, v73
	v_lshlrev_b32_e32 v70, 4, v180
	v_readlane_b32 s19, v251, 58
	s_add_u32 s12, s18, s0
	v_pk_mul_f32 v[66:67], v[66:67], v[72:73]
	v_mul_f32_e32 v72, 0x3d372713, v63
	v_mul_f32_e32 v72, v63, v72
	v_fma_f32 v72, v63, v72, v63
	v_mul_f32_e32 v72, 0x3f4c422a, v72
	v_mul_f32_e32 v72, 0xc038aa3b, v72
	v_exp_f32_e32 v72, v72
	v_ashrrev_i32_e32 v69, 31, v68
	v_ashrrev_i32_e32 v71, 31, v70
	s_addc_u32 s38, s19, 0
	v_add_f32_e32 v72, 1.0, v72
	v_rcp_f32_e32 v75, v72
	s_lshl_b64 s[0:1], s[40:41], 16
	s_add_u32 s0, s12, s0
	s_addc_u32 s1, s38, s1
	v_pk_mul_f32 v[72:73], v[62:63], v[74:75]
	v_lshl_add_u64 v[74:75], v[68:69], 0, v[70:71]
	v_cvt_pk_bf16_f32 v62, v64, v65
	v_cvt_pk_bf16_f32 v64, v60, v61
	v_lshlrev_b64 v[60:61], 5, v[74:75]
	v_lshlrev_b32_e32 v3, 4, v3
	v_cvt_pk_bf16_f32 v63, v66, v67
	v_lshl_add_u64 v[66:67], s[0:1], 0, v[60:61]
	v_and_b32_e32 v60, 16, v3
	v_mul_f32_e32 v3, 0x3d372713, v56
	v_mul_f32_e32 v3, v56, v3
	v_fma_f32 v3, v56, v3, v56
	v_mul_f32_e32 v3, 0x3f4c422a, v3
	v_mul_f32_e32 v3, 0xc038aa3b, v3
	v_exp_f32_e32 v3, v3
	v_mov_b32_e32 v61, v2
	v_cvt_pk_bf16_f32 v65, v72, v73
	v_lshl_add_u64 v[66:67], v[66:67], 0, v[60:61]
	v_add_f32_e32 v3, 1.0, v3
	global_store_dwordx4 v[66:67], v[62:65], off
	s_nop 1
	v_rcp_f32_e32 v64, v3
	v_mul_f32_e32 v3, 0x3d372713, v52
	v_mul_f32_e32 v3, v52, v3
	v_fma_f32 v3, v52, v3, v52
	v_mul_f32_e32 v3, 0x3f4c422a, v3
	v_mul_f32_e32 v3, 0xc038aa3b, v3
	v_exp_f32_e32 v3, v3
	v_add_u32_e32 v62, 0x100, v70
	v_ashrrev_i32_e32 v63, 31, v62
	v_lshl_add_u64 v[62:63], v[68:69], 0, v[62:63]
	v_add_f32_e32 v3, 1.0, v3
	v_rcp_f32_e32 v66, v3
	v_mul_f32_e32 v3, 0x3d372713, v57
	v_mul_f32_e32 v3, v57, v3
	v_fma_f32 v3, v57, v3, v57
	v_mul_f32_e32 v3, 0x3f4c422a, v3
	v_mul_f32_e32 v3, 0xc038aa3b, v3
	v_exp_f32_e32 v3, v3
	s_nop 0
	v_add_f32_e32 v3, 1.0, v3
	v_rcp_f32_e32 v65, v3
	v_mul_f32_e32 v3, 0x3d372713, v53
	v_mul_f32_e32 v3, v53, v3
	v_fma_f32 v3, v53, v3, v53
	v_mul_f32_e32 v3, 0x3f4c422a, v3
	v_mul_f32_e32 v3, 0xc038aa3b, v3
	v_exp_f32_e32 v3, v3
	v_pk_mul_f32 v[56:57], v[56:57], v[64:65]
	v_add_f32_e32 v3, 1.0, v3
	v_rcp_f32_e32 v67, v3
	v_mul_f32_e32 v3, 0x3d372713, v58
	v_mul_f32_e32 v3, v58, v3
	v_fma_f32 v3, v58, v3, v58
	v_mul_f32_e32 v3, 0x3f4c422a, v3
	v_mul_f32_e32 v3, 0xc038aa3b, v3
	v_exp_f32_e32 v3, v3
	v_pk_mul_f32 v[64:65], v[52:53], v[66:67]
	v_add_f32_e32 v3, 1.0, v3
	v_rcp_f32_e32 v52, v3
	v_mul_f32_e32 v3, 0x3d372713, v54
	v_mul_f32_e32 v3, v54, v3
	v_fma_f32 v3, v54, v3, v54
	v_mul_f32_e32 v3, 0x3f4c422a, v3
	v_mul_f32_e32 v3, 0xc038aa3b, v3
	v_exp_f32_e32 v3, v3
	s_nop 0
	v_add_f32_e32 v3, 1.0, v3
	v_rcp_f32_e32 v66, v3
	v_mul_f32_e32 v3, 0x3d372713, v59
	v_mul_f32_e32 v3, v59, v3
	v_fma_f32 v3, v59, v3, v59
	v_mul_f32_e32 v3, 0x3f4c422a, v3
	v_mul_f32_e32 v3, 0xc038aa3b, v3
	v_exp_f32_e32 v3, v3
	s_nop 0
	v_add_f32_e32 v3, 1.0, v3
	v_rcp_f32_e32 v53, v3
	v_mul_f32_e32 v3, 0x3d372713, v55
	v_mul_f32_e32 v3, v55, v3
	v_fma_f32 v3, v55, v3, v55
	v_mul_f32_e32 v3, 0x3f4c422a, v3
	v_mul_f32_e32 v3, 0xc038aa3b, v3
	v_exp_f32_e32 v3, v3
	v_pk_mul_f32 v[58:59], v[58:59], v[52:53]
	v_cvt_pk_bf16_f32 v52, v56, v57
	v_lshlrev_b64 v[56:57], 5, v[62:63]
	v_add_f32_e32 v3, 1.0, v3
	v_rcp_f32_e32 v67, v3
	v_mul_f32_e32 v3, 0x3d372713, v48
	v_mul_f32_e32 v3, v48, v3
	v_fma_f32 v3, v48, v3, v48
	v_mul_f32_e32 v3, 0x3f4c422a, v3
	v_mul_f32_e32 v3, 0xc038aa3b, v3
	v_exp_f32_e32 v3, v3
	v_pk_mul_f32 v[66:67], v[54:55], v[66:67]
	v_lshl_add_u64 v[56:57], s[0:1], 0, v[56:57]
	v_cvt_pk_bf16_f32 v53, v58, v59
	v_cvt_pk_bf16_f32 v54, v64, v65
	v_cvt_pk_bf16_f32 v55, v66, v67
	v_lshl_add_u64 v[56:57], v[56:57], 0, v[60:61]
	v_add_f32_e32 v3, 1.0, v3
	global_store_dwordx4 v[56:57], v[52:55], off
	s_nop 1
	v_rcp_f32_e32 v54, v3
	v_mul_f32_e32 v3, 0x3d372713, v44
	v_mul_f32_e32 v3, v44, v3
	v_fma_f32 v3, v44, v3, v44
	v_mul_f32_e32 v3, 0x3f4c422a, v3
	v_mul_f32_e32 v3, 0xc038aa3b, v3
	v_exp_f32_e32 v3, v3
	v_add_u32_e32 v52, 0x200, v70
	v_ashrrev_i32_e32 v53, 31, v52
	v_lshl_add_u64 v[52:53], v[68:69], 0, v[52:53]
	v_add_f32_e32 v3, 1.0, v3
	v_rcp_f32_e32 v56, v3
	v_mul_f32_e32 v3, 0x3d372713, v49
	v_mul_f32_e32 v3, v49, v3
	v_fma_f32 v3, v49, v3, v49
	v_mul_f32_e32 v3, 0x3f4c422a, v3
	v_mul_f32_e32 v3, 0xc038aa3b, v3
	v_exp_f32_e32 v3, v3
	s_nop 0
	v_add_f32_e32 v3, 1.0, v3
	v_rcp_f32_e32 v55, v3
	v_mul_f32_e32 v3, 0x3d372713, v45
	v_mul_f32_e32 v3, v45, v3
	v_fma_f32 v3, v45, v3, v45
	v_mul_f32_e32 v3, 0x3f4c422a, v3
	v_mul_f32_e32 v3, 0xc038aa3b, v3
	v_exp_f32_e32 v3, v3
	v_pk_mul_f32 v[48:49], v[48:49], v[54:55]
	v_add_f32_e32 v3, 1.0, v3
	v_rcp_f32_e32 v57, v3
	v_mul_f32_e32 v3, 0x3d372713, v50
	v_mul_f32_e32 v3, v50, v3
	v_fma_f32 v3, v50, v3, v50
	v_mul_f32_e32 v3, 0x3f4c422a, v3
	v_mul_f32_e32 v3, 0xc038aa3b, v3
	v_exp_f32_e32 v3, v3
	v_pk_mul_f32 v[54:55], v[44:45], v[56:57]
	v_add_f32_e32 v3, 1.0, v3
	v_rcp_f32_e32 v44, v3
	v_mul_f32_e32 v3, 0x3d372713, v46
	v_mul_f32_e32 v3, v46, v3
	v_fma_f32 v3, v46, v3, v46
	v_mul_f32_e32 v3, 0x3f4c422a, v3
	v_mul_f32_e32 v3, 0xc038aa3b, v3
	v_exp_f32_e32 v3, v3
	s_nop 0
	v_add_f32_e32 v3, 1.0, v3
	v_rcp_f32_e32 v56, v3
	v_mul_f32_e32 v3, 0x3d372713, v51
	v_mul_f32_e32 v3, v51, v3
	v_fma_f32 v3, v51, v3, v51
	v_mul_f32_e32 v3, 0x3f4c422a, v3
	v_mul_f32_e32 v3, 0xc038aa3b, v3
	v_exp_f32_e32 v3, v3
	s_nop 0
	v_add_f32_e32 v3, 1.0, v3
	v_rcp_f32_e32 v45, v3
	v_mul_f32_e32 v3, 0x3d372713, v47
	v_mul_f32_e32 v3, v47, v3
	v_fma_f32 v3, v47, v3, v47
	v_mul_f32_e32 v3, 0x3f4c422a, v3
	v_mul_f32_e32 v3, 0xc038aa3b, v3
	v_exp_f32_e32 v3, v3
	v_pk_mul_f32 v[50:51], v[50:51], v[44:45]
	v_cvt_pk_bf16_f32 v44, v48, v49
	v_lshlrev_b64 v[48:49], 5, v[52:53]
	v_add_f32_e32 v3, 1.0, v3
	v_rcp_f32_e32 v57, v3
	v_mul_f32_e32 v3, 0x3d372713, v40
	v_mul_f32_e32 v3, v40, v3
	v_fma_f32 v3, v40, v3, v40
	v_mul_f32_e32 v3, 0x3f4c422a, v3
	v_mul_f32_e32 v3, 0xc038aa3b, v3
	v_exp_f32_e32 v3, v3
	v_pk_mul_f32 v[56:57], v[46:47], v[56:57]
	v_lshl_add_u64 v[48:49], s[0:1], 0, v[48:49]
	v_cvt_pk_bf16_f32 v45, v50, v51
	v_cvt_pk_bf16_f32 v46, v54, v55
	v_cvt_pk_bf16_f32 v47, v56, v57
	v_lshl_add_u64 v[48:49], v[48:49], 0, v[60:61]
	v_add_f32_e32 v3, 1.0, v3
	global_store_dwordx4 v[48:49], v[44:47], off
	s_nop 1
	v_rcp_f32_e32 v46, v3
	v_mul_f32_e32 v3, 0x3d372713, v36
	v_mul_f32_e32 v3, v36, v3
	v_fma_f32 v3, v36, v3, v36
	v_mul_f32_e32 v3, 0x3f4c422a, v3
	v_mul_f32_e32 v3, 0xc038aa3b, v3
	v_exp_f32_e32 v3, v3
	v_add_u32_e32 v44, 0x300, v70
	v_ashrrev_i32_e32 v45, 31, v44
	v_lshl_add_u64 v[44:45], v[68:69], 0, v[44:45]
	v_add_f32_e32 v3, 1.0, v3
	v_rcp_f32_e32 v48, v3
	v_mul_f32_e32 v3, 0x3d372713, v41
	v_mul_f32_e32 v3, v41, v3
	v_fma_f32 v3, v41, v3, v41
	v_mul_f32_e32 v3, 0x3f4c422a, v3
	v_mul_f32_e32 v3, 0xc038aa3b, v3
	v_exp_f32_e32 v3, v3
	s_nop 0
	v_add_f32_e32 v3, 1.0, v3
	v_rcp_f32_e32 v47, v3
	v_mul_f32_e32 v3, 0x3d372713, v37
	v_mul_f32_e32 v3, v37, v3
	v_fma_f32 v3, v37, v3, v37
	v_mul_f32_e32 v3, 0x3f4c422a, v3
	v_mul_f32_e32 v3, 0xc038aa3b, v3
	v_exp_f32_e32 v3, v3
	v_pk_mul_f32 v[40:41], v[40:41], v[46:47]
	v_add_f32_e32 v3, 1.0, v3
	v_rcp_f32_e32 v49, v3
	v_mul_f32_e32 v3, 0x3d372713, v42
	v_mul_f32_e32 v3, v42, v3
	v_fma_f32 v3, v42, v3, v42
	v_mul_f32_e32 v3, 0x3f4c422a, v3
	v_mul_f32_e32 v3, 0xc038aa3b, v3
	v_exp_f32_e32 v3, v3
	v_pk_mul_f32 v[46:47], v[36:37], v[48:49]
	v_add_f32_e32 v3, 1.0, v3
	v_rcp_f32_e32 v36, v3
	v_mul_f32_e32 v3, 0x3d372713, v38
	v_mul_f32_e32 v3, v38, v3
	v_fma_f32 v3, v38, v3, v38
	v_mul_f32_e32 v3, 0x3f4c422a, v3
	v_mul_f32_e32 v3, 0xc038aa3b, v3
	v_exp_f32_e32 v3, v3
	s_nop 0
	v_add_f32_e32 v3, 1.0, v3
	v_rcp_f32_e32 v48, v3
	v_mul_f32_e32 v3, 0x3d372713, v43
	v_mul_f32_e32 v3, v43, v3
	v_fma_f32 v3, v43, v3, v43
	v_mul_f32_e32 v3, 0x3f4c422a, v3
	v_mul_f32_e32 v3, 0xc038aa3b, v3
	v_exp_f32_e32 v3, v3
	s_nop 0
	v_add_f32_e32 v3, 1.0, v3
	v_rcp_f32_e32 v37, v3
	v_mul_f32_e32 v3, 0x3d372713, v39
	v_mul_f32_e32 v3, v39, v3
	v_fma_f32 v3, v39, v3, v39
	v_mul_f32_e32 v3, 0x3f4c422a, v3
	v_mul_f32_e32 v3, 0xc038aa3b, v3
	v_exp_f32_e32 v3, v3
	v_pk_mul_f32 v[42:43], v[42:43], v[36:37]
	v_cvt_pk_bf16_f32 v36, v40, v41
	v_lshlrev_b64 v[40:41], 5, v[44:45]
	v_add_f32_e32 v3, 1.0, v3
	v_rcp_f32_e32 v49, v3
	v_mul_f32_e32 v3, 0x3d372713, v32
	v_mul_f32_e32 v3, v32, v3
	v_fma_f32 v3, v32, v3, v32
	v_mul_f32_e32 v3, 0x3f4c422a, v3
	v_mul_f32_e32 v3, 0xc038aa3b, v3
	v_exp_f32_e32 v3, v3
	v_pk_mul_f32 v[48:49], v[38:39], v[48:49]
	v_lshl_add_u64 v[40:41], s[0:1], 0, v[40:41]
	v_cvt_pk_bf16_f32 v37, v42, v43
	v_cvt_pk_bf16_f32 v38, v46, v47
	v_cvt_pk_bf16_f32 v39, v48, v49
	v_lshl_add_u64 v[40:41], v[40:41], 0, v[60:61]
	v_add_f32_e32 v3, 1.0, v3
	global_store_dwordx4 v[40:41], v[36:39], off
	s_nop 1
	v_rcp_f32_e32 v38, v3
	v_mul_f32_e32 v3, 0x3d372713, v28
	v_mul_f32_e32 v3, v28, v3
	v_fma_f32 v3, v28, v3, v28
	v_mul_f32_e32 v3, 0x3f4c422a, v3
	v_mul_f32_e32 v3, 0xc038aa3b, v3
	v_exp_f32_e32 v3, v3
	v_add_u32_e32 v36, 0x400, v70
	v_ashrrev_i32_e32 v37, 31, v36
	v_lshl_add_u64 v[36:37], v[68:69], 0, v[36:37]
	v_add_f32_e32 v3, 1.0, v3
	v_rcp_f32_e32 v40, v3
	v_mul_f32_e32 v3, 0x3d372713, v33
	v_mul_f32_e32 v3, v33, v3
	v_fma_f32 v3, v33, v3, v33
	v_mul_f32_e32 v3, 0x3f4c422a, v3
	v_mul_f32_e32 v3, 0xc038aa3b, v3
	v_exp_f32_e32 v3, v3
	s_nop 0
	v_add_f32_e32 v3, 1.0, v3
	v_rcp_f32_e32 v39, v3
	v_mul_f32_e32 v3, 0x3d372713, v29
	v_mul_f32_e32 v3, v29, v3
	v_fma_f32 v3, v29, v3, v29
	v_mul_f32_e32 v3, 0x3f4c422a, v3
	v_mul_f32_e32 v3, 0xc038aa3b, v3
	v_exp_f32_e32 v3, v3
	v_pk_mul_f32 v[32:33], v[32:33], v[38:39]
	v_add_f32_e32 v3, 1.0, v3
	v_rcp_f32_e32 v41, v3
	v_mul_f32_e32 v3, 0x3d372713, v34
	v_mul_f32_e32 v3, v34, v3
	v_fma_f32 v3, v34, v3, v34
	v_mul_f32_e32 v3, 0x3f4c422a, v3
	v_mul_f32_e32 v3, 0xc038aa3b, v3
	v_exp_f32_e32 v3, v3
	v_pk_mul_f32 v[38:39], v[28:29], v[40:41]
	v_add_f32_e32 v3, 1.0, v3
	v_rcp_f32_e32 v28, v3
	v_mul_f32_e32 v3, 0x3d372713, v30
	v_mul_f32_e32 v3, v30, v3
	v_fma_f32 v3, v30, v3, v30
	v_mul_f32_e32 v3, 0x3f4c422a, v3
	v_mul_f32_e32 v3, 0xc038aa3b, v3
	v_exp_f32_e32 v3, v3
	s_nop 0
	v_add_f32_e32 v3, 1.0, v3
	v_rcp_f32_e32 v40, v3
	v_mul_f32_e32 v3, 0x3d372713, v35
	v_mul_f32_e32 v3, v35, v3
	v_fma_f32 v3, v35, v3, v35
	v_mul_f32_e32 v3, 0x3f4c422a, v3
	v_mul_f32_e32 v3, 0xc038aa3b, v3
	v_exp_f32_e32 v3, v3
	s_nop 0
	v_add_f32_e32 v3, 1.0, v3
	v_rcp_f32_e32 v29, v3
	v_mul_f32_e32 v3, 0x3d372713, v31
	v_mul_f32_e32 v3, v31, v3
	v_fma_f32 v3, v31, v3, v31
	v_mul_f32_e32 v3, 0x3f4c422a, v3
	v_mul_f32_e32 v3, 0xc038aa3b, v3
	v_exp_f32_e32 v3, v3
	v_pk_mul_f32 v[34:35], v[34:35], v[28:29]
	v_cvt_pk_bf16_f32 v28, v32, v33
	v_lshlrev_b64 v[32:33], 5, v[36:37]
	v_add_f32_e32 v3, 1.0, v3
	v_rcp_f32_e32 v41, v3
	v_mul_f32_e32 v3, 0x3d372713, v24
	v_mul_f32_e32 v3, v24, v3
	v_fma_f32 v3, v24, v3, v24
	v_mul_f32_e32 v3, 0x3f4c422a, v3
	v_mul_f32_e32 v3, 0xc038aa3b, v3
	v_exp_f32_e32 v3, v3
	v_pk_mul_f32 v[40:41], v[30:31], v[40:41]
	v_lshl_add_u64 v[32:33], s[0:1], 0, v[32:33]
	v_cvt_pk_bf16_f32 v29, v34, v35
	v_cvt_pk_bf16_f32 v30, v38, v39
	v_cvt_pk_bf16_f32 v31, v40, v41
	v_lshl_add_u64 v[32:33], v[32:33], 0, v[60:61]
	v_add_f32_e32 v3, 1.0, v3
	global_store_dwordx4 v[32:33], v[28:31], off
	s_nop 1
	v_rcp_f32_e32 v30, v3
	v_mul_f32_e32 v3, 0x3d372713, v20
	v_mul_f32_e32 v3, v20, v3
	v_fma_f32 v3, v20, v3, v20
	v_mul_f32_e32 v3, 0x3f4c422a, v3
	v_mul_f32_e32 v3, 0xc038aa3b, v3
	v_exp_f32_e32 v3, v3
	v_add_u32_e32 v28, 0x500, v70
	v_ashrrev_i32_e32 v29, 31, v28
	v_lshl_add_u64 v[28:29], v[68:69], 0, v[28:29]
	v_add_f32_e32 v3, 1.0, v3
	v_rcp_f32_e32 v32, v3
	v_mul_f32_e32 v3, 0x3d372713, v25
	v_mul_f32_e32 v3, v25, v3
	v_fma_f32 v3, v25, v3, v25
	v_mul_f32_e32 v3, 0x3f4c422a, v3
	v_mul_f32_e32 v3, 0xc038aa3b, v3
	v_exp_f32_e32 v3, v3
	s_nop 0
	v_add_f32_e32 v3, 1.0, v3
	v_rcp_f32_e32 v31, v3
	v_mul_f32_e32 v3, 0x3d372713, v21
	v_mul_f32_e32 v3, v21, v3
	v_fma_f32 v3, v21, v3, v21
	v_mul_f32_e32 v3, 0x3f4c422a, v3
	v_mul_f32_e32 v3, 0xc038aa3b, v3
	v_exp_f32_e32 v3, v3
	v_pk_mul_f32 v[24:25], v[24:25], v[30:31]
	v_add_f32_e32 v3, 1.0, v3
	v_rcp_f32_e32 v33, v3
	v_mul_f32_e32 v3, 0x3d372713, v26
	v_mul_f32_e32 v3, v26, v3
	v_fma_f32 v3, v26, v3, v26
	v_mul_f32_e32 v3, 0x3f4c422a, v3
	v_mul_f32_e32 v3, 0xc038aa3b, v3
	v_exp_f32_e32 v3, v3
	v_pk_mul_f32 v[30:31], v[20:21], v[32:33]
	v_add_f32_e32 v3, 1.0, v3
	v_rcp_f32_e32 v20, v3
	v_mul_f32_e32 v3, 0x3d372713, v22
	v_mul_f32_e32 v3, v22, v3
	v_fma_f32 v3, v22, v3, v22
	v_mul_f32_e32 v3, 0x3f4c422a, v3
	v_mul_f32_e32 v3, 0xc038aa3b, v3
	v_exp_f32_e32 v3, v3
	s_nop 0
	v_add_f32_e32 v3, 1.0, v3
	v_rcp_f32_e32 v32, v3
	v_mul_f32_e32 v3, 0x3d372713, v27
	v_mul_f32_e32 v3, v27, v3
	v_fma_f32 v3, v27, v3, v27
	v_mul_f32_e32 v3, 0x3f4c422a, v3
	v_mul_f32_e32 v3, 0xc038aa3b, v3
	v_exp_f32_e32 v3, v3
	s_nop 0
	v_add_f32_e32 v3, 1.0, v3
	v_rcp_f32_e32 v21, v3
	v_mul_f32_e32 v3, 0x3d372713, v23
	v_mul_f32_e32 v3, v23, v3
	v_fma_f32 v3, v23, v3, v23
	v_mul_f32_e32 v3, 0x3f4c422a, v3
	v_mul_f32_e32 v3, 0xc038aa3b, v3
	v_exp_f32_e32 v3, v3
	v_pk_mul_f32 v[26:27], v[26:27], v[20:21]
	v_cvt_pk_bf16_f32 v20, v24, v25
	v_lshlrev_b64 v[24:25], 5, v[28:29]
	v_add_f32_e32 v3, 1.0, v3
	v_rcp_f32_e32 v33, v3
	v_mul_f32_e32 v3, 0x3d372713, v16
	v_mul_f32_e32 v3, v16, v3
	v_fma_f32 v3, v16, v3, v16
	v_mul_f32_e32 v3, 0x3f4c422a, v3
	v_mul_f32_e32 v3, 0xc038aa3b, v3
	v_exp_f32_e32 v3, v3
	v_pk_mul_f32 v[32:33], v[22:23], v[32:33]
	v_lshl_add_u64 v[24:25], s[0:1], 0, v[24:25]
	v_cvt_pk_bf16_f32 v21, v26, v27
	v_cvt_pk_bf16_f32 v22, v30, v31
	v_cvt_pk_bf16_f32 v23, v32, v33
	v_lshl_add_u64 v[24:25], v[24:25], 0, v[60:61]
	v_add_f32_e32 v3, 1.0, v3
	global_store_dwordx4 v[24:25], v[20:23], off
	s_nop 1
	v_rcp_f32_e32 v22, v3
	v_mul_f32_e32 v3, 0x3d372713, v12
	v_mul_f32_e32 v3, v12, v3
	v_fma_f32 v3, v12, v3, v12
	v_mul_f32_e32 v3, 0x3f4c422a, v3
	v_mul_f32_e32 v3, 0xc038aa3b, v3
	v_exp_f32_e32 v3, v3
	v_add_u32_e32 v20, 0x600, v70
	v_ashrrev_i32_e32 v21, 31, v20
	v_lshl_add_u64 v[20:21], v[68:69], 0, v[20:21]
	v_add_f32_e32 v3, 1.0, v3
	v_rcp_f32_e32 v24, v3
	v_mul_f32_e32 v3, 0x3d372713, v17
	v_mul_f32_e32 v3, v17, v3
	v_fma_f32 v3, v17, v3, v17
	v_mul_f32_e32 v3, 0x3f4c422a, v3
	v_mul_f32_e32 v3, 0xc038aa3b, v3
	v_exp_f32_e32 v3, v3
	s_nop 0
	v_add_f32_e32 v3, 1.0, v3
	v_rcp_f32_e32 v23, v3
	v_mul_f32_e32 v3, 0x3d372713, v13
	v_mul_f32_e32 v3, v13, v3
	v_fma_f32 v3, v13, v3, v13
	v_mul_f32_e32 v3, 0x3f4c422a, v3
	v_mul_f32_e32 v3, 0xc038aa3b, v3
	v_exp_f32_e32 v3, v3
	v_pk_mul_f32 v[16:17], v[16:17], v[22:23]
	v_add_f32_e32 v3, 1.0, v3
	v_rcp_f32_e32 v25, v3
	v_mul_f32_e32 v3, 0x3d372713, v18
	v_mul_f32_e32 v3, v18, v3
	v_fma_f32 v3, v18, v3, v18
	v_mul_f32_e32 v3, 0x3f4c422a, v3
	v_mul_f32_e32 v3, 0xc038aa3b, v3
	v_exp_f32_e32 v3, v3
	v_pk_mul_f32 v[22:23], v[12:13], v[24:25]
	v_add_f32_e32 v3, 1.0, v3
	v_rcp_f32_e32 v12, v3
	v_mul_f32_e32 v3, 0x3d372713, v14
	v_mul_f32_e32 v3, v14, v3
	v_fma_f32 v3, v14, v3, v14
	v_mul_f32_e32 v3, 0x3f4c422a, v3
	v_mul_f32_e32 v3, 0xc038aa3b, v3
	v_exp_f32_e32 v3, v3
	s_nop 0
	v_add_f32_e32 v3, 1.0, v3
	v_rcp_f32_e32 v24, v3
	v_mul_f32_e32 v3, 0x3d372713, v19
	v_mul_f32_e32 v3, v19, v3
	v_fma_f32 v3, v19, v3, v19
	v_mul_f32_e32 v3, 0x3f4c422a, v3
	v_mul_f32_e32 v3, 0xc038aa3b, v3
	v_exp_f32_e32 v3, v3
	s_nop 0
	v_add_f32_e32 v3, 1.0, v3
	v_rcp_f32_e32 v13, v3
	v_mul_f32_e32 v3, 0x3d372713, v15
	v_mul_f32_e32 v3, v15, v3
	v_fma_f32 v3, v15, v3, v15
	v_mul_f32_e32 v3, 0x3f4c422a, v3
	v_mul_f32_e32 v3, 0xc038aa3b, v3
	v_exp_f32_e32 v3, v3
	v_pk_mul_f32 v[18:19], v[18:19], v[12:13]
	v_cvt_pk_bf16_f32 v12, v16, v17
	v_lshlrev_b64 v[16:17], 5, v[20:21]
	v_add_f32_e32 v3, 1.0, v3
	v_rcp_f32_e32 v25, v3
	v_mul_f32_e32 v3, 0x3d372713, v8
	v_mul_f32_e32 v3, v8, v3
	v_fma_f32 v3, v8, v3, v8
	v_mul_f32_e32 v3, 0x3f4c422a, v3
	v_mul_f32_e32 v3, 0xc038aa3b, v3
	v_exp_f32_e32 v3, v3
	v_pk_mul_f32 v[24:25], v[14:15], v[24:25]
	v_lshl_add_u64 v[16:17], s[0:1], 0, v[16:17]
	v_cvt_pk_bf16_f32 v13, v18, v19
	v_cvt_pk_bf16_f32 v14, v22, v23
	v_cvt_pk_bf16_f32 v15, v24, v25
	v_lshl_add_u64 v[16:17], v[16:17], 0, v[60:61]
	v_add_f32_e32 v3, 1.0, v3
	global_store_dwordx4 v[16:17], v[12:15], off
	s_nop 1
	v_rcp_f32_e32 v14, v3
	v_mul_f32_e32 v3, 0x3d372713, v4
	v_mul_f32_e32 v3, v4, v3
	v_fma_f32 v3, v4, v3, v4
	v_mul_f32_e32 v3, 0x3f4c422a, v3
	v_mul_f32_e32 v3, 0xc038aa3b, v3
	v_exp_f32_e32 v3, v3
	v_add_u32_e32 v12, 0x700, v70
	v_ashrrev_i32_e32 v13, 31, v12
	v_lshl_add_u64 v[12:13], v[68:69], 0, v[12:13]
	v_add_f32_e32 v3, 1.0, v3
	v_rcp_f32_e32 v16, v3
	v_mul_f32_e32 v3, 0x3d372713, v9
	v_mul_f32_e32 v3, v9, v3
	v_fma_f32 v3, v9, v3, v9
	v_mul_f32_e32 v3, 0x3f4c422a, v3
	v_mul_f32_e32 v3, 0xc038aa3b, v3
	v_exp_f32_e32 v3, v3
	s_nop 0
	v_add_f32_e32 v3, 1.0, v3
	v_rcp_f32_e32 v15, v3
	v_mul_f32_e32 v3, 0x3d372713, v5
	v_mul_f32_e32 v3, v5, v3
	v_fma_f32 v3, v5, v3, v5
	v_mul_f32_e32 v3, 0x3f4c422a, v3
	v_mul_f32_e32 v3, 0xc038aa3b, v3
	v_exp_f32_e32 v3, v3
	v_pk_mul_f32 v[8:9], v[8:9], v[14:15]
	v_add_f32_e32 v3, 1.0, v3
	v_rcp_f32_e32 v17, v3
	v_mul_f32_e32 v3, 0x3d372713, v10
	v_mul_f32_e32 v3, v10, v3
	v_fma_f32 v3, v10, v3, v10
	v_mul_f32_e32 v3, 0x3f4c422a, v3
	v_mul_f32_e32 v3, 0xc038aa3b, v3
	v_exp_f32_e32 v3, v3
	v_pk_mul_f32 v[14:15], v[4:5], v[16:17]
	v_add_f32_e32 v3, 1.0, v3
	v_rcp_f32_e32 v4, v3
	v_mul_f32_e32 v3, 0x3d372713, v6
	v_mul_f32_e32 v3, v6, v3
	v_fma_f32 v3, v6, v3, v6
	v_mul_f32_e32 v3, 0x3f4c422a, v3
	v_mul_f32_e32 v3, 0xc038aa3b, v3
	v_exp_f32_e32 v3, v3
	s_nop 0
	v_add_f32_e32 v3, 1.0, v3
	v_rcp_f32_e32 v16, v3
	v_mul_f32_e32 v3, 0x3d372713, v11
	v_mul_f32_e32 v3, v11, v3
	v_fma_f32 v3, v11, v3, v11
	v_mul_f32_e32 v3, 0x3f4c422a, v3
	v_mul_f32_e32 v3, 0xc038aa3b, v3
	v_exp_f32_e32 v3, v3
	s_nop 0
	v_add_f32_e32 v3, 1.0, v3
	v_rcp_f32_e32 v5, v3
	v_mul_f32_e32 v3, 0x3d372713, v7
	v_mul_f32_e32 v3, v7, v3
	v_fma_f32 v3, v7, v3, v7
	v_mul_f32_e32 v3, 0x3f4c422a, v3
	v_mul_f32_e32 v3, 0xc038aa3b, v3
	v_exp_f32_e32 v3, v3
	v_pk_mul_f32 v[10:11], v[10:11], v[4:5]
	v_cvt_pk_bf16_f32 v4, v8, v9
	v_lshlrev_b64 v[8:9], 5, v[12:13]
	v_add_f32_e32 v3, 1.0, v3
	v_rcp_f32_e32 v17, v3
	v_lshl_add_u64 v[8:9], s[0:1], 0, v[8:9]
	v_cvt_pk_bf16_f32 v5, v10, v11
	v_lshl_add_u64 v[8:9], v[8:9], 0, v[60:61]
	v_pk_mul_f32 v[16:17], v[6:7], v[16:17]
	v_cvt_pk_bf16_f32 v6, v14, v15
	v_cvt_pk_bf16_f32 v7, v16, v17
	global_store_dwordx4 v[8:9], v[4:7], off
	s_branch .LBB0_780

.LBB0_1084:
	s_or_b64 exec, exec, s[0:1]
	v_mov_b32_e32 v68, v0
	s_waitcnt lgkmcnt(0)
	s_barrier
	s_lshl_b64 s[0:1], s[58:59], 5
	v_readlane_b32 s34, v251, 57
	v_readlane_b32 s35, v251, 58
	s_waitcnt vmcnt(0)
	v_ashrrev_i32_e32 v4, 4, v68
	v_lshlrev_b32_e32 v3, 19, v68
	s_add_u32 s60, s34, s0
	v_and_b32_e32 v3, 0x700000, v3
	v_readlane_b32 s0, v249, 53
	v_ashrrev_i32_e32 v5, 31, v4
	s_addc_u32 s61, s35, s1
	v_or_b32_e32 v6, s0, v3
	v_lshlrev_b64 v[158:159], 5, v[4:5]
	s_mov_b64 s[0:1], 0x400
	v_lshl_add_u64 v[160:161], v[158:159], 0, s[0:1]
	s_mov_b64 s[0:1], 0x800
	v_lshl_add_u64 v[162:163], v[158:159], 0, s[0:1]
	s_mov_b64 s[0:1], 0xc00
	v_lshl_add_u64 v[164:165], v[158:159], 0, s[0:1]
	v_readfirstlane_b32 s0, v68
	v_lshlrev_b32_e32 v14, 3, v68
	v_mov_b32_e32 v7, v2
	s_ashr_i32 s12, s0, 6
	v_lshl_add_u64 v[6:7], s[60:61], 0, v[6:7]
	v_and_b32_e32 v70, 8, v14
	s_cmp_lt_i32 s12, 8
	v_lshl_add_u64 v[8:9], v[6:7], 0, v[158:159]
	v_lshlrev_b32_e32 v12, 1, v70
	v_mov_b32_e32 v13, v2
	s_cselect_b64 s[62:63], -1, 0
	v_lshl_add_u64 v[8:9], v[8:9], 0, v[12:13]
	v_lshl_add_u64 v[10:11], v[6:7], 0, v[160:161]
	s_and_b64 s[0:1], s[62:63], exec
	v_lshl_add_u64 v[10:11], v[10:11], 0, v[12:13]
	global_load_dwordx4 v[52:55], v[8:9], off
	global_load_dwordx4 v[56:59], v[10:11], off
	v_lshl_add_u64 v[8:9], v[6:7], 0, v[162:163]
	v_lshl_add_u64 v[6:7], v[6:7], 0, v[164:165]
	s_cselect_b32 s0, s12, 7
	v_lshl_add_u64 v[8:9], v[8:9], 0, v[12:13]
	v_lshl_add_u64 v[6:7], v[6:7], 0, v[12:13]
	s_ashr_i32 s1, s0, 31
	global_load_dwordx4 v[60:63], v[8:9], off
	global_load_dwordx4 v[64:67], v[6:7], off
	v_lshlrev_b32_e32 v6, 8, v4
	v_xor_b32_e32 v4, v4, v68
	s_lshl_b64 s[0:1], s[0:1], 15
	v_and_b32_e32 v5, 63, v68
	v_lshlrev_b32_e32 v4, 4, v4
	s_add_u32 s0, s18, s0
	v_and_or_b32 v69, v4, s84, v6
	s_addc_u32 s1, s19, s1
	v_lshlrev_b32_e32 v4, 4, v5
	v_mov_b32_e32 v5, v2
	v_and_b32_e32 v177, 0x78, v14
	v_lshl_add_u64 v[166:167], s[0:1], 0, v[4:5]
	v_readlane_b32 s0, v249, 54
	v_and_b32_e32 v3, 15, v68
	v_bfe_u32 v157, v68, 4, 2
	v_or_b32_sdwa v4, v177, s0 dst_sel:WORD_1 dst_unused:UNUSED_PAD src0_sel:DWORD src1_sel:DWORD
	v_readlane_b32 s0, v248, 25
	v_and_b32_e32 v4, 0x3f00000, v4
	v_lshl_add_u64 v[4:5], s[60:61], 0, v[4:5]
	v_lshl_add_u64 v[6:7], v[4:5], 0, v[158:159]
	v_lshl_add_u64 v[8:9], v[4:5], 0, v[160:161]
	v_lshl_add_u64 v[6:7], v[6:7], 0, v[12:13]
	v_lshl_add_u64 v[8:9], v[8:9], 0, v[12:13]
	v_readlane_b32 s1, v248, 26
	global_load_dwordx4 v[16:19], v[6:7], off
	s_nop 0
	global_load_dwordx4 v[8:11], v[8:9], off
	v_lshl_add_u64 v[6:7], v[4:5], 0, v[162:163]
	v_lshl_add_u64 v[4:5], v[4:5], 0, v[164:165]
	s_mov_b32 s1, s21
	v_lshl_add_u64 v[6:7], v[6:7], 0, v[12:13]
	v_lshl_add_u64 v[4:5], v[4:5], 0, v[12:13]
	v_lshl_add_u64 v[32:33], v[166:167], 0, s[0:1]
	global_load_dwordx4 v[12:15], v[6:7], off
	s_nop 0
	global_load_dwordx4 v[4:7], v[4:5], off
	s_nop 0
	global_load_dwordx4 v[36:39], v[32:33], off sc0
	global_load_dwordx4 v[28:31], v[32:33], off offset:1024 sc0
	global_load_dwordx4 v[24:27], v[32:33], off offset:2048 sc0
	global_load_dwordx4 v[20:23], v[32:33], off offset:3072 sc0
	v_add_co_u32_e32 v32, vcc, s16, v32
	v_add_u32_e32 v178, 0, v69
	s_nop 0
	v_addc_co_u32_e32 v33, vcc, 0, v33, vcc
	global_load_dwordx4 v[48:51], v[32:33], off sc0
	global_load_dwordx4 v[44:47], v[32:33], off offset:1024 sc0
	global_load_dwordx4 v[40:43], v[32:33], off offset:2048 sc0
	s_nop 0
	global_load_dwordx4 v[32:35], v[32:33], off offset:3072 sc0
	s_mov_b32 s20, s0
	s_lshl_b32 s0, s12, 9
	s_add_i32 s83, s0, 0
	s_mov_b32 s88, 1
	s_waitcnt vmcnt(15)
	ds_write_b128 v178, v[52:55]
	s_waitcnt vmcnt(14)
	ds_write_b128 v178, v[56:59] offset:8192
	s_waitcnt vmcnt(13)
	ds_write_b128 v178, v[60:63] offset:16384
	s_waitcnt vmcnt(12)
	ds_write_b128 v178, v[64:67] offset:24576
	v_bitop3_b32 v53, v157, v68, 15 bitop3:0x78
	v_bitop3_b32 v54, v157, v3, 4 bitop3:0x36
	v_bitop3_b32 v55, v157, v3, 8 bitop3:0x36
	v_bitop3_b32 v56, v157, v3, 12 bitop3:0x36
	v_lshl_add_u32 v52, v3, 8, 0
	v_lshlrev_b32_e32 v53, 4, v53
	v_lshlrev_b32_e32 v54, 4, v54
	v_lshlrev_b32_e32 v55, 4, v55
	v_lshlrev_b32_e32 v56, 4, v56
	v_mov_b32_e32 v68, 0
	v_writelane_b32 v248, s20, 25
	s_mov_b32 s89, 0
	s_lshl_b32 s64, s12, 5
	s_or_b32 s65, s58, 16
	s_or_b32 s75, s58, 32
	s_or_b32 s76, s58, 48
	s_or_b32 s77, s58, 64
	s_or_b32 s78, s58, 0x50
	s_or_b32 s79, s58, 0x60
	s_or_b32 s82, s58, 0x70
	s_add_i32 s83, s83, 0x20000
	s_mov_b32 s90, 2
	s_mov_b32 s84, -2
	v_lshlrev_b32_e32 v168, 1, v70
	v_add_u32_e32 v179, v52, v53
	v_add_u32_e32 v180, v52, v54
	v_add_u32_e32 v181, v52, v55
	v_add_u32_e32 v182, v52, v56
	s_mov_b32 s85, 0
	s_mov_b32 s66, 0
	v_mov_b32_e32 v69, v68
	v_mov_b32_e32 v70, v68
	v_mov_b32_e32 v71, v68
	v_mov_b32_e32 v72, v68
	v_mov_b32_e32 v73, v68
	v_mov_b32_e32 v74, v68
	v_mov_b32_e32 v75, v68
	v_mov_b32_e32 v76, v68
	v_mov_b32_e32 v77, v68
	v_mov_b32_e32 v78, v68
	v_mov_b32_e32 v79, v68
	v_mov_b32_e32 v84, v68
	v_mov_b32_e32 v85, v68
	v_mov_b32_e32 v86, v68
	v_mov_b32_e32 v87, v68
	v_mov_b32_e32 v88, v68
	v_mov_b32_e32 v89, v68
	v_mov_b32_e32 v90, v68
	v_mov_b32_e32 v91, v68
	v_mov_b32_e32 v92, v68
	v_mov_b32_e32 v93, v68
	v_mov_b32_e32 v94, v68
	v_mov_b32_e32 v95, v68
	v_mov_b32_e32 v96, v68
	v_mov_b32_e32 v97, v68
	v_mov_b32_e32 v98, v68
	v_mov_b32_e32 v99, v68
	v_mov_b32_e32 v100, v68
	v_mov_b32_e32 v101, v68
	v_mov_b32_e32 v102, v68
	v_mov_b32_e32 v103, v68
	v_mov_b32_e32 v104, v68
	v_mov_b32_e32 v105, v68
	v_mov_b32_e32 v106, v68
	v_mov_b32_e32 v107, v68
	v_mov_b32_e32 v108, v68
	v_mov_b32_e32 v109, v68
	v_mov_b32_e32 v110, v68
	v_mov_b32_e32 v111, v68
	v_mov_b32_e32 v112, v68
	v_mov_b32_e32 v113, v68
	v_mov_b32_e32 v114, v68
	v_mov_b32_e32 v115, v68
	v_mov_b32_e32 v116, v68
	v_mov_b32_e32 v117, v68
	v_mov_b32_e32 v118, v68
	v_mov_b32_e32 v119, v68
	v_mov_b32_e32 v120, v68
	v_mov_b32_e32 v121, v68
	v_mov_b32_e32 v122, v68
	v_mov_b32_e32 v123, v68
	v_mov_b32_e32 v124, v68
	v_mov_b32_e32 v125, v68
	v_mov_b32_e32 v126, v68
	v_mov_b32_e32 v127, v68
	v_mov_b32_e32 v132, v68
	v_mov_b32_e32 v133, v68
	v_mov_b32_e32 v134, v68
	v_mov_b32_e32 v135, v68
	v_mov_b32_e32 v140, v68
	v_mov_b32_e32 v141, v68
	v_mov_b32_e32 v142, v68
	v_mov_b32_e32 v143, v68
	v_writelane_b32 v248, s21, 26
	s_waitcnt lgkmcnt(0)
	s_barrier
	s_branch .LBB0_1088

.LBB0_1088:
	s_add_i32 s0, s90, s95
	s_lshl_b32 s1, s0, 7
	s_add_i32 s12, s1, 0xfffffe00
	s_cmp_gt_i32 s0, 3
	s_cselect_b32 s12, s12, s1
	s_add_i32 s0, s89, s2
	s_cmp_lt_i32 s0, 2
	s_cselect_b32 s20, s0, 0
	s_add_i32 s0, s88, s95
	s_lshl_b32 s1, s0, 2
	s_add_i32 s38, s1, -16
	s_cmp_gt_i32 s0, 3
	s_cselect_b32 s0, s38, s1
	s_mov_b32 s1, s21
	s_lshl_b64 s[38:39], s[20:21], 18
	s_lshl_b64 s[0:1], s[0:1], 10
	v_or_b32_e32 v62, s12, v177
	v_lshl_add_u64 v[60:61], v[166:167], 0, s[38:39]
	v_lshl_add_u64 v[174:175], v[60:61], 0, s[0:1]
	v_ashrrev_i32_e32 v60, 4, v62
	ds_read_b128 v[52:55], v179
	ds_read_b128 v[56:59], v179 offset:4096
	ds_read_b128 v[80:83], v179 offset:8192
	ds_read_b128 v[128:131], v179 offset:12288
	v_ashrrev_i32_e32 v61, 31, v60
	ds_read_b128 v[136:139], v179 offset:16384
	ds_read_b128 v[144:147], v179 offset:20480
	ds_read_b128 v[148:151], v179 offset:24576
	ds_read_b128 v[152:155], v179 offset:28672
	v_lshlrev_b64 v[60:61], 20, v[60:61]
	v_lshl_add_u64 v[60:61], s[60:61], 0, v[60:61]
	v_lshl_add_u64 v[62:63], v[60:61], 0, v[162:163]
	v_mov_b32_e32 v169, v2
	v_lshl_add_u64 v[188:189], v[62:63], 0, v[168:169]
	v_lshl_add_u64 v[62:63], v[60:61], 0, v[164:165]
	v_lshl_add_u64 v[190:191], v[62:63], 0, v[168:169]
	v_lshl_add_u64 v[62:63], v[60:61], 0, v[158:159]
	v_lshl_add_u64 v[60:61], v[60:61], 0, v[160:161]
	v_lshl_add_u64 v[62:63], v[62:63], 0, v[168:169]
	v_lshl_add_u64 v[60:61], v[60:61], 0, v[168:169]
	global_load_dwordx4 v[64:67], v[62:63], off
	s_nop 0
	global_load_dwordx4 v[60:63], v[60:61], off
	s_waitcnt vmcnt(9) lgkmcnt(6)
	v_mfma_f32_16x16x32_bf16 v[124:127], v[36:39], v[56:59], v[124:127]
	s_waitcnt lgkmcnt(5)
	v_mfma_f32_16x16x32_bf16 v[116:119], v[36:39], v[80:83], v[116:119]
	s_waitcnt vmcnt(5)
	v_mfma_f32_16x16x32_bf16 v[80:83], v[48:51], v[80:83], v[112:115]
	s_waitcnt lgkmcnt(4)
	v_mfma_f32_16x16x32_bf16 v[108:111], v[36:39], v[128:131], v[108:111]
	v_mfma_f32_16x16x32_bf16 v[104:107], v[48:51], v[128:131], v[104:107]
	v_mfma_f32_16x16x32_bf16 v[140:143], v[36:39], v[52:55], v[140:143]
	v_mfma_f32_16x16x32_bf16 v[132:135], v[48:51], v[52:55], v[132:135]
	v_mfma_f32_16x16x32_bf16 v[120:123], v[48:51], v[56:59], v[120:123]
	ds_read_b128 v[112:115], v180
	ds_read_b128 v[128:131], v180 offset:4096
	ds_read_b128 v[170:173], v180 offset:8192
	ds_read_b128 v[184:187], v180 offset:12288
	global_load_dwordx4 v[56:59], v[188:189], off
	global_load_dwordx4 v[52:55], v[190:191], off
	s_waitcnt lgkmcnt(7)
	v_mfma_f32_16x16x32_bf16 v[100:103], v[36:39], v[136:139], v[100:103]
	v_mfma_f32_16x16x32_bf16 v[96:99], v[48:51], v[136:139], v[96:99]
	s_waitcnt lgkmcnt(6)
	v_mfma_f32_16x16x32_bf16 v[92:95], v[36:39], v[144:147], v[92:95]
	v_mfma_f32_16x16x32_bf16 v[88:91], v[48:51], v[144:147], v[88:91]
	s_waitcnt lgkmcnt(5)
	v_mfma_f32_16x16x32_bf16 v[84:87], v[36:39], v[148:151], v[84:87]
	v_mfma_f32_16x16x32_bf16 v[136:139], v[48:51], v[148:151], v[76:79]
	s_waitcnt lgkmcnt(4)
	v_mfma_f32_16x16x32_bf16 v[72:75], v[36:39], v[152:155], v[72:75]
	v_mfma_f32_16x16x32_bf16 v[68:71], v[48:51], v[152:155], v[68:71]
	ds_read_b128 v[144:147], v180 offset:16384
	ds_read_b128 v[148:151], v180 offset:20480
	ds_read_b128 v[152:155], v180 offset:24576
	ds_read_b128 v[188:191], v180 offset:28672
	v_add_co_u32_e32 v196, vcc, s16, v174
	s_nop 1
	v_addc_co_u32_e32 v197, vcc, 0, v175, vcc
	global_load_dwordx4 v[36:39], v[174:175], off sc0
	global_load_dwordx4 v[48:51], v[196:197], off sc0
	ds_write_b128 v178, v[16:19] offset:32768
	s_waitcnt lgkmcnt(8)
	v_mfma_f32_16x16x32_bf16 v[16:19], v[28:31], v[112:115], v[140:143]
	s_waitcnt vmcnt(8)
	v_mfma_f32_16x16x32_bf16 v[112:115], v[44:47], v[112:115], v[132:135]
	s_waitcnt lgkmcnt(7)
	v_mfma_f32_16x16x32_bf16 v[124:127], v[28:31], v[128:131], v[124:127]
	s_waitcnt lgkmcnt(6)
	v_mfma_f32_16x16x32_bf16 v[116:119], v[28:31], v[170:173], v[116:119]
	v_mfma_f32_16x16x32_bf16 v[80:83], v[44:47], v[170:173], v[80:83]
	s_waitcnt lgkmcnt(5)
	v_mfma_f32_16x16x32_bf16 v[108:111], v[28:31], v[184:187], v[108:111]
	v_mfma_f32_16x16x32_bf16 v[104:107], v[44:47], v[184:187], v[104:107]
	v_mfma_f32_16x16x32_bf16 v[120:123], v[44:47], v[128:131], v[120:123]
	ds_read_b128 v[128:131], v181
	ds_read_b128 v[132:135], v181 offset:4096
	ds_read_b128 v[140:143], v181 offset:8192
	ds_read_b128 v[170:173], v181 offset:12288
	global_load_dwordx4 v[76:79], v[174:175], off offset:1024 sc0
	ds_write_b128 v178, v[8:11] offset:40960
	s_waitcnt lgkmcnt(9)
	v_mfma_f32_16x16x32_bf16 v[8:11], v[28:31], v[144:147], v[100:103]
	v_mfma_f32_16x16x32_bf16 v[96:99], v[44:47], v[144:147], v[96:99]
	s_waitcnt lgkmcnt(8)
	v_mfma_f32_16x16x32_bf16 v[92:95], v[28:31], v[148:151], v[92:95]
	v_mfma_f32_16x16x32_bf16 v[88:91], v[44:47], v[148:151], v[88:91]
	s_waitcnt lgkmcnt(7)
	v_mfma_f32_16x16x32_bf16 v[84:87], v[28:31], v[152:155], v[84:87]
	v_mfma_f32_16x16x32_bf16 v[100:103], v[44:47], v[152:155], v[136:139]
	s_waitcnt lgkmcnt(6)
	v_mfma_f32_16x16x32_bf16 v[28:31], v[28:31], v[188:191], v[72:75]
	v_mfma_f32_16x16x32_bf16 v[136:139], v[44:47], v[188:191], v[68:71]
	ds_read_b128 v[144:147], v181 offset:16384
	ds_read_b128 v[148:151], v181 offset:20480
	ds_read_b128 v[152:155], v181 offset:24576
	ds_read_b128 v[184:187], v181 offset:28672
	global_load_dwordx4 v[72:75], v[174:175], off offset:2048 sc0
	global_load_dwordx4 v[44:47], v[196:197], off offset:1024 sc0
	ds_write_b128 v178, v[12:15] offset:49152
	s_waitcnt lgkmcnt(9)
	v_mfma_f32_16x16x32_bf16 v[12:15], v[24:27], v[128:131], v[16:19]
	s_waitcnt vmcnt(10)
	v_mfma_f32_16x16x32_bf16 v[16:19], v[40:43], v[128:131], v[112:115]
	s_waitcnt lgkmcnt(8)
	v_mfma_f32_16x16x32_bf16 v[112:115], v[24:27], v[132:135], v[124:127]
	s_waitcnt lgkmcnt(7)
	v_mfma_f32_16x16x32_bf16 v[116:119], v[24:27], v[140:143], v[116:119]
	v_mfma_f32_16x16x32_bf16 v[80:83], v[40:43], v[140:143], v[80:83]
	s_waitcnt lgkmcnt(6)
	v_mfma_f32_16x16x32_bf16 v[108:111], v[24:27], v[170:173], v[108:111]
	v_mfma_f32_16x16x32_bf16 v[104:107], v[40:43], v[170:173], v[104:107]
	v_mfma_f32_16x16x32_bf16 v[120:123], v[40:43], v[132:135], v[120:123]
	ds_read_b128 v[124:127], v182
	ds_read_b128 v[132:135], v182 offset:4096
	ds_read_b128 v[140:143], v182 offset:8192
	ds_read_b128 v[170:173], v182 offset:12288
	global_load_dwordx4 v[68:71], v[174:175], off offset:3072 sc0
	ds_write_b128 v178, v[4:7] offset:57344
	s_waitcnt lgkmcnt(9)
	v_mfma_f32_16x16x32_bf16 v[4:7], v[24:27], v[144:147], v[8:11]
	s_waitcnt lgkmcnt(8)
	v_mfma_f32_16x16x32_bf16 v[92:95], v[24:27], v[148:151], v[92:95]
	v_mfma_f32_16x16x32_bf16 v[88:91], v[40:43], v[148:151], v[88:91]
	s_waitcnt lgkmcnt(7)
	v_mfma_f32_16x16x32_bf16 v[84:87], v[24:27], v[152:155], v[84:87]
	s_waitcnt lgkmcnt(6)
	v_mfma_f32_16x16x32_bf16 v[24:27], v[24:27], v[184:187], v[28:31]
	v_mfma_f32_16x16x32_bf16 v[8:11], v[40:43], v[144:147], v[96:99]
	v_mfma_f32_16x16x32_bf16 v[148:151], v[40:43], v[152:155], v[100:103]
	v_mfma_f32_16x16x32_bf16 v[152:155], v[40:43], v[184:187], v[136:139]
	ds_read_b128 v[28:31], v182 offset:16384
	ds_read_b128 v[184:187], v182 offset:20480
	ds_read_b128 v[188:191], v182 offset:24576
	ds_read_b128 v[192:195], v182 offset:28672
	global_load_dwordx4 v[40:43], v[196:197], off offset:2048 sc0
	s_waitcnt lgkmcnt(8)
	v_mfma_f32_16x16x32_bf16 v[144:147], v[20:23], v[124:127], v[12:15]
	s_waitcnt vmcnt(11)
	v_mfma_f32_16x16x32_bf16 v[136:139], v[32:35], v[124:127], v[16:19]
	s_waitcnt lgkmcnt(7)
	v_mfma_f32_16x16x32_bf16 v[128:131], v[20:23], v[132:135], v[112:115]
	v_mfma_f32_16x16x32_bf16 v[124:127], v[32:35], v[132:135], v[120:123]
	s_waitcnt lgkmcnt(6)
	v_mfma_f32_16x16x32_bf16 v[116:119], v[20:23], v[140:143], v[116:119]
	v_mfma_f32_16x16x32_bf16 v[112:115], v[32:35], v[140:143], v[80:83]
	s_waitcnt lgkmcnt(5)
	v_mfma_f32_16x16x32_bf16 v[108:111], v[20:23], v[170:173], v[108:111]
	v_mfma_f32_16x16x32_bf16 v[104:107], v[32:35], v[170:173], v[104:107]
	global_load_dwordx4 v[80:83], v[196:197], off offset:3072 sc0
	s_waitcnt lgkmcnt(3)
	v_mfma_f32_16x16x32_bf16 v[100:103], v[20:23], v[28:31], v[4:7]
	v_mfma_f32_16x16x32_bf16 v[96:99], v[32:35], v[28:31], v[8:11]
	s_waitcnt lgkmcnt(2)
	v_mfma_f32_16x16x32_bf16 v[92:95], v[20:23], v[184:187], v[92:95]
	v_mfma_f32_16x16x32_bf16 v[88:91], v[32:35], v[184:187], v[88:91]
	s_waitcnt lgkmcnt(1)
	v_mfma_f32_16x16x32_bf16 v[84:87], v[20:23], v[188:191], v[84:87]
	v_mfma_f32_16x16x32_bf16 v[28:31], v[32:35], v[188:191], v[148:151]
	s_waitcnt lgkmcnt(0)
	v_mfma_f32_16x16x32_bf16 v[24:27], v[20:23], v[192:195], v[24:27]
	v_mfma_f32_16x16x32_bf16 v[20:23], v[32:35], v[192:195], v[152:155]
	s_add_i32 s66, s66, 1
	v_cndmask_b32_e64 v4, 0, 1, s[62:63]
	s_cmp_lg_u32 s66, 4
	v_cmp_ne_u32_e64 s[0:1], 1, v4
	s_cbranch_scc1 .LBB0_1094
	s_and_b64 vcc, exec, s[0:1]
	s_cbranch_vccnz .LBB0_1093
	s_add_i32 s12, s85, s2
	s_lshl_b32 s20, s12, 8
	s_add_i32 s38, s20, 0xfffffe00
	s_cmp_gt_i32 s12, 1
	s_cselect_b32 s12, s38, s20
	v_mov_b32_e32 v169, v3
	v_mov_b32_e32 v183, v157
	s_add_i32 s12, s12, s64
	v_readlane_b32 s34, v251, 57
	v_lshl_add_u32 v170, v183, 3, s12
	v_ashrrev_i32_e32 v171, 31, v170
	v_lshl_add_u64 v[8:9], v[170:171], 2, s[52:53]
	global_load_dwordx4 v[4:7], v[8:9], off offset:16
	s_nop 0
	global_load_dwordx4 v[8:11], v[8:9], off
	v_ashrrev_i32_e32 v12, 4, v170
	v_ashrrev_i32_e32 v13, 31, v12
	v_lshlrev_b64 v[12:13], 20, v[12:13]
	v_readlane_b32 s35, v251, 58
	v_add_u32_e32 v172, s58, v169
	v_lshlrev_b32_e32 v14, 4, v183
	v_lshl_add_u64 v[12:13], s[34:35], 0, v[12:13]
	v_and_b32_e32 v14, 16, v14
	v_mov_b32_e32 v15, v2
	v_ashrrev_i32_e32 v173, 31, v172
	v_lshl_add_u64 v[12:13], v[12:13], 0, v[14:15]
	v_lshlrev_b64 v[14:15], 5, v[172:173]
	v_lshl_add_u64 v[14:15], v[12:13], 0, v[14:15]
	global_load_dwordx4 v[152:155], v[14:15], off
	v_add_u32_e32 v14, 16, v172
	v_ashrrev_i32_e32 v15, 31, v14
	v_lshlrev_b64 v[14:15], 5, v[14:15]
	v_lshl_add_u64 v[14:15], v[12:13], 0, v[14:15]
	global_load_dwordx4 v[148:151], v[14:15], off
	v_add_u32_e32 v14, 32, v172
	v_ashrrev_i32_e32 v15, 31, v14
	v_lshlrev_b64 v[14:15], 5, v[14:15]
	v_lshl_add_u64 v[14:15], v[12:13], 0, v[14:15]
	global_load_dwordx4 v[140:143], v[14:15], off
	v_add_u32_e32 v14, 48, v172
	v_ashrrev_i32_e32 v15, 31, v14
	v_lshlrev_b64 v[14:15], 5, v[14:15]
	v_lshl_add_u64 v[14:15], v[12:13], 0, v[14:15]
	global_load_dwordx4 v[132:135], v[14:15], off
	v_add_u32_e32 v14, 64, v172
	v_ashrrev_i32_e32 v15, 31, v14
	v_lshlrev_b64 v[14:15], 5, v[14:15]
	v_lshl_add_u64 v[14:15], v[12:13], 0, v[14:15]
	global_load_dwordx4 v[120:123], v[14:15], off
	v_add_u32_e32 v14, 0x50, v172
	v_ashrrev_i32_e32 v15, 31, v14
	v_lshlrev_b64 v[14:15], 5, v[14:15]
	v_lshl_add_u64 v[14:15], v[12:13], 0, v[14:15]
	global_load_dwordx4 v[32:35], v[14:15], off
	v_add_u32_e32 v14, 0x60, v172
	v_ashrrev_i32_e32 v15, 31, v14
	v_lshlrev_b64 v[14:15], 5, v[14:15]
	v_lshl_add_u64 v[14:15], v[12:13], 0, v[14:15]
	global_load_dwordx4 v[16:19], v[14:15], off
	v_add_u32_e32 v14, 0x70, v172
	v_ashrrev_i32_e32 v15, 31, v14
	v_lshlrev_b64 v[14:15], 5, v[14:15]
	v_lshl_add_u64 v[12:13], v[12:13], 0, v[14:15]
	global_load_dwordx4 v[12:15], v[12:13], off
	v_cmp_eq_u32_e32 vcc, 0, v183
	s_waitcnt vmcnt(9)
	v_add_f32_e32 v136, v136, v4
	s_waitcnt vmcnt(8)
	v_add_f32_e32 v144, v144, v8
	v_add_f32_e32 v145, v145, v9
	v_add_f32_e32 v146, v146, v10
	v_add_f32_e32 v147, v147, v11
	v_mul_f32_e32 v144, 0xbfb8aa3b, v144
	v_mul_f32_e32 v145, 0xbfb8aa3b, v145
	v_add_f32_e32 v137, v137, v5
	v_mul_f32_e32 v146, 0xbfb8aa3b, v146
	v_add_f32_e32 v138, v138, v6
	v_mul_f32_e32 v147, 0xbfb8aa3b, v147
	v_add_f32_e32 v139, v139, v7
	v_exp_f32_e32 v144, v144
	v_mul_f32_e32 v136, 0xbfb8aa3b, v136
	v_exp_f32_e32 v145, v145
	v_mul_f32_e32 v137, 0xbfb8aa3b, v137
	v_exp_f32_e32 v146, v146
	v_mul_f32_e32 v138, 0xbfb8aa3b, v138
	v_exp_f32_e32 v147, v147
	v_mul_f32_e32 v139, 0xbfb8aa3b, v139
	v_exp_f32_e32 v136, v136
	v_exp_f32_e32 v137, v137
	v_exp_f32_e32 v138, v138
	v_exp_f32_e32 v139, v139
	v_add_f32_e32 v144, 1.0, v144
	v_add_f32_e32 v145, 1.0, v145
	v_add_f32_e32 v146, 1.0, v146
	v_add_f32_e32 v147, 1.0, v147
	v_rcp_f32_e32 v144, v144
	v_add_f32_e32 v136, 1.0, v136
	v_rcp_f32_e32 v145, v145
	v_add_f32_e32 v137, 1.0, v137
	v_rcp_f32_e32 v146, v146
	v_add_f32_e32 v138, 1.0, v138
	v_rcp_f32_e32 v147, v147
	v_add_f32_e32 v139, 1.0, v139
	v_add_f32_e32 v128, v128, v8
	v_add_f32_e32 v129, v129, v9
	v_rcp_f32_e32 v136, v136
	v_rcp_f32_e32 v137, v137
	v_rcp_f32_e32 v138, v138
	v_rcp_f32_e32 v139, v139
	v_mul_f32_e32 v128, 0xbfb8aa3b, v128
	v_add_f32_e32 v124, v124, v4
	v_mul_f32_e32 v129, 0xbfb8aa3b, v129
	v_add_f32_e32 v125, v125, v5
	v_add_f32_e32 v130, v130, v10
	v_add_f32_e32 v131, v131, v11
	v_exp_f32_e32 v128, v128
	v_mul_f32_e32 v124, 0xbfb8aa3b, v124
	v_exp_f32_e32 v129, v129
	v_mul_f32_e32 v125, 0xbfb8aa3b, v125
	v_mul_f32_e32 v130, 0xbfb8aa3b, v130
	v_add_f32_e32 v126, v126, v6
	v_mul_f32_e32 v131, 0xbfb8aa3b, v131
	v_add_f32_e32 v127, v127, v7
	s_waitcnt vmcnt(7)
	v_lshlrev_b32_e32 v174, 16, v152
	v_and_b32_e32 v175, 0xffff0000, v152
	v_lshlrev_b32_e32 v152, 16, v153
	v_and_b32_e32 v153, 0xffff0000, v153
	v_exp_f32_e32 v124, v124
	v_exp_f32_e32 v125, v125
	v_exp_f32_e32 v130, v130
	v_mul_f32_e32 v126, 0xbfb8aa3b, v126
	v_exp_f32_e32 v131, v131
	v_mul_f32_e32 v127, 0xbfb8aa3b, v127
	v_pk_mul_f32 v[144:145], v[144:145], v[174:175]
	v_lshlrev_b32_e32 v174, 16, v154
	v_and_b32_e32 v175, 0xffff0000, v154
	v_pk_mul_f32 v[146:147], v[146:147], v[152:153]
	v_lshlrev_b32_e32 v152, 16, v155
	v_and_b32_e32 v153, 0xffff0000, v155
	v_exp_f32_e32 v126, v126
	v_exp_f32_e32 v127, v127
	v_pk_mul_f32 v[136:137], v[136:137], v[174:175]
	v_pk_mul_f32 v[152:153], v[138:139], v[152:153]
	v_pk_mul_f32 v[174:175], v[136:137], v[136:137]
	v_pk_mul_f32 v[138:139], v[152:153], v[152:153]
	v_add_f32_e32 v128, 1.0, v128
	v_add_f32_e32 v129, 1.0, v129
	v_pk_fma_f32 v[174:175], v[144:145], v[144:145], v[174:175]
	v_pk_fma_f32 v[138:139], v[146:147], v[146:147], v[138:139]
	v_cvt_pk_bf16_f32 v144, v144, v145
	v_cvt_pk_bf16_f32 v145, v146, v147
	v_cvt_pk_bf16_f32 v146, v136, v137
	v_lshlrev_b64 v[136:137], 11, v[172:173]
	v_rcp_f32_e32 v128, v128
	v_add_f32_e32 v124, 1.0, v124
	v_rcp_f32_e32 v129, v129
	v_add_f32_e32 v125, 1.0, v125
	v_add_f32_e32 v130, 1.0, v130
	v_add_f32_e32 v131, 1.0, v131
	v_cvt_pk_bf16_f32 v147, v152, v153
	v_lshl_add_u64 v[152:153], s[36:37], 0, v[136:137]
	v_lshlrev_b64 v[136:137], 1, v[170:171]
	v_rcp_f32_e32 v124, v124
	v_rcp_f32_e32 v125, v125
	v_rcp_f32_e32 v130, v130
	v_add_f32_e32 v126, 1.0, v126
	v_rcp_f32_e32 v131, v131
	v_add_f32_e32 v127, 1.0, v127
	v_lshl_add_u64 v[152:153], v[152:153], 0, v[136:137]
	v_rcp_f32_e32 v126, v126
	v_rcp_f32_e32 v127, v127
	global_store_dwordx4 v[152:153], v[144:147], off offset:1024
	v_add_f32_e32 v116, v116, v8
	v_add_f32_e32 v117, v117, v9
	s_waitcnt vmcnt(7)
	v_lshlrev_b32_e32 v146, 16, v148
	v_and_b32_e32 v147, 0xffff0000, v148
	v_pk_mul_f32 v[128:129], v[128:129], v[146:147]
	v_lshlrev_b32_e32 v146, 16, v150
	v_and_b32_e32 v147, 0xffff0000, v150
	v_lshlrev_b32_e32 v148, 16, v149
	v_and_b32_e32 v149, 0xffff0000, v149
	v_mul_f32_e32 v116, 0xbfb8aa3b, v116
	v_add_f32_e32 v112, v112, v4
	v_mul_f32_e32 v117, 0xbfb8aa3b, v117
	v_add_f32_e32 v113, v113, v5
	v_add_f32_e32 v118, v118, v10
	v_add_f32_e32 v119, v119, v11
	v_pk_mul_f32 v[146:147], v[124:125], v[146:147]
	v_pk_mul_f32 v[130:131], v[130:131], v[148:149]
	v_lshlrev_b32_e32 v148, 16, v151
	v_and_b32_e32 v149, 0xffff0000, v151
	v_exp_f32_e32 v116, v116
	v_mul_f32_e32 v112, 0xbfb8aa3b, v112
	v_exp_f32_e32 v117, v117
	v_mul_f32_e32 v113, 0xbfb8aa3b, v113
	v_mul_f32_e32 v118, 0xbfb8aa3b, v118
	v_add_f32_e32 v114, v114, v6
	v_mul_f32_e32 v119, 0xbfb8aa3b, v119
	v_add_f32_e32 v115, v115, v7
	v_pk_mul_f32 v[124:125], v[146:147], v[146:147]
	v_pk_mul_f32 v[148:149], v[126:127], v[148:149]
	v_exp_f32_e32 v112, v112
	v_exp_f32_e32 v113, v113
	v_exp_f32_e32 v118, v118
	v_mul_f32_e32 v114, 0xbfb8aa3b, v114
	v_exp_f32_e32 v119, v119
	v_mul_f32_e32 v115, 0xbfb8aa3b, v115
	v_pk_fma_f32 v[124:125], v[128:129], v[128:129], v[124:125]
	v_pk_mul_f32 v[126:127], v[148:149], v[148:149]
	v_exp_f32_e32 v114, v114
	v_exp_f32_e32 v115, v115
	v_add_u32_e32 v144, s65, v169
	v_pk_fma_f32 v[126:127], v[130:131], v[130:131], v[126:127]
	v_add_f32_e32 v124, v124, v125
	v_add_f32_e32 v124, v126, v124
	v_ashrrev_i32_e32 v145, 31, v144
	v_add_f32_e32 v116, 1.0, v116
	v_add_f32_e32 v117, 1.0, v117
	v_add_f32_e32 v124, v127, v124
	v_cvt_pk_bf16_f32 v127, v130, v131
	v_lshlrev_b64 v[130:131], 11, v[144:145]
	v_rcp_f32_e32 v116, v116
	v_add_f32_e32 v112, 1.0, v112
	v_rcp_f32_e32 v117, v117
	v_add_f32_e32 v113, 1.0, v113
	v_add_f32_e32 v118, 1.0, v118
	v_add_f32_e32 v119, 1.0, v119
	v_lshl_add_u64 v[130:131], s[36:37], 0, v[130:131]
	v_rcp_f32_e32 v112, v112
	v_rcp_f32_e32 v113, v113
	v_rcp_f32_e32 v118, v118
	v_add_f32_e32 v114, 1.0, v114
	v_rcp_f32_e32 v119, v119
	v_add_f32_e32 v115, 1.0, v115
	v_cvt_pk_bf16_f32 v126, v128, v129
	v_cvt_pk_bf16_f32 v128, v146, v147
	v_cvt_pk_bf16_f32 v129, v148, v149
	v_lshl_add_u64 v[130:131], v[130:131], 0, v[136:137]
	v_rcp_f32_e32 v114, v114
	v_rcp_f32_e32 v115, v115
	global_store_dwordx4 v[130:131], v[126:129], off offset:1024
	v_add_f32_e32 v108, v108, v8
	v_add_f32_e32 v109, v109, v9
	s_waitcnt vmcnt(7)
	v_lshlrev_b32_e32 v128, 16, v140
	v_and_b32_e32 v129, 0xffff0000, v140
	v_pk_mul_f32 v[116:117], v[116:117], v[128:129]
	v_lshlrev_b32_e32 v128, 16, v142
	v_and_b32_e32 v129, 0xffff0000, v142
	v_lshlrev_b32_e32 v130, 16, v141
	v_and_b32_e32 v131, 0xffff0000, v141
	v_mul_f32_e32 v108, 0xbfb8aa3b, v108
	v_add_f32_e32 v104, v104, v4
	v_mul_f32_e32 v109, 0xbfb8aa3b, v109
	v_add_f32_e32 v105, v105, v5
	v_add_f32_e32 v110, v110, v10
	v_add_f32_e32 v111, v111, v11
	v_pk_mul_f32 v[128:129], v[112:113], v[128:129]
	v_pk_mul_f32 v[118:119], v[118:119], v[130:131]
	v_lshlrev_b32_e32 v130, 16, v143
	v_and_b32_e32 v131, 0xffff0000, v143
	v_exp_f32_e32 v108, v108
	v_mul_f32_e32 v104, 0xbfb8aa3b, v104
	v_exp_f32_e32 v109, v109
	v_mul_f32_e32 v105, 0xbfb8aa3b, v105
	v_mul_f32_e32 v110, 0xbfb8aa3b, v110
	v_add_f32_e32 v106, v106, v6
	v_mul_f32_e32 v111, 0xbfb8aa3b, v111
	v_add_f32_e32 v107, v107, v7
	v_pk_mul_f32 v[112:113], v[128:129], v[128:129]
	v_pk_mul_f32 v[130:131], v[114:115], v[130:131]
	v_exp_f32_e32 v104, v104
	v_exp_f32_e32 v105, v105
	v_exp_f32_e32 v110, v110
	v_mul_f32_e32 v106, 0xbfb8aa3b, v106
	v_exp_f32_e32 v111, v111
	v_mul_f32_e32 v107, 0xbfb8aa3b, v107
	v_pk_fma_f32 v[112:113], v[116:117], v[116:117], v[112:113]
	v_pk_mul_f32 v[114:115], v[130:131], v[130:131]
	v_exp_f32_e32 v106, v106
	v_exp_f32_e32 v107, v107
	v_add_u32_e32 v126, s75, v169
	v_pk_fma_f32 v[114:115], v[118:119], v[118:119], v[114:115]
	v_add_f32_e32 v112, v112, v113
	v_add_f32_e32 v112, v114, v112
	v_ashrrev_i32_e32 v127, 31, v126
	v_add_f32_e32 v108, 1.0, v108
	v_add_f32_e32 v109, 1.0, v109
	v_add_f32_e32 v112, v115, v112
	v_cvt_pk_bf16_f32 v115, v118, v119
	v_lshlrev_b64 v[118:119], 11, v[126:127]
	v_rcp_f32_e32 v108, v108
	v_add_f32_e32 v104, 1.0, v104
	v_rcp_f32_e32 v109, v109
	v_add_f32_e32 v105, 1.0, v105
	v_add_f32_e32 v110, 1.0, v110
	v_add_f32_e32 v111, 1.0, v111
	v_lshl_add_u64 v[118:119], s[36:37], 0, v[118:119]
	v_rcp_f32_e32 v104, v104
	v_rcp_f32_e32 v105, v105
	v_rcp_f32_e32 v110, v110
	v_add_f32_e32 v106, 1.0, v106
	v_rcp_f32_e32 v111, v111
	v_add_f32_e32 v107, 1.0, v107
	v_cvt_pk_bf16_f32 v114, v116, v117
	v_cvt_pk_bf16_f32 v116, v128, v129
	v_cvt_pk_bf16_f32 v117, v130, v131
	v_lshl_add_u64 v[118:119], v[118:119], 0, v[136:137]
	v_rcp_f32_e32 v106, v106
	v_rcp_f32_e32 v107, v107
	global_store_dwordx4 v[118:119], v[114:117], off offset:1024
	v_add_f32_e32 v100, v100, v8
	v_add_f32_e32 v101, v101, v9
	s_waitcnt vmcnt(7)
	v_lshlrev_b32_e32 v116, 16, v132
	v_and_b32_e32 v117, 0xffff0000, v132
	v_pk_mul_f32 v[108:109], v[108:109], v[116:117]
	v_lshlrev_b32_e32 v116, 16, v134
	v_and_b32_e32 v117, 0xffff0000, v134
	v_lshlrev_b32_e32 v118, 16, v133
	v_and_b32_e32 v119, 0xffff0000, v133
	v_mul_f32_e32 v100, 0xbfb8aa3b, v100
	v_add_f32_e32 v96, v96, v4
	v_mul_f32_e32 v101, 0xbfb8aa3b, v101
	v_add_f32_e32 v97, v97, v5
	v_add_f32_e32 v102, v102, v10
	v_add_f32_e32 v103, v103, v11
	v_pk_mul_f32 v[116:117], v[104:105], v[116:117]
	v_pk_mul_f32 v[110:111], v[110:111], v[118:119]
	v_lshlrev_b32_e32 v118, 16, v135
	v_and_b32_e32 v119, 0xffff0000, v135
	v_exp_f32_e32 v100, v100
	v_mul_f32_e32 v96, 0xbfb8aa3b, v96
	v_exp_f32_e32 v101, v101
	v_mul_f32_e32 v97, 0xbfb8aa3b, v97
	v_mul_f32_e32 v102, 0xbfb8aa3b, v102
	v_add_f32_e32 v98, v98, v6
	v_mul_f32_e32 v103, 0xbfb8aa3b, v103
	v_add_f32_e32 v99, v99, v7
	v_pk_mul_f32 v[104:105], v[116:117], v[116:117]
	v_pk_mul_f32 v[118:119], v[106:107], v[118:119]
	v_exp_f32_e32 v96, v96
	v_exp_f32_e32 v97, v97
	v_exp_f32_e32 v102, v102
	v_mul_f32_e32 v98, 0xbfb8aa3b, v98
	v_exp_f32_e32 v103, v103
	v_mul_f32_e32 v99, 0xbfb8aa3b, v99
	v_pk_fma_f32 v[104:105], v[108:109], v[108:109], v[104:105]
	v_pk_mul_f32 v[106:107], v[118:119], v[118:119]
	v_exp_f32_e32 v98, v98
	v_exp_f32_e32 v99, v99
	v_add_u32_e32 v114, s76, v169
	v_pk_fma_f32 v[106:107], v[110:111], v[110:111], v[106:107]
	v_add_f32_e32 v104, v104, v105
	v_add_f32_e32 v104, v106, v104
	v_ashrrev_i32_e32 v115, 31, v114
	v_add_f32_e32 v100, 1.0, v100
	v_add_f32_e32 v101, 1.0, v101
	v_add_f32_e32 v104, v107, v104
	v_cvt_pk_bf16_f32 v107, v110, v111
	v_lshlrev_b64 v[110:111], 11, v[114:115]
	v_rcp_f32_e32 v100, v100
	v_add_f32_e32 v96, 1.0, v96
	v_rcp_f32_e32 v101, v101
	v_add_f32_e32 v97, 1.0, v97
	v_add_f32_e32 v102, 1.0, v102
	v_add_f32_e32 v103, 1.0, v103
	v_lshl_add_u64 v[110:111], s[36:37], 0, v[110:111]
	v_rcp_f32_e32 v96, v96
	v_rcp_f32_e32 v97, v97
	v_rcp_f32_e32 v102, v102
	v_add_f32_e32 v98, 1.0, v98
	v_rcp_f32_e32 v103, v103
	v_add_f32_e32 v99, 1.0, v99
	v_cvt_pk_bf16_f32 v106, v108, v109
	v_cvt_pk_bf16_f32 v108, v116, v117
	v_cvt_pk_bf16_f32 v109, v118, v119
	v_lshl_add_u64 v[110:111], v[110:111], 0, v[136:137]
	v_rcp_f32_e32 v98, v98
	v_rcp_f32_e32 v99, v99
	global_store_dwordx4 v[110:111], v[106:109], off offset:1024
	s_waitcnt vmcnt(7)
	v_lshlrev_b32_e32 v110, 16, v121
	v_and_b32_e32 v111, 0xffff0000, v121
	v_lshlrev_b32_e32 v108, 16, v120
	v_and_b32_e32 v109, 0xffff0000, v120
	v_pk_mul_f32 v[100:101], v[100:101], v[108:109]
	v_lshlrev_b32_e32 v108, 16, v122
	v_and_b32_e32 v109, 0xffff0000, v122
	v_pk_mul_f32 v[108:109], v[96:97], v[108:109]
	v_pk_mul_f32 v[102:103], v[102:103], v[110:111]
	v_lshlrev_b32_e32 v110, 16, v123
	v_and_b32_e32 v111, 0xffff0000, v123
	v_pk_mul_f32 v[96:97], v[108:109], v[108:109]
	v_pk_mul_f32 v[110:111], v[98:99], v[110:111]
	v_pk_fma_f32 v[96:97], v[100:101], v[100:101], v[96:97]
	v_pk_mul_f32 v[98:99], v[110:111], v[110:111]
	v_add_u32_e32 v106, s77, v169
	v_pk_fma_f32 v[98:99], v[102:103], v[102:103], v[98:99]
	v_add_f32_e32 v96, v96, v97
	v_add_f32_e32 v96, v98, v96
	v_ashrrev_i32_e32 v107, 31, v106
	v_add_f32_e32 v96, v99, v96
	v_cvt_pk_bf16_f32 v99, v102, v103
	v_lshlrev_b64 v[102:103], 11, v[106:107]
	v_lshl_add_u64 v[102:103], s[36:37], 0, v[102:103]
	v_cvt_pk_bf16_f32 v98, v100, v101
	v_cvt_pk_bf16_f32 v100, v108, v109
	v_cvt_pk_bf16_f32 v101, v110, v111
	v_lshl_add_u64 v[102:103], v[102:103], 0, v[136:137]
	global_store_dwordx4 v[102:103], v[98:101], off offset:1024
	v_add_f32_e32 v92, v92, v8
	v_add_f32_e32 v93, v93, v9
	s_waitcnt vmcnt(7)
	v_lshlrev_b32_e32 v100, 16, v32
	v_and_b32_e32 v101, 0xffff0000, v32
	v_add_f32_e32 v32, v89, v5
	v_mul_f32_e32 v32, 0xbfb8aa3b, v32
	v_exp_f32_e32 v32, v32
	v_mul_f32_e32 v92, 0xbfb8aa3b, v92
	v_mul_f32_e32 v93, 0xbfb8aa3b, v93
	v_exp_f32_e32 v92, v92
	v_exp_f32_e32 v93, v93
	v_add_f32_e32 v32, 1.0, v32
	v_rcp_f32_e32 v89, v32
	v_add_f32_e32 v32, v94, v10
	v_mul_f32_e32 v32, 0xbfb8aa3b, v32
	v_exp_f32_e32 v32, v32
	v_add_f32_e32 v92, 1.0, v92
	v_add_f32_e32 v93, 1.0, v93
	v_rcp_f32_e32 v92, v92
	v_rcp_f32_e32 v93, v93
	v_add_f32_e32 v88, v88, v4
	v_add_f32_e32 v32, 1.0, v32
	v_mul_f32_e32 v88, 0xbfb8aa3b, v88
	v_rcp_f32_e32 v94, v32
	v_add_f32_e32 v32, v90, v6
	v_lshlrev_b32_e32 v102, 16, v33
	v_and_b32_e32 v103, 0xffff0000, v33
	v_add_f32_e32 v33, v91, v7
	v_exp_f32_e32 v88, v88
	v_pk_mul_f32 v[92:93], v[92:93], v[100:101]
	v_lshlrev_b32_e32 v100, 16, v34
	v_and_b32_e32 v101, 0xffff0000, v34
	v_mul_f32_e32 v32, 0xbfb8aa3b, v32
	v_add_f32_e32 v34, v95, v11
	v_mul_f32_e32 v33, 0xbfb8aa3b, v33
	v_exp_f32_e32 v32, v32
	v_mul_f32_e32 v34, 0xbfb8aa3b, v34
	v_exp_f32_e32 v33, v33
	v_exp_f32_e32 v34, v34
	v_add_f32_e32 v88, 1.0, v88
	v_rcp_f32_e32 v88, v88
	v_add_f32_e32 v32, 1.0, v32
	v_add_f32_e32 v33, 1.0, v33
	v_rcp_f32_e32 v32, v32
	v_add_f32_e32 v34, 1.0, v34
	v_rcp_f32_e32 v33, v33
	v_rcp_f32_e32 v95, v34
	v_pk_mul_f32 v[100:101], v[88:89], v[100:101]
	v_lshlrev_b32_e32 v34, 16, v35
	v_and_b32_e32 v35, 0xffff0000, v35
	v_pk_mul_f32 v[88:89], v[100:101], v[100:101]
	v_pk_mul_f32 v[34:35], v[32:33], v[34:35]
	v_pk_fma_f32 v[88:89], v[92:93], v[92:93], v[88:89]
	v_pk_mul_f32 v[94:95], v[94:95], v[102:103]
	v_pk_mul_f32 v[32:33], v[34:35], v[34:35]
	v_add_u32_e32 v98, s78, v169
	v_pk_fma_f32 v[32:33], v[94:95], v[94:95], v[32:33]
	v_add_f32_e32 v88, v88, v89
	v_add_f32_e32 v32, v32, v88
	v_ashrrev_i32_e32 v99, 31, v98
	v_add_f32_e32 v32, v33, v32
	v_cvt_pk_bf16_f32 v91, v34, v35
	v_lshlrev_b64 v[34:35], 11, v[98:99]
	v_add_f32_e32 v33, v84, v8
	v_lshl_add_u64 v[34:35], s[36:37], 0, v[34:35]
	v_mul_f32_e32 v33, 0xbfb8aa3b, v33
	v_cvt_pk_bf16_f32 v88, v92, v93
	v_cvt_pk_bf16_f32 v89, v94, v95
	v_cvt_pk_bf16_f32 v90, v100, v101
	v_lshl_add_u64 v[34:35], v[34:35], 0, v[136:137]
	v_exp_f32_e32 v33, v33
	global_store_dwordx4 v[34:35], v[88:91], off offset:1024
	v_add_f32_e32 v28, v28, v4
	v_mul_f32_e32 v28, 0xbfb8aa3b, v28
	s_waitcnt vmcnt(7)
	v_lshlrev_b32_e32 v88, 16, v16
	v_and_b32_e32 v89, 0xffff0000, v16
	v_add_f32_e32 v16, v29, v5
	v_mul_f32_e32 v16, 0xbfb8aa3b, v16
	v_exp_f32_e32 v16, v16
	v_add_f32_e32 v33, 1.0, v33
	v_rcp_f32_e32 v84, v33
	v_add_f32_e32 v33, v85, v9
	v_mul_f32_e32 v33, 0xbfb8aa3b, v33
	v_exp_f32_e32 v33, v33
	v_add_f32_e32 v16, 1.0, v16
	v_rcp_f32_e32 v29, v16
	v_add_f32_e32 v16, v86, v10
	v_mul_f32_e32 v16, 0xbfb8aa3b, v16
	v_exp_f32_e32 v16, v16
	v_add_f32_e32 v33, 1.0, v33
	v_rcp_f32_e32 v85, v33
	v_lshlrev_b32_e32 v90, 16, v17
	v_add_f32_e32 v16, 1.0, v16
	v_rcp_f32_e32 v86, v16
	v_add_f32_e32 v16, v30, v6
	v_and_b32_e32 v91, 0xffff0000, v17
	v_add_f32_e32 v17, v31, v7
	v_exp_f32_e32 v28, v28
	v_pk_mul_f32 v[84:85], v[84:85], v[88:89]
	v_lshlrev_b32_e32 v88, 16, v18
	v_and_b32_e32 v89, 0xffff0000, v18
	v_mul_f32_e32 v16, 0xbfb8aa3b, v16
	v_add_f32_e32 v18, v87, v11
	v_mul_f32_e32 v17, 0xbfb8aa3b, v17
	v_exp_f32_e32 v16, v16
	v_mul_f32_e32 v18, 0xbfb8aa3b, v18
	v_exp_f32_e32 v17, v17
	v_exp_f32_e32 v18, v18
	v_add_f32_e32 v28, 1.0, v28
	v_rcp_f32_e32 v28, v28
	v_add_f32_e32 v16, 1.0, v16
	v_add_f32_e32 v17, 1.0, v17
	v_rcp_f32_e32 v16, v16
	v_add_f32_e32 v18, 1.0, v18
	v_rcp_f32_e32 v17, v17
	v_add_f32_e32 v8, v24, v8
	v_add_f32_e32 v9, v25, v9
	v_rcp_f32_e32 v87, v18
	v_mul_f32_e32 v8, 0xbfb8aa3b, v8
	v_add_f32_e32 v4, v20, v4
	v_mul_f32_e32 v9, 0xbfb8aa3b, v9
	v_add_f32_e32 v5, v21, v5
	v_add_f32_e32 v10, v26, v10
	v_add_f32_e32 v11, v27, v11
	v_exp_f32_e32 v8, v8
	v_mul_f32_e32 v4, 0xbfb8aa3b, v4
	v_exp_f32_e32 v9, v9
	v_mul_f32_e32 v5, 0xbfb8aa3b, v5
	v_mul_f32_e32 v10, 0xbfb8aa3b, v10
	v_add_f32_e32 v6, v22, v6
	v_mul_f32_e32 v11, 0xbfb8aa3b, v11
	v_add_f32_e32 v7, v23, v7
	v_pk_mul_f32 v[28:29], v[28:29], v[88:89]
	v_lshlrev_b32_e32 v18, 16, v19
	v_and_b32_e32 v19, 0xffff0000, v19
	v_exp_f32_e32 v4, v4
	v_exp_f32_e32 v5, v5
	v_exp_f32_e32 v10, v10
	v_mul_f32_e32 v6, 0xbfb8aa3b, v6
	v_exp_f32_e32 v11, v11
	v_mul_f32_e32 v7, 0xbfb8aa3b, v7
	v_pk_mul_f32 v[88:89], v[28:29], v[28:29]
	v_pk_mul_f32 v[30:31], v[16:17], v[18:19]
	v_exp_f32_e32 v6, v6
	v_exp_f32_e32 v7, v7
	v_add_u32_e32 v34, s79, v169
	v_pk_fma_f32 v[88:89], v[84:85], v[84:85], v[88:89]
	v_pk_mul_f32 v[86:87], v[86:87], v[90:91]
	v_pk_mul_f32 v[16:17], v[30:31], v[30:31]
	v_add_f32_e32 v18, v88, v89
	v_pk_fma_f32 v[16:17], v[86:87], v[86:87], v[16:17]
	v_ashrrev_i32_e32 v35, 31, v34
	v_add_f32_e32 v8, 1.0, v8
	v_add_f32_e32 v9, 1.0, v9
	v_add_f32_e32 v16, v16, v18
	v_cvt_pk_bf16_f32 v18, v28, v29
	v_lshlrev_b64 v[28:29], 11, v[34:35]
	v_rcp_f32_e32 v8, v8
	v_add_f32_e32 v4, 1.0, v4
	v_rcp_f32_e32 v9, v9
	v_add_f32_e32 v5, 1.0, v5
	v_add_f32_e32 v10, 1.0, v10
	v_add_f32_e32 v11, 1.0, v11
	v_lshl_add_u64 v[28:29], s[36:37], 0, v[28:29]
	v_rcp_f32_e32 v4, v4
	v_rcp_f32_e32 v5, v5
	v_rcp_f32_e32 v10, v10
	v_add_f32_e32 v6, 1.0, v6
	v_rcp_f32_e32 v11, v11
	v_add_f32_e32 v7, 1.0, v7
	v_add_f32_e32 v33, v17, v16
	v_cvt_pk_bf16_f32 v16, v84, v85
	v_cvt_pk_bf16_f32 v17, v86, v87
	v_cvt_pk_bf16_f32 v19, v30, v31
	v_lshl_add_u64 v[28:29], v[28:29], 0, v[136:137]
	v_rcp_f32_e32 v6, v6
	v_rcp_f32_e32 v7, v7
	global_store_dwordx4 v[28:29], v[16:19], off offset:1024
	v_add_f32_e32 v154, v174, v175
	v_add_f32_e32 v138, v138, v154
	s_waitcnt vmcnt(7)
	v_lshlrev_b32_e32 v18, 16, v12
	v_and_b32_e32 v19, 0xffff0000, v12
	v_pk_mul_f32 v[8:9], v[8:9], v[18:19]
	v_lshlrev_b32_e32 v18, 16, v14
	v_and_b32_e32 v19, 0xffff0000, v14
	v_lshlrev_b32_e32 v12, 16, v13
	v_and_b32_e32 v13, 0xffff0000, v13
	v_pk_mul_f32 v[18:19], v[4:5], v[18:19]
	v_pk_mul_f32 v[10:11], v[10:11], v[12:13]
	v_lshlrev_b32_e32 v12, 16, v15
	v_and_b32_e32 v13, 0xffff0000, v15
	v_pk_mul_f32 v[4:5], v[18:19], v[18:19]
	v_pk_mul_f32 v[12:13], v[6:7], v[12:13]
	v_pk_fma_f32 v[4:5], v[8:9], v[8:9], v[4:5]
	v_pk_mul_f32 v[6:7], v[12:13], v[12:13]
	v_add_u32_e32 v16, s82, v169
	v_pk_fma_f32 v[6:7], v[10:11], v[10:11], v[6:7]
	v_add_f32_e32 v4, v4, v5
	v_add_f32_e32 v4, v6, v4
	v_ashrrev_i32_e32 v17, 31, v16
	v_add_f32_e32 v20, v7, v4
	v_cvt_pk_bf16_f32 v4, v8, v9
	v_lshlrev_b64 v[8:9], 11, v[16:17]
	v_lshl_add_u64 v[8:9], s[36:37], 0, v[8:9]
	v_add_f32_e32 v138, v139, v138
	v_cvt_pk_bf16_f32 v5, v10, v11
	v_cvt_pk_bf16_f32 v6, v18, v19
	v_cvt_pk_bf16_f32 v7, v12, v13
	v_lshl_add_u64 v[8:9], v[8:9], 0, v[136:137]
	global_store_dwordx4 v[8:9], v[4:7], off offset:1024
	v_mov_b32_e32 v8, v112
	v_mov_b32_e32 v10, v104
	v_mov_b32_e32 v4, v138
	s_nop 1
	v_permlane16_swap_b32 v4, v138
	v_mov_b32_e32 v6, v124
	v_add_f32_e32 v4, v4, v138
	v_mov_b32_e32 v5, v4
	s_nop 1
	v_permlane32_swap_b32 v5, v4
	s_nop 1
	v_permlane16_swap_b32 v124, v6
	v_mov_b32_e32 v12, v96
	v_add_f32_e32 v6, v124, v6
	v_mov_b32_e32 v7, v6
	s_nop 1
	v_permlane32_swap_b32 v7, v6
	s_nop 1
	v_permlane16_swap_b32 v8, v112
	v_mov_b32_e32 v14, v32
	v_add_f32_e32 v8, v8, v112
	v_mov_b32_e32 v9, v8
	s_nop 1
	v_permlane32_swap_b32 v8, v9
	s_nop 1
	v_permlane16_swap_b32 v104, v10
	v_mov_b32_e32 v16, v33
	v_add_f32_e32 v10, v104, v10
	v_mov_b32_e32 v11, v10
	s_nop 1
	v_permlane32_swap_b32 v11, v10
	s_nop 1
	v_permlane16_swap_b32 v96, v12
	v_mov_b32_e32 v18, v20
	v_add_f32_e32 v12, v96, v12
	v_mov_b32_e32 v13, v12
	s_nop 1
	v_permlane32_swap_b32 v12, v13
	s_nop 1
	v_permlane16_swap_b32 v14, v32
	s_nop 0
	v_add_f32_e32 v14, v14, v32
	v_mov_b32_e32 v15, v14
	s_nop 1
	v_permlane32_swap_b32 v15, v14
	s_nop 1
	v_permlane16_swap_b32 v33, v16
	s_nop 0
	v_add_f32_e32 v16, v33, v16
	v_mov_b32_e32 v17, v16
	s_nop 1
	v_permlane32_swap_b32 v17, v16
	s_nop 1
	v_permlane16_swap_b32 v18, v20
	s_nop 0
	v_add_f32_e32 v18, v18, v20
	v_mov_b32_e32 v19, v18
	s_nop 1
	v_permlane32_swap_b32 v18, v19
	s_and_saveexec_b64 s[38:39], vcc
	s_cbranch_execz .LBB0_1092
	v_add_f32_e32 v6, v7, v6
	v_add_f32_e32 v7, v5, v4
	v_lshl_add_u32 v4, v169, 2, s83
	v_add_f32_e32 v8, v8, v9
	v_add_u32_e32 v9, 0x1000, v4
	ds_read2_b32 v[4:5], v9 offset1:16
	v_add_f32_e32 v10, v11, v10
	v_add_f32_e32 v14, v15, v14
	v_add_f32_e32 v12, v12, v13
	v_add_f32_e32 v18, v18, v19
	s_waitcnt lgkmcnt(0)
	v_add_f32_e32 v4, v7, v4
	v_add_f32_e32 v5, v6, v5
	ds_write2_b32 v9, v4, v5 offset1:16
	ds_read2_b32 v[4:5], v9 offset0:32 offset1:48
	v_add_f32_e32 v16, v17, v16
	s_waitcnt lgkmcnt(0)
	v_add_f32_e32 v4, v8, v4
	v_add_f32_e32 v5, v10, v5
	ds_write2_b32 v9, v4, v5 offset0:32 offset1:48
	ds_read2_b32 v[4:5], v9 offset0:64 offset1:80
	s_waitcnt lgkmcnt(0)
	v_add_f32_e32 v4, v12, v4
	v_add_f32_e32 v5, v14, v5
	ds_write2_b32 v9, v4, v5 offset0:64 offset1:80
	ds_read2_b32 v[4:5], v9 offset0:96 offset1:112
	s_waitcnt lgkmcnt(0)
	v_add_f32_e32 v4, v16, v4
	v_add_f32_e32 v5, v18, v5
	ds_write2_b32 v9, v4, v5 offset0:96 offset1:112

.LBB0_1094:
	s_add_i32 s12, s90, 1
	s_add_i32 s20, s88, 1
	s_cmp_gt_i32 s89, 0
	s_cselect_b32 s38, s88, 0
	s_cmp_lg_u32 s12, 4
	s_cselect_b32 s90, s12, 0
	s_cmp_lt_i32 s88, 3
	s_cselect_b32 s39, s20, s38
	s_cselect_b32 s38, s89, 1
	s_add_i32 s12, s90, s95
	s_lshl_b32 s20, s12, 7
	s_add_i32 s67, s20, 0xfffffe00
	s_cmp_gt_i32 s12, 3
	s_cselect_b32 s12, s67, s20
	s_add_i32 s20, s38, s2
	s_cmp_lt_i32 s20, 2
	s_cselect_b32 s20, s20, 0
	s_add_i32 s67, s39, s95
	s_lshl_b32 s88, s67, 2
	s_add_i32 s89, s88, -16
	s_cmp_gt_i32 s67, 3
	s_cselect_b32 s88, s89, s88
	s_mov_b32 s89, s21
	s_lshl_b64 s[96:97], s[20:21], 18
	s_lshl_b64 s[88:89], s[88:89], 10
	v_or_b32_e32 v10, s12, v177
	v_lshl_add_u64 v[8:9], v[166:167], 0, s[96:97]
	v_lshl_add_u64 v[174:175], v[8:9], 0, s[88:89]
	v_ashrrev_i32_e32 v8, 4, v10
	s_waitcnt lgkmcnt(0)
	s_barrier
	ds_read_b128 v[4:7], v179 offset:32768
	ds_read_b128 v[12:15], v179 offset:36864
	ds_read_b128 v[32:35], v179 offset:40960
	ds_read_b128 v[120:123], v179 offset:45056
	v_ashrrev_i32_e32 v9, 31, v8
	ds_read_b128 v[132:135], v179 offset:49152
	ds_read_b128 v[140:143], v179 offset:53248
	ds_read_b128 v[148:151], v179 offset:57344
	ds_read_b128 v[152:155], v179 offset:61440
	v_lshlrev_b64 v[8:9], 20, v[8:9]
	v_lshl_add_u64 v[8:9], s[60:61], 0, v[8:9]
	v_lshl_add_u64 v[10:11], v[8:9], 0, v[162:163]
	v_mov_b32_e32 v169, v2
	v_lshl_add_u64 v[188:189], v[10:11], 0, v[168:169]
	v_lshl_add_u64 v[10:11], v[8:9], 0, v[164:165]
	v_lshl_add_u64 v[190:191], v[10:11], 0, v[168:169]
	v_lshl_add_u64 v[10:11], v[8:9], 0, v[158:159]
	v_lshl_add_u64 v[8:9], v[8:9], 0, v[160:161]
	v_lshl_add_u64 v[10:11], v[10:11], 0, v[168:169]
	v_lshl_add_u64 v[8:9], v[8:9], 0, v[168:169]
	global_load_dwordx4 v[16:19], v[10:11], off
	s_nop 0
	global_load_dwordx4 v[8:11], v[8:9], off
	s_waitcnt vmcnt(8) lgkmcnt(6)
	v_mfma_f32_16x16x32_bf16 v[124:127], v[48:51], v[12:15], v[124:127]
	s_waitcnt lgkmcnt(5)
	v_mfma_f32_16x16x32_bf16 v[116:119], v[36:39], v[32:35], v[116:119]
	v_mfma_f32_16x16x32_bf16 v[32:35], v[48:51], v[32:35], v[112:115]
	s_waitcnt lgkmcnt(4)
	v_mfma_f32_16x16x32_bf16 v[108:111], v[36:39], v[120:123], v[108:111]
	v_mfma_f32_16x16x32_bf16 v[104:107], v[48:51], v[120:123], v[104:107]
	v_mfma_f32_16x16x32_bf16 v[144:147], v[36:39], v[4:7], v[144:147]
	v_mfma_f32_16x16x32_bf16 v[136:139], v[48:51], v[4:7], v[136:139]
	v_mfma_f32_16x16x32_bf16 v[128:131], v[36:39], v[12:15], v[128:131]
	ds_read_b128 v[112:115], v180 offset:32768
	ds_read_b128 v[120:123], v180 offset:36864
	ds_read_b128 v[170:173], v180 offset:40960
	ds_read_b128 v[184:187], v180 offset:45056
	global_load_dwordx4 v[12:15], v[188:189], off
	global_load_dwordx4 v[4:7], v[190:191], off
	s_waitcnt lgkmcnt(7)
	v_mfma_f32_16x16x32_bf16 v[100:103], v[36:39], v[132:135], v[100:103]
	v_mfma_f32_16x16x32_bf16 v[96:99], v[48:51], v[132:135], v[96:99]
	s_waitcnt lgkmcnt(6)
	v_mfma_f32_16x16x32_bf16 v[92:95], v[36:39], v[140:143], v[92:95]
	v_mfma_f32_16x16x32_bf16 v[88:91], v[48:51], v[140:143], v[88:91]
	s_waitcnt lgkmcnt(5)
	v_mfma_f32_16x16x32_bf16 v[84:87], v[36:39], v[148:151], v[84:87]
	v_mfma_f32_16x16x32_bf16 v[132:135], v[48:51], v[148:151], v[28:31]
	s_waitcnt lgkmcnt(4)
	v_mfma_f32_16x16x32_bf16 v[24:27], v[36:39], v[152:155], v[24:27]
	v_mfma_f32_16x16x32_bf16 v[20:23], v[48:51], v[152:155], v[20:23]
	ds_read_b128 v[140:143], v180 offset:49152
	ds_read_b128 v[148:151], v180 offset:53248
	ds_read_b128 v[152:155], v180 offset:57344
	ds_read_b128 v[188:191], v180 offset:61440
	v_add_co_u32_e32 v192, vcc, s16, v174
	s_nop 1
	v_addc_co_u32_e32 v193, vcc, 0, v175, vcc
	global_load_dwordx4 v[36:39], v[174:175], off sc0
	global_load_dwordx4 v[48:51], v[192:193], off sc0
	ds_write_b128 v178, v[64:67]
	s_waitcnt vmcnt(11) lgkmcnt(8)
	v_mfma_f32_16x16x32_bf16 v[64:67], v[76:79], v[112:115], v[144:147]
	s_waitcnt vmcnt(9)
	v_mfma_f32_16x16x32_bf16 v[112:115], v[44:47], v[112:115], v[136:139]
	s_waitcnt lgkmcnt(7)
	v_mfma_f32_16x16x32_bf16 v[128:131], v[76:79], v[120:123], v[128:131]
	v_mfma_f32_16x16x32_bf16 v[120:123], v[44:47], v[120:123], v[124:127]
	s_waitcnt lgkmcnt(6)
	v_mfma_f32_16x16x32_bf16 v[116:119], v[76:79], v[170:173], v[116:119]
	v_mfma_f32_16x16x32_bf16 v[32:35], v[44:47], v[170:173], v[32:35]
	s_waitcnt lgkmcnt(5)
	v_mfma_f32_16x16x32_bf16 v[108:111], v[76:79], v[184:187], v[108:111]
	v_mfma_f32_16x16x32_bf16 v[104:107], v[44:47], v[184:187], v[104:107]
	ds_read_b128 v[124:127], v181 offset:32768
	ds_read_b128 v[136:139], v181 offset:36864
	ds_read_b128 v[144:147], v181 offset:40960
	ds_read_b128 v[170:173], v181 offset:45056
	global_load_dwordx4 v[28:31], v[174:175], off offset:1024 sc0
	ds_write_b128 v178, v[60:63] offset:8192
	s_waitcnt lgkmcnt(9)
	v_mfma_f32_16x16x32_bf16 v[60:63], v[76:79], v[140:143], v[100:103]
	v_mfma_f32_16x16x32_bf16 v[96:99], v[44:47], v[140:143], v[96:99]
	s_waitcnt lgkmcnt(8)
	v_mfma_f32_16x16x32_bf16 v[92:95], v[76:79], v[148:151], v[92:95]
	v_mfma_f32_16x16x32_bf16 v[88:91], v[44:47], v[148:151], v[88:91]
	s_waitcnt lgkmcnt(7)
	v_mfma_f32_16x16x32_bf16 v[84:87], v[76:79], v[152:155], v[84:87]
	v_mfma_f32_16x16x32_bf16 v[100:103], v[44:47], v[152:155], v[132:135]
	s_waitcnt lgkmcnt(6)
	v_mfma_f32_16x16x32_bf16 v[76:79], v[76:79], v[188:191], v[24:27]
	v_mfma_f32_16x16x32_bf16 v[132:135], v[44:47], v[188:191], v[20:23]
	ds_read_b128 v[140:143], v181 offset:49152
	ds_read_b128 v[148:151], v181 offset:53248
	ds_read_b128 v[152:155], v181 offset:57344
	ds_read_b128 v[184:187], v181 offset:61440
	global_load_dwordx4 v[24:27], v[174:175], off offset:2048 sc0
	global_load_dwordx4 v[44:47], v[192:193], off offset:1024 sc0
	ds_write_b128 v178, v[56:59] offset:16384
	s_waitcnt lgkmcnt(9)
	v_mfma_f32_16x16x32_bf16 v[56:59], v[72:75], v[124:127], v[64:67]
	s_waitcnt vmcnt(10)
	v_mfma_f32_16x16x32_bf16 v[64:67], v[40:43], v[124:127], v[112:115]
	s_waitcnt lgkmcnt(8)
	v_mfma_f32_16x16x32_bf16 v[112:115], v[72:75], v[136:139], v[128:131]
	v_mfma_f32_16x16x32_bf16 v[120:123], v[40:43], v[136:139], v[120:123]
	s_waitcnt lgkmcnt(7)
	v_mfma_f32_16x16x32_bf16 v[116:119], v[72:75], v[144:147], v[116:119]
	v_mfma_f32_16x16x32_bf16 v[32:35], v[40:43], v[144:147], v[32:35]
	s_waitcnt lgkmcnt(6)
	v_mfma_f32_16x16x32_bf16 v[108:111], v[72:75], v[170:173], v[108:111]
	v_mfma_f32_16x16x32_bf16 v[104:107], v[40:43], v[170:173], v[104:107]
	ds_read_b128 v[124:127], v182 offset:32768
	ds_read_b128 v[128:131], v182 offset:36864
	ds_read_b128 v[136:139], v182 offset:40960
	ds_read_b128 v[144:147], v182 offset:45056
	global_load_dwordx4 v[20:23], v[174:175], off offset:3072 sc0
	ds_write_b128 v178, v[52:55] offset:24576
	s_waitcnt lgkmcnt(9)
	v_mfma_f32_16x16x32_bf16 v[52:55], v[72:75], v[140:143], v[60:63]
	s_waitcnt lgkmcnt(8)
	v_mfma_f32_16x16x32_bf16 v[92:95], v[72:75], v[148:151], v[92:95]
	v_mfma_f32_16x16x32_bf16 v[88:91], v[40:43], v[148:151], v[88:91]
	s_waitcnt lgkmcnt(7)
	v_mfma_f32_16x16x32_bf16 v[84:87], v[72:75], v[152:155], v[84:87]
	s_waitcnt lgkmcnt(6)
	v_mfma_f32_16x16x32_bf16 v[72:75], v[72:75], v[184:187], v[76:79]
	v_mfma_f32_16x16x32_bf16 v[60:63], v[40:43], v[140:143], v[96:99]
	v_mfma_f32_16x16x32_bf16 v[148:151], v[40:43], v[152:155], v[100:103]
	v_mfma_f32_16x16x32_bf16 v[152:155], v[40:43], v[184:187], v[132:135]
	ds_read_b128 v[76:79], v182 offset:49152
	ds_read_b128 v[170:173], v182 offset:53248
	ds_read_b128 v[184:187], v182 offset:57344
	ds_read_b128 v[188:191], v182 offset:61440
	global_load_dwordx4 v[40:43], v[192:193], off offset:2048 sc0
	s_waitcnt lgkmcnt(8)
	v_mfma_f32_16x16x32_bf16 v[140:143], v[68:71], v[124:127], v[56:59]
	s_waitcnt vmcnt(11)
	v_mfma_f32_16x16x32_bf16 v[132:135], v[80:83], v[124:127], v[64:67]
	s_waitcnt lgkmcnt(7)
	v_mfma_f32_16x16x32_bf16 v[124:127], v[68:71], v[128:131], v[112:115]
	v_mfma_f32_16x16x32_bf16 v[120:123], v[80:83], v[128:131], v[120:123]
	s_waitcnt lgkmcnt(6)
	v_mfma_f32_16x16x32_bf16 v[116:119], v[68:71], v[136:139], v[116:119]
	v_mfma_f32_16x16x32_bf16 v[112:115], v[80:83], v[136:139], v[32:35]
	s_waitcnt lgkmcnt(5)
	v_mfma_f32_16x16x32_bf16 v[108:111], v[68:71], v[144:147], v[108:111]
	v_mfma_f32_16x16x32_bf16 v[104:107], v[80:83], v[144:147], v[104:107]
	global_load_dwordx4 v[32:35], v[192:193], off offset:3072 sc0
	s_waitcnt lgkmcnt(3)
	v_mfma_f32_16x16x32_bf16 v[100:103], v[68:71], v[76:79], v[52:55]
	v_mfma_f32_16x16x32_bf16 v[96:99], v[80:83], v[76:79], v[60:63]
	s_waitcnt lgkmcnt(2)
	v_mfma_f32_16x16x32_bf16 v[92:95], v[68:71], v[170:173], v[92:95]
	v_mfma_f32_16x16x32_bf16 v[88:91], v[80:83], v[170:173], v[88:91]
	s_waitcnt lgkmcnt(1)
	v_mfma_f32_16x16x32_bf16 v[84:87], v[68:71], v[184:187], v[84:87]
	v_mfma_f32_16x16x32_bf16 v[76:79], v[80:83], v[184:187], v[148:151]
	s_waitcnt lgkmcnt(0)
	v_mfma_f32_16x16x32_bf16 v[72:75], v[68:71], v[188:191], v[72:75]
	v_mfma_f32_16x16x32_bf16 v[68:71], v[80:83], v[188:191], v[152:155]
	s_add_i32 s66, s66, 1
	s_cmp_lg_u32 s66, 4
	s_cbranch_scc1 .LBB0_1087
	s_and_b64 vcc, exec, s[0:1]
	s_cbranch_vccnz .LBB0_1086
	s_add_i32 s0, s85, s2
	s_lshl_b32 s1, s0, 8
	s_add_i32 s12, s1, 0xfffffe00
	s_cmp_gt_i32 s0, 1
	s_cselect_b32 s0, s12, s1
	v_mov_b32_e32 v169, v3
	v_mov_b32_e32 v183, v157
	s_add_i32 s0, s0, s64
	v_mov_b32_e32 v63, v2
	v_lshl_add_u32 v170, v183, 3, s0
	v_ashrrev_i32_e32 v171, 31, v170
	v_lshl_add_u64 v[56:57], v[170:171], 2, s[52:53]
	global_load_dwordx4 v[52:55], v[56:57], off offset:16
	s_nop 0
	global_load_dwordx4 v[56:59], v[56:57], off
	v_ashrrev_i32_e32 v60, 4, v170
	v_ashrrev_i32_e32 v61, 31, v60
	v_readlane_b32 s0, v251, 57
	v_lshlrev_b64 v[60:61], 20, v[60:61]
	v_readlane_b32 s1, v251, 58
	v_add_u32_e32 v172, s58, v169
	v_lshlrev_b32_e32 v62, 4, v183
	v_lshl_add_u64 v[60:61], s[0:1], 0, v[60:61]
	v_and_b32_e32 v62, 16, v62
	v_ashrrev_i32_e32 v173, 31, v172
	v_lshl_add_u64 v[60:61], v[60:61], 0, v[62:63]
	v_lshlrev_b64 v[62:63], 5, v[172:173]
	v_lshl_add_u64 v[62:63], v[60:61], 0, v[62:63]
	global_load_dwordx4 v[152:155], v[62:63], off
	v_add_u32_e32 v62, 16, v172
	v_ashrrev_i32_e32 v63, 31, v62
	v_lshlrev_b64 v[62:63], 5, v[62:63]
	v_lshl_add_u64 v[62:63], v[60:61], 0, v[62:63]
	global_load_dwordx4 v[148:151], v[62:63], off
	v_add_u32_e32 v62, 32, v172
	v_ashrrev_i32_e32 v63, 31, v62
	v_lshlrev_b64 v[62:63], 5, v[62:63]
	v_lshl_add_u64 v[62:63], v[60:61], 0, v[62:63]
	global_load_dwordx4 v[144:147], v[62:63], off
	v_add_u32_e32 v62, 48, v172
	v_ashrrev_i32_e32 v63, 31, v62
	v_lshlrev_b64 v[62:63], 5, v[62:63]
	v_lshl_add_u64 v[62:63], v[60:61], 0, v[62:63]
	global_load_dwordx4 v[136:139], v[62:63], off
	v_add_u32_e32 v62, 64, v172
	v_ashrrev_i32_e32 v63, 31, v62
	v_lshlrev_b64 v[62:63], 5, v[62:63]
	v_lshl_add_u64 v[62:63], v[60:61], 0, v[62:63]
	global_load_dwordx4 v[128:131], v[62:63], off
	v_add_u32_e32 v62, 0x50, v172
	v_ashrrev_i32_e32 v63, 31, v62
	v_lshlrev_b64 v[62:63], 5, v[62:63]
	v_lshl_add_u64 v[62:63], v[60:61], 0, v[62:63]
	global_load_dwordx4 v[80:83], v[62:63], off
	v_add_u32_e32 v62, 0x60, v172
	v_ashrrev_i32_e32 v63, 31, v62
	v_lshlrev_b64 v[62:63], 5, v[62:63]
	v_lshl_add_u64 v[62:63], v[60:61], 0, v[62:63]
	global_load_dwordx4 v[64:67], v[62:63], off
	v_add_u32_e32 v62, 0x70, v172
	v_ashrrev_i32_e32 v63, 31, v62
	v_lshlrev_b64 v[62:63], 5, v[62:63]
	v_lshl_add_u64 v[60:61], v[60:61], 0, v[62:63]
	global_load_dwordx4 v[60:63], v[60:61], off
	v_cmp_eq_u32_e32 vcc, 0, v183
	s_waitcnt vmcnt(9)
	v_add_f32_e32 v132, v132, v52
	s_waitcnt vmcnt(8)
	v_add_f32_e32 v140, v140, v56
	v_add_f32_e32 v141, v141, v57
	v_add_f32_e32 v142, v142, v58
	v_add_f32_e32 v143, v143, v59
	v_mul_f32_e32 v140, 0xbfb8aa3b, v140
	v_mul_f32_e32 v141, 0xbfb8aa3b, v141
	v_add_f32_e32 v133, v133, v53
	v_mul_f32_e32 v142, 0xbfb8aa3b, v142
	v_add_f32_e32 v134, v134, v54
	v_mul_f32_e32 v143, 0xbfb8aa3b, v143
	v_add_f32_e32 v135, v135, v55
	v_exp_f32_e32 v140, v140
	v_mul_f32_e32 v132, 0xbfb8aa3b, v132
	v_exp_f32_e32 v141, v141
	v_mul_f32_e32 v133, 0xbfb8aa3b, v133
	v_exp_f32_e32 v142, v142
	v_mul_f32_e32 v134, 0xbfb8aa3b, v134
	v_exp_f32_e32 v143, v143
	v_mul_f32_e32 v135, 0xbfb8aa3b, v135
	v_exp_f32_e32 v132, v132
	v_exp_f32_e32 v133, v133
	v_exp_f32_e32 v134, v134
	v_exp_f32_e32 v135, v135
	v_add_f32_e32 v140, 1.0, v140
	v_add_f32_e32 v141, 1.0, v141
	v_add_f32_e32 v142, 1.0, v142
	v_add_f32_e32 v143, 1.0, v143
	v_rcp_f32_e32 v140, v140
	v_add_f32_e32 v132, 1.0, v132
	v_rcp_f32_e32 v141, v141
	v_add_f32_e32 v133, 1.0, v133
	v_rcp_f32_e32 v142, v142
	v_add_f32_e32 v134, 1.0, v134
	v_rcp_f32_e32 v143, v143
	v_add_f32_e32 v135, 1.0, v135
	v_add_f32_e32 v124, v124, v56
	v_add_f32_e32 v125, v125, v57
	v_rcp_f32_e32 v132, v132
	v_rcp_f32_e32 v133, v133
	v_rcp_f32_e32 v134, v134
	v_rcp_f32_e32 v135, v135
	v_mul_f32_e32 v124, 0xbfb8aa3b, v124
	v_add_f32_e32 v120, v120, v52
	v_mul_f32_e32 v125, 0xbfb8aa3b, v125
	v_add_f32_e32 v121, v121, v53
	v_add_f32_e32 v126, v126, v58
	v_add_f32_e32 v127, v127, v59
	v_exp_f32_e32 v124, v124
	v_mul_f32_e32 v120, 0xbfb8aa3b, v120
	v_exp_f32_e32 v125, v125
	v_mul_f32_e32 v121, 0xbfb8aa3b, v121
	v_mul_f32_e32 v126, 0xbfb8aa3b, v126
	v_add_f32_e32 v122, v122, v54
	v_mul_f32_e32 v127, 0xbfb8aa3b, v127
	v_add_f32_e32 v123, v123, v55
	s_waitcnt vmcnt(7)
	v_lshlrev_b32_e32 v174, 16, v152
	v_and_b32_e32 v175, 0xffff0000, v152
	v_lshlrev_b32_e32 v152, 16, v153
	v_and_b32_e32 v153, 0xffff0000, v153
	v_exp_f32_e32 v120, v120
	v_exp_f32_e32 v121, v121
	v_exp_f32_e32 v126, v126
	v_mul_f32_e32 v122, 0xbfb8aa3b, v122
	v_exp_f32_e32 v127, v127
	v_mul_f32_e32 v123, 0xbfb8aa3b, v123
	v_pk_mul_f32 v[140:141], v[140:141], v[174:175]
	v_lshlrev_b32_e32 v174, 16, v154
	v_and_b32_e32 v175, 0xffff0000, v154
	v_pk_mul_f32 v[142:143], v[142:143], v[152:153]
	v_lshlrev_b32_e32 v152, 16, v155
	v_and_b32_e32 v153, 0xffff0000, v155
	v_exp_f32_e32 v122, v122
	v_exp_f32_e32 v123, v123
	v_pk_mul_f32 v[132:133], v[132:133], v[174:175]
	v_pk_mul_f32 v[152:153], v[134:135], v[152:153]
	v_pk_mul_f32 v[174:175], v[132:133], v[132:133]
	v_pk_mul_f32 v[134:135], v[152:153], v[152:153]
	v_add_f32_e32 v124, 1.0, v124
	v_add_f32_e32 v125, 1.0, v125
	v_pk_fma_f32 v[174:175], v[140:141], v[140:141], v[174:175]
	v_pk_fma_f32 v[134:135], v[142:143], v[142:143], v[134:135]
	v_cvt_pk_bf16_f32 v140, v140, v141
	v_cvt_pk_bf16_f32 v141, v142, v143
	v_cvt_pk_bf16_f32 v142, v132, v133
	v_lshlrev_b64 v[132:133], 11, v[172:173]
	v_rcp_f32_e32 v124, v124
	v_add_f32_e32 v120, 1.0, v120
	v_rcp_f32_e32 v125, v125
	v_add_f32_e32 v121, 1.0, v121
	v_add_f32_e32 v126, 1.0, v126
	v_add_f32_e32 v127, 1.0, v127
	v_cvt_pk_bf16_f32 v143, v152, v153
	v_lshl_add_u64 v[152:153], s[36:37], 0, v[132:133]
	v_lshlrev_b64 v[132:133], 1, v[170:171]
	v_rcp_f32_e32 v120, v120
	v_rcp_f32_e32 v121, v121
	v_rcp_f32_e32 v126, v126
	v_add_f32_e32 v122, 1.0, v122
	v_rcp_f32_e32 v127, v127
	v_add_f32_e32 v123, 1.0, v123
	v_lshl_add_u64 v[152:153], v[152:153], 0, v[132:133]
	v_rcp_f32_e32 v122, v122
	v_rcp_f32_e32 v123, v123
	global_store_dwordx4 v[152:153], v[140:143], off offset:1024
	v_add_f32_e32 v116, v116, v56
	v_add_f32_e32 v117, v117, v57
	s_waitcnt vmcnt(7)
	v_lshlrev_b32_e32 v142, 16, v148
	v_and_b32_e32 v143, 0xffff0000, v148
	v_pk_mul_f32 v[124:125], v[124:125], v[142:143]
	v_lshlrev_b32_e32 v142, 16, v150
	v_and_b32_e32 v143, 0xffff0000, v150
	v_lshlrev_b32_e32 v148, 16, v149
	v_and_b32_e32 v149, 0xffff0000, v149
	v_mul_f32_e32 v116, 0xbfb8aa3b, v116
	v_add_f32_e32 v112, v112, v52
	v_mul_f32_e32 v117, 0xbfb8aa3b, v117
	v_add_f32_e32 v113, v113, v53
	v_add_f32_e32 v118, v118, v58
	v_add_f32_e32 v119, v119, v59
	v_pk_mul_f32 v[142:143], v[120:121], v[142:143]
	v_pk_mul_f32 v[126:127], v[126:127], v[148:149]
	v_lshlrev_b32_e32 v148, 16, v151
	v_and_b32_e32 v149, 0xffff0000, v151
	v_exp_f32_e32 v116, v116
	v_mul_f32_e32 v112, 0xbfb8aa3b, v112
	v_exp_f32_e32 v117, v117
	v_mul_f32_e32 v113, 0xbfb8aa3b, v113
	v_mul_f32_e32 v118, 0xbfb8aa3b, v118
	v_add_f32_e32 v114, v114, v54
	v_mul_f32_e32 v119, 0xbfb8aa3b, v119
	v_add_f32_e32 v115, v115, v55
	v_pk_mul_f32 v[120:121], v[142:143], v[142:143]
	v_pk_mul_f32 v[148:149], v[122:123], v[148:149]
	v_exp_f32_e32 v112, v112
	v_exp_f32_e32 v113, v113
	v_exp_f32_e32 v118, v118
	v_mul_f32_e32 v114, 0xbfb8aa3b, v114
	v_exp_f32_e32 v119, v119
	v_mul_f32_e32 v115, 0xbfb8aa3b, v115
	v_pk_fma_f32 v[120:121], v[124:125], v[124:125], v[120:121]
	v_pk_mul_f32 v[122:123], v[148:149], v[148:149]
	v_exp_f32_e32 v114, v114
	v_exp_f32_e32 v115, v115
	v_add_u32_e32 v140, s65, v169
	v_pk_fma_f32 v[122:123], v[126:127], v[126:127], v[122:123]
	v_add_f32_e32 v120, v120, v121
	v_add_f32_e32 v120, v122, v120
	v_ashrrev_i32_e32 v141, 31, v140
	v_add_f32_e32 v116, 1.0, v116
	v_add_f32_e32 v117, 1.0, v117
	v_add_f32_e32 v120, v123, v120
	v_cvt_pk_bf16_f32 v123, v126, v127
	v_lshlrev_b64 v[126:127], 11, v[140:141]
	v_rcp_f32_e32 v116, v116
	v_add_f32_e32 v112, 1.0, v112
	v_rcp_f32_e32 v117, v117
	v_add_f32_e32 v113, 1.0, v113
	v_add_f32_e32 v118, 1.0, v118
	v_add_f32_e32 v119, 1.0, v119
	v_lshl_add_u64 v[126:127], s[36:37], 0, v[126:127]
	v_rcp_f32_e32 v112, v112
	v_rcp_f32_e32 v113, v113
	v_rcp_f32_e32 v118, v118
	v_add_f32_e32 v114, 1.0, v114
	v_rcp_f32_e32 v119, v119
	v_add_f32_e32 v115, 1.0, v115
	v_cvt_pk_bf16_f32 v122, v124, v125
	v_cvt_pk_bf16_f32 v124, v142, v143
	v_cvt_pk_bf16_f32 v125, v148, v149
	v_lshl_add_u64 v[126:127], v[126:127], 0, v[132:133]
	v_rcp_f32_e32 v114, v114
	v_rcp_f32_e32 v115, v115
	global_store_dwordx4 v[126:127], v[122:125], off offset:1024
	v_add_f32_e32 v108, v108, v56
	v_add_f32_e32 v109, v109, v57
	s_waitcnt vmcnt(7)
	v_lshlrev_b32_e32 v124, 16, v144
	v_and_b32_e32 v125, 0xffff0000, v144
	v_pk_mul_f32 v[116:117], v[116:117], v[124:125]
	v_lshlrev_b32_e32 v124, 16, v146
	v_and_b32_e32 v125, 0xffff0000, v146
	v_lshlrev_b32_e32 v126, 16, v145
	v_and_b32_e32 v127, 0xffff0000, v145
	v_mul_f32_e32 v108, 0xbfb8aa3b, v108
	v_add_f32_e32 v104, v104, v52
	v_mul_f32_e32 v109, 0xbfb8aa3b, v109
	v_add_f32_e32 v105, v105, v53
	v_add_f32_e32 v110, v110, v58
	v_add_f32_e32 v111, v111, v59
	v_pk_mul_f32 v[124:125], v[112:113], v[124:125]
	v_pk_mul_f32 v[118:119], v[118:119], v[126:127]
	v_lshlrev_b32_e32 v126, 16, v147
	v_and_b32_e32 v127, 0xffff0000, v147
	v_exp_f32_e32 v108, v108
	v_mul_f32_e32 v104, 0xbfb8aa3b, v104
	v_exp_f32_e32 v109, v109
	v_mul_f32_e32 v105, 0xbfb8aa3b, v105
	v_mul_f32_e32 v110, 0xbfb8aa3b, v110
	v_add_f32_e32 v106, v106, v54
	v_mul_f32_e32 v111, 0xbfb8aa3b, v111
	v_add_f32_e32 v107, v107, v55
	v_pk_mul_f32 v[112:113], v[124:125], v[124:125]
	v_pk_mul_f32 v[126:127], v[114:115], v[126:127]
	v_exp_f32_e32 v104, v104
	v_exp_f32_e32 v105, v105
	v_exp_f32_e32 v110, v110
	v_mul_f32_e32 v106, 0xbfb8aa3b, v106
	v_exp_f32_e32 v111, v111
	v_mul_f32_e32 v107, 0xbfb8aa3b, v107
	v_pk_fma_f32 v[112:113], v[116:117], v[116:117], v[112:113]
	v_pk_mul_f32 v[114:115], v[126:127], v[126:127]
	v_exp_f32_e32 v106, v106
	v_exp_f32_e32 v107, v107
	v_add_u32_e32 v122, s75, v169
	v_pk_fma_f32 v[114:115], v[118:119], v[118:119], v[114:115]
	v_add_f32_e32 v112, v112, v113
	v_add_f32_e32 v112, v114, v112
	v_ashrrev_i32_e32 v123, 31, v122
	v_add_f32_e32 v108, 1.0, v108
	v_add_f32_e32 v109, 1.0, v109
	v_add_f32_e32 v112, v115, v112
	v_cvt_pk_bf16_f32 v115, v118, v119
	v_lshlrev_b64 v[118:119], 11, v[122:123]
	v_rcp_f32_e32 v108, v108
	v_add_f32_e32 v104, 1.0, v104
	v_rcp_f32_e32 v109, v109
	v_add_f32_e32 v105, 1.0, v105
	v_add_f32_e32 v110, 1.0, v110
	v_add_f32_e32 v111, 1.0, v111
	v_lshl_add_u64 v[118:119], s[36:37], 0, v[118:119]
	v_rcp_f32_e32 v104, v104
	v_rcp_f32_e32 v105, v105
	v_rcp_f32_e32 v110, v110
	v_add_f32_e32 v106, 1.0, v106
	v_rcp_f32_e32 v111, v111
	v_add_f32_e32 v107, 1.0, v107
	v_cvt_pk_bf16_f32 v114, v116, v117
	v_cvt_pk_bf16_f32 v116, v124, v125
	v_cvt_pk_bf16_f32 v117, v126, v127
	v_lshl_add_u64 v[118:119], v[118:119], 0, v[132:133]
	v_rcp_f32_e32 v106, v106
	v_rcp_f32_e32 v107, v107
	global_store_dwordx4 v[118:119], v[114:117], off offset:1024
	v_add_f32_e32 v100, v100, v56
	v_add_f32_e32 v101, v101, v57
	s_waitcnt vmcnt(7)
	v_lshlrev_b32_e32 v116, 16, v136
	v_and_b32_e32 v117, 0xffff0000, v136
	v_pk_mul_f32 v[108:109], v[108:109], v[116:117]
	v_lshlrev_b32_e32 v116, 16, v138
	v_and_b32_e32 v117, 0xffff0000, v138
	v_lshlrev_b32_e32 v118, 16, v137
	v_and_b32_e32 v119, 0xffff0000, v137
	v_mul_f32_e32 v100, 0xbfb8aa3b, v100
	v_add_f32_e32 v96, v96, v52
	v_mul_f32_e32 v101, 0xbfb8aa3b, v101
	v_add_f32_e32 v97, v97, v53
	v_add_f32_e32 v102, v102, v58
	v_add_f32_e32 v103, v103, v59
	v_pk_mul_f32 v[116:117], v[104:105], v[116:117]
	v_pk_mul_f32 v[110:111], v[110:111], v[118:119]
	v_lshlrev_b32_e32 v118, 16, v139
	v_and_b32_e32 v119, 0xffff0000, v139
	v_exp_f32_e32 v100, v100
	v_mul_f32_e32 v96, 0xbfb8aa3b, v96
	v_exp_f32_e32 v101, v101
	v_mul_f32_e32 v97, 0xbfb8aa3b, v97
	v_mul_f32_e32 v102, 0xbfb8aa3b, v102
	v_add_f32_e32 v98, v98, v54
	v_mul_f32_e32 v103, 0xbfb8aa3b, v103
	v_add_f32_e32 v99, v99, v55
	v_pk_mul_f32 v[104:105], v[116:117], v[116:117]
	v_pk_mul_f32 v[118:119], v[106:107], v[118:119]
	v_exp_f32_e32 v96, v96
	v_exp_f32_e32 v97, v97
	v_exp_f32_e32 v102, v102
	v_mul_f32_e32 v98, 0xbfb8aa3b, v98
	v_exp_f32_e32 v103, v103
	v_mul_f32_e32 v99, 0xbfb8aa3b, v99
	v_pk_fma_f32 v[104:105], v[108:109], v[108:109], v[104:105]
	v_pk_mul_f32 v[106:107], v[118:119], v[118:119]
	v_exp_f32_e32 v98, v98
	v_exp_f32_e32 v99, v99
	v_add_u32_e32 v114, s76, v169
	v_pk_fma_f32 v[106:107], v[110:111], v[110:111], v[106:107]
	v_add_f32_e32 v104, v104, v105
	v_add_f32_e32 v104, v106, v104
	v_ashrrev_i32_e32 v115, 31, v114
	v_add_f32_e32 v100, 1.0, v100
	v_add_f32_e32 v101, 1.0, v101
	v_add_f32_e32 v104, v107, v104
	v_cvt_pk_bf16_f32 v107, v110, v111
	v_lshlrev_b64 v[110:111], 11, v[114:115]
	v_rcp_f32_e32 v100, v100
	v_add_f32_e32 v96, 1.0, v96
	v_rcp_f32_e32 v101, v101
	v_add_f32_e32 v97, 1.0, v97
	v_add_f32_e32 v102, 1.0, v102
	v_add_f32_e32 v103, 1.0, v103
	v_lshl_add_u64 v[110:111], s[36:37], 0, v[110:111]
	v_rcp_f32_e32 v96, v96
	v_rcp_f32_e32 v97, v97
	v_rcp_f32_e32 v102, v102
	v_add_f32_e32 v98, 1.0, v98
	v_rcp_f32_e32 v103, v103
	v_add_f32_e32 v99, 1.0, v99
	v_cvt_pk_bf16_f32 v106, v108, v109
	v_cvt_pk_bf16_f32 v108, v116, v117
	v_cvt_pk_bf16_f32 v109, v118, v119
	v_lshl_add_u64 v[110:111], v[110:111], 0, v[132:133]
	v_rcp_f32_e32 v98, v98
	v_rcp_f32_e32 v99, v99
	global_store_dwordx4 v[110:111], v[106:109], off offset:1024
	s_waitcnt vmcnt(7)
	v_lshlrev_b32_e32 v110, 16, v129
	v_and_b32_e32 v111, 0xffff0000, v129
	v_lshlrev_b32_e32 v108, 16, v128
	v_and_b32_e32 v109, 0xffff0000, v128
	v_pk_mul_f32 v[100:101], v[100:101], v[108:109]
	v_lshlrev_b32_e32 v108, 16, v130
	v_and_b32_e32 v109, 0xffff0000, v130
	v_pk_mul_f32 v[108:109], v[96:97], v[108:109]
	v_pk_mul_f32 v[102:103], v[102:103], v[110:111]
	v_lshlrev_b32_e32 v110, 16, v131
	v_and_b32_e32 v111, 0xffff0000, v131
	v_pk_mul_f32 v[96:97], v[108:109], v[108:109]
	v_pk_mul_f32 v[110:111], v[98:99], v[110:111]
	v_pk_fma_f32 v[96:97], v[100:101], v[100:101], v[96:97]
	v_pk_mul_f32 v[98:99], v[110:111], v[110:111]
	v_add_u32_e32 v106, s77, v169
	v_pk_fma_f32 v[98:99], v[102:103], v[102:103], v[98:99]
	v_add_f32_e32 v96, v96, v97
	v_add_f32_e32 v96, v98, v96
	v_ashrrev_i32_e32 v107, 31, v106
	v_add_f32_e32 v96, v99, v96
	v_cvt_pk_bf16_f32 v99, v102, v103
	v_lshlrev_b64 v[102:103], 11, v[106:107]
	v_lshl_add_u64 v[102:103], s[36:37], 0, v[102:103]
	v_cvt_pk_bf16_f32 v98, v100, v101
	v_cvt_pk_bf16_f32 v100, v108, v109
	v_cvt_pk_bf16_f32 v101, v110, v111
	v_lshl_add_u64 v[102:103], v[102:103], 0, v[132:133]
	global_store_dwordx4 v[102:103], v[98:101], off offset:1024
	v_add_f32_e32 v92, v92, v56
	v_add_f32_e32 v93, v93, v57
	s_waitcnt vmcnt(7)
	v_lshlrev_b32_e32 v100, 16, v80
	v_and_b32_e32 v101, 0xffff0000, v80
	v_add_f32_e32 v80, v89, v53
	v_mul_f32_e32 v80, 0xbfb8aa3b, v80
	v_exp_f32_e32 v80, v80
	v_mul_f32_e32 v92, 0xbfb8aa3b, v92
	v_mul_f32_e32 v93, 0xbfb8aa3b, v93
	v_exp_f32_e32 v92, v92
	v_exp_f32_e32 v93, v93
	v_add_f32_e32 v80, 1.0, v80
	v_rcp_f32_e32 v89, v80
	v_add_f32_e32 v80, v94, v58
	v_mul_f32_e32 v80, 0xbfb8aa3b, v80
	v_exp_f32_e32 v80, v80
	v_add_f32_e32 v92, 1.0, v92
	v_add_f32_e32 v93, 1.0, v93
	v_rcp_f32_e32 v92, v92
	v_rcp_f32_e32 v93, v93
	v_add_f32_e32 v88, v88, v52
	v_add_f32_e32 v80, 1.0, v80
	v_mul_f32_e32 v88, 0xbfb8aa3b, v88
	v_rcp_f32_e32 v94, v80
	v_add_f32_e32 v80, v90, v54
	v_lshlrev_b32_e32 v102, 16, v81
	v_and_b32_e32 v103, 0xffff0000, v81
	v_add_f32_e32 v81, v91, v55
	v_exp_f32_e32 v88, v88
	v_pk_mul_f32 v[92:93], v[92:93], v[100:101]
	v_lshlrev_b32_e32 v100, 16, v82
	v_and_b32_e32 v101, 0xffff0000, v82
	v_mul_f32_e32 v80, 0xbfb8aa3b, v80
	v_add_f32_e32 v82, v95, v59
	v_mul_f32_e32 v81, 0xbfb8aa3b, v81
	v_exp_f32_e32 v80, v80
	v_mul_f32_e32 v82, 0xbfb8aa3b, v82
	v_exp_f32_e32 v81, v81
	v_exp_f32_e32 v82, v82
	v_add_f32_e32 v88, 1.0, v88
	v_rcp_f32_e32 v88, v88
	v_add_f32_e32 v80, 1.0, v80
	v_add_f32_e32 v81, 1.0, v81
	v_rcp_f32_e32 v80, v80
	v_add_f32_e32 v82, 1.0, v82
	v_rcp_f32_e32 v81, v81
	v_rcp_f32_e32 v95, v82
	v_pk_mul_f32 v[100:101], v[88:89], v[100:101]
	v_lshlrev_b32_e32 v82, 16, v83
	v_and_b32_e32 v83, 0xffff0000, v83
	v_pk_mul_f32 v[88:89], v[100:101], v[100:101]
	v_pk_mul_f32 v[82:83], v[80:81], v[82:83]
	v_pk_fma_f32 v[88:89], v[92:93], v[92:93], v[88:89]
	v_pk_mul_f32 v[94:95], v[94:95], v[102:103]
	v_pk_mul_f32 v[80:81], v[82:83], v[82:83]
	v_add_u32_e32 v98, s78, v169
	v_pk_fma_f32 v[80:81], v[94:95], v[94:95], v[80:81]
	v_add_f32_e32 v88, v88, v89
	v_add_f32_e32 v80, v80, v88
	v_ashrrev_i32_e32 v99, 31, v98
	v_add_f32_e32 v80, v81, v80
	v_cvt_pk_bf16_f32 v91, v82, v83
	v_lshlrev_b64 v[82:83], 11, v[98:99]
	v_add_f32_e32 v81, v84, v56
	v_lshl_add_u64 v[82:83], s[36:37], 0, v[82:83]
	v_mul_f32_e32 v81, 0xbfb8aa3b, v81
	v_cvt_pk_bf16_f32 v88, v92, v93
	v_cvt_pk_bf16_f32 v89, v94, v95
	v_cvt_pk_bf16_f32 v90, v100, v101
	v_lshl_add_u64 v[82:83], v[82:83], 0, v[132:133]
	v_exp_f32_e32 v81, v81
	global_store_dwordx4 v[82:83], v[88:91], off offset:1024
	v_add_f32_e32 v76, v76, v52
	v_mul_f32_e32 v76, 0xbfb8aa3b, v76
	s_waitcnt vmcnt(7)
	v_lshlrev_b32_e32 v88, 16, v64
	v_and_b32_e32 v89, 0xffff0000, v64
	v_add_f32_e32 v64, v77, v53
	v_mul_f32_e32 v64, 0xbfb8aa3b, v64
	v_exp_f32_e32 v64, v64
	v_add_f32_e32 v81, 1.0, v81
	v_rcp_f32_e32 v84, v81
	v_add_f32_e32 v81, v85, v57
	v_mul_f32_e32 v81, 0xbfb8aa3b, v81
	v_exp_f32_e32 v81, v81
	v_add_f32_e32 v64, 1.0, v64
	v_rcp_f32_e32 v77, v64
	v_add_f32_e32 v64, v86, v58
	v_mul_f32_e32 v64, 0xbfb8aa3b, v64
	v_exp_f32_e32 v64, v64
	v_add_f32_e32 v81, 1.0, v81
	v_rcp_f32_e32 v85, v81
	v_lshlrev_b32_e32 v90, 16, v65
	v_add_f32_e32 v64, 1.0, v64
	v_rcp_f32_e32 v86, v64
	v_add_f32_e32 v64, v78, v54
	v_and_b32_e32 v91, 0xffff0000, v65
	v_add_f32_e32 v65, v79, v55
	v_exp_f32_e32 v76, v76
	v_pk_mul_f32 v[84:85], v[84:85], v[88:89]
	v_lshlrev_b32_e32 v88, 16, v66
	v_and_b32_e32 v89, 0xffff0000, v66
	v_mul_f32_e32 v64, 0xbfb8aa3b, v64
	v_add_f32_e32 v66, v87, v59
	v_mul_f32_e32 v65, 0xbfb8aa3b, v65
	v_exp_f32_e32 v64, v64
	v_mul_f32_e32 v66, 0xbfb8aa3b, v66
	v_exp_f32_e32 v65, v65
	v_exp_f32_e32 v66, v66
	v_add_f32_e32 v76, 1.0, v76
	v_rcp_f32_e32 v76, v76
	v_add_f32_e32 v64, 1.0, v64
	v_add_f32_e32 v65, 1.0, v65
	v_rcp_f32_e32 v64, v64
	v_add_f32_e32 v66, 1.0, v66
	v_rcp_f32_e32 v65, v65
	v_add_f32_e32 v56, v72, v56
	v_add_f32_e32 v57, v73, v57
	v_rcp_f32_e32 v87, v66
	v_mul_f32_e32 v56, 0xbfb8aa3b, v56
	v_add_f32_e32 v52, v68, v52
	v_mul_f32_e32 v57, 0xbfb8aa3b, v57
	v_add_f32_e32 v53, v69, v53
	v_add_f32_e32 v58, v74, v58
	v_add_f32_e32 v59, v75, v59
	v_exp_f32_e32 v56, v56
	v_mul_f32_e32 v52, 0xbfb8aa3b, v52
	v_exp_f32_e32 v57, v57
	v_mul_f32_e32 v53, 0xbfb8aa3b, v53
	v_mul_f32_e32 v58, 0xbfb8aa3b, v58
	v_add_f32_e32 v54, v70, v54
	v_mul_f32_e32 v59, 0xbfb8aa3b, v59
	v_add_f32_e32 v55, v71, v55
	v_pk_mul_f32 v[76:77], v[76:77], v[88:89]
	v_lshlrev_b32_e32 v66, 16, v67
	v_and_b32_e32 v67, 0xffff0000, v67
	v_exp_f32_e32 v52, v52
	v_exp_f32_e32 v53, v53
	v_exp_f32_e32 v58, v58
	v_mul_f32_e32 v54, 0xbfb8aa3b, v54
	v_exp_f32_e32 v59, v59
	v_mul_f32_e32 v55, 0xbfb8aa3b, v55
	v_pk_mul_f32 v[88:89], v[76:77], v[76:77]
	v_pk_mul_f32 v[78:79], v[64:65], v[66:67]
	v_exp_f32_e32 v54, v54
	v_exp_f32_e32 v55, v55
	v_add_u32_e32 v82, s79, v169
	v_pk_fma_f32 v[88:89], v[84:85], v[84:85], v[88:89]
	v_pk_mul_f32 v[86:87], v[86:87], v[90:91]
	v_pk_mul_f32 v[64:65], v[78:79], v[78:79]
	v_add_f32_e32 v66, v88, v89
	v_pk_fma_f32 v[64:65], v[86:87], v[86:87], v[64:65]
	v_ashrrev_i32_e32 v83, 31, v82
	v_add_f32_e32 v56, 1.0, v56
	v_add_f32_e32 v57, 1.0, v57
	v_add_f32_e32 v64, v64, v66
	v_cvt_pk_bf16_f32 v66, v76, v77
	v_lshlrev_b64 v[76:77], 11, v[82:83]
	v_rcp_f32_e32 v56, v56
	v_add_f32_e32 v52, 1.0, v52
	v_rcp_f32_e32 v57, v57
	v_add_f32_e32 v53, 1.0, v53
	v_add_f32_e32 v58, 1.0, v58
	v_add_f32_e32 v59, 1.0, v59
	v_lshl_add_u64 v[76:77], s[36:37], 0, v[76:77]
	v_rcp_f32_e32 v52, v52
	v_rcp_f32_e32 v53, v53
	v_rcp_f32_e32 v58, v58
	v_add_f32_e32 v54, 1.0, v54
	v_rcp_f32_e32 v59, v59
	v_add_f32_e32 v55, 1.0, v55
	v_add_f32_e32 v81, v65, v64
	v_cvt_pk_bf16_f32 v64, v84, v85
	v_cvt_pk_bf16_f32 v65, v86, v87
	v_cvt_pk_bf16_f32 v67, v78, v79
	v_lshl_add_u64 v[76:77], v[76:77], 0, v[132:133]
	v_rcp_f32_e32 v54, v54
	v_rcp_f32_e32 v55, v55
	global_store_dwordx4 v[76:77], v[64:67], off offset:1024
	v_add_f32_e32 v154, v174, v175
	v_add_f32_e32 v134, v134, v154
	s_waitcnt vmcnt(7)
	v_lshlrev_b32_e32 v66, 16, v60
	v_and_b32_e32 v67, 0xffff0000, v60
	v_pk_mul_f32 v[56:57], v[56:57], v[66:67]
	v_lshlrev_b32_e32 v66, 16, v62
	v_and_b32_e32 v67, 0xffff0000, v62
	v_lshlrev_b32_e32 v60, 16, v61
	v_and_b32_e32 v61, 0xffff0000, v61
	v_pk_mul_f32 v[66:67], v[52:53], v[66:67]
	v_pk_mul_f32 v[58:59], v[58:59], v[60:61]
	v_lshlrev_b32_e32 v60, 16, v63
	v_and_b32_e32 v61, 0xffff0000, v63
	v_pk_mul_f32 v[52:53], v[66:67], v[66:67]
	v_pk_mul_f32 v[60:61], v[54:55], v[60:61]
	v_pk_fma_f32 v[52:53], v[56:57], v[56:57], v[52:53]
	v_pk_mul_f32 v[54:55], v[60:61], v[60:61]
	v_add_u32_e32 v64, s82, v169
	v_pk_fma_f32 v[54:55], v[58:59], v[58:59], v[54:55]
	v_add_f32_e32 v52, v52, v53
	v_add_f32_e32 v52, v54, v52
	v_ashrrev_i32_e32 v65, 31, v64
	v_add_f32_e32 v68, v55, v52
	v_cvt_pk_bf16_f32 v52, v56, v57
	v_lshlrev_b64 v[56:57], 11, v[64:65]
	v_lshl_add_u64 v[56:57], s[36:37], 0, v[56:57]
	v_add_f32_e32 v134, v135, v134
	v_cvt_pk_bf16_f32 v53, v58, v59
	v_cvt_pk_bf16_f32 v54, v66, v67
	v_cvt_pk_bf16_f32 v55, v60, v61
	v_lshl_add_u64 v[56:57], v[56:57], 0, v[132:133]
	global_store_dwordx4 v[56:57], v[52:55], off offset:1024
	v_mov_b32_e32 v56, v112
	v_mov_b32_e32 v58, v104
	v_mov_b32_e32 v52, v134
	s_nop 1
	v_permlane16_swap_b32 v52, v134
	v_mov_b32_e32 v54, v120
	v_add_f32_e32 v52, v52, v134
	v_mov_b32_e32 v53, v52
	s_nop 1
	v_permlane32_swap_b32 v53, v52
	s_nop 1
	v_permlane16_swap_b32 v120, v54
	v_mov_b32_e32 v60, v96
	v_add_f32_e32 v54, v120, v54
	v_mov_b32_e32 v55, v54
	s_nop 1
	v_permlane32_swap_b32 v55, v54
	s_nop 1
	v_permlane16_swap_b32 v56, v112
	v_mov_b32_e32 v62, v80
	v_add_f32_e32 v56, v56, v112
	v_mov_b32_e32 v57, v56
	s_nop 1
	v_permlane32_swap_b32 v56, v57
	s_nop 1
	v_permlane16_swap_b32 v58, v104
	v_mov_b32_e32 v64, v81
	v_add_f32_e32 v58, v58, v104
	v_mov_b32_e32 v59, v58
	s_nop 1
	v_permlane32_swap_b32 v59, v58
	s_nop 1
	v_permlane16_swap_b32 v96, v60
	v_mov_b32_e32 v66, v68
	v_add_f32_e32 v60, v96, v60
	v_mov_b32_e32 v61, v60
	s_nop 1
	v_permlane32_swap_b32 v60, v61
	s_nop 1
	v_permlane16_swap_b32 v62, v80
	s_nop 0
	v_add_f32_e32 v62, v62, v80
	v_mov_b32_e32 v63, v62
	s_nop 1
	v_permlane32_swap_b32 v63, v62
	s_nop 1
	v_permlane16_swap_b32 v81, v64
	s_nop 0
	v_add_f32_e32 v64, v81, v64
	v_mov_b32_e32 v65, v64
	s_nop 1
	v_permlane32_swap_b32 v65, v64
	s_nop 1
	v_permlane16_swap_b32 v66, v68
	s_nop 0
	v_add_f32_e32 v66, v66, v68
	v_mov_b32_e32 v67, v66
	s_nop 1
	v_permlane32_swap_b32 v66, v67
	s_and_saveexec_b64 s[0:1], vcc
	s_cbranch_execz .LBB0_1085
	v_add_f32_e32 v54, v55, v54
	v_add_f32_e32 v55, v53, v52
	v_lshl_add_u32 v52, v169, 2, s83
	v_add_f32_e32 v56, v56, v57
	v_add_u32_e32 v57, 0x1000, v52
	ds_read2_b32 v[52:53], v57 offset1:16
	v_add_f32_e32 v58, v59, v58
	v_add_f32_e32 v62, v63, v62
	v_add_f32_e32 v60, v60, v61
	v_add_f32_e32 v66, v66, v67
	s_waitcnt lgkmcnt(0)
	v_add_f32_e32 v52, v55, v52
	v_add_f32_e32 v53, v54, v53
	ds_write2_b32 v57, v52, v53 offset1:16
	ds_read2_b32 v[52:53], v57 offset0:32 offset1:48
	v_add_f32_e32 v64, v65, v64
	s_waitcnt lgkmcnt(0)
	v_add_f32_e32 v52, v56, v52
	v_add_f32_e32 v53, v58, v53
	ds_write2_b32 v57, v52, v53 offset0:32 offset1:48
	ds_read2_b32 v[52:53], v57 offset0:64 offset1:80
	s_waitcnt lgkmcnt(0)
	v_add_f32_e32 v52, v60, v52
	v_add_f32_e32 v53, v62, v53
	ds_write2_b32 v57, v52, v53 offset0:64 offset1:80
	ds_read2_b32 v[52:53], v57 offset0:96 offset1:112
	s_waitcnt lgkmcnt(0)
	v_add_f32_e32 v52, v64, v52
	v_add_f32_e32 v53, v66, v53
	ds_write2_b32 v57, v52, v53 offset0:96 offset1:112
	s_branch .LBB0_1085

.LBB0_1100:
	s_or_b64 exec, exec, s[0:1]
	v_mov_b32_e32 v3, v0
	s_waitcnt lgkmcnt(0)
	s_barrier
	s_lshl_b64 s[60:61], s[58:59], 11
	s_add_u32 s0, s36, s60
	s_waitcnt vmcnt(8)
	v_ashrrev_i32_e32 v4, 4, v3
	v_lshlrev_b32_e32 v5, 3, v3
	v_and_b32_e32 v157, 0x78, v5
	v_ashrrev_i32_e32 v5, 31, v4
	s_addc_u32 s1, s37, s61
	v_lshlrev_b64 v[6:7], 11, v[4:5]
	v_lshl_add_u64 v[148:149], s[0:1], 0, v[6:7]
	s_mov_b64 s[0:1], 0x10000
	v_lshl_add_u64 v[150:151], v[148:149], 0, s[0:1]
	s_mov_b64 s[0:1], 0x20000
	v_lshl_add_u64 v[152:153], v[148:149], 0, s[0:1]
	s_mov_b64 s[0:1], 0x30000
	v_lshl_add_u64 v[154:155], v[148:149], 0, s[0:1]
	v_readfirstlane_b32 s0, v3
	s_ashr_i32 s12, s0, 6
	s_cmp_lt_i32 s12, 8
	s_cselect_b64 s[62:63], -1, 0
	s_and_b64 s[0:1], s[62:63], exec
	s_cselect_b32 s0, s12, 7
	s_ashr_i32 s1, s0, 31
	s_lshl_b64 s[0:1], s[0:1], 16
	v_readlane_b32 s34, v248, 27
	v_and_b32_e32 v5, 63, v3
	s_add_u32 s0, s72, s0
	s_waitcnt vmcnt(2)
	v_mov_b32_e32 v23, v2
	v_readlane_b32 s35, v248, 28
	v_lshlrev_b32_e32 v12, 8, v4
	v_xor_b32_e32 v4, v4, v3
	v_lshlrev_b32_e32 v22, 4, v5
	s_addc_u32 s1, s73, s1
	v_lshlrev_b32_e32 v6, 1, v157
	v_mov_b32_e32 v7, v2
	s_mov_b32 s35, s21
	v_and_b32_e32 v177, 15, v3
	v_bfe_u32 v178, v3, 4, 2
	v_lshlrev_b32_e32 v4, 4, v4
	s_movk_i32 s84, 0xf0
	v_lshl_add_u64 v[158:159], s[0:1], 0, v[22:23]
	v_lshl_add_u64 v[8:9], v[148:149], 0, v[6:7]
	v_lshl_add_u64 v[10:11], v[150:151], 0, v[6:7]
	v_lshl_add_u64 v[20:21], v[152:153], 0, v[6:7]
	v_lshl_add_u64 v[6:7], v[154:155], 0, v[6:7]
	v_bitop3_b32 v5, v178, v177, 4 bitop3:0x36
	v_bitop3_b32 v13, v178, v177, 8 bitop3:0x36
	v_bitop3_b32 v14, v178, v177, 12 bitop3:0x36
	v_and_or_b32 v4, v4, s84, v12
	s_waitcnt vmcnt(0)
	v_lshl_add_u64 v[32:33], v[158:159], 0, s[34:35]
	global_load_dwordx4 v[52:55], v[8:9], off
	global_load_dwordx4 v[64:67], v[6:7], off
	global_load_dwordx4 v[56:59], v[10:11], off
	global_load_dwordx4 v[16:19], v[8:9], off offset:256
	global_load_dwordx4 v[60:63], v[20:21], off
	v_lshlrev_b32_e32 v69, 4, v5
	v_lshlrev_b32_e32 v70, 4, v13
	v_lshlrev_b32_e32 v71, 4, v14
	v_add_u32_e32 v179, 0, v4
	global_load_dwordx4 v[12:15], v[10:11], off offset:256
	s_nop 0
	global_load_dwordx4 v[8:11], v[20:21], off offset:256
	s_nop 0
	global_load_dwordx4 v[4:7], v[6:7], off offset:256
	s_nop 0
	global_load_dwordx4 v[36:39], v[32:33], off sc0
	global_load_dwordx4 v[28:31], v[32:33], off offset:1024 sc0
	global_load_dwordx4 v[24:27], v[32:33], off offset:2048 sc0
	global_load_dwordx4 v[20:23], v[32:33], off offset:3072 sc0
	v_add_co_u32_e32 v32, vcc, s14, v32
	v_bitop3_b32 v3, v178, v3, 15 bitop3:0x78
	s_nop 0
	v_addc_co_u32_e32 v33, vcc, 0, v33, vcc
	global_load_dwordx4 v[48:51], v[32:33], off sc0
	global_load_dwordx4 v[44:47], v[32:33], off offset:1024 sc0
	global_load_dwordx4 v[40:43], v[32:33], off offset:2048 sc0
	s_nop 0
	global_load_dwordx4 v[32:35], v[32:33], off offset:3072 sc0
	s_lshl_b32 s64, s12, 5
	s_lshl_b32 s12, s12, 9
	v_lshl_add_u32 v68, v177, 8, 0
	v_lshlrev_b32_e32 v3, 4, v3
	s_add_i32 s20, s12, 0
	s_mov_b32 s0, s34
	s_mov_b32 s66, 1
	s_mov_b32 s67, 0
	s_ashr_i32 s65, s64, 31
	v_writelane_b32 v248, s0, 27
	s_add_i32 s20, s20, 0x20000
	s_mov_b32 s76, 2
	s_mov_b32 s59, -2
	v_add_u32_e32 v180, v68, v3
	v_add_u32_e32 v181, v68, v69
	s_waitcnt vmcnt(15)
	ds_write_b128 v179, v[52:55]
	s_waitcnt vmcnt(13)
	ds_write_b128 v179, v[56:59] offset:8192
	s_waitcnt vmcnt(11)
	ds_write_b128 v179, v[60:63] offset:16384
	ds_write_b128 v179, v[64:67] offset:24576
	v_mov_b32_e32 v52, 0
	v_add_u32_e32 v182, v68, v70
	v_add_u32_e32 v183, v68, v71
	s_mov_b32 s75, 0
	s_mov_b32 s39, 0
	v_mov_b32_e32 v53, v52
	v_mov_b32_e32 v54, v52
	v_mov_b32_e32 v55, v52
	v_mov_b32_e32 v56, v52
	v_mov_b32_e32 v57, v52
	v_mov_b32_e32 v58, v52
	v_mov_b32_e32 v59, v52
	v_mov_b32_e32 v60, v52
	v_mov_b32_e32 v61, v52
	v_mov_b32_e32 v62, v52
	v_mov_b32_e32 v63, v52
	v_mov_b32_e32 v64, v52
	v_mov_b32_e32 v65, v52
	v_mov_b32_e32 v66, v52
	v_mov_b32_e32 v67, v52
	v_mov_b32_e32 v68, v52
	v_mov_b32_e32 v69, v52
	v_mov_b32_e32 v70, v52
	v_mov_b32_e32 v71, v52
	v_mov_b32_e32 v72, v52
	v_mov_b32_e32 v73, v52
	v_mov_b32_e32 v74, v52
	v_mov_b32_e32 v75, v52
	v_mov_b32_e32 v76, v52
	v_mov_b32_e32 v77, v52
	v_mov_b32_e32 v78, v52
	v_mov_b32_e32 v79, v52
	v_mov_b32_e32 v80, v52
	v_mov_b32_e32 v81, v52
	v_mov_b32_e32 v82, v52
	v_mov_b32_e32 v83, v52
	v_mov_b32_e32 v84, v52
	v_mov_b32_e32 v85, v52
	v_mov_b32_e32 v86, v52
	v_mov_b32_e32 v87, v52
	v_mov_b32_e32 v88, v52
	v_mov_b32_e32 v89, v52
	v_mov_b32_e32 v90, v52
	v_mov_b32_e32 v91, v52
	v_mov_b32_e32 v104, v52
	v_mov_b32_e32 v105, v52
	v_mov_b32_e32 v106, v52
	v_mov_b32_e32 v107, v52
	v_mov_b32_e32 v108, v52
	v_mov_b32_e32 v109, v52
	v_mov_b32_e32 v110, v52
	v_mov_b32_e32 v111, v52
	v_mov_b32_e32 v112, v52
	v_mov_b32_e32 v113, v52
	v_mov_b32_e32 v114, v52
	v_mov_b32_e32 v115, v52
	v_mov_b32_e32 v116, v52
	v_mov_b32_e32 v117, v52
	v_mov_b32_e32 v118, v52
	v_mov_b32_e32 v119, v52
	v_mov_b32_e32 v120, v52
	v_mov_b32_e32 v121, v52
	v_mov_b32_e32 v122, v52
	v_mov_b32_e32 v123, v52
	v_mov_b32_e32 v124, v52
	v_mov_b32_e32 v125, v52
	v_mov_b32_e32 v126, v52
	v_mov_b32_e32 v127, v52
	v_writelane_b32 v248, s1, 28
	s_waitcnt lgkmcnt(0)
	s_barrier
	s_branch .LBB0_1104

.LBB0_1108:
	s_lshl_b32 s0, s76, 7
	s_add_i32 s1, s0, 0xfffffc00
	s_cmp_gt_i32 s76, 7
	s_cselect_b32 s0, s1, s0
	v_or_b32_e32 v92, s0, v157
	s_add_i32 s0, s67, s23
	s_add_i32 s1, s0, -4
	s_cmp_gt_i32 s0, 3
	s_cselect_b32 s0, s1, s0
	s_lshl_b32 s12, s66, 2
	ds_read_b128 v[100:103], v180
	ds_read_b128 v[128:131], v180 offset:4096
	ds_read_b128 v[132:135], v180 offset:8192
	ds_read_b128 v[136:139], v180 offset:12288
	ds_read_b128 v[140:143], v180 offset:16384
	ds_read_b128 v[144:147], v180 offset:20480
	ds_read_b128 v[160:163], v180 offset:24576
	ds_read_b128 v[164:167], v180 offset:28672
	s_ashr_i32 s1, s0, 31
	s_sub_i32 s38, s12, 32
	s_cmp_gt_i32 s66, 7
	s_cselect_b32 s66, s38, s12
	s_ashr_i32 s67, s66, 31
	s_lshl_b64 s[0:1], s[0:1], 19
	v_ashrrev_i32_e32 v93, 31, v92
	v_lshl_add_u64 v[94:95], v[158:159], 0, s[0:1]
	s_lshl_b64 s[0:1], s[66:67], 10
	v_lshlrev_b64 v[92:93], 1, v[92:93]
	v_lshl_add_u64 v[192:193], v[94:95], 0, s[0:1]
	v_lshl_add_u64 v[184:185], v[152:153], 0, v[92:93]
	v_lshl_add_u64 v[186:187], v[154:155], 0, v[92:93]
	v_lshl_add_u64 v[94:95], v[148:149], 0, v[92:93]
	v_lshl_add_u64 v[92:93], v[150:151], 0, v[92:93]
	global_load_dwordx4 v[96:99], v[94:95], off
	s_nop 0
	global_load_dwordx4 v[92:95], v[92:93], off
	s_waitcnt vmcnt(9) lgkmcnt(7)
	v_mfma_f32_16x16x32_bf16 v[124:127], v[36:39], v[100:103], v[124:127]
	s_waitcnt vmcnt(5)
	v_mfma_f32_16x16x32_bf16 v[100:103], v[48:51], v[100:103], v[120:123]
	s_waitcnt lgkmcnt(6)
	v_mfma_f32_16x16x32_bf16 v[116:119], v[36:39], v[128:131], v[116:119]
	v_mfma_f32_16x16x32_bf16 v[112:115], v[48:51], v[128:131], v[112:115]
	s_waitcnt lgkmcnt(5)
	v_mfma_f32_16x16x32_bf16 v[108:111], v[36:39], v[132:135], v[108:111]
	v_mfma_f32_16x16x32_bf16 v[104:107], v[48:51], v[132:135], v[104:107]
	s_waitcnt lgkmcnt(4)
	v_mfma_f32_16x16x32_bf16 v[120:123], v[36:39], v[136:139], v[88:91]
	v_mfma_f32_16x16x32_bf16 v[128:131], v[48:51], v[136:139], v[84:87]
	ds_read_b128 v[132:135], v181
	ds_read_b128 v[136:139], v181 offset:4096
	ds_read_b128 v[168:171], v181 offset:8192
	ds_read_b128 v[172:175], v181 offset:12288
	global_load_dwordx4 v[88:91], v[184:185], off
	global_load_dwordx4 v[84:87], v[186:187], off
	s_waitcnt lgkmcnt(7)
	v_mfma_f32_16x16x32_bf16 v[80:83], v[36:39], v[140:143], v[80:83]
	v_mfma_f32_16x16x32_bf16 v[76:79], v[48:51], v[140:143], v[76:79]
	s_waitcnt lgkmcnt(6)
	v_mfma_f32_16x16x32_bf16 v[72:75], v[36:39], v[144:147], v[72:75]
	v_mfma_f32_16x16x32_bf16 v[68:71], v[48:51], v[144:147], v[68:71]
	s_waitcnt lgkmcnt(5)
	v_mfma_f32_16x16x32_bf16 v[64:67], v[36:39], v[160:163], v[64:67]
	s_waitcnt lgkmcnt(4)
	v_mfma_f32_16x16x32_bf16 v[56:59], v[36:39], v[164:167], v[56:59]
	v_mfma_f32_16x16x32_bf16 v[52:55], v[48:51], v[164:167], v[52:55]
	v_mfma_f32_16x16x32_bf16 v[140:143], v[48:51], v[160:163], v[60:63]
	ds_read_b128 v[144:147], v181 offset:16384
	ds_read_b128 v[160:163], v181 offset:20480
	ds_read_b128 v[164:167], v181 offset:24576
	ds_read_b128 v[184:187], v181 offset:28672
	v_add_co_u32_e32 v194, vcc, s14, v192
	s_nop 1
	v_addc_co_u32_e32 v195, vcc, 0, v193, vcc
	global_load_dwordx4 v[36:39], v[192:193], off sc0
	global_load_dwordx4 v[48:51], v[194:195], off sc0
	ds_write_b128 v179, v[16:19] offset:32768
	s_waitcnt vmcnt(8) lgkmcnt(8)
	v_mfma_f32_16x16x32_bf16 v[100:103], v[44:47], v[132:135], v[100:103]
	s_waitcnt lgkmcnt(7)
	v_mfma_f32_16x16x32_bf16 v[116:119], v[28:31], v[136:139], v[116:119]
	v_mfma_f32_16x16x32_bf16 v[112:115], v[44:47], v[136:139], v[112:115]
	s_waitcnt lgkmcnt(6)
	v_mfma_f32_16x16x32_bf16 v[108:111], v[28:31], v[168:171], v[108:111]
	v_mfma_f32_16x16x32_bf16 v[104:107], v[44:47], v[168:171], v[104:107]
	s_waitcnt lgkmcnt(5)
	v_mfma_f32_16x16x32_bf16 v[120:123], v[28:31], v[172:175], v[120:123]
	v_mfma_f32_16x16x32_bf16 v[16:19], v[28:31], v[132:135], v[124:127]
	v_mfma_f32_16x16x32_bf16 v[124:127], v[44:47], v[172:175], v[128:131]
	s_nop 2
	ds_read_b128 v[128:131], v182
	ds_read_b128 v[132:135], v182 offset:4096
	ds_read_b128 v[136:139], v182 offset:8192
	ds_read_b128 v[168:171], v182 offset:12288
	global_load_dwordx4 v[60:63], v[192:193], off offset:1024 sc0
	ds_write_b128 v179, v[12:15] offset:40960
	s_waitcnt lgkmcnt(9)
	v_mfma_f32_16x16x32_bf16 v[12:15], v[28:31], v[144:147], v[80:83]
	v_mfma_f32_16x16x32_bf16 v[76:79], v[44:47], v[144:147], v[76:79]
	s_waitcnt lgkmcnt(8)
	v_mfma_f32_16x16x32_bf16 v[72:75], v[28:31], v[160:163], v[72:75]
	v_mfma_f32_16x16x32_bf16 v[68:71], v[44:47], v[160:163], v[68:71]
	s_waitcnt lgkmcnt(7)
	v_mfma_f32_16x16x32_bf16 v[64:67], v[28:31], v[164:167], v[64:67]
	v_mfma_f32_16x16x32_bf16 v[80:83], v[44:47], v[164:167], v[140:143]
	s_waitcnt lgkmcnt(6)
	v_mfma_f32_16x16x32_bf16 v[28:31], v[28:31], v[184:187], v[56:59]
	v_mfma_f32_16x16x32_bf16 v[140:143], v[44:47], v[184:187], v[52:55]
	ds_read_b128 v[144:147], v182 offset:16384
	ds_read_b128 v[160:163], v182 offset:20480
	ds_read_b128 v[164:167], v182 offset:24576
	ds_read_b128 v[172:175], v182 offset:28672
	global_load_dwordx4 v[56:59], v[192:193], off offset:2048 sc0
	global_load_dwordx4 v[44:47], v[194:195], off offset:1024 sc0
	ds_write_b128 v179, v[8:11] offset:49152
	s_waitcnt lgkmcnt(9)
	v_mfma_f32_16x16x32_bf16 v[8:11], v[24:27], v[128:131], v[16:19]
	s_waitcnt vmcnt(10)
	v_mfma_f32_16x16x32_bf16 v[16:19], v[40:43], v[128:131], v[100:103]
	s_waitcnt lgkmcnt(8)
	v_mfma_f32_16x16x32_bf16 v[100:103], v[24:27], v[132:135], v[116:119]
	v_mfma_f32_16x16x32_bf16 v[112:115], v[40:43], v[132:135], v[112:115]
	s_waitcnt lgkmcnt(7)
	v_mfma_f32_16x16x32_bf16 v[108:111], v[24:27], v[136:139], v[108:111]
	v_mfma_f32_16x16x32_bf16 v[104:107], v[40:43], v[136:139], v[104:107]
	s_waitcnt lgkmcnt(6)
	v_mfma_f32_16x16x32_bf16 v[132:135], v[24:27], v[168:171], v[120:123]
	v_mfma_f32_16x16x32_bf16 v[124:127], v[40:43], v[168:171], v[124:127]
	ds_read_b128 v[116:119], v183
	ds_read_b128 v[168:171], v183 offset:4096
	ds_read_b128 v[184:187], v183 offset:8192
	ds_read_b128 v[188:191], v183 offset:12288
	global_load_dwordx4 v[52:55], v[192:193], off offset:3072 sc0
	ds_write_b128 v179, v[4:7] offset:57344
	s_waitcnt lgkmcnt(9)
	v_mfma_f32_16x16x32_bf16 v[12:15], v[24:27], v[144:147], v[12:15]
	v_mfma_f32_16x16x32_bf16 v[76:79], v[40:43], v[144:147], v[76:79]
	s_waitcnt lgkmcnt(8)
	v_mfma_f32_16x16x32_bf16 v[72:75], v[24:27], v[160:163], v[72:75]
	v_mfma_f32_16x16x32_bf16 v[68:71], v[40:43], v[160:163], v[68:71]
	s_waitcnt lgkmcnt(7)
	v_mfma_f32_16x16x32_bf16 v[64:67], v[24:27], v[164:167], v[64:67]
	s_waitcnt lgkmcnt(6)
	v_mfma_f32_16x16x32_bf16 v[24:27], v[24:27], v[172:175], v[28:31]
	v_mfma_f32_16x16x32_bf16 v[144:147], v[40:43], v[164:167], v[80:83]
	v_mfma_f32_16x16x32_bf16 v[140:143], v[40:43], v[172:175], v[140:143]
	s_nop 0
	ds_read_b128 v[28:31], v183 offset:16384
	ds_read_b128 v[160:163], v183 offset:20480
	ds_read_b128 v[164:167], v183 offset:24576
	ds_read_b128 v[172:175], v183 offset:28672
	global_load_dwordx4 v[40:43], v[194:195], off offset:2048 sc0
	s_waitcnt lgkmcnt(8)
	v_mfma_f32_16x16x32_bf16 v[136:139], v[20:23], v[116:119], v[8:11]
	s_waitcnt vmcnt(11)
	v_mfma_f32_16x16x32_bf16 v[128:131], v[32:35], v[116:119], v[16:19]
	s_waitcnt lgkmcnt(7)
	v_mfma_f32_16x16x32_bf16 v[120:123], v[20:23], v[168:171], v[100:103]
	v_mfma_f32_16x16x32_bf16 v[116:119], v[32:35], v[168:171], v[112:115]
	s_waitcnt lgkmcnt(6)
	v_mfma_f32_16x16x32_bf16 v[112:115], v[20:23], v[184:187], v[108:111]
	v_mfma_f32_16x16x32_bf16 v[108:111], v[32:35], v[184:187], v[104:107]
	s_waitcnt lgkmcnt(5)
	v_mfma_f32_16x16x32_bf16 v[104:107], v[20:23], v[188:191], v[132:135]
	v_mfma_f32_16x16x32_bf16 v[6:9], v[32:35], v[188:191], v[124:127]
	global_load_dwordx4 v[100:103], v[194:195], off offset:3072 sc0
	s_waitcnt lgkmcnt(3)
	v_mfma_f32_16x16x32_bf16 v[80:83], v[20:23], v[28:31], v[12:15]
	v_mfma_f32_16x16x32_bf16 v[76:79], v[32:35], v[28:31], v[76:79]
	s_waitcnt lgkmcnt(2)
	v_mfma_f32_16x16x32_bf16 v[72:75], v[20:23], v[160:163], v[72:75]
	v_mfma_f32_16x16x32_bf16 v[68:71], v[32:35], v[160:163], v[68:71]
	s_waitcnt lgkmcnt(1)
	v_mfma_f32_16x16x32_bf16 v[64:67], v[20:23], v[164:167], v[64:67]
	v_mfma_f32_16x16x32_bf16 v[28:31], v[32:35], v[164:167], v[144:147]
	s_waitcnt lgkmcnt(0)
	v_mfma_f32_16x16x32_bf16 v[24:27], v[20:23], v[172:175], v[24:27]
	v_mfma_f32_16x16x32_bf16 v[20:23], v[32:35], v[172:175], v[140:143]
	s_cmp_eq_u32 s39, 3
	s_cselect_b64 s[0:1], -1, 0
	s_and_b64 s[0:1], s[0:1], s[62:63]
	s_andn2_b64 vcc, exec, s[0:1]
	s_cbranch_vccnz .LBB0_1110
	v_mov_b32_e32 v3, v177
	v_mov_b32_e32 v4, v178
	s_nop 0
	v_lshl_add_u32 v3, v3, 2, 0
	v_add_u32_e32 v3, 0x20800, v3
	ds_read2_b32 v[4:5], v3 offset1:16
	ds_read2_b32 v[10:11], v3 offset0:32 offset1:48
	ds_read2_b32 v[12:13], v3 offset0:64 offset1:80
	ds_read2_b32 v[14:15], v3 offset0:96 offset1:112
	s_waitcnt lgkmcnt(3)
	v_pk_mul_f32 v[138:139], v[138:139], v[4:5] op_sel_hi:[1,0]
	v_pk_mul_f32 v[136:137], v[136:137], v[4:5] op_sel_hi:[1,0]
	v_pk_mul_f32 v[130:131], v[130:131], v[4:5] op_sel_hi:[1,0]
	v_pk_mul_f32 v[128:129], v[128:129], v[4:5] op_sel_hi:[1,0]
	v_mov_b32_e32 v4, v5
	v_pk_mul_f32 v[122:123], v[122:123], v[4:5] op_sel_hi:[1,0]
	v_pk_mul_f32 v[120:121], v[120:121], v[4:5] op_sel_hi:[1,0]
	v_pk_mul_f32 v[118:119], v[118:119], v[4:5] op_sel_hi:[1,0]
	v_pk_mul_f32 v[116:117], v[116:117], v[4:5] op_sel_hi:[1,0]
	s_waitcnt lgkmcnt(2)
	v_mov_b32_e32 v4, v11
	v_pk_mul_f32 v[106:107], v[106:107], v[4:5] op_sel_hi:[1,0]
	v_pk_mul_f32 v[104:105], v[104:105], v[4:5] op_sel_hi:[1,0]
	v_pk_mul_f32 v[8:9], v[8:9], v[4:5] op_sel_hi:[1,0]
	v_pk_mul_f32 v[6:7], v[6:7], v[4:5] op_sel_hi:[1,0]
	s_waitcnt lgkmcnt(1)
	v_mov_b32_e32 v4, v13
	v_pk_mul_f32 v[74:75], v[74:75], v[4:5] op_sel_hi:[1,0]
	v_pk_mul_f32 v[72:73], v[72:73], v[4:5] op_sel_hi:[1,0]
	v_pk_mul_f32 v[70:71], v[70:71], v[4:5] op_sel_hi:[1,0]
	v_pk_mul_f32 v[68:69], v[68:69], v[4:5] op_sel_hi:[1,0]
	s_waitcnt lgkmcnt(0)
	v_mov_b32_e32 v4, v15
	v_pk_mul_f32 v[114:115], v[114:115], v[10:11] op_sel_hi:[1,0]
	v_pk_mul_f32 v[112:113], v[112:113], v[10:11] op_sel_hi:[1,0]
	v_pk_mul_f32 v[110:111], v[110:111], v[10:11] op_sel_hi:[1,0]
	v_pk_mul_f32 v[108:109], v[108:109], v[10:11] op_sel_hi:[1,0]
	v_pk_mul_f32 v[82:83], v[82:83], v[12:13] op_sel_hi:[1,0]
	v_pk_mul_f32 v[80:81], v[80:81], v[12:13] op_sel_hi:[1,0]
	v_pk_mul_f32 v[78:79], v[78:79], v[12:13] op_sel_hi:[1,0]
	v_pk_mul_f32 v[76:77], v[76:77], v[12:13] op_sel_hi:[1,0]
	v_pk_mul_f32 v[66:67], v[66:67], v[14:15] op_sel_hi:[1,0]
	v_pk_mul_f32 v[64:65], v[64:65], v[14:15] op_sel_hi:[1,0]
	v_pk_mul_f32 v[30:31], v[30:31], v[14:15] op_sel_hi:[1,0]
	v_pk_mul_f32 v[28:29], v[28:29], v[14:15] op_sel_hi:[1,0]
	v_pk_mul_f32 v[26:27], v[26:27], v[4:5] op_sel_hi:[1,0]
	v_pk_mul_f32 v[24:25], v[24:25], v[4:5] op_sel_hi:[1,0]
	v_pk_mul_f32 v[22:23], v[22:23], v[4:5] op_sel_hi:[1,0]
	v_pk_mul_f32 v[20:21], v[20:21], v[4:5] op_sel_hi:[1,0]

.LBB0_1120:
	s_add_i32 s12, s76, 1
	s_cmp_lg_u32 s12, 8
	s_cselect_b32 s38, s12, 0
	s_lshl_b32 s12, s38, 7
	s_add_i32 s39, s12, 0xfffffc00
	s_cmp_gt_i32 s38, 7
	s_cselect_b32 s12, s39, s12
	v_or_b32_e32 v4, s12, v157
	s_add_i32 s12, s78, s23
	s_add_i32 s39, s12, -4
	s_cmp_gt_i32 s12, 3
	s_cselect_b32 s82, s39, s12
	s_lshl_b32 s12, s77, 2
	ds_read_b128 v[32:35], v180 offset:32768
	ds_read_b128 v[124:127], v180 offset:36864
	ds_read_b128 v[132:135], v180 offset:40960
	ds_read_b128 v[140:143], v180 offset:45056
	ds_read_b128 v[144:147], v180 offset:49152
	ds_read_b128 v[160:163], v180 offset:53248
	ds_read_b128 v[164:167], v180 offset:57344
	ds_read_b128 v[168:171], v180 offset:61440
	s_ashr_i32 s83, s82, 31
	s_sub_i32 s39, s12, 32
	s_cmp_gt_i32 s77, 7
	s_cselect_b32 s76, s39, s12
	s_ashr_i32 s77, s76, 31
	s_lshl_b64 s[82:83], s[82:83], 19
	v_ashrrev_i32_e32 v5, 31, v4
	v_lshl_add_u64 v[10:11], v[158:159], 0, s[82:83]
	s_lshl_b64 s[76:77], s[76:77], 10
	v_lshlrev_b64 v[4:5], 1, v[4:5]
	v_lshl_add_u64 v[196:197], v[10:11], 0, s[76:77]
	v_lshl_add_u64 v[10:11], v[152:153], 0, v[4:5]
	v_lshl_add_u64 v[184:185], v[154:155], 0, v[4:5]
	v_lshl_add_u64 v[12:13], v[148:149], 0, v[4:5]
	v_lshl_add_u64 v[4:5], v[150:151], 0, v[4:5]
	global_load_dwordx4 v[16:19], v[12:13], off
	s_nop 0
	global_load_dwordx4 v[12:15], v[4:5], off
	s_waitcnt vmcnt(9) lgkmcnt(7)
	v_mfma_f32_16x16x32_bf16 v[136:139], v[36:39], v[32:35], v[136:139]
	s_waitcnt vmcnt(8)
	v_mfma_f32_16x16x32_bf16 v[32:35], v[48:51], v[32:35], v[128:131]
	s_waitcnt lgkmcnt(6)
	v_mfma_f32_16x16x32_bf16 v[120:123], v[36:39], v[124:127], v[120:123]
	v_mfma_f32_16x16x32_bf16 v[116:119], v[48:51], v[124:127], v[116:119]
	s_waitcnt lgkmcnt(5)
	v_mfma_f32_16x16x32_bf16 v[112:115], v[36:39], v[132:135], v[112:115]
	v_mfma_f32_16x16x32_bf16 v[108:111], v[48:51], v[132:135], v[108:111]
	s_waitcnt lgkmcnt(4)
	v_mfma_f32_16x16x32_bf16 v[104:107], v[36:39], v[140:143], v[104:107]
	v_mfma_f32_16x16x32_bf16 v[124:127], v[48:51], v[140:143], v[6:9]
	ds_read_b128 v[128:131], v181 offset:32768
	ds_read_b128 v[132:135], v181 offset:36864
	ds_read_b128 v[140:143], v181 offset:40960
	ds_read_b128 v[172:175], v181 offset:45056
	global_load_dwordx4 v[8:11], v[10:11], off
	s_nop 0
	global_load_dwordx4 v[4:7], v[184:185], off
	s_waitcnt lgkmcnt(7)
	v_mfma_f32_16x16x32_bf16 v[80:83], v[36:39], v[144:147], v[80:83]
	v_mfma_f32_16x16x32_bf16 v[76:79], v[48:51], v[144:147], v[76:79]
	s_waitcnt lgkmcnt(6)
	v_mfma_f32_16x16x32_bf16 v[72:75], v[36:39], v[160:163], v[72:75]
	v_mfma_f32_16x16x32_bf16 v[68:71], v[48:51], v[160:163], v[68:71]
	s_waitcnt lgkmcnt(5)
	v_mfma_f32_16x16x32_bf16 v[64:67], v[36:39], v[164:167], v[64:67]
	s_waitcnt lgkmcnt(4)
	v_mfma_f32_16x16x32_bf16 v[24:27], v[36:39], v[168:171], v[24:27]
	v_mfma_f32_16x16x32_bf16 v[20:23], v[48:51], v[168:171], v[20:23]
	v_mfma_f32_16x16x32_bf16 v[144:147], v[48:51], v[164:167], v[28:31]
	ds_read_b128 v[160:163], v181 offset:49152
	ds_read_b128 v[164:167], v181 offset:53248
	ds_read_b128 v[168:171], v181 offset:57344
	ds_read_b128 v[184:187], v181 offset:61440
	v_add_co_u32_e32 v198, vcc, s14, v196
	s_nop 1
	v_addc_co_u32_e32 v199, vcc, 0, v197, vcc
	global_load_dwordx4 v[36:39], v[196:197], off sc0
	global_load_dwordx4 v[48:51], v[198:199], off sc0
	ds_write_b128 v179, v[96:99]
	s_waitcnt vmcnt(9) lgkmcnt(8)
	v_mfma_f32_16x16x32_bf16 v[32:35], v[44:47], v[128:131], v[32:35]
	s_waitcnt lgkmcnt(7)
	v_mfma_f32_16x16x32_bf16 v[120:123], v[60:63], v[132:135], v[120:123]
	v_mfma_f32_16x16x32_bf16 v[116:119], v[44:47], v[132:135], v[116:119]
	s_waitcnt lgkmcnt(6)
	v_mfma_f32_16x16x32_bf16 v[112:115], v[60:63], v[140:143], v[112:115]
	v_mfma_f32_16x16x32_bf16 v[108:111], v[44:47], v[140:143], v[108:111]
	s_waitcnt lgkmcnt(5)
	v_mfma_f32_16x16x32_bf16 v[104:107], v[60:63], v[172:175], v[104:107]
	v_mfma_f32_16x16x32_bf16 v[124:127], v[44:47], v[172:175], v[124:127]
	v_mfma_f32_16x16x32_bf16 v[96:99], v[60:63], v[128:131], v[136:139]
	ds_read_b128 v[128:131], v182 offset:32768
	ds_read_b128 v[132:135], v182 offset:36864
	s_nop 0
	ds_read_b128 v[136:139], v182 offset:40960
	ds_read_b128 v[140:143], v182 offset:45056
	global_load_dwordx4 v[28:31], v[196:197], off offset:1024 sc0
	ds_write_b128 v179, v[92:95] offset:8192
	s_waitcnt lgkmcnt(9)
	v_mfma_f32_16x16x32_bf16 v[80:83], v[60:63], v[160:163], v[80:83]
	v_mfma_f32_16x16x32_bf16 v[76:79], v[44:47], v[160:163], v[76:79]
	s_waitcnt lgkmcnt(8)
	v_mfma_f32_16x16x32_bf16 v[72:75], v[60:63], v[164:167], v[72:75]
	v_mfma_f32_16x16x32_bf16 v[68:71], v[44:47], v[164:167], v[68:71]
	s_waitcnt lgkmcnt(7)
	v_mfma_f32_16x16x32_bf16 v[64:67], v[60:63], v[168:171], v[64:67]
	s_waitcnt lgkmcnt(6)
	v_mfma_f32_16x16x32_bf16 v[60:63], v[60:63], v[184:187], v[24:27]
	v_mfma_f32_16x16x32_bf16 v[92:95], v[44:47], v[168:171], v[144:147]
	v_mfma_f32_16x16x32_bf16 v[144:147], v[44:47], v[184:187], v[20:23]
	ds_read_b128 v[160:163], v182 offset:49152
	ds_read_b128 v[164:167], v182 offset:53248
	ds_read_b128 v[168:171], v182 offset:57344
	ds_read_b128 v[172:175], v182 offset:61440
	global_load_dwordx4 v[24:27], v[196:197], off offset:2048 sc0
	global_load_dwordx4 v[44:47], v[198:199], off offset:1024 sc0
	ds_write_b128 v179, v[88:91] offset:16384
	s_waitcnt lgkmcnt(9)
	v_mfma_f32_16x16x32_bf16 v[88:91], v[56:59], v[128:131], v[96:99]
	s_waitcnt vmcnt(10)
	v_mfma_f32_16x16x32_bf16 v[32:35], v[40:43], v[128:131], v[32:35]
	s_waitcnt lgkmcnt(8)
	v_mfma_f32_16x16x32_bf16 v[96:99], v[56:59], v[132:135], v[120:123]
	v_mfma_f32_16x16x32_bf16 v[128:131], v[40:43], v[132:135], v[116:119]
	s_waitcnt lgkmcnt(7)
	v_mfma_f32_16x16x32_bf16 v[132:135], v[56:59], v[136:139], v[112:115]
	v_mfma_f32_16x16x32_bf16 v[136:139], v[40:43], v[136:139], v[108:111]
	s_waitcnt lgkmcnt(6)
	v_mfma_f32_16x16x32_bf16 v[184:187], v[56:59], v[140:143], v[104:107]
	v_mfma_f32_16x16x32_bf16 v[140:143], v[40:43], v[140:143], v[124:127]
	s_nop 1
	ds_read_b128 v[104:107], v183 offset:32768
	ds_read_b128 v[108:111], v183 offset:36864
	ds_read_b128 v[188:191], v183 offset:40960
	ds_read_b128 v[192:195], v183 offset:45056
	global_load_dwordx4 v[20:23], v[196:197], off offset:3072 sc0
	ds_write_b128 v179, v[84:87] offset:24576
	s_waitcnt lgkmcnt(9)
	v_mfma_f32_16x16x32_bf16 v[80:83], v[56:59], v[160:163], v[80:83]
	v_mfma_f32_16x16x32_bf16 v[76:79], v[40:43], v[160:163], v[76:79]
	s_waitcnt lgkmcnt(8)
	v_mfma_f32_16x16x32_bf16 v[72:75], v[56:59], v[164:167], v[72:75]
	v_mfma_f32_16x16x32_bf16 v[68:71], v[40:43], v[164:167], v[68:71]
	s_waitcnt lgkmcnt(7)
	v_mfma_f32_16x16x32_bf16 v[64:67], v[56:59], v[168:171], v[64:67]
	s_waitcnt lgkmcnt(6)
	v_mfma_f32_16x16x32_bf16 v[56:59], v[56:59], v[172:175], v[60:63]
	v_mfma_f32_16x16x32_bf16 v[92:95], v[40:43], v[168:171], v[92:95]
	v_mfma_f32_16x16x32_bf16 v[144:147], v[40:43], v[172:175], v[144:147]
	s_nop 0
	ds_read_b128 v[60:63], v183 offset:49152
	ds_read_b128 v[160:163], v183 offset:53248
	ds_read_b128 v[164:167], v183 offset:57344
	ds_read_b128 v[168:171], v183 offset:61440
	global_load_dwordx4 v[40:43], v[198:199], off offset:2048 sc0
	s_waitcnt lgkmcnt(8)
	v_mfma_f32_16x16x32_bf16 v[124:127], v[52:55], v[104:107], v[88:91]
	s_waitcnt vmcnt(11)
	v_mfma_f32_16x16x32_bf16 v[120:123], v[100:103], v[104:107], v[32:35]
	s_waitcnt lgkmcnt(7)
	v_mfma_f32_16x16x32_bf16 v[116:119], v[52:55], v[108:111], v[96:99]
	v_mfma_f32_16x16x32_bf16 v[112:115], v[100:103], v[108:111], v[128:131]
	s_waitcnt lgkmcnt(6)
	v_mfma_f32_16x16x32_bf16 v[108:111], v[52:55], v[188:191], v[132:135]
	v_mfma_f32_16x16x32_bf16 v[104:107], v[100:103], v[188:191], v[136:139]
	s_waitcnt lgkmcnt(5)
	v_mfma_f32_16x16x32_bf16 v[88:91], v[52:55], v[192:195], v[184:187]
	v_mfma_f32_16x16x32_bf16 v[84:87], v[100:103], v[192:195], v[140:143]
	global_load_dwordx4 v[32:35], v[198:199], off offset:3072 sc0
	s_waitcnt lgkmcnt(3)
	v_mfma_f32_16x16x32_bf16 v[80:83], v[52:55], v[60:63], v[80:83]
	v_mfma_f32_16x16x32_bf16 v[76:79], v[100:103], v[60:63], v[76:79]
	s_waitcnt lgkmcnt(2)
	v_mfma_f32_16x16x32_bf16 v[72:75], v[52:55], v[160:163], v[72:75]
	v_mfma_f32_16x16x32_bf16 v[68:71], v[100:103], v[160:163], v[68:71]
	s_waitcnt lgkmcnt(1)
	v_mfma_f32_16x16x32_bf16 v[64:67], v[52:55], v[164:167], v[64:67]
	v_mfma_f32_16x16x32_bf16 v[60:63], v[100:103], v[164:167], v[92:95]
	s_waitcnt lgkmcnt(0)
	v_mfma_f32_16x16x32_bf16 v[56:59], v[52:55], v[168:171], v[56:59]
	v_mfma_f32_16x16x32_bf16 v[52:55], v[100:103], v[168:171], v[144:147]
	s_cmp_eq_u32 s79, 3
	s_cselect_b64 s[76:77], -1, 0
	s_and_b64 s[76:77], s[76:77], s[62:63]
	s_andn2_b64 vcc, exec, s[76:77]
	s_cbranch_vccnz .LBB0_1122
	v_mov_b32_e32 v3, v177
	v_mov_b32_e32 v92, v178
	s_nop 0
	v_lshl_add_u32 v3, v3, 2, 0
	v_add_u32_e32 v3, 0x20800, v3
	ds_read2_b32 v[92:93], v3 offset1:16
	ds_read2_b32 v[94:95], v3 offset0:32 offset1:48
	ds_read2_b32 v[96:97], v3 offset0:64 offset1:80
	ds_read2_b32 v[98:99], v3 offset0:96 offset1:112
	s_waitcnt lgkmcnt(3)
	v_pk_mul_f32 v[126:127], v[126:127], v[92:93] op_sel_hi:[1,0]
	v_pk_mul_f32 v[124:125], v[124:125], v[92:93] op_sel_hi:[1,0]
	v_pk_mul_f32 v[122:123], v[122:123], v[92:93] op_sel_hi:[1,0]
	v_pk_mul_f32 v[120:121], v[120:121], v[92:93] op_sel_hi:[1,0]
	v_mov_b32_e32 v92, v93
	v_pk_mul_f32 v[118:119], v[118:119], v[92:93] op_sel_hi:[1,0]
	v_pk_mul_f32 v[116:117], v[116:117], v[92:93] op_sel_hi:[1,0]
	v_pk_mul_f32 v[114:115], v[114:115], v[92:93] op_sel_hi:[1,0]
	v_pk_mul_f32 v[112:113], v[112:113], v[92:93] op_sel_hi:[1,0]
	s_waitcnt lgkmcnt(2)
	v_mov_b32_e32 v92, v95
	v_pk_mul_f32 v[90:91], v[90:91], v[92:93] op_sel_hi:[1,0]
	v_pk_mul_f32 v[88:89], v[88:89], v[92:93] op_sel_hi:[1,0]
	v_pk_mul_f32 v[86:87], v[86:87], v[92:93] op_sel_hi:[1,0]
	v_pk_mul_f32 v[84:85], v[84:85], v[92:93] op_sel_hi:[1,0]
	s_waitcnt lgkmcnt(1)
	v_mov_b32_e32 v92, v97
	v_pk_mul_f32 v[74:75], v[74:75], v[92:93] op_sel_hi:[1,0]
	v_pk_mul_f32 v[72:73], v[72:73], v[92:93] op_sel_hi:[1,0]
	v_pk_mul_f32 v[70:71], v[70:71], v[92:93] op_sel_hi:[1,0]
	v_pk_mul_f32 v[68:69], v[68:69], v[92:93] op_sel_hi:[1,0]
	s_waitcnt lgkmcnt(0)
	v_mov_b32_e32 v92, v99
	v_pk_mul_f32 v[110:111], v[110:111], v[94:95] op_sel_hi:[1,0]
	v_pk_mul_f32 v[108:109], v[108:109], v[94:95] op_sel_hi:[1,0]
	v_pk_mul_f32 v[106:107], v[106:107], v[94:95] op_sel_hi:[1,0]
	v_pk_mul_f32 v[104:105], v[104:105], v[94:95] op_sel_hi:[1,0]
	v_pk_mul_f32 v[82:83], v[82:83], v[96:97] op_sel_hi:[1,0]
	v_pk_mul_f32 v[80:81], v[80:81], v[96:97] op_sel_hi:[1,0]
	v_pk_mul_f32 v[78:79], v[78:79], v[96:97] op_sel_hi:[1,0]
	v_pk_mul_f32 v[76:77], v[76:77], v[96:97] op_sel_hi:[1,0]
	v_pk_mul_f32 v[66:67], v[66:67], v[98:99] op_sel_hi:[1,0]
	v_pk_mul_f32 v[64:65], v[64:65], v[98:99] op_sel_hi:[1,0]
	v_pk_mul_f32 v[62:63], v[62:63], v[98:99] op_sel_hi:[1,0]
	v_pk_mul_f32 v[60:61], v[60:61], v[98:99] op_sel_hi:[1,0]
	v_pk_mul_f32 v[58:59], v[58:59], v[92:93] op_sel_hi:[1,0]
	v_pk_mul_f32 v[56:57], v[56:57], v[92:93] op_sel_hi:[1,0]
	v_pk_mul_f32 v[54:55], v[54:55], v[92:93] op_sel_hi:[1,0]
	v_pk_mul_f32 v[52:53], v[52:53], v[92:93] op_sel_hi:[1,0]
.LBB0_1122:
	s_add_i32 s39, s79, 1
	s_cmp_lg_u32 s39, 8
	s_cbranch_scc1 .LBB0_1103
	s_and_b64 vcc, exec, s[0:1]
	s_cbranch_vccnz .LBB0_1102
	s_add_i32 s0, s75, s23
	v_mov_b32_e32 v184, v178
	v_mov_b32_e32 v3, v177
	s_lshl_b32 s1, s0, 8
	s_add_i32 s12, s1, 0xfffffc00
	v_add_u32_e32 v92, s58, v3
	s_cmp_gt_i32 s0, 3
	v_ashrrev_i32_e32 v93, 31, v92
	v_lshlrev_b64 v[92:93], 11, v[92:93]
	s_cselect_b32 s0, s12, s1
	v_lshl_add_u64 v[92:93], s[6:7], 0, v[92:93]
	s_ashr_i32 s1, s0, 31
	v_lshl_add_u64 v[92:93], s[0:1], 1, v[92:93]
	v_lshlrev_b32_e32 v94, 3, v184
	v_lshl_add_u64 v[92:93], s[64:65], 1, v[92:93]
	v_ashrrev_i32_e32 v95, 31, v94
	v_lshl_add_u64 v[190:191], v[94:95], 1, v[92:93]
	global_load_dwordx4 v[186:189], v[190:191], off
	v_add_co_u32_e32 v172, vcc, s14, v190
	s_mov_b32 s0, 0x20000
	s_nop 0
	v_addc_co_u32_e32 v173, vcc, 0, v191, vcc
	global_load_dwordx4 v[140:143], v[172:173], off
	v_add_co_u32_e32 v170, vcc, s15, v190
	v_lshl_add_u32 v164, v3, 2, 0
	s_nop 0
	v_addc_co_u32_e32 v171, vcc, 0, v191, vcc
	global_load_dwordx4 v[136:139], v[170:171], off
	v_add_co_u32_e32 v166, vcc, s3, v190
	v_add_u32_e32 v164, 0x20400, v164
	s_nop 0
	v_addc_co_u32_e32 v167, vcc, 0, v191, vcc
	global_load_dwordx4 v[132:135], v[166:167], off
	v_add_co_u32_e32 v162, vcc, s0, v190
	s_mov_b32 s0, 0x28000
	s_nop 0
	v_addc_co_u32_e32 v163, vcc, 0, v191, vcc
	global_load_dwordx4 v[128:131], v[162:163], off
	v_add_co_u32_e32 v160, vcc, s0, v190
	s_mov_b32 s0, 0x30000
	s_nop 0
	v_addc_co_u32_e32 v161, vcc, 0, v191, vcc
	global_load_dwordx4 v[100:103], v[160:161], off
	v_add_co_u32_e32 v146, vcc, s0, v190
	s_mov_b32 s0, 0x38000
	s_nop 0
	v_addc_co_u32_e32 v147, vcc, 0, v191, vcc
	global_load_dwordx4 v[96:99], v[146:147], off
	v_add_co_u32_e32 v144, vcc, s0, v190
	s_waitcnt vmcnt(6)
	v_lshlrev_b32_e32 v194, 16, v186
	v_addc_co_u32_e32 v145, vcc, 0, v191, vcc
	global_load_dwordx4 v[92:95], v[144:145], off sc0
	ds_read2_b32 v[192:193], v164 offset1:16
	ds_read2_b32 v[174:175], v164 offset0:32 offset1:48
	ds_read2_b32 v[168:169], v164 offset0:64 offset1:80
	ds_read2_b32 v[164:165], v164 offset0:96 offset1:112
	v_and_b32_e32 v195, 0xffff0000, v186
	v_lshlrev_b32_e32 v186, 16, v187
	v_and_b32_e32 v187, 0xffff0000, v187
	s_waitcnt lgkmcnt(3)
	v_pk_fma_f32 v[126:127], v[126:127], v[192:193], v[186:187] op_sel_hi:[1,0,1]
	v_pk_fma_f32 v[124:125], v[124:125], v[192:193], v[194:195] op_sel_hi:[1,0,1]
	v_lshlrev_b32_e32 v186, 16, v188
	v_and_b32_e32 v187, 0xffff0000, v188
	v_lshlrev_b32_e32 v188, 16, v189
	v_and_b32_e32 v189, 0xffff0000, v189
	v_pk_fma_f32 v[188:189], v[122:123], v[192:193], v[188:189] op_sel_hi:[1,0,1]
	v_pk_fma_f32 v[186:187], v[120:121], v[192:193], v[186:187] op_sel_hi:[1,0,1]
	v_mul_f32_e32 v120, v125, v125
	v_fmac_f32_e32 v120, v124, v124
	v_cvt_pk_bf16_f32 v122, v124, v125
	v_cvt_pk_bf16_f32 v123, v126, v127
	v_cvt_pk_bf16_f32 v124, v186, v187
	v_cvt_pk_bf16_f32 v125, v188, v189
	v_fmac_f32_e32 v120, v126, v126
	global_store_dwordx4 v[190:191], v[122:125], off
	v_mov_b32_e32 v126, v193
	v_mul_f32_e32 v121, v187, v187
	s_waitcnt vmcnt(7)
	v_lshlrev_b32_e32 v122, 16, v140
	v_and_b32_e32 v123, 0xffff0000, v140
	v_lshlrev_b32_e32 v124, 16, v141
	v_and_b32_e32 v125, 0xffff0000, v141
	v_pk_fma_f32 v[118:119], v[118:119], v[126:127], v[124:125] op_sel_hi:[1,0,1]
	v_pk_fma_f32 v[116:117], v[116:117], v[126:127], v[122:123] op_sel_hi:[1,0,1]
	v_lshlrev_b32_e32 v122, 16, v142
	v_and_b32_e32 v123, 0xffff0000, v142
	v_lshlrev_b32_e32 v124, 16, v143
	v_and_b32_e32 v125, 0xffff0000, v143
	v_pk_fma_f32 v[124:125], v[114:115], v[126:127], v[124:125] op_sel_hi:[1,0,1]
	v_pk_fma_f32 v[114:115], v[112:113], v[126:127], v[122:123] op_sel_hi:[1,0,1]
	v_mul_f32_e32 v112, v117, v117
	v_mul_f32_e32 v113, v115, v115
	v_fmac_f32_e32 v121, v186, v186
	v_fmac_f32_e32 v112, v116, v116
	v_fmac_f32_e32 v113, v114, v114
	v_fmac_f32_e32 v121, v188, v188
	v_fmac_f32_e32 v112, v118, v118
	v_fmac_f32_e32 v113, v124, v124
	v_fmac_f32_e32 v120, v127, v127
	v_fmac_f32_e32 v121, v189, v189
	v_fmac_f32_e32 v112, v119, v119
	v_fmac_f32_e32 v113, v125, v125
	v_add_f32_e32 v120, v120, v121
	v_add_f32_e32 v121, v112, v113
	v_cvt_pk_bf16_f32 v112, v116, v117
	v_cvt_pk_bf16_f32 v113, v118, v119
	v_cvt_pk_bf16_f32 v114, v114, v115
	v_cvt_pk_bf16_f32 v115, v124, v125
	global_store_dwordx4 v[172:173], v[112:115], off
	v_cmp_eq_u32_e32 vcc, 0, v184
	s_waitcnt vmcnt(7)
	v_lshlrev_b32_e32 v112, 16, v136
	v_and_b32_e32 v113, 0xffff0000, v136
	v_lshlrev_b32_e32 v114, 16, v137
	v_and_b32_e32 v115, 0xffff0000, v137
	s_waitcnt lgkmcnt(2)
	v_pk_fma_f32 v[110:111], v[110:111], v[174:175], v[114:115] op_sel_hi:[1,0,1]
	v_pk_fma_f32 v[108:109], v[108:109], v[174:175], v[112:113] op_sel_hi:[1,0,1]
	v_lshlrev_b32_e32 v112, 16, v138
	v_and_b32_e32 v113, 0xffff0000, v138
	v_lshlrev_b32_e32 v114, 16, v139
	v_and_b32_e32 v115, 0xffff0000, v139
	v_pk_fma_f32 v[114:115], v[106:107], v[174:175], v[114:115] op_sel_hi:[1,0,1]
	v_pk_fma_f32 v[106:107], v[104:105], v[174:175], v[112:113] op_sel_hi:[1,0,1]
	v_mul_f32_e32 v104, v109, v109
	v_mul_f32_e32 v105, v107, v107
	v_fmac_f32_e32 v104, v108, v108
	v_fmac_f32_e32 v105, v106, v106
	v_fmac_f32_e32 v104, v110, v110
	v_fmac_f32_e32 v105, v114, v114
	v_fmac_f32_e32 v104, v111, v111
	v_fmac_f32_e32 v105, v115, v115
	v_add_f32_e32 v112, v104, v105
	v_cvt_pk_bf16_f32 v104, v108, v109
	v_cvt_pk_bf16_f32 v105, v110, v111
	v_cvt_pk_bf16_f32 v106, v106, v107
	v_cvt_pk_bf16_f32 v107, v114, v115
	global_store_dwordx4 v[170:171], v[104:107], off
	v_mov_b32_e32 v108, v175
	s_waitcnt vmcnt(7)
	v_lshlrev_b32_e32 v104, 16, v132
	v_and_b32_e32 v105, 0xffff0000, v132
	v_lshlrev_b32_e32 v106, 16, v133
	v_and_b32_e32 v107, 0xffff0000, v133
	v_pk_fma_f32 v[90:91], v[90:91], v[108:109], v[106:107] op_sel_hi:[1,0,1]
	v_pk_fma_f32 v[88:89], v[88:89], v[108:109], v[104:105] op_sel_hi:[1,0,1]
	v_lshlrev_b32_e32 v104, 16, v134
	v_and_b32_e32 v105, 0xffff0000, v134
	v_lshlrev_b32_e32 v106, 16, v135
	v_and_b32_e32 v107, 0xffff0000, v135
	v_pk_fma_f32 v[106:107], v[86:87], v[108:109], v[106:107] op_sel_hi:[1,0,1]
	v_pk_fma_f32 v[86:87], v[84:85], v[108:109], v[104:105] op_sel_hi:[1,0,1]
	v_mul_f32_e32 v84, v89, v89
	v_mul_f32_e32 v85, v87, v87
	v_fmac_f32_e32 v84, v88, v88
	v_fmac_f32_e32 v85, v86, v86
	v_fmac_f32_e32 v84, v90, v90
	v_fmac_f32_e32 v85, v106, v106
	v_fmac_f32_e32 v84, v91, v91
	v_fmac_f32_e32 v85, v107, v107
	v_add_f32_e32 v104, v84, v85
	v_cvt_pk_bf16_f32 v84, v88, v89
	v_cvt_pk_bf16_f32 v85, v90, v91
	v_cvt_pk_bf16_f32 v86, v86, v87
	v_cvt_pk_bf16_f32 v87, v106, v107
	global_store_dwordx4 v[166:167], v[84:87], off
	s_waitcnt vmcnt(7)
	s_nop 0
	v_lshlrev_b32_e32 v84, 16, v128
	v_and_b32_e32 v85, 0xffff0000, v128
	v_lshlrev_b32_e32 v86, 16, v129
	v_and_b32_e32 v87, 0xffff0000, v129
	s_waitcnt lgkmcnt(1)
	v_pk_fma_f32 v[82:83], v[82:83], v[168:169], v[86:87] op_sel_hi:[1,0,1]
	v_pk_fma_f32 v[80:81], v[80:81], v[168:169], v[84:85] op_sel_hi:[1,0,1]
	v_lshlrev_b32_e32 v84, 16, v130
	v_and_b32_e32 v85, 0xffff0000, v130
	v_lshlrev_b32_e32 v86, 16, v131
	v_and_b32_e32 v87, 0xffff0000, v131
	v_pk_fma_f32 v[86:87], v[78:79], v[168:169], v[86:87] op_sel_hi:[1,0,1]
	v_pk_fma_f32 v[78:79], v[76:77], v[168:169], v[84:85] op_sel_hi:[1,0,1]
	v_mul_f32_e32 v76, v81, v81
	v_mul_f32_e32 v77, v79, v79
	v_fmac_f32_e32 v76, v80, v80
	v_fmac_f32_e32 v77, v78, v78
	v_fmac_f32_e32 v76, v82, v82
	v_fmac_f32_e32 v77, v86, v86
	v_fmac_f32_e32 v76, v83, v83
	v_fmac_f32_e32 v77, v87, v87
	v_add_f32_e32 v84, v76, v77
	v_cvt_pk_bf16_f32 v76, v80, v81
	v_cvt_pk_bf16_f32 v77, v82, v83
	v_cvt_pk_bf16_f32 v78, v78, v79
	v_cvt_pk_bf16_f32 v79, v86, v87
	global_store_dwordx4 v[162:163], v[76:79], off
	v_mov_b32_e32 v80, v169
	s_waitcnt vmcnt(7)
	v_lshlrev_b32_e32 v76, 16, v100
	v_and_b32_e32 v77, 0xffff0000, v100
	v_lshlrev_b32_e32 v78, 16, v101
	v_and_b32_e32 v79, 0xffff0000, v101
	v_pk_fma_f32 v[74:75], v[74:75], v[80:81], v[78:79] op_sel_hi:[1,0,1]
	v_pk_fma_f32 v[72:73], v[72:73], v[80:81], v[76:77] op_sel_hi:[1,0,1]
	v_lshlrev_b32_e32 v76, 16, v102
	v_and_b32_e32 v77, 0xffff0000, v102
	v_lshlrev_b32_e32 v78, 16, v103
	v_and_b32_e32 v79, 0xffff0000, v103
	v_pk_fma_f32 v[78:79], v[70:71], v[80:81], v[78:79] op_sel_hi:[1,0,1]
	v_pk_fma_f32 v[70:71], v[68:69], v[80:81], v[76:77] op_sel_hi:[1,0,1]
	v_mul_f32_e32 v68, v73, v73
	v_mul_f32_e32 v69, v71, v71
	v_fmac_f32_e32 v68, v72, v72
	v_fmac_f32_e32 v69, v70, v70
	v_fmac_f32_e32 v68, v74, v74
	v_fmac_f32_e32 v69, v78, v78
	v_fmac_f32_e32 v68, v75, v75
	v_fmac_f32_e32 v69, v79, v79
	v_add_f32_e32 v76, v68, v69
	v_cvt_pk_bf16_f32 v68, v72, v73
	v_cvt_pk_bf16_f32 v69, v74, v75
	v_cvt_pk_bf16_f32 v70, v70, v71
	v_cvt_pk_bf16_f32 v71, v78, v79
	global_store_dwordx4 v[160:161], v[68:71], off
	s_waitcnt vmcnt(7)
	s_nop 0
	v_lshlrev_b32_e32 v68, 16, v96
	v_and_b32_e32 v69, 0xffff0000, v96
	v_lshlrev_b32_e32 v70, 16, v97
	v_and_b32_e32 v71, 0xffff0000, v97
	s_waitcnt lgkmcnt(0)
	v_pk_fma_f32 v[66:67], v[66:67], v[164:165], v[70:71] op_sel_hi:[1,0,1]
	v_pk_fma_f32 v[64:65], v[64:65], v[164:165], v[68:69] op_sel_hi:[1,0,1]
	v_lshlrev_b32_e32 v68, 16, v98
	v_and_b32_e32 v69, 0xffff0000, v98
	v_lshlrev_b32_e32 v70, 16, v99
	v_and_b32_e32 v71, 0xffff0000, v99
	v_pk_fma_f32 v[70:71], v[62:63], v[164:165], v[70:71] op_sel_hi:[1,0,1]
	v_pk_fma_f32 v[62:63], v[60:61], v[164:165], v[68:69] op_sel_hi:[1,0,1]
	v_mul_f32_e32 v60, v65, v65
	v_mul_f32_e32 v61, v63, v63
	v_fmac_f32_e32 v60, v64, v64
	v_fmac_f32_e32 v61, v62, v62
	v_fmac_f32_e32 v60, v66, v66
	v_fmac_f32_e32 v61, v70, v70
	v_fmac_f32_e32 v60, v67, v67
	v_fmac_f32_e32 v61, v71, v71
	v_add_f32_e32 v68, v60, v61
	v_cvt_pk_bf16_f32 v60, v64, v65
	v_cvt_pk_bf16_f32 v61, v66, v67
	v_cvt_pk_bf16_f32 v62, v62, v63
	v_cvt_pk_bf16_f32 v63, v70, v71
	global_store_dwordx4 v[146:147], v[60:63], off
	v_mov_b32_e32 v64, v165
	s_waitcnt vmcnt(7)
	v_lshlrev_b32_e32 v60, 16, v92
	v_and_b32_e32 v61, 0xffff0000, v92
	v_lshlrev_b32_e32 v62, 16, v93
	v_and_b32_e32 v63, 0xffff0000, v93
	v_pk_fma_f32 v[58:59], v[58:59], v[64:65], v[62:63] op_sel_hi:[1,0,1]
	v_pk_fma_f32 v[56:57], v[56:57], v[64:65], v[60:61] op_sel_hi:[1,0,1]
	v_lshlrev_b32_e32 v60, 16, v94
	v_and_b32_e32 v61, 0xffff0000, v94
	v_lshlrev_b32_e32 v62, 16, v95
	v_and_b32_e32 v63, 0xffff0000, v95
	v_pk_fma_f32 v[62:63], v[54:55], v[64:65], v[62:63] op_sel_hi:[1,0,1]
	v_pk_fma_f32 v[54:55], v[52:53], v[64:65], v[60:61] op_sel_hi:[1,0,1]
	v_mul_f32_e32 v52, v57, v57
	v_mul_f32_e32 v53, v55, v55
	v_fmac_f32_e32 v52, v56, v56
	v_fmac_f32_e32 v53, v54, v54
	v_fmac_f32_e32 v52, v58, v58
	v_fmac_f32_e32 v53, v62, v62
	v_fmac_f32_e32 v52, v59, v59
	v_fmac_f32_e32 v53, v63, v63
	v_add_f32_e32 v66, v52, v53
	v_cvt_pk_bf16_f32 v52, v56, v57
	v_cvt_pk_bf16_f32 v53, v58, v59
	v_cvt_pk_bf16_f32 v54, v54, v55
	v_cvt_pk_bf16_f32 v55, v62, v63
	global_store_dwordx4 v[144:145], v[52:55], off
	v_mov_b32_e32 v56, v112
	v_mov_b32_e32 v58, v104
	v_mov_b32_e32 v52, v120
	s_nop 1
	v_permlane16_swap_b32 v120, v52
	v_mov_b32_e32 v54, v121
	v_add_f32_e32 v52, v120, v52
	v_mov_b32_e32 v53, v52
	s_nop 1
	v_permlane32_swap_b32 v52, v53
	s_nop 1
	v_permlane16_swap_b32 v54, v121
	v_mov_b32_e32 v60, v84
	v_add_f32_e32 v54, v54, v121
	v_mov_b32_e32 v55, v54
	s_nop 1
	v_permlane32_swap_b32 v54, v55
	s_nop 1
	v_permlane16_swap_b32 v112, v56
	v_mov_b32_e32 v62, v76
	v_add_f32_e32 v56, v112, v56
	v_mov_b32_e32 v57, v56
	s_nop 1
	v_permlane32_swap_b32 v57, v56
	s_nop 1
	v_permlane16_swap_b32 v58, v104
	v_mov_b32_e32 v64, v68
	v_add_f32_e32 v58, v58, v104
	v_mov_b32_e32 v59, v58
	s_nop 1
	v_permlane32_swap_b32 v58, v59
	s_nop 1
	v_permlane16_swap_b32 v60, v84
	v_mov_b32_e32 v67, v66
	v_add_f32_e32 v60, v60, v84
	v_mov_b32_e32 v61, v60
	s_nop 1
	v_permlane32_swap_b32 v61, v60
	s_nop 1
	v_permlane16_swap_b32 v76, v62
	s_nop 0
	v_add_f32_e32 v62, v76, v62
	v_mov_b32_e32 v63, v62
	s_nop 1
	v_permlane32_swap_b32 v63, v62
	s_nop 1
	v_permlane16_swap_b32 v64, v68
	s_nop 0
	v_add_f32_e32 v64, v64, v68
	v_mov_b32_e32 v65, v64
	s_nop 1
	v_permlane32_swap_b32 v64, v65
	s_nop 1
	v_permlane16_swap_b32 v67, v66
	s_nop 0
	v_add_f32_e32 v66, v67, v66
	v_mov_b32_e32 v67, v66
	s_nop 1
	v_permlane32_swap_b32 v67, v66
	s_and_saveexec_b64 s[0:1], vcc
	s_cbranch_execz .LBB0_1101
	v_lshl_add_u32 v3, v3, 2, s20
	v_add_u32_e32 v3, 0x2000, v3
	v_add_f32_e32 v54, v54, v55
	v_add_f32_e32 v55, v52, v53
	ds_read2_b32 v[52:53], v3 offset1:16
	v_add_f32_e32 v58, v58, v59
	v_add_f32_e32 v56, v57, v56
	v_add_f32_e32 v62, v63, v62
	v_add_f32_e32 v60, v61, v60
	s_waitcnt lgkmcnt(0)
	v_add_f32_e32 v52, v55, v52
	v_add_f32_e32 v53, v54, v53
	ds_write2_b32 v3, v52, v53 offset1:16
	ds_read2_b32 v[52:53], v3 offset0:32 offset1:48
	v_add_f32_e32 v66, v67, v66
	v_add_f32_e32 v64, v64, v65
	s_waitcnt lgkmcnt(0)
	v_add_f32_e32 v52, v56, v52
	v_add_f32_e32 v53, v58, v53
	ds_write2_b32 v3, v52, v53 offset0:32 offset1:48
	ds_read2_b32 v[52:53], v3 offset0:64 offset1:80
	s_waitcnt lgkmcnt(0)
	v_add_f32_e32 v52, v60, v52
	v_add_f32_e32 v53, v62, v53
	ds_write2_b32 v3, v52, v53 offset0:64 offset1:80
	ds_read2_b32 v[52:53], v3 offset0:96 offset1:112
	s_waitcnt lgkmcnt(0)
	v_add_f32_e32 v52, v64, v52
	v_add_f32_e32 v53, v66, v53
	ds_write2_b32 v3, v52, v53 offset0:96 offset1:112
	s_branch .LBB0_1101

.LBB0_1128:
	s_or_b64 exec, exec, s[0:1]
	v_mov_b32_e32 v54, v0
	s_waitcnt lgkmcnt(0)
	s_barrier
	s_add_u32 s0, s6, s60
	v_ashrrev_i32_e32 v52, 4, v54
	v_ashrrev_i32_e32 v53, 31, v52
	s_addc_u32 s1, s7, s61
	v_lshlrev_b32_e32 v3, 3, v54
	s_waitcnt vmcnt(8)
	v_lshlrev_b64 v[4:5], 11, v[52:53]
	v_and_b32_e32 v3, 0x78, v3
	v_readlane_b32 s12, v247, 9
	v_lshl_add_u64 v[100:101], s[0:1], 0, v[4:5]
	s_mov_b64 s[0:1], 0x10000
	v_or_b32_e32 v6, s12, v3
	v_lshl_add_u64 v[102:103], v[100:101], 0, s[0:1]
	s_mov_b64 s[0:1], 0x20000
	v_lshlrev_b32_e32 v4, 1, v6
	v_mov_b32_e32 v5, v2
	v_lshl_add_u64 v[104:105], v[100:101], 0, s[0:1]
	s_mov_b64 s[0:1], 0x30000
	v_lshl_add_u64 v[6:7], v[100:101], 0, v[4:5]
	v_lshl_add_u64 v[106:107], v[100:101], 0, s[0:1]
	v_lshl_add_u64 v[8:9], v[102:103], 0, v[4:5]
	global_load_dwordx4 v[20:23], v[6:7], off
	global_load_dwordx4 v[24:27], v[8:9], off
	v_lshl_add_u64 v[6:7], v[104:105], 0, v[4:5]
	v_lshl_add_u64 v[4:5], v[106:107], 0, v[4:5]
	v_readlane_b32 s0, v247, 10
	global_load_dwordx4 v[28:31], v[6:7], off
	global_load_dwordx4 v[32:35], v[4:5], off
	v_or_b32_e32 v4, s0, v3
	v_lshlrev_b32_e32 v4, 1, v4
	v_mov_b32_e32 v5, v2
	v_lshl_add_u64 v[6:7], v[100:101], 0, v[4:5]
	v_lshl_add_u64 v[8:9], v[102:103], 0, v[4:5]
	global_load_dwordx4 v[44:47], v[6:7], off
	global_load_dwordx4 v[36:39], v[8:9], off
	v_lshl_add_u64 v[6:7], v[104:105], 0, v[4:5]
	v_lshl_add_u64 v[4:5], v[106:107], 0, v[4:5]
	global_load_dwordx4 v[48:51], v[6:7], off
	global_load_dwordx4 v[40:43], v[4:5], off
	v_readfirstlane_b32 s0, v54
	s_ashr_i32 s0, s0, 6
	s_cmp_gt_i32 s0, 2
	s_cselect_b64 s[58:59], -1, 0
	s_cmp_lt_i32 s0, 3
	s_cselect_b64 s[60:61], -1, 0
	s_and_b64 s[38:39], s[60:61], exec
	s_cselect_b32 s38, s0, 2
	s_ashr_i32 s39, s38, 31
	s_lshl_b64 s[38:39], s[38:39], 15
	v_and_b32_e32 v53, 63, v54
	s_add_u32 s38, s26, s38
	s_addc_u32 s39, s27, s39
	v_lshlrev_b32_e32 v4, 4, v53
	v_mov_b32_e32 v5, v2
	v_lshl_add_u64 v[108:109], s[38:39], 0, v[4:5]
	s_and_b64 vcc, exec, s[58:59]
	s_cbranch_vccnz .LBB0_1130
	v_readlane_b32 s34, v248, 17
	v_readlane_b32 s35, v248, 18
	s_mov_b32 s35, s21
	s_mov_b32 s12, s34
	v_lshl_add_u64 v[16:17], v[108:109], 0, s[34:35]
	global_load_dwordx4 v[4:7], v[16:17], off sc0
	global_load_dwordx4 v[8:11], v[16:17], off offset:1024 sc0
	global_load_dwordx4 v[12:15], v[16:17], off offset:2048 sc0
	s_nop 0
	global_load_dwordx4 v[16:19], v[16:17], off offset:3072 sc0
	v_writelane_b32 v248, s12, 17
	s_nop 1
	v_writelane_b32 v248, s13, 18

.LBB0_1135:
	s_andn2_b64 vcc, exec, s[38:39]
	s_cbranch_vccnz .LBB0_1137
	s_add_i32 s12, s63, s81
	ds_read_b128 v[20:23], v115
	ds_read_b128 v[24:27], v115 offset:4096
	s_waitcnt vmcnt(1)
	ds_read_b128 v[28:31], v115 offset:8192
	s_waitcnt vmcnt(0)
	ds_read_b128 v[32:35], v115 offset:12288
	ds_read_b128 v[120:123], v115 offset:16384
	ds_read_b128 v[124:127], v115 offset:20480
	ds_read_b128 v[128:131], v115 offset:24576
	ds_read_b128 v[132:135], v115 offset:28672
	s_lshl_b32 s38, s12, 2
	s_sub_i32 s39, s38, 32
	s_cmp_gt_i32 s12, 7
	s_cselect_b32 s38, s39, s38
	s_ashr_i32 s39, s38, 31
	s_waitcnt vmcnt(2)
	v_lshlrev_b64 v[52:53], 1, v[110:111]
	s_lshl_b64 s[38:39], s[38:39], 10
	s_waitcnt vmcnt(0)
	v_lshl_add_u64 v[56:57], v[104:105], 0, v[52:53]
	v_lshl_add_u64 v[58:59], v[106:107], 0, v[52:53]
	v_lshl_add_u64 v[54:55], v[100:101], 0, v[52:53]
	v_lshl_add_u64 v[52:53], v[102:103], 0, v[52:53]
	v_lshl_add_u64 v[144:145], v[108:109], 0, s[38:39]
	global_load_dwordx4 v[60:63], v[54:55], off
	s_nop 0
	global_load_dwordx4 v[52:55], v[52:53], off
	s_waitcnt lgkmcnt(7)
	v_mfma_f32_16x16x32_bf16 v[96:99], v[4:7], v[20:23], v[96:99]
	s_waitcnt lgkmcnt(6)
	v_mfma_f32_16x16x32_bf16 v[24:27], v[4:7], v[24:27], v[88:91]
	s_waitcnt lgkmcnt(5)
	v_mfma_f32_16x16x32_bf16 v[28:31], v[4:7], v[28:31], v[92:95]
	s_waitcnt lgkmcnt(4)
	v_mfma_f32_16x16x32_bf16 v[32:35], v[4:7], v[32:35], v[84:87]
	s_nop 2
	ds_read_b128 v[84:87], v116
	ds_read_b128 v[88:91], v116 offset:4096
	ds_read_b128 v[92:95], v116 offset:8192
	ds_read_b128 v[136:139], v116 offset:12288
	global_load_dwordx4 v[64:67], v[56:57], off
	s_nop 0
	global_load_dwordx4 v[56:59], v[58:59], off
	s_waitcnt lgkmcnt(7)
	v_mfma_f32_16x16x32_bf16 v[80:83], v[4:7], v[120:123], v[80:83]
	s_waitcnt lgkmcnt(6)
	v_mfma_f32_16x16x32_bf16 v[72:75], v[4:7], v[124:127], v[72:75]
	s_waitcnt lgkmcnt(5)
	v_mfma_f32_16x16x32_bf16 v[76:79], v[4:7], v[128:131], v[76:79]
	s_waitcnt lgkmcnt(4)
	v_mfma_f32_16x16x32_bf16 v[68:71], v[4:7], v[132:135], v[68:71]
	ds_read_b128 v[120:123], v116 offset:16384
	ds_read_b128 v[124:127], v116 offset:20480
	ds_read_b128 v[128:131], v116 offset:24576
	ds_read_b128 v[132:135], v116 offset:28672
	global_load_dwordx4 v[20:23], v[144:145], off sc0
	ds_write_b128 v114, v[44:47] offset:32768
	s_waitcnt lgkmcnt(8)
	v_mfma_f32_16x16x32_bf16 v[44:47], v[8:11], v[84:87], v[96:99]
	s_waitcnt lgkmcnt(7)
	v_mfma_f32_16x16x32_bf16 v[84:87], v[8:11], v[88:91], v[24:27]
	s_waitcnt lgkmcnt(6)
	v_mfma_f32_16x16x32_bf16 v[88:91], v[8:11], v[92:95], v[28:31]
	s_waitcnt lgkmcnt(5)
	v_mfma_f32_16x16x32_bf16 v[32:35], v[8:11], v[136:139], v[32:35]
	ds_read_b128 v[92:95], v117
	ds_read_b128 v[96:99], v117 offset:4096
	ds_read_b128 v[136:139], v117 offset:8192
	ds_read_b128 v[140:143], v117 offset:12288
	global_load_dwordx4 v[24:27], v[144:145], off offset:1024 sc0
	ds_write_b128 v114, v[36:39] offset:40960
	s_waitcnt lgkmcnt(8)
	v_mfma_f32_16x16x32_bf16 v[72:75], v[8:11], v[124:127], v[72:75]
	s_waitcnt lgkmcnt(7)
	v_mfma_f32_16x16x32_bf16 v[76:79], v[8:11], v[128:131], v[76:79]
	s_waitcnt lgkmcnt(6)
	v_mfma_f32_16x16x32_bf16 v[68:71], v[8:11], v[132:135], v[68:71]
	v_mfma_f32_16x16x32_bf16 v[36:39], v[8:11], v[120:123], v[80:83]
	s_nop 2
	ds_read_b128 v[80:83], v117 offset:16384
	ds_read_b128 v[120:123], v117 offset:20480
	ds_read_b128 v[124:127], v117 offset:24576
	ds_read_b128 v[128:131], v117 offset:28672
	global_load_dwordx4 v[28:31], v[144:145], off offset:2048 sc0
	ds_write_b128 v114, v[48:51] offset:49152
	s_waitcnt lgkmcnt(8)
	v_mfma_f32_16x16x32_bf16 v[48:51], v[12:15], v[96:99], v[84:87]
	s_waitcnt lgkmcnt(7)
	v_mfma_f32_16x16x32_bf16 v[84:87], v[12:15], v[136:139], v[88:91]
	v_mfma_f32_16x16x32_bf16 v[44:47], v[12:15], v[92:95], v[44:47]
	s_waitcnt lgkmcnt(6)
	v_mfma_f32_16x16x32_bf16 v[132:135], v[12:15], v[140:143], v[32:35]
	ds_read_b128 v[88:91], v118
	ds_read_b128 v[92:95], v118 offset:4096
	ds_read_b128 v[136:139], v118 offset:8192
	ds_read_b128 v[140:143], v118 offset:12288
	global_load_dwordx4 v[32:35], v[144:145], off offset:3072 sc0
	ds_write_b128 v114, v[40:43] offset:57344
	s_waitcnt lgkmcnt(7)
	v_mfma_f32_16x16x32_bf16 v[76:79], v[12:15], v[124:127], v[76:79]
	s_waitcnt lgkmcnt(6)
	v_mfma_f32_16x16x32_bf16 v[68:71], v[12:15], v[128:131], v[68:71]
	v_mfma_f32_16x16x32_bf16 v[36:39], v[12:15], v[80:83], v[36:39]
	v_mfma_f32_16x16x32_bf16 v[40:43], v[12:15], v[120:123], v[72:75]
	s_nop 2
	ds_read_b128 v[72:75], v118 offset:16384
	ds_read_b128 v[120:123], v118 offset:20480
	ds_read_b128 v[124:127], v118 offset:24576
	ds_read_b128 v[128:131], v118 offset:28672
	s_waitcnt lgkmcnt(8)
	v_mfma_f32_16x16x32_bf16 v[96:99], v[16:19], v[88:91], v[44:47]
	s_waitcnt lgkmcnt(7)
	v_mfma_f32_16x16x32_bf16 v[88:91], v[16:19], v[92:95], v[48:51]
	s_waitcnt lgkmcnt(6)
	v_mfma_f32_16x16x32_bf16 v[92:95], v[16:19], v[136:139], v[84:87]
	s_waitcnt lgkmcnt(5)
	v_mfma_f32_16x16x32_bf16 v[84:87], v[16:19], v[140:143], v[132:135]
	s_waitcnt lgkmcnt(3)
	v_mfma_f32_16x16x32_bf16 v[80:83], v[16:19], v[72:75], v[36:39]
	s_waitcnt lgkmcnt(2)
	v_mfma_f32_16x16x32_bf16 v[72:75], v[16:19], v[120:123], v[40:43]
	s_waitcnt lgkmcnt(1)
	v_mfma_f32_16x16x32_bf16 v[76:79], v[16:19], v[124:127], v[76:79]
	s_waitcnt lgkmcnt(0)
	v_mfma_f32_16x16x32_bf16 v[68:71], v[16:19], v[128:131], v[68:71]

.LBB0_1146:
	s_andn2_b64 vcc, exec, s[38:39]
	s_cbranch_vccnz .LBB0_1148
	s_add_i32 s0, s63, s81
	s_waitcnt vmcnt(3)
	ds_read_b128 v[4:7], v115 offset:32768
	s_waitcnt vmcnt(2)
	ds_read_b128 v[8:11], v115 offset:36864
	s_waitcnt vmcnt(1)
	ds_read_b128 v[12:15], v115 offset:40960
	s_waitcnt vmcnt(0)
	ds_read_b128 v[16:19], v115 offset:45056
	ds_read_b128 v[120:123], v115 offset:49152
	ds_read_b128 v[124:127], v115 offset:53248
	ds_read_b128 v[128:131], v115 offset:57344
	ds_read_b128 v[132:135], v115 offset:61440
	s_lshl_b32 s1, s0, 2
	s_sub_i32 s12, s1, 32
	s_cmp_gt_i32 s0, 7
	s_cselect_b32 s0, s12, s1
	s_ashr_i32 s1, s0, 31
	v_lshlrev_b64 v[36:37], 1, v[110:111]
	s_lshl_b64 s[0:1], s[0:1], 10
	v_lshl_add_u64 v[40:41], v[104:105], 0, v[36:37]
	v_lshl_add_u64 v[42:43], v[106:107], 0, v[36:37]
	v_lshl_add_u64 v[38:39], v[100:101], 0, v[36:37]
	v_lshl_add_u64 v[36:37], v[102:103], 0, v[36:37]
	v_lshl_add_u64 v[144:145], v[108:109], 0, s[0:1]
	global_load_dwordx4 v[44:47], v[38:39], off
	s_nop 0
	global_load_dwordx4 v[36:39], v[36:37], off
	s_waitcnt lgkmcnt(7)
	v_mfma_f32_16x16x32_bf16 v[96:99], v[20:23], v[4:7], v[96:99]
	s_waitcnt lgkmcnt(6)
	v_mfma_f32_16x16x32_bf16 v[8:11], v[20:23], v[8:11], v[88:91]
	s_waitcnt lgkmcnt(5)
	v_mfma_f32_16x16x32_bf16 v[12:15], v[20:23], v[12:15], v[92:95]
	s_waitcnt lgkmcnt(4)
	v_mfma_f32_16x16x32_bf16 v[16:19], v[20:23], v[16:19], v[84:87]
	s_nop 2
	ds_read_b128 v[84:87], v116 offset:32768
	ds_read_b128 v[88:91], v116 offset:36864
	ds_read_b128 v[92:95], v116 offset:40960
	ds_read_b128 v[136:139], v116 offset:45056
	global_load_dwordx4 v[48:51], v[40:41], off
	s_nop 0
	global_load_dwordx4 v[40:43], v[42:43], off
	s_waitcnt lgkmcnt(7)
	v_mfma_f32_16x16x32_bf16 v[80:83], v[20:23], v[120:123], v[80:83]
	s_waitcnt lgkmcnt(6)
	v_mfma_f32_16x16x32_bf16 v[72:75], v[20:23], v[124:127], v[72:75]
	s_waitcnt lgkmcnt(5)
	v_mfma_f32_16x16x32_bf16 v[76:79], v[20:23], v[128:131], v[76:79]
	s_waitcnt lgkmcnt(4)
	v_mfma_f32_16x16x32_bf16 v[68:71], v[20:23], v[132:135], v[68:71]
	ds_read_b128 v[120:123], v116 offset:49152
	ds_read_b128 v[124:127], v116 offset:53248
	ds_read_b128 v[128:131], v116 offset:57344
	ds_read_b128 v[132:135], v116 offset:61440
	global_load_dwordx4 v[4:7], v[144:145], off sc0
	ds_write_b128 v114, v[60:63]
	s_waitcnt lgkmcnt(8)
	v_mfma_f32_16x16x32_bf16 v[60:63], v[24:27], v[84:87], v[96:99]
	s_waitcnt lgkmcnt(7)
	v_mfma_f32_16x16x32_bf16 v[84:87], v[24:27], v[88:91], v[8:11]
	s_waitcnt lgkmcnt(6)
	v_mfma_f32_16x16x32_bf16 v[88:91], v[24:27], v[92:95], v[12:15]
	s_waitcnt lgkmcnt(5)
	v_mfma_f32_16x16x32_bf16 v[16:19], v[24:27], v[136:139], v[16:19]
	ds_read_b128 v[92:95], v117 offset:32768
	ds_read_b128 v[96:99], v117 offset:36864
	ds_read_b128 v[136:139], v117 offset:40960
	ds_read_b128 v[140:143], v117 offset:45056
	global_load_dwordx4 v[8:11], v[144:145], off offset:1024 sc0
	ds_write_b128 v114, v[52:55] offset:8192
	s_waitcnt lgkmcnt(8)
	v_mfma_f32_16x16x32_bf16 v[72:75], v[24:27], v[124:127], v[72:75]
	s_waitcnt lgkmcnt(7)
	v_mfma_f32_16x16x32_bf16 v[76:79], v[24:27], v[128:131], v[76:79]
	s_waitcnt lgkmcnt(6)
	v_mfma_f32_16x16x32_bf16 v[68:71], v[24:27], v[132:135], v[68:71]
	v_mfma_f32_16x16x32_bf16 v[52:55], v[24:27], v[120:123], v[80:83]
	s_nop 2
	ds_read_b128 v[80:83], v117 offset:49152
	ds_read_b128 v[120:123], v117 offset:53248
	ds_read_b128 v[124:127], v117 offset:57344
	ds_read_b128 v[128:131], v117 offset:61440
	global_load_dwordx4 v[12:15], v[144:145], off offset:2048 sc0
	ds_write_b128 v114, v[64:67] offset:16384
	s_waitcnt lgkmcnt(8)
	v_mfma_f32_16x16x32_bf16 v[64:67], v[28:31], v[96:99], v[84:87]
	s_waitcnt lgkmcnt(7)
	v_mfma_f32_16x16x32_bf16 v[84:87], v[28:31], v[136:139], v[88:91]
	v_mfma_f32_16x16x32_bf16 v[60:63], v[28:31], v[92:95], v[60:63]
	s_waitcnt lgkmcnt(6)
	v_mfma_f32_16x16x32_bf16 v[132:135], v[28:31], v[140:143], v[16:19]
	ds_read_b128 v[88:91], v118 offset:32768
	ds_read_b128 v[92:95], v118 offset:36864
	ds_read_b128 v[136:139], v118 offset:40960
	ds_read_b128 v[140:143], v118 offset:45056
	global_load_dwordx4 v[16:19], v[144:145], off offset:3072 sc0
	ds_write_b128 v114, v[56:59] offset:24576
	s_waitcnt lgkmcnt(7)
	v_mfma_f32_16x16x32_bf16 v[76:79], v[28:31], v[124:127], v[76:79]
	s_waitcnt lgkmcnt(6)
	v_mfma_f32_16x16x32_bf16 v[68:71], v[28:31], v[128:131], v[68:71]
	v_mfma_f32_16x16x32_bf16 v[52:55], v[28:31], v[80:83], v[52:55]
	v_mfma_f32_16x16x32_bf16 v[56:59], v[28:31], v[120:123], v[72:75]
	s_nop 2
	ds_read_b128 v[72:75], v118 offset:49152
	ds_read_b128 v[120:123], v118 offset:53248
	ds_read_b128 v[124:127], v118 offset:57344
	ds_read_b128 v[128:131], v118 offset:61440
	s_waitcnt lgkmcnt(8)
	v_mfma_f32_16x16x32_bf16 v[96:99], v[32:35], v[88:91], v[60:63]
	s_waitcnt lgkmcnt(7)
	v_mfma_f32_16x16x32_bf16 v[88:91], v[32:35], v[92:95], v[64:67]
	s_waitcnt lgkmcnt(6)
	v_mfma_f32_16x16x32_bf16 v[92:95], v[32:35], v[136:139], v[84:87]
	s_waitcnt lgkmcnt(5)
	v_mfma_f32_16x16x32_bf16 v[84:87], v[32:35], v[140:143], v[132:135]
	s_waitcnt lgkmcnt(3)
	v_mfma_f32_16x16x32_bf16 v[80:83], v[32:35], v[72:75], v[52:55]
	s_waitcnt lgkmcnt(2)
	v_mfma_f32_16x16x32_bf16 v[72:75], v[32:35], v[120:123], v[56:59]
	s_waitcnt lgkmcnt(1)
	v_mfma_f32_16x16x32_bf16 v[76:79], v[32:35], v[124:127], v[76:79]
	s_waitcnt lgkmcnt(0)
	v_mfma_f32_16x16x32_bf16 v[68:71], v[32:35], v[128:131], v[68:71]

.LBB0_1256:
	s_or_b64 exec, exec, s[38:39]
	v_mov_b32_e32 v34, v0
	s_waitcnt lgkmcnt(0)
	s_barrier
	s_movk_i32 s18, 0x100
	v_ashrrev_i32_e32 v35, 4, v34
	v_lshl_add_u32 v4, v35, 2, 0
	v_add_u32_e32 v233, 0x24d80, v4
	ds_read2_b32 v[6:7], v233 offset1:32
	v_lshlrev_b32_e32 v4, 3, v34
	v_and_b32_e32 v234, 0x78, v4
	v_readfirstlane_b32 s12, v34
	v_cmp_gt_i32_e64 s[48:49], s18, v34
	s_waitcnt lgkmcnt(0)
	v_lshlrev_b32_e32 v252, 11, v6
	v_lshlrev_b32_e32 v253, 11, v7
	v_ashrrev_i32_e32 v5, 31, v6
	v_mov_b32_e32 v4, v6
	v_lshlrev_b64 v[4:5], 11, v[4:5]
	v_lshl_add_u64 v[8:9], s[6:7], 0, v[4:5]
	v_lshlrev_b32_e32 v4, 1, v234
	v_mov_b32_e32 v5, v2
	v_lshl_add_u64 v[10:11], v[8:9], 0, v[4:5]
	v_ashrrev_i32_e32 v9, 31, v7
	v_mov_b32_e32 v8, v7
	v_lshlrev_b64 v[6:7], 11, v[8:9]
	ds_read2_b32 v[8:9], v233 offset0:64 offset1:96
	v_lshl_add_u64 v[6:7], s[6:7], 0, v[6:7]
	v_lshl_add_u64 v[12:13], v[6:7], 0, v[4:5]
	global_load_dwordx4 v[14:17], v[10:11], off
	global_load_dwordx4 v[18:21], v[12:13], off
	s_waitcnt lgkmcnt(0)
	v_lshlrev_b32_e32 v254, 11, v8
	v_lshlrev_b32_e32 v255, 11, v9
	v_ashrrev_i32_e32 v7, 31, v8
	v_mov_b32_e32 v6, v8
	v_lshlrev_b64 v[6:7], 11, v[6:7]
	v_lshl_add_u64 v[6:7], s[6:7], 0, v[6:7]
	v_lshl_add_u64 v[30:31], v[6:7], 0, v[4:5]
	v_ashrrev_i32_e32 v7, 31, v9
	v_mov_b32_e32 v6, v9
	v_lshlrev_b64 v[6:7], 11, v[6:7]
	v_lshl_add_u64 v[6:7], s[6:7], 0, v[6:7]
	v_lshl_add_u64 v[32:33], v[6:7], 0, v[4:5]
	global_load_dwordx4 v[22:25], v[30:31], off sc0
	global_load_dwordx4 v[26:29], v[32:33], off
	s_and_saveexec_b64 s[38:39], s[48:49]
	s_cbranch_execz .LBB0_1258
	ds_read_b32 v6, v233 offset:512
	s_waitcnt lgkmcnt(0)
	v_ashrrev_i32_e32 v7, 31, v6
	v_lshlrev_b64 v[6:7], 11, v[6:7]
	v_lshl_add_u64 v[6:7], s[6:7], 0, v[6:7]
	v_lshl_add_u64 v[6:7], v[6:7], 0, v[4:5]
	global_load_dwordx4 v[6:9], v[6:7], off
.LBB0_1258:
	s_or_b64 exec, exec, s[38:39]
	global_load_dwordx4 v[106:109], v[10:11], off offset:256
	global_load_dwordx4 v[94:97], v[12:13], off offset:256
	global_load_dwordx4 v[98:101], v[30:31], off offset:256 sc0
	global_load_dwordx4 v[90:93], v[32:33], off offset:256
	s_and_saveexec_b64 s[38:39], s[48:49]
	s_cbranch_execz .LBB0_1260
	ds_read_b32 v10, v233 offset:512
	v_mov_b32_e32 v5, v2
	s_waitcnt lgkmcnt(0)
	v_ashrrev_i32_e32 v11, 31, v10
	v_lshlrev_b64 v[10:11], 11, v[10:11]
	v_lshl_add_u64 v[10:11], s[6:7], 0, v[10:11]
	v_lshl_add_u64 v[4:5], v[10:11], 0, v[4:5]
	global_load_dwordx4 v[10:13], v[4:5], off offset:256 sc0
.LBB0_1260:
	s_or_b64 exec, exec, s[38:39]
	s_lshl_b32 s20, s64, 20
	s_add_u32 s20, s68, s20
	s_addc_u32 s46, s69, 0
	s_ashr_i32 s38, s12, 6
	s_ashr_i32 s39, s38, 31
	s_lshl_b64 s[42:43], s[38:39], 16
	v_and_b32_e32 v4, 63, v34
	s_add_u32 s42, s20, s42
	s_addc_u32 s43, s46, s43
	v_lshlrev_b32_e32 v30, 4, v4
	v_mov_b32_e32 v31, v2
	v_lshl_add_u64 v[214:215], s[42:43], 0, v[30:31]
	global_load_dwordx4 v[166:169], v30, s[42:43] sc0
	global_load_dwordx4 v[146:149], v30, s[42:43] offset:1024 sc0
	global_load_dwordx4 v[114:117], v30, s[42:43] offset:2048 sc0
	global_load_dwordx4 v[110:113], v30, s[42:43] offset:3072 sc0
	v_add_co_u32_e32 v30, vcc, s14, v214
	v_lshlrev_b32_e32 v5, 8, v35
	s_nop 0
	v_addc_co_u32_e32 v31, vcc, 0, v215, vcc
	global_load_dwordx4 v[174:177], v[30:31], off sc0
	global_load_dwordx4 v[170:173], v[30:31], off offset:1024 sc0
	global_load_dwordx4 v[154:157], v[30:31], off offset:2048 sc0
	global_load_dwordx4 v[138:141], v[30:31], off offset:3072 sc0
	v_xor_b32_e32 v30, v35, v34
	v_lshlrev_b32_e32 v30, 4, v30
	v_and_or_b32 v5, v30, s84, v5
	v_add_u32_e32 v235, 0, v5
	s_waitcnt vmcnt(15)
	ds_write_b128 v235, v[14:17]
	s_waitcnt vmcnt(14)
	ds_write_b128 v235, v[18:21] offset:8192
	s_waitcnt vmcnt(13)
	ds_write_b128 v235, v[22:25] offset:16384
	s_waitcnt vmcnt(12)
	ds_write_b128 v235, v[26:29] offset:24576
	s_and_saveexec_b64 s[42:43], s[48:49]
	ds_write_b128 v235, v[6:9] offset:32768
	s_or_b64 exec, exec, s[42:43]
	v_add_u32_e32 v3, 15, v3
	v_and_b32_e32 v236, 15, v34
	v_lshrrev_b32_e32 v237, 4, v4
	v_ashrrev_i32_e32 v3, 4, v3
	s_xor_b64 s[62:63], s[0:1], -1
	v_lshl_add_u32 v4, v236, 8, 0
	v_cmp_lt_i32_e64 s[0:1], 3, v3
	v_cmp_lt_i32_e64 s[42:43], 0, v3
	v_cmp_lt_i32_e64 s[46:47], 6, v3
	v_bitop3_b32 v3, v237, v236, 4 bitop3:0x36
	v_lshl_add_u32 v241, v3, 4, v4
	v_bitop3_b32 v3, v237, v236, 8 bitop3:0x36
	v_bitop3_b32 v5, v237, v34, 15 bitop3:0x78
	v_lshl_add_u32 v242, v3, 4, v4
	v_bitop3_b32 v3, v237, v236, 12 bitop3:0x36
	v_lshl_add_u32 v238, v5, 4, v4
	v_lshl_add_u32 v243, v3, 4, v4
	v_mov_b32_e32 v4, v2
	v_mov_b32_e32 v5, v2
	s_mov_b32 s20, 0
	v_mov_b32_e32 v3, v2
	v_mov_b64_e32 v[16:17], v[4:5]
	v_mov_b64_e32 v[44:45], v[4:5]
	v_mov_b64_e32 v[48:49], v[4:5]
	v_mov_b64_e32 v[52:53], v[4:5]
	v_mov_b64_e32 v[56:57], v[4:5]
	v_mov_b64_e32 v[60:61], v[4:5]
	v_mov_b64_e32 v[64:65], v[4:5]
	v_mov_b64_e32 v[68:69], v[4:5]
	v_mov_b64_e32 v[72:73], v[4:5]
	v_mov_b64_e32 v[76:77], v[4:5]
	v_mov_b64_e32 v[80:81], v[4:5]
	v_mov_b64_e32 v[84:85], v[4:5]
	v_mov_b64_e32 v[88:89], v[4:5]
	v_mov_b64_e32 v[104:105], v[4:5]
	v_mov_b64_e32 v[120:121], v[4:5]
	v_mov_b64_e32 v[136:137], v[4:5]
	v_mov_b64_e32 v[164:165], v[4:5]
	v_mov_b64_e32 v[184:185], v[4:5]
	v_add_u32_e32 v239, 0x9000, v235
	s_lshl_b32 s65, s38, 4
	v_add_u32_e32 v240, 0x9000, v238
	v_add_u32_e32 v244, 0x9000, v241
	v_add_u32_e32 v245, 0x9000, v242
	v_add_u32_e32 v246, 0x9000, v243
	s_mov_b32 s67, 2
	s_mov_b32 s66, 1
	s_mov_b32 s73, -2
	v_mov_b64_e32 v[14:15], v[2:3]
	v_mov_b64_e32 v[42:43], v[2:3]
	v_mov_b64_e32 v[46:47], v[2:3]
	v_mov_b64_e32 v[50:51], v[2:3]
	v_mov_b64_e32 v[54:55], v[2:3]
	v_mov_b64_e32 v[58:59], v[2:3]
	v_mov_b64_e32 v[62:63], v[2:3]
	v_mov_b64_e32 v[66:67], v[2:3]
	v_mov_b64_e32 v[70:71], v[2:3]
	v_mov_b64_e32 v[74:75], v[2:3]
	v_mov_b64_e32 v[78:79], v[2:3]
	v_mov_b64_e32 v[82:83], v[2:3]
	v_mov_b64_e32 v[86:87], v[2:3]
	v_mov_b64_e32 v[102:103], v[2:3]
	v_mov_b64_e32 v[118:119], v[2:3]
	v_mov_b64_e32 v[134:135], v[2:3]
	v_mov_b64_e32 v[162:163], v[2:3]
	v_mov_b64_e32 v[182:183], v[2:3]
	s_mov_b32 s74, s20
	s_mov_b32 s75, s20
	s_waitcnt lgkmcnt(0)
	s_barrier
	s_branch .LBB0_1264

.LBB0_1274:
	s_and_saveexec_b64 s[38:39], s[48:49]
	s_cbranch_execz .LBB0_1276
	ds_read_b32 v6, v233 offset:512
	s_waitcnt lgkmcnt(0)
	v_ashrrev_i32_e32 v7, 31, v6
	v_lshlrev_b64 v[6:7], 11, v[6:7]
	v_lshl_add_u64 v[6:7], s[6:7], 0, v[6:7]
	v_lshl_add_u64 v[4:5], v[4:5], 1, v[6:7]
	global_load_dwordx4 v[6:9], v[4:5], off sc0

.LBB0_1280:
	s_lshl_b32 s38, s66, 2
	s_ashr_i32 s39, s38, 31
	s_lshl_b64 s[76:77], s[20:21], 19
	s_lshl_b64 s[38:39], s[38:39], 10
	v_lshl_add_u64 v[4:5], v[214:215], 0, s[76:77]
	v_lshl_add_u64 v[4:5], v[4:5], 0, s[38:39]
	s_waitcnt vmcnt(18)
	v_add_co_u32_e32 v150, vcc, 0x8000, v4
	s_nop 1
	v_addc_co_u32_e32 v151, vcc, 0, v5, vcc
	global_load_dwordx4 v[166:169], v[4:5], off sc0
	global_load_dwordx4 v[174:177], v[150:151], off
	s_waitcnt vmcnt(11) lgkmcnt(2)
	v_mfma_f32_16x16x32_bf16 v[182:185], v[146:149], v[18:21], v[182:185]
	s_waitcnt vmcnt(8)
	v_mfma_f32_16x16x32_bf16 v[162:165], v[170:173], v[18:21], v[162:165]
	s_waitcnt lgkmcnt(1)
	v_mfma_f32_16x16x32_bf16 v[134:137], v[146:149], v[22:25], v[134:137]
	v_mfma_f32_16x16x32_bf16 v[118:121], v[170:173], v[22:25], v[118:121]
	s_waitcnt lgkmcnt(0)
	v_mfma_f32_16x16x32_bf16 v[102:105], v[146:149], v[34:37], v[102:105]
	v_mfma_f32_16x16x32_bf16 v[86:89], v[170:173], v[34:37], v[86:89]

.LBB0_1284:
	global_load_dwordx4 v[186:189], v[4:5], off offset:1024 sc0
	s_waitcnt vmcnt(18)
	ds_write_b128 v239, v[106:109]
	s_waitcnt vmcnt(12) lgkmcnt(3)
	v_mfma_f32_16x16x32_bf16 v[82:85], v[146:149], v[198:201], v[82:85]
	s_waitcnt vmcnt(9)
	v_mfma_f32_16x16x32_bf16 v[78:81], v[170:173], v[198:201], v[78:81]
	s_waitcnt lgkmcnt(2)
	v_mfma_f32_16x16x32_bf16 v[74:77], v[146:149], v[194:197], v[74:77]
	v_mfma_f32_16x16x32_bf16 v[70:73], v[170:173], v[194:197], v[70:73]
	s_waitcnt lgkmcnt(1)
	v_mfma_f32_16x16x32_bf16 v[66:69], v[146:149], v[202:205], v[66:69]
	v_mfma_f32_16x16x32_bf16 v[62:65], v[170:173], v[202:205], v[62:65]

.LBB0_1288:
	global_load_dwordx4 v[158:161], v[4:5], off offset:2048 sc0
	s_waitcnt vmcnt(18)
	ds_write_b128 v235, v[94:97] offset:45056
	s_waitcnt vmcnt(13) lgkmcnt(3)
	v_mfma_f32_16x16x32_bf16 v[58:61], v[146:149], v[18:21], v[58:61]
	s_waitcnt vmcnt(10)
	v_mfma_f32_16x16x32_bf16 v[54:57], v[170:173], v[18:21], v[54:57]
	v_mfma_f32_16x16x32_bf16 v[50:53], v[146:149], v[22:25], v[50:53]
	v_mfma_f32_16x16x32_bf16 v[46:49], v[170:173], v[22:25], v[46:49]
	s_waitcnt lgkmcnt(2)
	v_mfma_f32_16x16x32_bf16 v[42:45], v[146:149], v[34:37], v[42:45]
	v_mfma_f32_16x16x32_bf16 v[14:17], v[170:173], v[34:37], v[14:17]

.LBB0_1292:
	v_add_co_u32_e32 v94, vcc, 0x8000, v4
	s_waitcnt vmcnt(17)
	ds_write_b128 v235, v[98:101] offset:53248
	v_addc_co_u32_e32 v95, vcc, 0, v5, vcc
	global_load_dwordx4 v[170:173], v[94:95], off offset:1024 sc0
	s_waitcnt vmcnt(13) lgkmcnt(4)
	v_mfma_f32_16x16x32_bf16 v[182:185], v[114:117], v[198:201], v[182:185]
	s_waitcnt vmcnt(10)
	v_mfma_f32_16x16x32_bf16 v[162:165], v[154:157], v[198:201], v[162:165]
	s_waitcnt lgkmcnt(3)
	v_mfma_f32_16x16x32_bf16 v[134:137], v[114:117], v[194:197], v[134:137]
	v_mfma_f32_16x16x32_bf16 v[118:121], v[154:157], v[194:197], v[118:121]
	s_waitcnt lgkmcnt(2)
	v_mfma_f32_16x16x32_bf16 v[102:105], v[114:117], v[202:205], v[102:105]
	v_mfma_f32_16x16x32_bf16 v[86:89], v[154:157], v[202:205], v[86:89]

.LBB0_1296:
	global_load_dwordx4 v[150:153], v[4:5], off offset:3072 sc0
	s_waitcnt vmcnt(18)
	ds_write_b128 v235, v[90:93] offset:61440
	s_waitcnt vmcnt(14) lgkmcnt(4)
	v_mfma_f32_16x16x32_bf16 v[82:85], v[114:117], v[18:21], v[82:85]
	s_waitcnt vmcnt(11)
	v_mfma_f32_16x16x32_bf16 v[78:81], v[154:157], v[18:21], v[78:81]
	s_waitcnt lgkmcnt(3)
	v_mfma_f32_16x16x32_bf16 v[74:77], v[114:117], v[22:25], v[74:77]
	v_mfma_f32_16x16x32_bf16 v[70:73], v[154:157], v[22:25], v[70:73]
	s_waitcnt lgkmcnt(2)
	v_mfma_f32_16x16x32_bf16 v[66:69], v[114:117], v[34:37], v[66:69]
	v_mfma_f32_16x16x32_bf16 v[62:65], v[154:157], v[34:37], v[62:65]

.LBB0_1300:
	v_add_co_u32_e32 v90, vcc, 0x8000, v4
	s_nop 1
	v_addc_co_u32_e32 v91, vcc, 0, v5, vcc
	global_load_dwordx4 v[190:193], v[90:91], off offset:2048 sc0
	s_and_saveexec_b64 s[38:39], s[48:49]
	ds_write_b128 v239, v[10:13] offset:32768
	s_or_b64 exec, exec, s[38:39]
	s_waitcnt vmcnt(15) lgkmcnt(2)
	v_mfma_f32_16x16x32_bf16 v[58:61], v[114:117], v[198:201], v[58:61]
	s_waitcnt vmcnt(12)
	v_mfma_f32_16x16x32_bf16 v[54:57], v[154:157], v[198:201], v[54:57]
	v_mfma_f32_16x16x32_bf16 v[50:53], v[114:117], v[194:197], v[50:53]
	v_mfma_f32_16x16x32_bf16 v[46:49], v[154:157], v[194:197], v[46:49]
	s_waitcnt lgkmcnt(1)
	v_mfma_f32_16x16x32_bf16 v[42:45], v[114:117], v[202:205], v[42:45]
	v_mfma_f32_16x16x32_bf16 v[14:17], v[154:157], v[202:205], v[14:17]

.LBB0_1306:
	v_add_co_u32_e32 v4, vcc, 0x8000, v4
	s_nop 1
	v_addc_co_u32_e32 v5, vcc, 0, v5, vcc
	global_load_dwordx4 v[178:181], v[4:5], off offset:3072 sc0
	s_waitcnt vmcnt(14) lgkmcnt(2)
	v_mfma_f32_16x16x32_bf16 v[182:185], v[110:113], v[18:21], v[182:185]
	s_waitcnt vmcnt(12)
	v_mfma_f32_16x16x32_bf16 v[162:165], v[138:141], v[18:21], v[162:165]
	s_waitcnt lgkmcnt(1)
	v_mfma_f32_16x16x32_bf16 v[134:137], v[110:113], v[22:25], v[134:137]
	v_mfma_f32_16x16x32_bf16 v[118:121], v[138:141], v[22:25], v[118:121]
	s_waitcnt lgkmcnt(0)
	v_mfma_f32_16x16x32_bf16 v[102:105], v[110:113], v[34:37], v[102:105]
	v_mfma_f32_16x16x32_bf16 v[86:89], v[138:141], v[34:37], v[86:89]

.LBB0_1326:
	s_and_saveexec_b64 s[38:39], s[48:49]
	s_cbranch_execz .LBB0_1328
	ds_read_b32 v10, v233 offset:512
	s_waitcnt lgkmcnt(0)
	v_ashrrev_i32_e32 v11, 31, v10
	v_lshlrev_b64 v[10:11], 11, v[10:11]
	v_lshl_add_u64 v[10:11], s[6:7], 0, v[10:11]
	v_lshl_add_u64 v[4:5], v[4:5], 1, v[10:11]
	global_load_dwordx4 v[10:13], v[4:5], off sc0

.LBB0_1332:
	s_add_i32 s12, s66, 1
	s_cmp_gt_i32 s20, 0
	s_cselect_b32 s38, s66, 0
	s_cmp_lt_i32 s66, 7
	s_cselect_b32 s66, s12, s38
	s_cselect_b32 s20, s20, 1
	s_lshl_b32 s38, s66, 2
	s_ashr_i32 s39, s38, 31
	s_lshl_b64 s[76:77], s[20:21], 19
	s_lshl_b64 s[38:39], s[38:39], 10
	v_lshl_add_u64 v[4:5], v[214:215], 0, s[76:77]
	v_lshl_add_u64 v[4:5], v[4:5], 0, s[38:39]
	s_waitcnt vmcnt(18)
	v_add_co_u32_e32 v110, vcc, 0x8000, v4
	s_nop 1
	v_addc_co_u32_e32 v111, vcc, 0, v5, vcc
	global_load_dwordx4 v[166:169], v[4:5], off sc0
	global_load_dwordx4 v[174:177], v[110:111], off sc0
	s_waitcnt vmcnt(11) lgkmcnt(2)
	v_mfma_f32_16x16x32_bf16 v[182:185], v[186:189], v[26:29], v[182:185]
	s_waitcnt vmcnt(9)
	v_mfma_f32_16x16x32_bf16 v[162:165], v[170:173], v[26:29], v[162:165]
	s_waitcnt lgkmcnt(1)
	v_mfma_f32_16x16x32_bf16 v[134:137], v[186:189], v[30:33], v[134:137]
	v_mfma_f32_16x16x32_bf16 v[118:121], v[170:173], v[30:33], v[118:121]
	s_waitcnt lgkmcnt(0)
	v_mfma_f32_16x16x32_bf16 v[102:105], v[186:189], v[38:41], v[102:105]
	v_mfma_f32_16x16x32_bf16 v[86:89], v[170:173], v[38:41], v[86:89]

.LBB0_1336:
	global_load_dwordx4 v[146:149], v[4:5], off offset:1024 sc0
	s_waitcnt vmcnt(18)
	ds_write_b128 v235, v[142:145]
	s_waitcnt vmcnt(12) lgkmcnt(3)
	v_mfma_f32_16x16x32_bf16 v[82:85], v[186:189], v[198:201], v[82:85]
	s_waitcnt vmcnt(10)
	v_mfma_f32_16x16x32_bf16 v[78:81], v[170:173], v[198:201], v[78:81]
	s_waitcnt lgkmcnt(2)
	v_mfma_f32_16x16x32_bf16 v[74:77], v[186:189], v[194:197], v[74:77]
	v_mfma_f32_16x16x32_bf16 v[70:73], v[170:173], v[194:197], v[70:73]
	s_waitcnt lgkmcnt(1)
	v_mfma_f32_16x16x32_bf16 v[66:69], v[186:189], v[202:205], v[66:69]
	v_mfma_f32_16x16x32_bf16 v[62:65], v[170:173], v[202:205], v[62:65]

.LBB0_1340:
	global_load_dwordx4 v[114:117], v[4:5], off offset:2048 sc0
	s_waitcnt vmcnt(18)
	ds_write_b128 v235, v[126:129] offset:8192
	s_waitcnt vmcnt(13) lgkmcnt(3)
	v_mfma_f32_16x16x32_bf16 v[58:61], v[186:189], v[26:29], v[58:61]
	s_waitcnt vmcnt(11)
	v_mfma_f32_16x16x32_bf16 v[54:57], v[170:173], v[26:29], v[54:57]
	v_mfma_f32_16x16x32_bf16 v[50:53], v[186:189], v[30:33], v[50:53]
	v_mfma_f32_16x16x32_bf16 v[46:49], v[170:173], v[30:33], v[46:49]
	s_waitcnt lgkmcnt(2)
	v_mfma_f32_16x16x32_bf16 v[42:45], v[186:189], v[38:41], v[42:45]
	v_mfma_f32_16x16x32_bf16 v[14:17], v[170:173], v[38:41], v[14:17]

.LBB0_1344:
	v_add_co_u32_e32 v110, vcc, 0x8000, v4
	s_waitcnt vmcnt(17)
	ds_write_b128 v235, v[130:133] offset:16384
	v_addc_co_u32_e32 v111, vcc, 0, v5, vcc
	global_load_dwordx4 v[170:173], v[110:111], off offset:1024 sc0
	s_waitcnt vmcnt(13) lgkmcnt(4)
	v_mfma_f32_16x16x32_bf16 v[182:185], v[158:161], v[198:201], v[182:185]
	s_waitcnt vmcnt(10)
	v_mfma_f32_16x16x32_bf16 v[162:165], v[190:193], v[198:201], v[162:165]
	s_waitcnt lgkmcnt(3)
	v_mfma_f32_16x16x32_bf16 v[134:137], v[158:161], v[194:197], v[134:137]
	v_mfma_f32_16x16x32_bf16 v[118:121], v[190:193], v[194:197], v[118:121]
	s_waitcnt lgkmcnt(2)
	v_mfma_f32_16x16x32_bf16 v[102:105], v[158:161], v[202:205], v[102:105]
	v_mfma_f32_16x16x32_bf16 v[86:89], v[190:193], v[202:205], v[86:89]

.LBB0_1348:
	global_load_dwordx4 v[110:113], v[4:5], off offset:3072 sc0
	s_waitcnt vmcnt(18)
	ds_write_b128 v235, v[122:125] offset:24576
	s_waitcnt vmcnt(14) lgkmcnt(4)
	v_mfma_f32_16x16x32_bf16 v[82:85], v[158:161], v[26:29], v[82:85]
	s_waitcnt vmcnt(11)
	v_mfma_f32_16x16x32_bf16 v[78:81], v[190:193], v[26:29], v[78:81]
	s_waitcnt lgkmcnt(3)
	v_mfma_f32_16x16x32_bf16 v[74:77], v[158:161], v[30:33], v[74:77]
	v_mfma_f32_16x16x32_bf16 v[70:73], v[190:193], v[30:33], v[70:73]
	s_waitcnt lgkmcnt(2)
	v_mfma_f32_16x16x32_bf16 v[66:69], v[158:161], v[38:41], v[66:69]
	v_mfma_f32_16x16x32_bf16 v[62:65], v[190:193], v[38:41], v[62:65]

.LBB0_1352:
	v_add_co_u32_e32 v122, vcc, 0x8000, v4
	s_nop 1
	v_addc_co_u32_e32 v123, vcc, 0, v5, vcc
	global_load_dwordx4 v[154:157], v[122:123], off offset:2048 sc0
	s_and_saveexec_b64 s[38:39], s[48:49]
	ds_write_b128 v235, v[6:9] offset:32768
	s_or_b64 exec, exec, s[38:39]
	s_waitcnt vmcnt(15) lgkmcnt(2)
	v_mfma_f32_16x16x32_bf16 v[58:61], v[158:161], v[198:201], v[58:61]
	s_waitcnt vmcnt(12)
	v_mfma_f32_16x16x32_bf16 v[54:57], v[190:193], v[198:201], v[54:57]
	v_mfma_f32_16x16x32_bf16 v[50:53], v[158:161], v[194:197], v[50:53]
	v_mfma_f32_16x16x32_bf16 v[46:49], v[190:193], v[194:197], v[46:49]
	s_waitcnt lgkmcnt(1)
	v_mfma_f32_16x16x32_bf16 v[42:45], v[158:161], v[202:205], v[42:45]
	v_mfma_f32_16x16x32_bf16 v[14:17], v[190:193], v[202:205], v[14:17]

.LBB0_1358:
	v_add_co_u32_e32 v4, vcc, 0x8000, v4
	s_nop 1
	v_addc_co_u32_e32 v5, vcc, 0, v5, vcc
	global_load_dwordx4 v[138:141], v[4:5], off offset:3072 sc0
	s_waitcnt vmcnt(14) lgkmcnt(2)
	v_mfma_f32_16x16x32_bf16 v[182:185], v[150:153], v[26:29], v[182:185]
	s_waitcnt vmcnt(12)
	v_mfma_f32_16x16x32_bf16 v[162:165], v[178:181], v[26:29], v[162:165]
	s_waitcnt lgkmcnt(1)
	v_mfma_f32_16x16x32_bf16 v[134:137], v[150:153], v[30:33], v[134:137]
	v_mfma_f32_16x16x32_bf16 v[118:121], v[178:181], v[30:33], v[118:121]
	s_waitcnt lgkmcnt(0)
	v_mfma_f32_16x16x32_bf16 v[102:105], v[150:153], v[38:41], v[102:105]
	v_mfma_f32_16x16x32_bf16 v[86:89], v[178:181], v[38:41], v[86:89]

.LBB0_1368:
	s_lshl_b32 s12, s64, 19
	v_mov_b32_e32 v3, v0
	s_add_u32 s12, s70, s12
	s_addc_u32 s20, s71, 0
	v_readfirstlane_b32 s38, v3
	s_ashr_i32 s38, s38, 6
	s_ashr_i32 s39, s38, 31
	s_lshl_b64 s[48:49], s[38:39], 14
	v_and_b32_e32 v4, 63, v3
	s_add_u32 s48, s12, s48
	s_addc_u32 s49, s20, s49
	v_lshlrev_b32_e32 v4, 4, v4
	v_mov_b32_e32 v5, v2
	s_waitcnt vmcnt(7)
	v_lshl_add_u64 v[166:167], s[48:49], 0, v[4:5]
	global_load_dwordx4 v[126:129], v4, s[48:49] sc0
	global_load_dwordx4 v[114:117], v4, s[48:49] offset:1024 sc0
	global_load_dwordx4 v[106:109], v4, s[48:49] offset:2048 sc0
	global_load_dwordx4 v[94:97], v4, s[48:49] offset:3072 sc0
	v_add_co_u32_e32 v4, vcc, s94, v166
	v_and_b32_e32 v168, 15, v3
	s_nop 0
	v_addc_co_u32_e32 v5, vcc, 0, v167, vcc
	global_load_dwordx4 v[130:133], v[4:5], off sc0
	global_load_dwordx4 v[122:125], v[4:5], off offset:1024 sc0
	global_load_dwordx4 v[118:121], v[4:5], off offset:2048 sc0
	global_load_dwordx4 v[110:113], v[4:5], off offset:3072 sc0
	v_bfe_u32 v169, v3, 4, 2
	v_lshlrev_b32_e32 v4, 8, v168
	s_add_i32 s12, 0, 0x12000
	s_waitcnt vmcnt(11)
	v_add_u32_e32 v170, s12, v4
	v_bitop3_b32 v3, v169, v3, 15 bitop3:0x78
	s_add_i32 s12, 0, 0x1b000
	v_lshlrev_b32_e32 v171, 4, v3
	v_add_u32_e32 v172, s12, v4
	s_lshl_b32 s12, s38, 5
	v_bitop3_b32 v3, v169, v168, 4 bitop3:0x36
	s_ashr_i32 s20, s12, 31
	v_lshlrev_b32_e32 v173, 4, v3
	v_bitop3_b32 v3, v169, v168, 8 bitop3:0x36
	v_lshlrev_b32_e32 v174, 4, v3
	v_bitop3_b32 v3, v169, v168, 12 bitop3:0x36
	s_add_u32 s66, s10, s12
	s_mov_b32 s64, 0
	v_lshlrev_b32_e32 v175, 4, v3
	s_addc_u32 s67, s11, s20
	s_mov_b32 s73, 1
	s_mov_b64 s[48:49], 0
	s_barrier
	s_branch .LBB0_1370

.LBB0_1384:
	s_ashr_i32 s65, s64, 31
	s_lshl_b32 s20, s73, 2
	s_lshl_b64 s[38:39], s[64:65], 17
	s_lshl_b64 s[74:75], s[20:21], 10
	v_lshl_add_u64 v[4:5], v[166:167], 0, s[38:39]
	v_lshl_add_u64 v[4:5], v[4:5], 0, s[74:75]
	s_waitcnt vmcnt(3)
	v_add_co_u32_e32 v130, vcc, 0x2000, v4
	s_nop 1
	v_addc_co_u32_e32 v131, vcc, 0, v5, vcc
	global_load_dwordx4 v[126:129], v[4:5], off sc0
	s_nop 0
	global_load_dwordx4 v[130:133], v[130:131], off
	s_waitcnt lgkmcnt(2)
	v_mfma_f32_16x16x32_bf16 v[102:105], v[114:117], v[6:9], v[102:105]
	s_waitcnt vmcnt(4)
	v_mfma_f32_16x16x32_bf16 v[98:101], v[122:125], v[6:9], v[98:101]
	s_waitcnt lgkmcnt(1)
	v_mfma_f32_16x16x32_bf16 v[90:93], v[114:117], v[10:13], v[90:93]
	v_mfma_f32_16x16x32_bf16 v[86:89], v[122:125], v[10:13], v[86:89]
	s_waitcnt lgkmcnt(0)
	v_mfma_f32_16x16x32_bf16 v[74:77], v[114:117], v[22:25], v[74:77]
	v_mfma_f32_16x16x32_bf16 v[70:73], v[122:125], v[22:25], v[70:73]

.LBB0_1388:
	global_load_dwordx4 v[146:149], v[4:5], off offset:1024 sc0
	s_waitcnt lgkmcnt(1)
	v_mfma_f32_16x16x32_bf16 v[82:85], v[114:117], v[158:161], v[82:85]
	s_waitcnt vmcnt(5)
	v_mfma_f32_16x16x32_bf16 v[78:81], v[122:125], v[158:161], v[78:81]
	v_mfma_f32_16x16x32_bf16 v[66:69], v[114:117], v[154:157], v[66:69]
	v_mfma_f32_16x16x32_bf16 v[62:65], v[122:125], v[154:157], v[62:65]
	s_waitcnt lgkmcnt(0)
	v_mfma_f32_16x16x32_bf16 v[50:53], v[114:117], v[162:165], v[50:53]
	v_mfma_f32_16x16x32_bf16 v[46:49], v[122:125], v[162:165], v[46:49]

.LBB0_1392:
	global_load_dwordx4 v[138:141], v[4:5], off offset:2048 sc0
	s_waitcnt lgkmcnt(1)
	v_mfma_f32_16x16x32_bf16 v[58:61], v[114:117], v[6:9], v[58:61]
	s_waitcnt vmcnt(6)
	v_mfma_f32_16x16x32_bf16 v[54:57], v[122:125], v[6:9], v[54:57]
	v_mfma_f32_16x16x32_bf16 v[42:45], v[114:117], v[10:13], v[42:45]
	v_mfma_f32_16x16x32_bf16 v[38:41], v[122:125], v[10:13], v[38:41]
	s_waitcnt lgkmcnt(0)
	v_mfma_f32_16x16x32_bf16 v[34:37], v[114:117], v[22:25], v[34:37]
	v_mfma_f32_16x16x32_bf16 v[30:33], v[122:125], v[22:25], v[30:33]

.LBB0_1396:
	v_add_co_u32_e32 v114, vcc, 0x2000, v4
	s_nop 1
	v_addc_co_u32_e32 v115, vcc, 0, v5, vcc
	global_load_dwordx4 v[122:125], v[114:115], off offset:1024 sc0
	s_waitcnt lgkmcnt(1)
	v_mfma_f32_16x16x32_bf16 v[102:105], v[106:109], v[158:161], v[102:105]
	s_waitcnt vmcnt(6)
	v_mfma_f32_16x16x32_bf16 v[98:101], v[118:121], v[158:161], v[98:101]
	v_mfma_f32_16x16x32_bf16 v[90:93], v[106:109], v[154:157], v[90:93]
	v_mfma_f32_16x16x32_bf16 v[86:89], v[118:121], v[154:157], v[86:89]
	s_waitcnt lgkmcnt(0)
	v_mfma_f32_16x16x32_bf16 v[74:77], v[106:109], v[162:165], v[74:77]
	v_mfma_f32_16x16x32_bf16 v[70:73], v[118:121], v[162:165], v[70:73]

.LBB0_1400:
	global_load_dwordx4 v[134:137], v[4:5], off offset:3072 sc0
	s_waitcnt lgkmcnt(1)
	v_mfma_f32_16x16x32_bf16 v[82:85], v[106:109], v[6:9], v[82:85]
	s_waitcnt vmcnt(7)
	v_mfma_f32_16x16x32_bf16 v[78:81], v[118:121], v[6:9], v[78:81]
	v_mfma_f32_16x16x32_bf16 v[66:69], v[106:109], v[10:13], v[66:69]
	v_mfma_f32_16x16x32_bf16 v[62:65], v[118:121], v[10:13], v[62:65]
	s_waitcnt lgkmcnt(0)
	v_mfma_f32_16x16x32_bf16 v[50:53], v[106:109], v[22:25], v[50:53]
	v_mfma_f32_16x16x32_bf16 v[46:49], v[118:121], v[22:25], v[46:49]

.LBB0_1404:
	v_add_co_u32_e32 v114, vcc, 0x2000, v4
	s_nop 1
	v_addc_co_u32_e32 v115, vcc, 0, v5, vcc
	global_load_dwordx4 v[150:153], v[114:115], off offset:2048 sc0
	s_waitcnt lgkmcnt(1)
	v_mfma_f32_16x16x32_bf16 v[58:61], v[106:109], v[158:161], v[58:61]
	s_waitcnt vmcnt(8)
	v_mfma_f32_16x16x32_bf16 v[54:57], v[118:121], v[158:161], v[54:57]
	v_mfma_f32_16x16x32_bf16 v[42:45], v[106:109], v[154:157], v[42:45]
	v_mfma_f32_16x16x32_bf16 v[38:41], v[118:121], v[154:157], v[38:41]
	s_waitcnt lgkmcnt(0)
	v_mfma_f32_16x16x32_bf16 v[34:37], v[106:109], v[162:165], v[34:37]
	v_mfma_f32_16x16x32_bf16 v[30:33], v[118:121], v[162:165], v[30:33]

.LBB0_1408:
	v_add_co_u32_e32 v4, vcc, 0x2000, v4
	s_nop 1
	v_addc_co_u32_e32 v5, vcc, 0, v5, vcc
	global_load_dwordx4 v[142:145], v[4:5], off offset:3072 sc0
	s_waitcnt vmcnt(10) lgkmcnt(1)
	v_mfma_f32_16x16x32_bf16 v[102:105], v[94:97], v[6:9], v[102:105]
	s_waitcnt vmcnt(8)
	v_mfma_f32_16x16x32_bf16 v[98:101], v[110:113], v[6:9], v[98:101]
	v_mfma_f32_16x16x32_bf16 v[90:93], v[94:97], v[10:13], v[90:93]
	v_mfma_f32_16x16x32_bf16 v[86:89], v[110:113], v[10:13], v[86:89]
	s_waitcnt lgkmcnt(0)
	v_mfma_f32_16x16x32_bf16 v[74:77], v[94:97], v[22:25], v[74:77]
	v_mfma_f32_16x16x32_bf16 v[70:73], v[110:113], v[22:25], v[70:73]

.LBB0_1430:
	s_cmp_lt_i32 s64, 3
	s_cselect_b64 s[38:39], -1, 0
	s_and_b64 s[74:75], s[38:39], exec
	s_cselect_b32 s12, 0, s73
	s_cmp_gt_i32 s73, 0
	s_cselect_b64 s[74:75], -1, 0
	s_and_b64 s[76:77], s[74:75], exec
	s_cselect_b32 s73, s12, 1
	s_and_b64 s[38:39], s[74:75], s[38:39]
	s_cmp_lg_u64 s[38:39], 0
	s_addc_u32 s64, s64, 0
	s_ashr_i32 s65, s64, 31
	s_lshl_b32 s20, s73, 2
	s_lshl_b64 s[38:39], s[64:65], 17
	s_lshl_b64 s[74:75], s[20:21], 10
	v_lshl_add_u64 v[4:5], v[166:167], 0, s[38:39]
	v_lshl_add_u64 v[4:5], v[4:5], 0, s[74:75]
	s_waitcnt vmcnt(10)
	v_add_co_u32_e32 v94, vcc, 0x2000, v4
	s_nop 1
	v_addc_co_u32_e32 v95, vcc, 0, v5, vcc
	global_load_dwordx4 v[126:129], v[4:5], off sc0
	global_load_dwordx4 v[130:133], v[94:95], off sc0
	s_waitcnt vmcnt(7) lgkmcnt(2)
	v_mfma_f32_16x16x32_bf16 v[102:105], v[146:149], v[14:17], v[102:105]
	s_waitcnt vmcnt(5)
	v_mfma_f32_16x16x32_bf16 v[98:101], v[122:125], v[14:17], v[98:101]
	s_waitcnt lgkmcnt(1)
	v_mfma_f32_16x16x32_bf16 v[90:93], v[146:149], v[18:21], v[90:93]
	v_mfma_f32_16x16x32_bf16 v[86:89], v[122:125], v[18:21], v[86:89]
	s_waitcnt lgkmcnt(0)
	v_mfma_f32_16x16x32_bf16 v[74:77], v[146:149], v[26:29], v[74:77]
	v_mfma_f32_16x16x32_bf16 v[70:73], v[122:125], v[26:29], v[70:73]

.LBB0_1434:
	global_load_dwordx4 v[114:117], v[4:5], off offset:1024 sc0
	s_waitcnt vmcnt(8) lgkmcnt(1)
	v_mfma_f32_16x16x32_bf16 v[82:85], v[146:149], v[158:161], v[82:85]
	s_waitcnt vmcnt(6)
	v_mfma_f32_16x16x32_bf16 v[78:81], v[122:125], v[158:161], v[78:81]
	v_mfma_f32_16x16x32_bf16 v[66:69], v[146:149], v[154:157], v[66:69]
	v_mfma_f32_16x16x32_bf16 v[62:65], v[122:125], v[154:157], v[62:65]
	s_waitcnt lgkmcnt(0)
	v_mfma_f32_16x16x32_bf16 v[50:53], v[146:149], v[162:165], v[50:53]
	v_mfma_f32_16x16x32_bf16 v[46:49], v[122:125], v[162:165], v[46:49]

.LBB0_1438:
	global_load_dwordx4 v[106:109], v[4:5], off offset:2048 sc0
	s_waitcnt vmcnt(9) lgkmcnt(1)
	v_mfma_f32_16x16x32_bf16 v[58:61], v[146:149], v[14:17], v[58:61]
	s_waitcnt vmcnt(7)
	v_mfma_f32_16x16x32_bf16 v[54:57], v[122:125], v[14:17], v[54:57]
	v_mfma_f32_16x16x32_bf16 v[42:45], v[146:149], v[18:21], v[42:45]
	v_mfma_f32_16x16x32_bf16 v[38:41], v[122:125], v[18:21], v[38:41]
	s_waitcnt lgkmcnt(0)
	v_mfma_f32_16x16x32_bf16 v[34:37], v[146:149], v[26:29], v[34:37]
	v_mfma_f32_16x16x32_bf16 v[30:33], v[122:125], v[26:29], v[30:33]

.LBB0_1442:
	v_add_co_u32_e32 v94, vcc, 0x2000, v4
	s_nop 1
	v_addc_co_u32_e32 v95, vcc, 0, v5, vcc
	global_load_dwordx4 v[122:125], v[94:95], off offset:1024 sc0
	s_waitcnt vmcnt(9) lgkmcnt(1)
	v_mfma_f32_16x16x32_bf16 v[102:105], v[138:141], v[158:161], v[102:105]
	s_waitcnt vmcnt(6)
	v_mfma_f32_16x16x32_bf16 v[98:101], v[150:153], v[158:161], v[98:101]
	v_mfma_f32_16x16x32_bf16 v[90:93], v[138:141], v[154:157], v[90:93]
	v_mfma_f32_16x16x32_bf16 v[86:89], v[150:153], v[154:157], v[86:89]
	s_waitcnt lgkmcnt(0)
	v_mfma_f32_16x16x32_bf16 v[74:77], v[138:141], v[162:165], v[74:77]
	v_mfma_f32_16x16x32_bf16 v[70:73], v[150:153], v[162:165], v[70:73]

.LBB0_1446:
	global_load_dwordx4 v[94:97], v[4:5], off offset:3072 sc0
	s_waitcnt vmcnt(10) lgkmcnt(1)
	v_mfma_f32_16x16x32_bf16 v[82:85], v[138:141], v[14:17], v[82:85]
	s_waitcnt vmcnt(7)
	v_mfma_f32_16x16x32_bf16 v[78:81], v[150:153], v[14:17], v[78:81]
	v_mfma_f32_16x16x32_bf16 v[66:69], v[138:141], v[18:21], v[66:69]
	v_mfma_f32_16x16x32_bf16 v[62:65], v[150:153], v[18:21], v[62:65]
	s_waitcnt lgkmcnt(0)
	v_mfma_f32_16x16x32_bf16 v[50:53], v[138:141], v[26:29], v[50:53]
	v_mfma_f32_16x16x32_bf16 v[46:49], v[150:153], v[26:29], v[46:49]

.LBB0_1450:
	s_waitcnt vmcnt(14)
	v_add_co_u32_e32 v110, vcc, 0x2000, v4
	s_nop 1
	v_addc_co_u32_e32 v111, vcc, 0, v5, vcc
	global_load_dwordx4 v[118:121], v[110:111], off offset:2048 sc0
	s_waitcnt vmcnt(11) lgkmcnt(1)
	v_mfma_f32_16x16x32_bf16 v[58:61], v[138:141], v[158:161], v[58:61]
	s_waitcnt vmcnt(8)
	v_mfma_f32_16x16x32_bf16 v[54:57], v[150:153], v[158:161], v[54:57]
	v_mfma_f32_16x16x32_bf16 v[42:45], v[138:141], v[154:157], v[42:45]
	v_mfma_f32_16x16x32_bf16 v[38:41], v[150:153], v[154:157], v[38:41]
	s_waitcnt lgkmcnt(0)
	v_mfma_f32_16x16x32_bf16 v[34:37], v[138:141], v[162:165], v[34:37]
	v_mfma_f32_16x16x32_bf16 v[30:33], v[150:153], v[162:165], v[30:33]

.LBB0_1454:
	v_add_co_u32_e32 v4, vcc, 0x2000, v4
	s_nop 1
	v_addc_co_u32_e32 v5, vcc, 0, v5, vcc
	global_load_dwordx4 v[110:113], v[4:5], off offset:3072 sc0
	s_waitcnt vmcnt(10) lgkmcnt(1)
	v_mfma_f32_16x16x32_bf16 v[102:105], v[134:137], v[14:17], v[102:105]
	s_waitcnt vmcnt(8)
	v_mfma_f32_16x16x32_bf16 v[98:101], v[142:145], v[14:17], v[98:101]
	v_mfma_f32_16x16x32_bf16 v[90:93], v[134:137], v[18:21], v[90:93]
	v_mfma_f32_16x16x32_bf16 v[86:89], v[142:145], v[18:21], v[86:89]
	s_waitcnt lgkmcnt(0)
	v_mfma_f32_16x16x32_bf16 v[74:77], v[134:137], v[26:29], v[74:77]
	v_mfma_f32_16x16x32_bf16 v[70:73], v[142:145], v[26:29], v[70:73]

.LBB0_1548:
	s_lshl_b32 s40, s56, 7
	v_mov_b32_e32 v92, v0
	s_waitcnt vmcnt(0)
	s_waitcnt lgkmcnt(0)
	s_barrier
	s_ashr_i32 s41, s40, 31
	s_lshl_b64 s[0:1], s[40:41], 10
	v_ashrrev_i32_e32 v84, 4, v92
	v_add_u32_e32 v86, 32, v84
	v_add_u32_e32 v88, 64, v84
	s_add_u32 s0, s53, s0
	v_lshlrev_b32_e32 v4, 3, v92
	v_ashrrev_i32_e32 v85, 31, v84
	v_ashrrev_i32_e32 v87, 31, v86
	v_ashrrev_i32_e32 v89, 31, v88
	s_addc_u32 s1, s54, s1
	v_and_b32_e32 v165, 0x78, v4
	v_lshlrev_b64 v[4:5], 10, v[84:85]
	v_lshlrev_b64 v[12:13], 10, v[86:87]
	v_lshlrev_b64 v[20:21], 10, v[88:89]
	v_lshl_add_u64 v[168:169], s[0:1], 0, v[4:5]
	v_lshlrev_b32_e32 v28, 2, v165
	v_mov_b32_e32 v29, v2
	v_lshl_add_u64 v[170:171], s[0:1], 0, v[12:13]
	v_lshl_add_u64 v[172:173], s[0:1], 0, v[20:21]
	v_lshl_add_u64 v[40:41], v[168:169], 0, v[28:29]
	v_lshl_add_u64 v[48:49], v[170:171], 0, v[28:29]
	v_lshl_add_u64 v[56:57], v[172:173], 0, v[28:29]
	global_load_dwordx4 v[4:7], v[40:41], off offset:16
	global_load_dwordx4 v[8:11], v[40:41], off
	global_load_dwordx4 v[12:15], v[48:49], off offset:16
	global_load_dwordx4 v[16:19], v[48:49], off
	global_load_dwordx4 v[20:23], v[56:57], off offset:16
	global_load_dwordx4 v[24:27], v[56:57], off
	v_add_u32_e32 v90, 0x60, v84
	v_ashrrev_i32_e32 v91, 31, v90
	v_lshlrev_b64 v[30:31], 10, v[90:91]
	v_lshl_add_u64 v[174:175], s[0:1], 0, v[30:31]
	v_lshl_add_u64 v[64:65], v[174:175], 0, v[28:29]
	v_readlane_b32 s0, v251, 59
	v_readlane_b32 s1, v251, 60
	v_lshlrev_b32_e32 v168, 9, v84
	v_mov_b32_e32 v169, v2
	v_lshlrev_b32_e32 v244, 1, v165
	v_mov_b32_e32 v245, v2
	v_lshl_add_u64 v[168:169], s[0:1], 0, v[168:169]
	s_mov_b64 s[0:1], 0x4000
	v_lshl_add_u64 v[170:171], v[168:169], 0, s[0:1]
	s_mov_b64 s[0:1], 0x8000
	v_lshl_add_u64 v[172:173], v[168:169], 0, s[0:1]
	s_mov_b64 s[0:1], 0xc000
	v_lshl_add_u64 v[174:175], v[168:169], 0, s[0:1]
	v_lshl_add_u64 v[236:237], v[168:169], 0, v[244:245]
	v_lshl_add_u64 v[238:239], v[170:171], 0, v[244:245]
	v_lshl_add_u64 v[240:241], v[172:173], 0, v[244:245]
	v_lshl_add_u64 v[242:243], v[174:175], 0, v[244:245]
	s_mov_b64 s[0:1], 0x200
	v_lshl_add_u64 v[168:169], v[168:169], 0, s[0:1]
	v_lshl_add_u64 v[170:171], v[170:171], 0, s[0:1]
	v_lshl_add_u64 v[172:173], v[172:173], 0, s[0:1]
	v_lshl_add_u64 v[174:175], v[174:175], 0, s[0:1]
	global_load_dwordx4 v[28:31], v[64:65], off
	global_load_dwordx4 v[32:35], v[64:65], off offset:16
	global_load_dwordx4 v[36:39], v[40:41], off offset:512
	s_nop 0
	global_load_dwordx4 v[40:43], v[40:41], off offset:528
	s_nop 0
	global_load_dwordx4 v[44:47], v[48:49], off offset:512
	s_nop 0
	global_load_dwordx4 v[48:51], v[48:49], off offset:528
	s_nop 0
	global_load_dwordx4 v[52:55], v[56:57], off offset:512
	s_nop 0
	global_load_dwordx4 v[56:59], v[56:57], off offset:528
	s_nop 0
	global_load_dwordx4 v[60:63], v[64:65], off offset:512
	s_nop 0
	global_load_dwordx4 v[64:67], v[64:65], off offset:528
	s_lshl_b64 s[0:1], s[40:41], 11
	v_readfirstlane_b32 s12, v92
	s_add_u32 s0, s8, s0
	s_addc_u32 s1, s9, s1
	s_ashr_i32 s12, s12, 6
	s_cmp_lt_i32 s12, 8
	s_cselect_b64 s[38:39], -1, 0
	s_and_b64 s[42:43], s[38:39], exec
	s_cselect_b32 s41, s12, 7
	s_mul_hi_i32 s43, s41, 0x14000
	s_mul_i32 s41, s41, 0x14000
	v_and_b32_e32 v68, 63, v92
	s_add_u32 s42, s20, s41
	v_readlane_b32 s18, v248, 29
	v_mov_b32_e32 v69, v2
	v_lshlrev_b32_e32 v68, 4, v68
	s_addc_u32 s43, s52, s43
	v_readlane_b32 s19, v248, 30
	v_xor_b32_e32 v71, v84, v92
	v_lshl_add_u64 v[176:177], s[42:43], 0, v[68:69]
	s_mov_b32 s19, s21
	v_lshlrev_b32_e32 v70, 8, v84
	v_lshlrev_b32_e32 v71, 4, v71
	v_and_or_b32 v93, v71, s84, v70
	v_bfe_u32 v192, v92, 4, 2
	v_and_b32_e32 v167, 15, v92
	v_add_u32_e32 v193, 0, v93
	s_lshl_b32 s42, s12, 13
	s_lshl_b32 s41, s12, 5
	s_lshl_b32 s12, s12, 9
	s_mov_b32 s26, s18
	s_add_i32 s48, s42, 0
	s_add_i32 s49, s12, 0
	s_mov_b32 s60, 2
	s_mov_b32 s58, 1
	v_writelane_b32 v248, s26, 29
	s_mov_b32 s59, 0
	s_ashr_i32 s47, s41, 31
	s_add_i32 s48, s48, 0x10000
	s_add_i32 s49, s49, 0x20000
	s_mov_b32 s50, -2
	s_mov_b32 s51, 0
	s_mov_b32 s42, 0
	v_writelane_b32 v248, s27, 30
	s_waitcnt vmcnt(9)
	v_cvt_pk_bf16_f32 v80, v28, v29
	s_waitcnt vmcnt(8)
	v_cvt_pk_bf16_f32 v82, v32, v33
	v_lshl_add_u64 v[32:33], v[176:177], 0, s[18:19]
	v_cvt_pk_bf16_f32 v71, v6, v7
	v_cvt_pk_bf16_f32 v76, v24, v25
	v_cvt_pk_bf16_f32 v77, v26, v27
	v_cvt_pk_bf16_f32 v78, v20, v21
	v_cvt_pk_bf16_f32 v79, v22, v23
	v_cvt_pk_bf16_f32 v81, v30, v31
	s_waitcnt vmcnt(6)
	v_cvt_pk_bf16_f32 v6, v40, v41
	v_cvt_pk_bf16_f32 v7, v42, v43
	global_load_dwordx4 v[40:43], v[32:33], off sc0
	global_load_dwordx4 v[28:31], v[32:33], off offset:1024 sc0
	global_load_dwordx4 v[24:27], v[32:33], off offset:2048 sc0
	global_load_dwordx4 v[20:23], v[32:33], off offset:3072 sc0
	v_add_co_u32_e32 v32, vcc, s22, v32
	v_cvt_pk_bf16_f32 v68, v8, v9
	s_nop 0
	v_addc_co_u32_e32 v33, vcc, 0, v33, vcc
	v_cvt_pk_bf16_f32 v69, v10, v11
	v_cvt_pk_bf16_f32 v70, v4, v5
	v_cvt_pk_bf16_f32 v74, v12, v13
	v_cvt_pk_bf16_f32 v4, v36, v37
	v_cvt_pk_bf16_f32 v5, v38, v39
	s_waitcnt vmcnt(9)
	v_cvt_pk_bf16_f32 v8, v44, v45
	v_cvt_pk_bf16_f32 v9, v46, v47
	s_waitcnt vmcnt(8)
	v_cvt_pk_bf16_f32 v10, v48, v49
	v_cvt_pk_bf16_f32 v11, v50, v51
	s_waitcnt vmcnt(7)
	v_cvt_pk_bf16_f32 v12, v52, v53
	v_cvt_pk_bf16_f32 v13, v54, v55
	global_load_dwordx4 v[52:55], v[32:33], off sc0
	global_load_dwordx4 v[48:51], v[32:33], off offset:1024 sc0
	global_load_dwordx4 v[44:47], v[32:33], off offset:2048 sc0
	global_load_dwordx4 v[36:39], v[32:33], off offset:3072 sc0
	v_bitop3_b32 v32, v192, v92, 15 bitop3:0x78
	v_cvt_pk_bf16_f32 v83, v34, v35
	v_lshlrev_b32_e32 v35, 4, v32
	v_bitop3_b32 v32, v192, v167, 4 bitop3:0x36
	v_cvt_pk_bf16_f32 v75, v14, v15
	s_waitcnt vmcnt(10)
	v_cvt_pk_bf16_f32 v14, v56, v57
	v_lshlrev_b32_e32 v56, 4, v32
	v_bitop3_b32 v32, v192, v167, 8 bitop3:0x36
	v_lshlrev_b32_e32 v57, 4, v32
	v_bitop3_b32 v32, v192, v167, 12 bitop3:0x36
	v_cvt_pk_bf16_f32 v15, v58, v59
	v_lshlrev_b32_e32 v58, 4, v32
	v_lshlrev_b64 v[32:33], 11, v[84:85]
	v_lshl_add_u64 v[178:179], s[0:1], 0, v[32:33]
	v_lshlrev_b64 v[32:33], 11, v[86:87]
	v_lshl_add_u64 v[180:181], s[0:1], 0, v[32:33]
	v_lshlrev_b64 v[32:33], 11, v[88:89]
	v_cvt_pk_bf16_f32 v72, v16, v17
	v_cvt_pk_bf16_f32 v73, v18, v19
	global_store_dwordx4 v[236:237], v[68:71], off
	global_store_dwordx4 v[238:239], v[72:75], off
	global_store_dwordx4 v[240:241], v[76:79], off
	global_store_dwordx4 v[242:243], v[80:83], off
	ds_write_b128 v193, v[68:71]
	ds_write_b128 v193, v[72:75] offset:8192
	ds_write_b128 v193, v[76:79] offset:16384
	ds_write_b128 v193, v[80:83] offset:24576
	v_lshl_add_u32 v34, v167, 8, 0
	v_lshl_add_u64 v[182:183], s[0:1], 0, v[32:33]
	v_lshlrev_b64 v[32:33], 11, v[90:91]
	v_mov_b32_e32 v68, 0
	s_waitcnt vmcnt(13)
	v_cvt_pk_bf16_f32 v16, v60, v61
	v_cvt_pk_bf16_f32 v17, v62, v63
	s_waitcnt vmcnt(12)
	v_cvt_pk_bf16_f32 v18, v64, v65
	v_cvt_pk_bf16_f32 v19, v66, v67
	global_store_dwordx4 v[236:237], v[4:7], off offset:256
	global_store_dwordx4 v[238:239], v[8:11], off offset:256
	global_store_dwordx4 v[240:241], v[12:15], off offset:256
	global_store_dwordx4 v[242:243], v[16:19], off offset:256
	v_lshl_add_u64 v[184:185], s[0:1], 0, v[32:33]
	v_add_u32_e32 v194, v34, v35
	v_add_u32_e32 v195, v34, v56
	v_add_u32_e32 v196, v34, v57
	v_add_u32_e32 v197, v34, v58
	v_mov_b32_e32 v69, v68
	v_mov_b32_e32 v70, v68
	v_mov_b32_e32 v71, v68
	v_mov_b32_e32 v72, v68
	v_mov_b32_e32 v73, v68
	v_mov_b32_e32 v74, v68
	v_mov_b32_e32 v75, v68
	v_mov_b32_e32 v76, v68
	v_mov_b32_e32 v77, v68
	v_mov_b32_e32 v78, v68
	v_mov_b32_e32 v79, v68
	v_mov_b32_e32 v84, v68
	v_mov_b32_e32 v85, v68
	v_mov_b32_e32 v86, v68
	v_mov_b32_e32 v87, v68
	v_mov_b32_e32 v88, v68
	v_mov_b32_e32 v89, v68
	v_mov_b32_e32 v90, v68
	v_mov_b32_e32 v91, v68
	v_mov_b32_e32 v92, v68
	v_mov_b32_e32 v93, v68
	v_mov_b32_e32 v94, v68
	v_mov_b32_e32 v95, v68
	v_mov_b32_e32 v96, v68
	v_mov_b32_e32 v97, v68
	v_mov_b32_e32 v98, v68
	v_mov_b32_e32 v99, v68
	v_mov_b32_e32 v100, v68
	v_mov_b32_e32 v101, v68
	v_mov_b32_e32 v102, v68
	v_mov_b32_e32 v103, v68
	v_mov_b32_e32 v60, v68
	v_mov_b32_e32 v61, v68
	v_mov_b32_e32 v62, v68
	v_mov_b32_e32 v63, v68
	v_mov_b32_e32 v64, v68
	v_mov_b32_e32 v65, v68
	v_mov_b32_e32 v66, v68
	v_mov_b32_e32 v67, v68
	v_mov_b32_e32 v104, v68
	v_mov_b32_e32 v105, v68
	v_mov_b32_e32 v106, v68
	v_mov_b32_e32 v107, v68
	v_mov_b32_e32 v108, v68
	v_mov_b32_e32 v109, v68
	v_mov_b32_e32 v110, v68
	v_mov_b32_e32 v111, v68
	v_mov_b32_e32 v116, v68
	v_mov_b32_e32 v117, v68
	v_mov_b32_e32 v118, v68
	v_mov_b32_e32 v119, v68
	v_mov_b32_e32 v120, v68
	v_mov_b32_e32 v121, v68
	v_mov_b32_e32 v122, v68
	v_mov_b32_e32 v123, v68
	v_mov_b32_e32 v132, v68
	v_mov_b32_e32 v133, v68
	v_mov_b32_e32 v134, v68
	v_mov_b32_e32 v135, v68
	v_mov_b32_e32 v136, v68
	v_mov_b32_e32 v137, v68
	v_mov_b32_e32 v138, v68
	v_mov_b32_e32 v139, v68
	s_waitcnt lgkmcnt(0)
	s_barrier
	s_branch .LBB0_1552

.LBB0_1556:
	ds_read_b128 v[152:155], v194
	ds_read_b128 v[148:151], v194 offset:4096
	ds_read_b128 v[140:143], v194 offset:8192
	ds_read_b128 v[144:147], v194 offset:12288
	ds_read_b128 v[128:131], v194 offset:16384
	ds_read_b128 v[124:127], v194 offset:20480
	ds_read_b128 v[112:115], v194 offset:24576
	ds_read_b128 v[80:83], v194 offset:28672
	s_lshl_b32 s0, s60, 7
	s_add_i32 s1, s0, 0xfffffb00
	s_cmp_gt_i32 s60, 9
	s_cselect_b32 s0, s1, s0
	v_or_b32_e32 v186, s0, v165
	s_movk_i32 s0, 0xff
	v_cmp_lt_i32_e32 vcc, s0, v186
	v_mov_b32_e32 v187, v2
	s_nop 0
	v_cndmask_b32_e32 v32, v168, v178, vcc
	v_cndmask_b32_e32 v33, v169, v179, vcc
	v_lshl_add_u64 v[32:33], v[186:187], 1, v[32:33]
	global_load_dwordx4 v[32:35], v[32:33], off offset:-512
	v_cndmask_b32_e32 v56, v170, v180, vcc
	v_cndmask_b32_e32 v57, v171, v181, vcc
	v_lshl_add_u64 v[56:57], v[186:187], 1, v[56:57]
	global_load_dwordx4 v[56:59], v[56:57], off offset:-512
	s_waitcnt vmcnt(7) lgkmcnt(7)
	v_mfma_f32_16x16x32_bf16 v[136:139], v[40:43], v[152:155], v[136:139]
	s_waitcnt vmcnt(3)
	v_mfma_f32_16x16x32_bf16 v[132:135], v[52:55], v[152:155], v[132:135]
	s_waitcnt lgkmcnt(6)
	v_mfma_f32_16x16x32_bf16 v[120:123], v[40:43], v[148:151], v[120:123]
	v_mfma_f32_16x16x32_bf16 v[116:119], v[52:55], v[148:151], v[116:119]
	s_waitcnt lgkmcnt(5)
	v_mfma_f32_16x16x32_bf16 v[108:111], v[40:43], v[140:143], v[108:111]
	v_mfma_f32_16x16x32_bf16 v[104:107], v[52:55], v[140:143], v[104:107]
	s_waitcnt lgkmcnt(4)
	v_mfma_f32_16x16x32_bf16 v[140:143], v[40:43], v[144:147], v[64:67]
	v_mfma_f32_16x16x32_bf16 v[144:147], v[52:55], v[144:147], v[60:63]
	ds_read_b128 v[160:163], v195
	ds_read_b128 v[156:159], v195 offset:4096
	ds_read_b128 v[152:155], v195 offset:8192
	ds_read_b128 v[148:151], v195 offset:12288
	v_cndmask_b32_e32 v60, v172, v182, vcc
	v_cndmask_b32_e32 v61, v173, v183, vcc
	v_lshl_add_u64 v[60:61], v[186:187], 1, v[60:61]
	global_load_dwordx4 v[60:63], v[60:61], off offset:-512
	v_cndmask_b32_e32 v64, v174, v184, vcc
	v_cndmask_b32_e32 v65, v175, v185, vcc
	v_lshl_add_u64 v[64:65], v[186:187], 1, v[64:65]
	global_load_dwordx4 v[64:67], v[64:65], off offset:-512
	s_add_i32 s0, s59, s23
	s_add_i32 s1, s0, -4
	s_cmp_gt_i32 s0, 3
	s_cselect_b32 s0, s1, s0
	s_lshl_b32 s1, s58, 2
	s_sub_i32 s12, s1, 40
	s_cmp_gt_i32 s58, 9
	s_cselect_b32 s1, s12, s1
	s_mul_hi_i32 s43, s0, 0x280
	s_mulk_i32 s0, 0x280
	s_ashr_i32 s12, s1, 31
	s_add_u32 s0, s0, s1
	s_addc_u32 s1, s43, s12
	s_lshl_b64 s[0:1], s[0:1], 10
	v_lshl_add_u64 v[186:187], v[176:177], 0, s[0:1]
	s_waitcnt lgkmcnt(7)
	v_mfma_f32_16x16x32_bf16 v[100:103], v[40:43], v[128:131], v[100:103]
	v_mfma_f32_16x16x32_bf16 v[96:99], v[52:55], v[128:131], v[96:99]
	s_waitcnt lgkmcnt(6)
	v_mfma_f32_16x16x32_bf16 v[92:95], v[40:43], v[124:127], v[92:95]
	v_mfma_f32_16x16x32_bf16 v[88:91], v[52:55], v[124:127], v[88:91]
	s_waitcnt lgkmcnt(5)
	v_mfma_f32_16x16x32_bf16 v[84:87], v[40:43], v[112:115], v[84:87]
	v_mfma_f32_16x16x32_bf16 v[112:115], v[52:55], v[112:115], v[76:79]
	s_waitcnt lgkmcnt(4)
	v_mfma_f32_16x16x32_bf16 v[72:75], v[40:43], v[80:83], v[72:75]
	v_mfma_f32_16x16x32_bf16 v[68:71], v[52:55], v[80:83], v[68:71]
	ds_read_b128 v[80:83], v195 offset:16384
	ds_read_b128 v[124:127], v195 offset:20480
	ds_read_b128 v[128:131], v195 offset:24576
	ds_read_b128 v[198:201], v195 offset:28672
	v_add_co_u32_e32 v214, vcc, s22, v186
	s_nop 1
	v_addc_co_u32_e32 v215, vcc, 0, v187, vcc
	global_load_dwordx4 v[40:43], v[186:187], off sc0
	global_load_dwordx4 v[52:55], v[214:215], off sc0
	ds_write_b128 v193, v[4:7] offset:32768
	s_waitcnt lgkmcnt(8)
	v_mfma_f32_16x16x32_bf16 v[4:7], v[28:31], v[160:163], v[136:139]
	s_waitcnt lgkmcnt(7)
	v_mfma_f32_16x16x32_bf16 v[120:123], v[28:31], v[156:159], v[120:123]
	s_waitcnt lgkmcnt(6)
	v_mfma_f32_16x16x32_bf16 v[108:111], v[28:31], v[152:155], v[108:111]
	s_waitcnt vmcnt(4)
	v_mfma_f32_16x16x32_bf16 v[104:107], v[48:51], v[152:155], v[104:107]
	s_waitcnt lgkmcnt(5)
	v_mfma_f32_16x16x32_bf16 v[136:139], v[28:31], v[148:151], v[140:143]
	v_mfma_f32_16x16x32_bf16 v[140:143], v[48:51], v[148:151], v[144:147]
	v_mfma_f32_16x16x32_bf16 v[132:135], v[48:51], v[160:163], v[132:135]
	v_mfma_f32_16x16x32_bf16 v[116:119], v[48:51], v[156:159], v[116:119]
	s_nop 0
	ds_read_b128 v[144:147], v196
	ds_read_b128 v[148:151], v196 offset:4096
	ds_read_b128 v[152:155], v196 offset:8192
	ds_read_b128 v[156:159], v196 offset:12288
	global_load_dwordx4 v[76:79], v[186:187], off offset:1024 sc0
	ds_write_b128 v193, v[8:11] offset:40960
	s_waitcnt lgkmcnt(9)
	v_mfma_f32_16x16x32_bf16 v[8:11], v[28:31], v[80:83], v[100:103]
	v_mfma_f32_16x16x32_bf16 v[80:83], v[48:51], v[80:83], v[96:99]
	s_waitcnt lgkmcnt(8)
	v_mfma_f32_16x16x32_bf16 v[92:95], v[28:31], v[124:127], v[92:95]
	v_mfma_f32_16x16x32_bf16 v[88:91], v[48:51], v[124:127], v[88:91]
	s_waitcnt lgkmcnt(7)
	v_mfma_f32_16x16x32_bf16 v[84:87], v[28:31], v[128:131], v[84:87]
	v_mfma_f32_16x16x32_bf16 v[96:99], v[48:51], v[128:131], v[112:115]
	s_waitcnt lgkmcnt(6)
	v_mfma_f32_16x16x32_bf16 v[28:31], v[28:31], v[198:201], v[72:75]
	v_mfma_f32_16x16x32_bf16 v[100:103], v[48:51], v[198:201], v[68:71]
	ds_read_b128 v[112:115], v196 offset:16384
	ds_read_b128 v[124:127], v196 offset:20480
	ds_read_b128 v[128:131], v196 offset:24576
	ds_read_b128 v[160:163], v196 offset:28672
	global_load_dwordx4 v[72:75], v[186:187], off offset:2048 sc0
	global_load_dwordx4 v[48:51], v[214:215], off offset:1024 sc0
	ds_write_b128 v193, v[12:15] offset:49152
	s_waitcnt lgkmcnt(8)
	v_mfma_f32_16x16x32_bf16 v[120:123], v[24:27], v[148:151], v[120:123]
	s_waitcnt lgkmcnt(7)
	v_mfma_f32_16x16x32_bf16 v[108:111], v[24:27], v[152:155], v[108:111]
	s_waitcnt vmcnt(6)
	v_mfma_f32_16x16x32_bf16 v[104:107], v[44:47], v[152:155], v[104:107]
	v_mfma_f32_16x16x32_bf16 v[4:7], v[24:27], v[144:147], v[4:7]
	v_mfma_f32_16x16x32_bf16 v[12:15], v[44:47], v[144:147], v[132:135]
	v_mfma_f32_16x16x32_bf16 v[116:119], v[44:47], v[148:151], v[116:119]
	s_waitcnt lgkmcnt(6)
	v_mfma_f32_16x16x32_bf16 v[132:135], v[24:27], v[156:159], v[136:139]
	v_mfma_f32_16x16x32_bf16 v[144:147], v[44:47], v[156:159], v[140:143]
	s_nop 1
	ds_read_b128 v[136:139], v197
	ds_read_b128 v[148:151], v197 offset:4096
	ds_read_b128 v[152:155], v197 offset:8192
	ds_read_b128 v[156:159], v197 offset:12288
	global_load_dwordx4 v[68:71], v[186:187], off offset:3072 sc0
	ds_write_b128 v193, v[16:19] offset:57344
	s_waitcnt lgkmcnt(9)
	v_mfma_f32_16x16x32_bf16 v[8:11], v[24:27], v[112:115], v[8:11]
	s_waitcnt lgkmcnt(8)
	v_mfma_f32_16x16x32_bf16 v[92:95], v[24:27], v[124:127], v[92:95]
	v_mfma_f32_16x16x32_bf16 v[88:91], v[44:47], v[124:127], v[88:91]
	s_waitcnt lgkmcnt(7)
	v_mfma_f32_16x16x32_bf16 v[84:87], v[24:27], v[128:131], v[84:87]
	s_waitcnt lgkmcnt(6)
	v_mfma_f32_16x16x32_bf16 v[24:27], v[24:27], v[160:163], v[28:31]
	v_mfma_f32_16x16x32_bf16 v[198:201], v[44:47], v[112:115], v[80:83]
	v_mfma_f32_16x16x32_bf16 v[128:131], v[44:47], v[128:131], v[96:99]
	v_mfma_f32_16x16x32_bf16 v[160:163], v[44:47], v[160:163], v[100:103]
	ds_read_b128 v[28:31], v197 offset:16384
	ds_read_b128 v[202:205], v197 offset:20480
	ds_read_b128 v[224:227], v197 offset:24576
	ds_read_b128 v[228:231], v197 offset:28672
	global_load_dwordx4 v[44:47], v[214:215], off offset:2048 sc0
	s_waitcnt lgkmcnt(8)
	v_mfma_f32_16x16x32_bf16 v[140:143], v[20:23], v[136:139], v[4:7]
	s_waitcnt vmcnt(7)
	v_mfma_f32_16x16x32_bf16 v[136:139], v[36:39], v[136:139], v[12:15]
	s_waitcnt lgkmcnt(7)
	v_mfma_f32_16x16x32_bf16 v[124:127], v[20:23], v[148:151], v[120:123]
	v_mfma_f32_16x16x32_bf16 v[120:123], v[36:39], v[148:151], v[116:119]
	s_waitcnt lgkmcnt(6)
	v_mfma_f32_16x16x32_bf16 v[112:115], v[20:23], v[152:155], v[108:111]
	v_mfma_f32_16x16x32_bf16 v[108:111], v[36:39], v[152:155], v[104:107]
	s_waitcnt lgkmcnt(5)
	v_mfma_f32_16x16x32_bf16 v[104:107], v[20:23], v[156:159], v[132:135]
	v_mfma_f32_16x16x32_bf16 v[16:19], v[36:39], v[156:159], v[144:147]
	global_load_dwordx4 v[80:83], v[214:215], off offset:3072 sc0
	s_waitcnt lgkmcnt(3)
	v_mfma_f32_16x16x32_bf16 v[100:103], v[20:23], v[28:31], v[8:11]
	v_mfma_f32_16x16x32_bf16 v[96:99], v[36:39], v[28:31], v[198:201]
	s_waitcnt lgkmcnt(2)
	v_mfma_f32_16x16x32_bf16 v[92:95], v[20:23], v[202:205], v[92:95]
	v_mfma_f32_16x16x32_bf16 v[88:91], v[36:39], v[202:205], v[88:91]
	s_waitcnt lgkmcnt(1)
	v_mfma_f32_16x16x32_bf16 v[84:87], v[20:23], v[224:227], v[84:87]
	v_mfma_f32_16x16x32_bf16 v[28:31], v[36:39], v[224:227], v[128:131]
	s_waitcnt lgkmcnt(0)
	v_mfma_f32_16x16x32_bf16 v[24:27], v[20:23], v[228:231], v[24:27]
	v_mfma_f32_16x16x32_bf16 v[20:23], v[36:39], v[228:231], v[160:163]
	s_cmp_eq_u32 s42, 1
	s_cselect_b64 s[0:1], -1, 0
	s_and_b64 s[0:1], s[0:1], s[38:39]
	s_andn2_b64 vcc, exec, s[0:1]
	s_cbranch_vccnz .LBB0_1574
	v_mov_b32_e32 v4, v192
	v_mov_b32_e32 v6, v167
	v_cvt_pk_bf16_f32 v5, v142, v143
	v_lshlrev_b32_e32 v7, 7, v4
	v_lshlrev_b32_e32 v6, 3, v6
	v_cvt_pk_bf16_f32 v4, v140, v141
	v_add3_u32 v8, s48, v7, v6
	v_cvt_pk_bf16_f32 v6, v136, v137
	v_cvt_pk_bf16_f32 v7, v138, v139
	ds_write2st64_b64 v8, v[4:5], v[6:7] offset1:1
	v_cvt_pk_bf16_f32 v4, v124, v125
	v_cvt_pk_bf16_f32 v5, v126, v127
	v_cvt_pk_bf16_f32 v6, v120, v121
	v_cvt_pk_bf16_f32 v7, v122, v123
	ds_write2st64_b64 v8, v[4:5], v[6:7] offset0:2 offset1:3
	v_cvt_pk_bf16_f32 v4, v112, v113
	v_cvt_pk_bf16_f32 v5, v114, v115
	v_cvt_pk_bf16_f32 v6, v108, v109
	v_cvt_pk_bf16_f32 v7, v110, v111
	ds_write2st64_b64 v8, v[4:5], v[6:7] offset0:4 offset1:5
	v_cvt_pk_bf16_f32 v4, v104, v105
	v_cvt_pk_bf16_f32 v5, v106, v107
	v_cvt_pk_bf16_f32 v6, v16, v17
	v_cvt_pk_bf16_f32 v7, v18, v19
	ds_write2st64_b64 v8, v[4:5], v[6:7] offset0:6 offset1:7
	v_cvt_pk_bf16_f32 v4, v100, v101
	v_cvt_pk_bf16_f32 v5, v102, v103
	v_cvt_pk_bf16_f32 v6, v96, v97
	v_cvt_pk_bf16_f32 v7, v98, v99
	ds_write2st64_b64 v8, v[4:5], v[6:7] offset0:8 offset1:9
	v_cvt_pk_bf16_f32 v4, v92, v93
	v_cvt_pk_bf16_f32 v5, v94, v95
	v_cvt_pk_bf16_f32 v6, v88, v89
	v_cvt_pk_bf16_f32 v7, v90, v91
	ds_write2st64_b64 v8, v[4:5], v[6:7] offset0:10 offset1:11
	v_cvt_pk_bf16_f32 v4, v84, v85
	v_cvt_pk_bf16_f32 v5, v86, v87
	v_cvt_pk_bf16_f32 v6, v28, v29
	v_cvt_pk_bf16_f32 v7, v30, v31
	ds_write2st64_b64 v8, v[4:5], v[6:7] offset0:12 offset1:13
	v_cvt_pk_bf16_f32 v6, v20, v21
	v_mov_b32_e32 v20, 0
	v_cvt_pk_bf16_f32 v4, v24, v25
	v_cvt_pk_bf16_f32 v5, v26, v27
	v_cvt_pk_bf16_f32 v7, v22, v23
	v_mov_b32_e32 v21, v20
	v_mov_b32_e32 v22, v20
	v_mov_b32_e32 v23, v20
	v_mov_b32_e32 v24, v20
	v_mov_b32_e32 v25, v20
	v_mov_b32_e32 v26, v20
	v_mov_b32_e32 v27, v20
	v_mov_b32_e32 v28, v20
	v_mov_b32_e32 v29, v20
	v_mov_b32_e32 v30, v20
	v_mov_b32_e32 v31, v20
	v_mov_b32_e32 v84, v20
	v_mov_b32_e32 v85, v20
	v_mov_b32_e32 v86, v20
	v_mov_b32_e32 v87, v20
	v_mov_b32_e32 v88, v20
	v_mov_b32_e32 v89, v20
	v_mov_b32_e32 v90, v20
	v_mov_b32_e32 v91, v20
	v_mov_b32_e32 v92, v20
	v_mov_b32_e32 v93, v20
	v_mov_b32_e32 v94, v20
	v_mov_b32_e32 v95, v20
	v_mov_b32_e32 v96, v20
	v_mov_b32_e32 v97, v20
	v_mov_b32_e32 v98, v20
	v_mov_b32_e32 v99, v20
	v_mov_b32_e32 v100, v20
	v_mov_b32_e32 v101, v20
	v_mov_b32_e32 v102, v20
	v_mov_b32_e32 v103, v20
	v_mov_b32_e32 v16, v20
	v_mov_b32_e32 v17, v20
	v_mov_b32_e32 v18, v20
	v_mov_b32_e32 v19, v20
	v_mov_b32_e32 v104, v20
	v_mov_b32_e32 v105, v20
	v_mov_b32_e32 v106, v20
	v_mov_b32_e32 v107, v20
	v_mov_b32_e32 v108, v20
	v_mov_b32_e32 v109, v20
	v_mov_b32_e32 v110, v20
	v_mov_b32_e32 v111, v20
	v_mov_b32_e32 v112, v20
	v_mov_b32_e32 v113, v20
	v_mov_b32_e32 v114, v20
	v_mov_b32_e32 v115, v20
	v_mov_b32_e32 v120, v20
	v_mov_b32_e32 v121, v20
	v_mov_b32_e32 v122, v20
	v_mov_b32_e32 v123, v20
	v_mov_b32_e32 v124, v20
	v_mov_b32_e32 v125, v20
	v_mov_b32_e32 v126, v20
	v_mov_b32_e32 v127, v20
	v_mov_b32_e32 v136, v20
	v_mov_b32_e32 v137, v20
	v_mov_b32_e32 v138, v20
	v_mov_b32_e32 v139, v20
	v_mov_b32_e32 v140, v20
	v_mov_b32_e32 v141, v20
	v_mov_b32_e32 v142, v20
	v_mov_b32_e32 v143, v20
	ds_write2st64_b64 v8, v[4:5], v[6:7] offset0:14 offset1:15

.LBB0_1584:
	ds_read_b128 v[152:155], v194 offset:32768
	ds_read_b128 v[148:151], v194 offset:36864
	ds_read_b128 v[144:147], v194 offset:40960
	ds_read_b128 v[12:15], v194 offset:45056
	ds_read_b128 v[132:135], v194 offset:49152
	ds_read_b128 v[128:131], v194 offset:53248
	ds_read_b128 v[116:119], v194 offset:57344
	ds_read_b128 v[36:39], v194 offset:61440
	s_add_i32 s12, s60, 1
	s_cmp_lg_u32 s12, 10
	s_cselect_b32 s60, s12, 0
	s_lshl_b32 s12, s60, 7
	s_add_i32 s42, s12, 0xfffffb00
	s_cmp_gt_i32 s60, 9
	s_cselect_b32 s12, s42, s12
	v_or_b32_e32 v186, s12, v165
	s_movk_i32 s12, 0xff
	v_cmp_lt_i32_e32 vcc, s12, v186
	v_mov_b32_e32 v187, v2
	s_nop 0
	v_cndmask_b32_e32 v4, v168, v178, vcc
	v_cndmask_b32_e32 v5, v169, v179, vcc
	v_lshl_add_u64 v[4:5], v[186:187], 1, v[4:5]
	global_load_dwordx4 v[4:7], v[4:5], off offset:-512
	v_cndmask_b32_e32 v8, v170, v180, vcc
	v_cndmask_b32_e32 v9, v171, v181, vcc
	v_lshl_add_u64 v[8:9], v[186:187], 1, v[8:9]
	global_load_dwordx4 v[8:11], v[8:9], off offset:-512
	s_waitcnt vmcnt(7) lgkmcnt(7)
	v_mfma_f32_16x16x32_bf16 v[140:143], v[40:43], v[152:155], v[140:143]
	s_waitcnt vmcnt(6)
	v_mfma_f32_16x16x32_bf16 v[136:139], v[52:55], v[152:155], v[136:139]
	s_waitcnt lgkmcnt(6)
	v_mfma_f32_16x16x32_bf16 v[124:127], v[40:43], v[148:151], v[124:127]
	v_mfma_f32_16x16x32_bf16 v[120:123], v[52:55], v[148:151], v[120:123]
	s_waitcnt lgkmcnt(5)
	v_mfma_f32_16x16x32_bf16 v[112:115], v[40:43], v[144:147], v[112:115]
	v_mfma_f32_16x16x32_bf16 v[108:111], v[52:55], v[144:147], v[108:111]
	s_waitcnt lgkmcnt(4)
	v_mfma_f32_16x16x32_bf16 v[104:107], v[40:43], v[12:15], v[104:107]
	v_mfma_f32_16x16x32_bf16 v[144:147], v[52:55], v[12:15], v[16:19]
	ds_read_b128 v[160:163], v195 offset:32768
	ds_read_b128 v[156:159], v195 offset:36864
	ds_read_b128 v[152:155], v195 offset:40960
	ds_read_b128 v[148:151], v195 offset:45056
	v_cndmask_b32_e32 v12, v172, v182, vcc
	v_cndmask_b32_e32 v13, v173, v183, vcc
	v_lshl_add_u64 v[12:13], v[186:187], 1, v[12:13]
	global_load_dwordx4 v[12:15], v[12:13], off offset:-512
	v_cndmask_b32_e32 v16, v174, v184, vcc
	v_cndmask_b32_e32 v17, v175, v185, vcc
	v_lshl_add_u64 v[16:17], v[186:187], 1, v[16:17]
	global_load_dwordx4 v[16:19], v[16:17], off offset:-512
	s_add_i32 s12, s62, s23
	s_add_i32 s42, s12, -4
	s_cmp_gt_i32 s12, 3
	s_cselect_b32 s12, s42, s12
	s_lshl_b32 s42, s61, 2
	s_sub_i32 s43, s42, 40
	s_cmp_gt_i32 s61, 9
	s_cselect_b32 s42, s43, s42
	s_mul_hi_i32 s61, s12, 0x280
	s_mulk_i32 s12, 0x280
	s_ashr_i32 s43, s42, 31
	s_add_u32 s42, s12, s42
	s_addc_u32 s43, s61, s43
	s_lshl_b64 s[42:43], s[42:43], 10
	v_lshl_add_u64 v[186:187], v[176:177], 0, s[42:43]
	s_waitcnt lgkmcnt(7)
	v_mfma_f32_16x16x32_bf16 v[100:103], v[40:43], v[132:135], v[100:103]
	v_mfma_f32_16x16x32_bf16 v[96:99], v[52:55], v[132:135], v[96:99]
	s_waitcnt lgkmcnt(6)
	v_mfma_f32_16x16x32_bf16 v[92:95], v[40:43], v[128:131], v[92:95]
	v_mfma_f32_16x16x32_bf16 v[88:91], v[52:55], v[128:131], v[88:91]
	s_waitcnt lgkmcnt(5)
	v_mfma_f32_16x16x32_bf16 v[84:87], v[40:43], v[116:119], v[84:87]
	v_mfma_f32_16x16x32_bf16 v[116:119], v[52:55], v[116:119], v[28:31]
	s_waitcnt lgkmcnt(4)
	v_mfma_f32_16x16x32_bf16 v[24:27], v[40:43], v[36:39], v[24:27]
	v_mfma_f32_16x16x32_bf16 v[20:23], v[52:55], v[36:39], v[20:23]
	ds_read_b128 v[36:39], v195 offset:49152
	ds_read_b128 v[128:131], v195 offset:53248
	ds_read_b128 v[132:135], v195 offset:57344
	ds_read_b128 v[198:201], v195 offset:61440
	v_add_co_u32_e32 v214, vcc, s22, v186
	s_nop 1
	v_addc_co_u32_e32 v215, vcc, 0, v187, vcc
	global_load_dwordx4 v[40:43], v[186:187], off sc0
	global_load_dwordx4 v[52:55], v[214:215], off sc0
	ds_write_b128 v193, v[32:35]
	s_waitcnt vmcnt(5) lgkmcnt(8)
	v_mfma_f32_16x16x32_bf16 v[136:139], v[48:51], v[160:163], v[136:139]
	s_waitcnt lgkmcnt(7)
	v_mfma_f32_16x16x32_bf16 v[120:123], v[48:51], v[156:159], v[120:123]
	s_waitcnt lgkmcnt(6)
	v_mfma_f32_16x16x32_bf16 v[108:111], v[48:51], v[152:155], v[108:111]
	s_waitcnt lgkmcnt(5)
	v_mfma_f32_16x16x32_bf16 v[104:107], v[76:79], v[148:151], v[104:107]
	v_mfma_f32_16x16x32_bf16 v[32:35], v[76:79], v[160:163], v[140:143]
	v_mfma_f32_16x16x32_bf16 v[124:127], v[76:79], v[156:159], v[124:127]
	v_mfma_f32_16x16x32_bf16 v[112:115], v[76:79], v[152:155], v[112:115]
	v_mfma_f32_16x16x32_bf16 v[140:143], v[48:51], v[148:151], v[144:147]
	s_nop 2
	ds_read_b128 v[144:147], v196 offset:32768
	ds_read_b128 v[148:151], v196 offset:36864
	ds_read_b128 v[152:155], v196 offset:40960
	ds_read_b128 v[156:159], v196 offset:45056
	global_load_dwordx4 v[28:31], v[186:187], off offset:1024 sc0
	ds_write_b128 v193, v[56:59] offset:8192
	s_waitcnt lgkmcnt(9)
	v_mfma_f32_16x16x32_bf16 v[56:59], v[76:79], v[36:39], v[100:103]
	v_mfma_f32_16x16x32_bf16 v[36:39], v[48:51], v[36:39], v[96:99]
	s_waitcnt lgkmcnt(8)
	v_mfma_f32_16x16x32_bf16 v[92:95], v[76:79], v[128:131], v[92:95]
	v_mfma_f32_16x16x32_bf16 v[88:91], v[48:51], v[128:131], v[88:91]
	s_waitcnt lgkmcnt(7)
	v_mfma_f32_16x16x32_bf16 v[84:87], v[76:79], v[132:135], v[84:87]
	v_mfma_f32_16x16x32_bf16 v[96:99], v[48:51], v[132:135], v[116:119]
	s_waitcnt lgkmcnt(6)
	v_mfma_f32_16x16x32_bf16 v[76:79], v[76:79], v[198:201], v[24:27]
	v_mfma_f32_16x16x32_bf16 v[100:103], v[48:51], v[198:201], v[20:23]
	ds_read_b128 v[116:119], v196 offset:49152
	ds_read_b128 v[128:131], v196 offset:53248
	ds_read_b128 v[132:135], v196 offset:57344
	ds_read_b128 v[160:163], v196 offset:61440
	global_load_dwordx4 v[24:27], v[186:187], off offset:2048 sc0
	global_load_dwordx4 v[48:51], v[214:215], off offset:1024 sc0
	ds_write_b128 v193, v[60:63] offset:16384
	s_waitcnt vmcnt(6) lgkmcnt(9)
	v_mfma_f32_16x16x32_bf16 v[60:63], v[44:47], v[144:147], v[136:139]
	v_mfma_f32_16x16x32_bf16 v[32:35], v[72:75], v[144:147], v[32:35]
	s_waitcnt lgkmcnt(8)
	v_mfma_f32_16x16x32_bf16 v[124:127], v[72:75], v[148:151], v[124:127]
	v_mfma_f32_16x16x32_bf16 v[144:147], v[44:47], v[148:151], v[120:123]
	s_waitcnt lgkmcnt(7)
	v_mfma_f32_16x16x32_bf16 v[112:115], v[72:75], v[152:155], v[112:115]
	v_mfma_f32_16x16x32_bf16 v[148:151], v[44:47], v[152:155], v[108:111]
	s_waitcnt lgkmcnt(6)
	v_mfma_f32_16x16x32_bf16 v[152:155], v[72:75], v[156:159], v[104:107]
	v_mfma_f32_16x16x32_bf16 v[140:143], v[44:47], v[156:159], v[140:143]
	s_nop 1
	ds_read_b128 v[104:107], v197 offset:32768
	ds_read_b128 v[108:111], v197 offset:36864
	ds_read_b128 v[156:159], v197 offset:40960
	ds_read_b128 v[198:201], v197 offset:45056
	global_load_dwordx4 v[20:23], v[186:187], off offset:3072 sc0
	ds_write_b128 v193, v[64:67] offset:24576
	s_waitcnt lgkmcnt(9)
	v_mfma_f32_16x16x32_bf16 v[56:59], v[72:75], v[116:119], v[56:59]
	s_waitcnt lgkmcnt(8)
	v_mfma_f32_16x16x32_bf16 v[92:95], v[72:75], v[128:131], v[92:95]
	v_mfma_f32_16x16x32_bf16 v[88:91], v[44:47], v[128:131], v[88:91]
	s_waitcnt lgkmcnt(7)
	v_mfma_f32_16x16x32_bf16 v[84:87], v[72:75], v[132:135], v[84:87]
	s_waitcnt lgkmcnt(6)
	v_mfma_f32_16x16x32_bf16 v[72:75], v[72:75], v[160:163], v[76:79]
	v_mfma_f32_16x16x32_bf16 v[202:205], v[44:47], v[116:119], v[36:39]
	v_mfma_f32_16x16x32_bf16 v[128:131], v[44:47], v[132:135], v[96:99]
	v_mfma_f32_16x16x32_bf16 v[160:163], v[44:47], v[160:163], v[100:103]
	ds_read_b128 v[76:79], v197 offset:49152
	ds_read_b128 v[224:227], v197 offset:53248
	ds_read_b128 v[228:231], v197 offset:57344
	ds_read_b128 v[232:235], v197 offset:61440
	global_load_dwordx4 v[44:47], v[214:215], off offset:2048 sc0
	s_waitcnt lgkmcnt(8)
	v_mfma_f32_16x16x32_bf16 v[136:139], v[68:71], v[104:107], v[32:35]
	s_waitcnt vmcnt(7)
	v_mfma_f32_16x16x32_bf16 v[132:135], v[80:83], v[104:107], v[60:63]
	s_waitcnt lgkmcnt(7)
	v_mfma_f32_16x16x32_bf16 v[120:123], v[68:71], v[108:111], v[124:127]
	v_mfma_f32_16x16x32_bf16 v[116:119], v[80:83], v[108:111], v[144:147]
	s_waitcnt lgkmcnt(6)
	v_mfma_f32_16x16x32_bf16 v[108:111], v[68:71], v[156:159], v[112:115]
	v_mfma_f32_16x16x32_bf16 v[104:107], v[80:83], v[156:159], v[148:151]
	s_waitcnt lgkmcnt(5)
	v_mfma_f32_16x16x32_bf16 v[64:67], v[68:71], v[198:201], v[152:155]
	v_mfma_f32_16x16x32_bf16 v[60:63], v[80:83], v[198:201], v[140:143]
	global_load_dwordx4 v[36:39], v[214:215], off offset:3072 sc0
	s_waitcnt lgkmcnt(3)
	v_mfma_f32_16x16x32_bf16 v[100:103], v[68:71], v[76:79], v[56:59]
	v_mfma_f32_16x16x32_bf16 v[96:99], v[80:83], v[76:79], v[202:205]
	s_waitcnt lgkmcnt(2)
	v_mfma_f32_16x16x32_bf16 v[92:95], v[68:71], v[224:227], v[92:95]
	v_mfma_f32_16x16x32_bf16 v[88:91], v[80:83], v[224:227], v[88:91]
	s_waitcnt lgkmcnt(1)
	v_mfma_f32_16x16x32_bf16 v[84:87], v[68:71], v[228:231], v[84:87]
	v_mfma_f32_16x16x32_bf16 v[76:79], v[80:83], v[228:231], v[128:131]
	s_waitcnt lgkmcnt(0)
	v_mfma_f32_16x16x32_bf16 v[72:75], v[68:71], v[232:235], v[72:75]
	v_mfma_f32_16x16x32_bf16 v[68:71], v[80:83], v[232:235], v[160:163]
	s_cmp_eq_u32 s63, 1
	s_cselect_b64 s[42:43], -1, 0
	s_and_b64 s[42:43], s[42:43], s[38:39]
	s_andn2_b64 vcc, exec, s[42:43]
	s_cbranch_vccnz .LBB0_1602
	v_mov_b32_e32 v32, v192
	v_mov_b32_e32 v34, v167
	v_cvt_pk_bf16_f32 v33, v138, v139
	v_lshlrev_b32_e32 v35, 7, v32
	v_lshlrev_b32_e32 v34, 3, v34
	v_cvt_pk_bf16_f32 v32, v136, v137
	v_add3_u32 v56, s48, v35, v34
	v_cvt_pk_bf16_f32 v34, v132, v133
	v_cvt_pk_bf16_f32 v35, v134, v135
	ds_write2st64_b64 v56, v[32:33], v[34:35] offset1:1
	v_cvt_pk_bf16_f32 v32, v120, v121
	v_cvt_pk_bf16_f32 v33, v122, v123
	v_cvt_pk_bf16_f32 v34, v116, v117
	v_cvt_pk_bf16_f32 v35, v118, v119
	ds_write2st64_b64 v56, v[32:33], v[34:35] offset0:2 offset1:3
	v_cvt_pk_bf16_f32 v32, v108, v109
	v_cvt_pk_bf16_f32 v33, v110, v111
	v_cvt_pk_bf16_f32 v34, v104, v105
	v_cvt_pk_bf16_f32 v35, v106, v107
	ds_write2st64_b64 v56, v[32:33], v[34:35] offset0:4 offset1:5
	v_cvt_pk_bf16_f32 v32, v64, v65
	v_cvt_pk_bf16_f32 v33, v66, v67
	v_cvt_pk_bf16_f32 v34, v60, v61
	v_cvt_pk_bf16_f32 v35, v62, v63
	ds_write2st64_b64 v56, v[32:33], v[34:35] offset0:6 offset1:7
	v_cvt_pk_bf16_f32 v32, v100, v101
	v_cvt_pk_bf16_f32 v33, v102, v103
	v_cvt_pk_bf16_f32 v34, v96, v97
	v_cvt_pk_bf16_f32 v35, v98, v99
	ds_write2st64_b64 v56, v[32:33], v[34:35] offset0:8 offset1:9
	v_cvt_pk_bf16_f32 v32, v92, v93
	v_cvt_pk_bf16_f32 v33, v94, v95
	v_cvt_pk_bf16_f32 v34, v88, v89
	v_cvt_pk_bf16_f32 v35, v90, v91
	ds_write2st64_b64 v56, v[32:33], v[34:35] offset0:10 offset1:11
	v_cvt_pk_bf16_f32 v32, v84, v85
	v_cvt_pk_bf16_f32 v33, v86, v87
	v_cvt_pk_bf16_f32 v34, v76, v77
	v_cvt_pk_bf16_f32 v35, v78, v79
	ds_write2st64_b64 v56, v[32:33], v[34:35] offset0:12 offset1:13
	v_cvt_pk_bf16_f32 v34, v68, v69
	v_mov_b32_e32 v68, 0
	v_cvt_pk_bf16_f32 v32, v72, v73
	v_cvt_pk_bf16_f32 v33, v74, v75
	v_cvt_pk_bf16_f32 v35, v70, v71
	v_mov_b32_e32 v69, v68
	v_mov_b32_e32 v70, v68
	v_mov_b32_e32 v71, v68
	v_mov_b32_e32 v72, v68
	v_mov_b32_e32 v73, v68
	v_mov_b32_e32 v74, v68
	v_mov_b32_e32 v75, v68
	v_mov_b32_e32 v76, v68
	v_mov_b32_e32 v77, v68
	v_mov_b32_e32 v78, v68
	v_mov_b32_e32 v79, v68
	v_mov_b32_e32 v84, v68
	v_mov_b32_e32 v85, v68
	v_mov_b32_e32 v86, v68
	v_mov_b32_e32 v87, v68
	v_mov_b32_e32 v88, v68
	v_mov_b32_e32 v89, v68
	v_mov_b32_e32 v90, v68
	v_mov_b32_e32 v91, v68
	v_mov_b32_e32 v92, v68
	v_mov_b32_e32 v93, v68
	v_mov_b32_e32 v94, v68
	v_mov_b32_e32 v95, v68
	v_mov_b32_e32 v96, v68
	v_mov_b32_e32 v97, v68
	v_mov_b32_e32 v98, v68
	v_mov_b32_e32 v99, v68
	v_mov_b32_e32 v100, v68
	v_mov_b32_e32 v101, v68
	v_mov_b32_e32 v102, v68
	v_mov_b32_e32 v103, v68
	v_mov_b32_e32 v60, v68
	v_mov_b32_e32 v61, v68
	v_mov_b32_e32 v62, v68
	v_mov_b32_e32 v63, v68
	v_mov_b32_e32 v64, v68
	v_mov_b32_e32 v65, v68
	v_mov_b32_e32 v66, v68
	v_mov_b32_e32 v67, v68
	v_mov_b32_e32 v104, v68
	v_mov_b32_e32 v105, v68
	v_mov_b32_e32 v106, v68
	v_mov_b32_e32 v107, v68
	v_mov_b32_e32 v108, v68
	v_mov_b32_e32 v109, v68
	v_mov_b32_e32 v110, v68
	v_mov_b32_e32 v111, v68
	v_mov_b32_e32 v116, v68
	v_mov_b32_e32 v117, v68
	v_mov_b32_e32 v118, v68
	v_mov_b32_e32 v119, v68
	v_mov_b32_e32 v120, v68
	v_mov_b32_e32 v121, v68
	v_mov_b32_e32 v122, v68
	v_mov_b32_e32 v123, v68
	v_mov_b32_e32 v132, v68
	v_mov_b32_e32 v133, v68
	v_mov_b32_e32 v134, v68
	v_mov_b32_e32 v135, v68
	v_mov_b32_e32 v136, v68
	v_mov_b32_e32 v137, v68
	v_mov_b32_e32 v138, v68
	v_mov_b32_e32 v139, v68
	ds_write2st64_b64 v56, v[32:33], v[34:35] offset0:14 offset1:15
.LBB0_1602:
	s_add_i32 s42, s63, 1
	s_cmp_lg_u32 s42, 10
	s_cbranch_scc1 .LBB0_1551
	s_and_b64 vcc, exec, s[0:1]
	s_cbranch_vccnz .LBB0_1550
	s_add_i32 s0, s51, s23
	s_lshl_b32 s1, s0, 8
	s_add_i32 s12, s1, 0xfffffc00
	s_cmp_gt_i32 s0, 3
	s_cselect_b32 s0, s12, s1
	v_mov_b32_e32 v153, v192
	v_mov_b32_e32 v152, v167
	s_ashr_i32 s1, s0, 31
	s_add_u32 s0, s0, s41
	v_add_u32_e32 v32, s40, v152
	v_lshlrev_b32_e32 v34, 3, v153
	v_ashrrev_i32_e32 v33, 31, v32
	v_ashrrev_i32_e32 v35, 31, v34
	s_addc_u32 s1, s1, s47
	v_lshlrev_b64 v[32:33], 10, v[32:33]
	v_lshl_add_u64 v[34:35], s[0:1], 0, v[34:35]
	v_lshl_add_u64 v[32:33], v[34:35], 0, v[32:33]
	v_lshlrev_b64 v[186:187], 1, v[32:33]
	v_lshl_add_u64 v[32:33], s[8:9], 0, v[186:187]
	global_load_dwordx4 v[156:159], v[32:33], off sc0
	v_add_co_u32_e32 v34, vcc, s14, v32
	s_mov_b32 s3, 0x10000
	s_nop 0
	v_addc_co_u32_e32 v35, vcc, 0, v33, vcc
	global_load_dwordx4 v[140:143], v[34:35], off
	v_add_co_u32_e32 v34, vcc, s3, v32
	s_mov_b32 s12, 0x18000
	s_nop 0
	v_addc_co_u32_e32 v35, vcc, 0, v33, vcc
	global_load_dwordx4 v[128:131], v[34:35], off
	v_add_co_u32_e32 v34, vcc, s12, v32
	s_mov_b32 s1, 0x20000
	s_nop 0
	v_addc_co_u32_e32 v35, vcc, 0, v33, vcc
	global_load_dwordx4 v[124:127], v[34:35], off
	v_add_co_u32_e32 v34, vcc, s1, v32
	s_mov_b32 s18, 0x28000
	s_nop 0
	v_addc_co_u32_e32 v35, vcc, 0, v33, vcc
	global_load_dwordx4 v[112:115], v[34:35], off
	v_add_co_u32_e32 v34, vcc, s18, v32
	s_mov_b32 s0, 0x30000
	s_nop 0
	v_addc_co_u32_e32 v35, vcc, 0, v33, vcc
	global_load_dwordx4 v[80:83], v[34:35], off
	v_add_co_u32_e32 v34, vcc, s0, v32
	s_mov_b32 s19, 0x38000
	s_nop 0
	v_addc_co_u32_e32 v35, vcc, 0, v33, vcc
	v_add_co_u32_e32 v32, vcc, s19, v32
	v_lshl_add_u32 v144, v152, 2, 0
	s_nop 0
	v_addc_co_u32_e32 v33, vcc, 0, v33, vcc
	v_add_u32_e32 v144, 0x20000, v144
	global_load_dwordx4 v[56:59], v[34:35], off
	v_lshlrev_b32_e32 v154, 7, v153
	global_load_dwordx4 v[32:35], v[32:33], off sc0
	ds_read2_b32 v[150:151], v144 offset1:16
	ds_read2_b32 v[148:149], v144 offset0:32 offset1:48
	ds_read2_b32 v[146:147], v144 offset0:64 offset1:80
	ds_read2_b32 v[144:145], v144 offset0:96 offset1:112
	v_lshlrev_b32_e32 v155, 3, v152
	s_waitcnt lgkmcnt(3)
	v_mul_f32_e32 v136, v136, v150
	v_mul_f32_e32 v137, v137, v150
	v_mul_f32_e32 v136, 0xbfb8aa3b, v136
	v_mul_f32_e32 v132, v132, v150
	v_mul_f32_e32 v137, 0xbfb8aa3b, v137
	v_mul_f32_e32 v133, v133, v150
	v_mul_f32_e32 v138, v138, v150
	v_mul_f32_e32 v139, v139, v150
	v_exp_f32_e32 v136, v136
	v_mul_f32_e32 v132, 0xbfb8aa3b, v132
	v_exp_f32_e32 v137, v137
	v_mul_f32_e32 v133, 0xbfb8aa3b, v133
	v_mul_f32_e32 v138, 0xbfb8aa3b, v138
	v_mul_f32_e32 v134, v134, v150
	v_mul_f32_e32 v139, 0xbfb8aa3b, v139
	v_mul_f32_e32 v135, v135, v150
	v_exp_f32_e32 v132, v132
	v_exp_f32_e32 v133, v133
	v_exp_f32_e32 v138, v138
	v_mul_f32_e32 v134, 0xbfb8aa3b, v134
	v_exp_f32_e32 v139, v139
	v_mul_f32_e32 v135, 0xbfb8aa3b, v135
	v_add3_u32 v154, s48, v154, v155
	v_exp_f32_e32 v134, v134
	v_exp_f32_e32 v135, v135
	ds_read2st64_b64 v[160:163], v154 offset1:1
	v_add_f32_e32 v136, 1.0, v136
	v_add_f32_e32 v137, 1.0, v137
	v_rcp_f32_e32 v136, v136
	v_add_f32_e32 v132, 1.0, v132
	v_rcp_f32_e32 v137, v137
	v_add_f32_e32 v133, 1.0, v133
	v_add_f32_e32 v138, 1.0, v138
	v_add_f32_e32 v139, 1.0, v139
	v_rcp_f32_e32 v132, v132
	v_rcp_f32_e32 v133, v133
	v_rcp_f32_e32 v138, v138
	v_add_f32_e32 v134, 1.0, v134
	v_rcp_f32_e32 v139, v139
	v_add_f32_e32 v135, 1.0, v135
	v_rcp_f32_e32 v134, v134
	v_rcp_f32_e32 v135, v135
	s_waitcnt vmcnt(7)
	v_lshlrev_b32_e32 v198, 16, v156
	v_and_b32_e32 v199, 0xffff0000, v156
	s_waitcnt lgkmcnt(0)
	v_lshlrev_b32_e32 v200, 16, v160
	v_and_b32_e32 v201, 0xffff0000, v160
	v_pk_fma_f32 v[136:137], v[136:137], v[200:201], v[198:199]
	v_lshlrev_b32_e32 v198, 16, v158
	v_and_b32_e32 v199, 0xffff0000, v158
	v_lshlrev_b32_e32 v200, 16, v162
	v_and_b32_e32 v201, 0xffff0000, v162
	v_lshlrev_b32_e32 v156, 16, v157
	v_and_b32_e32 v157, 0xffff0000, v157
	v_lshlrev_b32_e32 v160, 16, v161
	v_and_b32_e32 v161, 0xffff0000, v161
	v_pk_fma_f32 v[198:199], v[132:133], v[200:201], v[198:199]
	v_pk_fma_f32 v[156:157], v[138:139], v[160:161], v[156:157]
	v_lshlrev_b32_e32 v138, 16, v159
	v_and_b32_e32 v139, 0xffff0000, v159
	v_lshlrev_b32_e32 v158, 16, v163
	v_and_b32_e32 v159, 0xffff0000, v163
	v_pk_mul_f32 v[132:133], v[198:199], v[198:199]
	v_pk_fma_f32 v[158:159], v[134:135], v[158:159], v[138:139]
	v_mul_f32_e32 v120, v120, v151
	v_mul_f32_e32 v121, v121, v151
	v_pk_fma_f32 v[132:133], v[136:137], v[136:137], v[132:133]
	v_pk_mul_f32 v[134:135], v[158:159], v[158:159]
	v_mul_f32_e32 v120, 0xbfb8aa3b, v120
	v_mul_f32_e32 v116, v116, v151
	v_mul_f32_e32 v121, 0xbfb8aa3b, v121
	v_mul_f32_e32 v117, v117, v151
	v_mul_f32_e32 v122, v122, v151
	v_mul_f32_e32 v123, v123, v151
	v_pk_fma_f32 v[134:135], v[156:157], v[156:157], v[134:135]
	v_add_f32_e32 v132, v132, v133
	v_exp_f32_e32 v120, v120
	v_mul_f32_e32 v116, 0xbfb8aa3b, v116
	v_exp_f32_e32 v121, v121
	v_mul_f32_e32 v117, 0xbfb8aa3b, v117
	v_mul_f32_e32 v122, 0xbfb8aa3b, v122
	v_mul_f32_e32 v118, v118, v151
	v_mul_f32_e32 v123, 0xbfb8aa3b, v123
	v_mul_f32_e32 v119, v119, v151
	v_add_f32_e32 v132, v134, v132
	v_exp_f32_e32 v116, v116
	v_exp_f32_e32 v117, v117
	v_exp_f32_e32 v122, v122
	v_mul_f32_e32 v118, 0xbfb8aa3b, v118
	v_exp_f32_e32 v123, v123
	v_mul_f32_e32 v119, 0xbfb8aa3b, v119
	v_add_f32_e32 v138, v135, v132
	v_cvt_pk_bf16_f32 v132, v136, v137
	v_cvt_pk_bf16_f32 v133, v156, v157
	v_cvt_pk_bf16_f32 v134, v198, v199
	v_cvt_pk_bf16_f32 v135, v158, v159
	v_lshl_add_u64 v[136:137], s[6:7], 0, v[186:187]
	v_exp_f32_e32 v118, v118
	v_exp_f32_e32 v119, v119
	global_store_dwordx4 v[136:137], v[132:135], off
	ds_read2st64_b64 v[132:135], v154 offset0:2 offset1:3
	v_add_f32_e32 v120, 1.0, v120
	v_add_f32_e32 v121, 1.0, v121
	v_rcp_f32_e32 v120, v120
	v_add_f32_e32 v116, 1.0, v116
	v_rcp_f32_e32 v121, v121
	v_add_f32_e32 v117, 1.0, v117
	v_add_f32_e32 v122, 1.0, v122
	v_add_f32_e32 v123, 1.0, v123
	v_rcp_f32_e32 v116, v116
	v_rcp_f32_e32 v117, v117
	v_rcp_f32_e32 v122, v122
	v_add_f32_e32 v118, 1.0, v118
	v_rcp_f32_e32 v123, v123
	v_add_f32_e32 v119, 1.0, v119
	v_rcp_f32_e32 v118, v118
	v_rcp_f32_e32 v119, v119
	s_waitcnt vmcnt(7)
	v_lshlrev_b32_e32 v156, 16, v140
	v_and_b32_e32 v157, 0xffff0000, v140
	s_waitcnt lgkmcnt(0)
	v_lshlrev_b32_e32 v158, 16, v132
	v_and_b32_e32 v159, 0xffff0000, v132
	v_pk_fma_f32 v[120:121], v[120:121], v[158:159], v[156:157]
	v_lshlrev_b32_e32 v156, 16, v142
	v_and_b32_e32 v157, 0xffff0000, v142
	v_lshlrev_b32_e32 v158, 16, v134
	v_and_b32_e32 v159, 0xffff0000, v134
	v_lshlrev_b32_e32 v140, 16, v141
	v_and_b32_e32 v141, 0xffff0000, v141
	v_lshlrev_b32_e32 v132, 16, v133
	v_and_b32_e32 v133, 0xffff0000, v133
	v_pk_fma_f32 v[156:157], v[116:117], v[158:159], v[156:157]
	v_pk_fma_f32 v[122:123], v[122:123], v[132:133], v[140:141]
	v_lshlrev_b32_e32 v132, 16, v143
	v_and_b32_e32 v133, 0xffff0000, v143
	v_lshlrev_b32_e32 v134, 16, v135
	v_and_b32_e32 v135, 0xffff0000, v135
	v_pk_mul_f32 v[116:117], v[156:157], v[156:157]
	v_pk_fma_f32 v[132:133], v[118:119], v[134:135], v[132:133]
	v_pk_fma_f32 v[116:117], v[120:121], v[120:121], v[116:117]
	v_pk_mul_f32 v[118:119], v[132:133], v[132:133]
	v_mul_f32_e32 v108, v108, v148
	v_mul_f32_e32 v109, v109, v148
	v_pk_fma_f32 v[118:119], v[122:123], v[122:123], v[118:119]
	v_add_f32_e32 v116, v116, v117
	v_mul_f32_e32 v108, 0xbfb8aa3b, v108
	v_mul_f32_e32 v104, v104, v148
	v_mul_f32_e32 v109, 0xbfb8aa3b, v109
	v_mul_f32_e32 v105, v105, v148
	v_add_f32_e32 v116, v118, v116
	v_exp_f32_e32 v108, v108
	v_mul_f32_e32 v104, 0xbfb8aa3b, v104
	v_exp_f32_e32 v109, v109
	v_mul_f32_e32 v105, 0xbfb8aa3b, v105
	v_add_f32_e32 v116, v119, v116
	v_cvt_pk_bf16_f32 v119, v122, v123
	v_add_co_u32_e32 v122, vcc, s14, v136
	v_exp_f32_e32 v104, v104
	v_exp_f32_e32 v105, v105
	v_cvt_pk_bf16_f32 v118, v120, v121
	v_cvt_pk_bf16_f32 v120, v156, v157
	v_cvt_pk_bf16_f32 v121, v132, v133
	v_addc_co_u32_e32 v123, vcc, 0, v137, vcc
	global_store_dwordx4 v[122:123], v[118:121], off
	ds_read2st64_b64 v[118:121], v154 offset0:4 offset1:5
	v_add_f32_e32 v108, 1.0, v108
	v_add_f32_e32 v109, 1.0, v109
	v_rcp_f32_e32 v108, v108
	v_add_f32_e32 v104, 1.0, v104
	v_rcp_f32_e32 v109, v109
	v_add_f32_e32 v105, 1.0, v105
	v_rcp_f32_e32 v104, v104
	v_rcp_f32_e32 v105, v105
	s_waitcnt vmcnt(7)
	v_lshlrev_b32_e32 v122, 16, v128
	v_and_b32_e32 v123, 0xffff0000, v128
	s_waitcnt lgkmcnt(0)
	v_lshlrev_b32_e32 v132, 16, v118
	v_and_b32_e32 v133, 0xffff0000, v118
	v_pk_fma_f32 v[122:123], v[108:109], v[132:133], v[122:123]
	v_lshlrev_b32_e32 v108, 16, v130
	v_and_b32_e32 v109, 0xffff0000, v130
	v_lshlrev_b32_e32 v132, 16, v120
	v_and_b32_e32 v133, 0xffff0000, v120
	v_pk_fma_f32 v[132:133], v[104:105], v[132:133], v[108:109]
	v_mul_f32_e32 v108, v110, v148
	v_mul_f32_e32 v109, v111, v148
	v_mul_f32_e32 v108, 0xbfb8aa3b, v108
	v_mul_f32_e32 v106, v106, v148
	v_mul_f32_e32 v109, 0xbfb8aa3b, v109
	v_mul_f32_e32 v107, v107, v148
	v_exp_f32_e32 v108, v108
	v_mul_f32_e32 v106, 0xbfb8aa3b, v106
	v_exp_f32_e32 v109, v109
	v_mul_f32_e32 v107, 0xbfb8aa3b, v107
	v_exp_f32_e32 v106, v106
	v_exp_f32_e32 v107, v107
	v_add_f32_e32 v108, 1.0, v108
	v_add_f32_e32 v109, 1.0, v109
	v_rcp_f32_e32 v108, v108
	v_add_f32_e32 v106, 1.0, v106
	v_rcp_f32_e32 v109, v109
	v_add_f32_e32 v107, 1.0, v107
	v_rcp_f32_e32 v106, v106
	v_rcp_f32_e32 v107, v107
	v_lshlrev_b32_e32 v110, 16, v129
	v_and_b32_e32 v111, 0xffff0000, v129
	v_lshlrev_b32_e32 v118, 16, v119
	v_and_b32_e32 v119, 0xffff0000, v119
	v_pk_fma_f32 v[110:111], v[108:109], v[118:119], v[110:111]
	v_lshlrev_b32_e32 v108, 16, v131
	v_and_b32_e32 v109, 0xffff0000, v131
	v_lshlrev_b32_e32 v118, 16, v121
	v_and_b32_e32 v119, 0xffff0000, v121
	v_pk_mul_f32 v[104:105], v[132:133], v[132:133]
	v_pk_fma_f32 v[118:119], v[106:107], v[118:119], v[108:109]
	v_mul_f32_e32 v64, v64, v149
	v_mul_f32_e32 v65, v65, v149
	v_pk_fma_f32 v[104:105], v[122:123], v[122:123], v[104:105]
	v_pk_mul_f32 v[106:107], v[118:119], v[118:119]
	v_mul_f32_e32 v64, 0xbfb8aa3b, v64
	v_mul_f32_e32 v60, v60, v149
	v_mul_f32_e32 v65, 0xbfb8aa3b, v65
	v_mul_f32_e32 v61, v61, v149
	v_pk_fma_f32 v[106:107], v[110:111], v[110:111], v[106:107]
	v_add_f32_e32 v104, v104, v105
	v_exp_f32_e32 v64, v64
	v_mul_f32_e32 v60, 0xbfb8aa3b, v60
	v_exp_f32_e32 v65, v65
	v_mul_f32_e32 v61, 0xbfb8aa3b, v61
	v_add_f32_e32 v104, v106, v104
	v_cvt_pk_bf16_f32 v105, v110, v111
	v_add_co_u32_e32 v110, vcc, s3, v136
	v_exp_f32_e32 v60, v60
	v_exp_f32_e32 v61, v61
	v_add_f32_e32 v108, v107, v104
	v_cvt_pk_bf16_f32 v104, v122, v123
	v_cvt_pk_bf16_f32 v106, v132, v133
	v_cvt_pk_bf16_f32 v107, v118, v119
	v_addc_co_u32_e32 v111, vcc, 0, v137, vcc
	global_store_dwordx4 v[110:111], v[104:107], off
	ds_read2st64_b64 v[104:107], v154 offset0:6 offset1:7
	v_add_f32_e32 v64, 1.0, v64
	v_add_f32_e32 v65, 1.0, v65
	v_rcp_f32_e32 v64, v64
	v_add_f32_e32 v60, 1.0, v60
	v_rcp_f32_e32 v65, v65
	v_add_f32_e32 v61, 1.0, v61
	v_rcp_f32_e32 v60, v60
	v_rcp_f32_e32 v61, v61
	s_waitcnt vmcnt(7)
	v_lshlrev_b32_e32 v110, 16, v124
	v_and_b32_e32 v111, 0xffff0000, v124
	s_waitcnt lgkmcnt(0)
	v_lshlrev_b32_e32 v118, 16, v104
	v_and_b32_e32 v119, 0xffff0000, v104
	v_pk_fma_f32 v[110:111], v[64:65], v[118:119], v[110:111]
	v_lshlrev_b32_e32 v64, 16, v126
	v_and_b32_e32 v65, 0xffff0000, v126
	v_lshlrev_b32_e32 v118, 16, v106
	v_and_b32_e32 v119, 0xffff0000, v106
	v_pk_fma_f32 v[118:119], v[60:61], v[118:119], v[64:65]
	v_mul_f32_e32 v64, v66, v149
	v_mul_f32_e32 v65, v67, v149
	v_mul_f32_e32 v64, 0xbfb8aa3b, v64
	v_mul_f32_e32 v62, v62, v149
	v_mul_f32_e32 v65, 0xbfb8aa3b, v65
	v_mul_f32_e32 v63, v63, v149
	v_exp_f32_e32 v64, v64
	v_mul_f32_e32 v62, 0xbfb8aa3b, v62
	v_exp_f32_e32 v65, v65
	v_mul_f32_e32 v63, 0xbfb8aa3b, v63
	v_exp_f32_e32 v62, v62
	v_exp_f32_e32 v63, v63
	v_add_f32_e32 v64, 1.0, v64
	v_add_f32_e32 v65, 1.0, v65
	v_rcp_f32_e32 v64, v64
	v_add_f32_e32 v62, 1.0, v62
	v_rcp_f32_e32 v65, v65
	v_add_f32_e32 v63, 1.0, v63
	v_rcp_f32_e32 v62, v62
	v_rcp_f32_e32 v63, v63
	v_lshlrev_b32_e32 v66, 16, v125
	v_and_b32_e32 v67, 0xffff0000, v125
	v_lshlrev_b32_e32 v104, 16, v105
	v_and_b32_e32 v105, 0xffff0000, v105
	v_pk_fma_f32 v[66:67], v[64:65], v[104:105], v[66:67]
	v_lshlrev_b32_e32 v64, 16, v127
	v_and_b32_e32 v65, 0xffff0000, v127
	v_lshlrev_b32_e32 v104, 16, v107
	v_and_b32_e32 v105, 0xffff0000, v107
	v_pk_mul_f32 v[60:61], v[118:119], v[118:119]
	v_pk_fma_f32 v[104:105], v[62:63], v[104:105], v[64:65]
	v_mul_f32_e32 v65, v100, v146
	v_pk_fma_f32 v[60:61], v[110:111], v[110:111], v[60:61]
	v_pk_mul_f32 v[62:63], v[104:105], v[104:105]
	v_mul_f32_e32 v65, 0xbfb8aa3b, v65
	v_pk_fma_f32 v[62:63], v[66:67], v[66:67], v[62:63]
	v_add_f32_e32 v60, v60, v61
	v_exp_f32_e32 v65, v65
	v_add_f32_e32 v60, v62, v60
	v_cvt_pk_bf16_f32 v61, v66, v67
	v_add_co_u32_e32 v66, vcc, s12, v136
	v_add_f32_e32 v64, v63, v60
	v_cvt_pk_bf16_f32 v60, v110, v111
	v_cvt_pk_bf16_f32 v62, v118, v119
	v_cvt_pk_bf16_f32 v63, v104, v105
	v_addc_co_u32_e32 v67, vcc, 0, v137, vcc
	global_store_dwordx4 v[66:67], v[60:63], off
	ds_read2st64_b64 v[60:63], v154 offset0:8 offset1:9
	v_add_f32_e32 v65, 1.0, v65
	v_rcp_f32_e32 v66, v65
	v_mul_f32_e32 v65, v96, v146
	v_mul_f32_e32 v65, 0xbfb8aa3b, v65
	v_exp_f32_e32 v65, v65
	s_waitcnt lgkmcnt(0)
	v_lshlrev_b32_e32 v104, 16, v60
	v_and_b32_e32 v105, 0xffff0000, v60
	v_mul_f32_e32 v60, v97, v146
	v_mul_f32_e32 v60, 0xbfb8aa3b, v60
	v_exp_f32_e32 v60, v60
	v_add_f32_e32 v65, 1.0, v65
	v_rcp_f32_e32 v96, v65
	v_mul_f32_e32 v65, v101, v146
	v_mul_f32_e32 v65, 0xbfb8aa3b, v65
	v_exp_f32_e32 v65, v65
	v_add_f32_e32 v60, 1.0, v60
	v_rcp_f32_e32 v97, v60
	v_mul_f32_e32 v60, v102, v146
	v_mul_f32_e32 v60, 0xbfb8aa3b, v60
	v_exp_f32_e32 v60, v60
	v_add_f32_e32 v65, 1.0, v65
	v_rcp_f32_e32 v67, v65
	s_waitcnt vmcnt(7)
	v_lshlrev_b32_e32 v100, 16, v112
	v_add_f32_e32 v60, 1.0, v60
	v_and_b32_e32 v101, 0xffff0000, v112
	v_rcp_f32_e32 v102, v60
	v_mul_f32_e32 v60, v98, v146
	v_lshlrev_b32_e32 v106, 16, v61
	v_and_b32_e32 v107, 0xffff0000, v61
	v_mul_f32_e32 v61, v99, v146
	v_pk_fma_f32 v[66:67], v[66:67], v[104:105], v[100:101]
	v_lshlrev_b32_e32 v104, 16, v62
	v_and_b32_e32 v105, 0xffff0000, v62
	v_mul_f32_e32 v60, 0xbfb8aa3b, v60
	v_mul_f32_e32 v62, v103, v146
	v_mul_f32_e32 v61, 0xbfb8aa3b, v61
	v_exp_f32_e32 v60, v60
	v_mul_f32_e32 v62, 0xbfb8aa3b, v62
	v_exp_f32_e32 v61, v61
	v_exp_f32_e32 v62, v62
	v_add_f32_e32 v60, 1.0, v60
	v_rcp_f32_e32 v60, v60
	v_add_f32_e32 v61, 1.0, v61
	v_add_f32_e32 v62, 1.0, v62
	v_rcp_f32_e32 v61, v61
	v_rcp_f32_e32 v103, v62
	v_lshlrev_b32_e32 v100, 16, v114
	v_and_b32_e32 v101, 0xffff0000, v114
	v_pk_fma_f32 v[96:97], v[96:97], v[104:105], v[100:101]
	v_lshlrev_b32_e32 v98, 16, v115
	v_and_b32_e32 v99, 0xffff0000, v115
	v_lshlrev_b32_e32 v62, 16, v63
	v_and_b32_e32 v63, 0xffff0000, v63
	v_pk_mul_f32 v[100:101], v[96:97], v[96:97]
	v_lshlrev_b32_e32 v104, 16, v113
	v_and_b32_e32 v105, 0xffff0000, v113
	v_pk_fma_f32 v[98:99], v[60:61], v[62:63], v[98:99]
	v_pk_fma_f32 v[100:101], v[66:67], v[66:67], v[100:101]
	v_pk_fma_f32 v[102:103], v[102:103], v[106:107], v[104:105]
	v_pk_mul_f32 v[60:61], v[98:99], v[98:99]
	v_add_f32_e32 v62, v100, v101
	v_pk_fma_f32 v[60:61], v[102:103], v[102:103], v[60:61]
	v_cvt_pk_bf16_f32 v63, v98, v99
	v_add_f32_e32 v60, v60, v62
	v_add_f32_e32 v65, v61, v60
	v_cvt_pk_bf16_f32 v60, v66, v67
	v_add_co_u32_e32 v66, vcc, s1, v136
	v_cvt_pk_bf16_f32 v61, v102, v103
	v_cvt_pk_bf16_f32 v62, v96, v97
	v_addc_co_u32_e32 v67, vcc, 0, v137, vcc
	global_store_dwordx4 v[66:67], v[60:63], off
	ds_read2st64_b64 v[60:63], v154 offset0:10 offset1:11
	v_mul_f32_e32 v67, v88, v147
	v_mul_f32_e32 v67, 0xbfb8aa3b, v67
	v_exp_f32_e32 v67, v67
	v_mul_f32_e32 v66, v92, v147
	s_waitcnt lgkmcnt(0)
	v_lshlrev_b32_e32 v96, 16, v60
	v_and_b32_e32 v97, 0xffff0000, v60
	v_mul_f32_e32 v60, v89, v147
	v_add_f32_e32 v67, 1.0, v67
	v_mul_f32_e32 v60, 0xbfb8aa3b, v60
	v_rcp_f32_e32 v88, v67
	v_mul_f32_e32 v67, v93, v147
	v_exp_f32_e32 v60, v60
	v_mul_f32_e32 v66, 0xbfb8aa3b, v66
	v_mul_f32_e32 v67, 0xbfb8aa3b, v67
	v_exp_f32_e32 v66, v66
	v_exp_f32_e32 v67, v67
	v_add_f32_e32 v60, 1.0, v60
	v_rcp_f32_e32 v89, v60
	v_mul_f32_e32 v60, v94, v147
	v_add_f32_e32 v66, 1.0, v66
	v_add_f32_e32 v67, 1.0, v67
	v_mul_f32_e32 v60, 0xbfb8aa3b, v60
	v_rcp_f32_e32 v66, v66
	v_rcp_f32_e32 v67, v67
	v_exp_f32_e32 v60, v60
	s_waitcnt vmcnt(7)
	v_lshlrev_b32_e32 v92, 16, v80
	v_and_b32_e32 v93, 0xffff0000, v80
	v_pk_fma_f32 v[66:67], v[66:67], v[96:97], v[92:93]
	v_lshlrev_b32_e32 v92, 16, v82
	v_and_b32_e32 v93, 0xffff0000, v82
	v_lshlrev_b32_e32 v96, 16, v62
	v_and_b32_e32 v97, 0xffff0000, v62
	v_add_f32_e32 v60, 1.0, v60
	v_mul_f32_e32 v62, v95, v147
	v_pk_fma_f32 v[88:89], v[88:89], v[96:97], v[92:93]
	v_rcp_f32_e32 v94, v60
	v_mul_f32_e32 v60, v90, v147
	v_mul_f32_e32 v62, 0xbfb8aa3b, v62
	v_lshlrev_b32_e32 v96, 16, v61
	v_and_b32_e32 v97, 0xffff0000, v61
	v_mul_f32_e32 v61, v91, v147
	v_mul_f32_e32 v60, 0xbfb8aa3b, v60
	v_exp_f32_e32 v62, v62
	v_mul_f32_e32 v61, 0xbfb8aa3b, v61
	v_exp_f32_e32 v60, v60
	v_exp_f32_e32 v61, v61
	v_add_f32_e32 v62, 1.0, v62
	v_rcp_f32_e32 v95, v62
	v_add_f32_e32 v60, 1.0, v60
	v_add_f32_e32 v61, 1.0, v61
	v_rcp_f32_e32 v60, v60
	v_rcp_f32_e32 v61, v61
	v_lshlrev_b32_e32 v80, 16, v81
	v_and_b32_e32 v81, 0xffff0000, v81
	v_pk_fma_f32 v[94:95], v[94:95], v[96:97], v[80:81]
	v_lshlrev_b32_e32 v80, 16, v83
	v_and_b32_e32 v81, 0xffff0000, v83
	v_lshlrev_b32_e32 v62, 16, v63
	v_and_b32_e32 v63, 0xffff0000, v63
	v_pk_mul_f32 v[92:93], v[88:89], v[88:89]
	v_pk_fma_f32 v[62:63], v[60:61], v[62:63], v[80:81]
	v_pk_fma_f32 v[92:93], v[66:67], v[66:67], v[92:93]
	v_pk_mul_f32 v[60:61], v[62:63], v[62:63]
	v_add_f32_e32 v80, v92, v93
	v_pk_fma_f32 v[60:61], v[94:95], v[94:95], v[60:61]
	v_cvt_pk_bf16_f32 v83, v62, v63
	v_add_f32_e32 v60, v60, v80
	v_add_f32_e32 v60, v61, v60
	v_mul_f32_e32 v61, v84, v144
	v_mul_f32_e32 v61, 0xbfb8aa3b, v61
	v_exp_f32_e32 v61, v61
	v_add_co_u32_e32 v62, vcc, s18, v136
	v_cvt_pk_bf16_f32 v80, v66, v67
	v_cvt_pk_bf16_f32 v81, v94, v95
	v_cvt_pk_bf16_f32 v82, v88, v89
	v_addc_co_u32_e32 v63, vcc, 0, v137, vcc
	v_add_f32_e32 v61, 1.0, v61
	global_store_dwordx4 v[62:63], v[80:83], off
	v_rcp_f32_e32 v62, v61
	v_mul_f32_e32 v61, v76, v144
	v_mul_f32_e32 v61, 0xbfb8aa3b, v61
	v_exp_f32_e32 v61, v61
	s_waitcnt vmcnt(7)
	v_lshlrev_b32_e32 v84, 16, v56
	ds_read2st64_b64 v[80:83], v154 offset0:12 offset1:13
	v_lshlrev_b32_e32 v76, 16, v58
	v_add_f32_e32 v61, 1.0, v61
	v_rcp_f32_e32 v66, v61
	v_mul_f32_e32 v61, v85, v144
	v_and_b32_e32 v85, 0xffff0000, v56
	v_mul_f32_e32 v56, v77, v144
	v_mul_f32_e32 v56, 0xbfb8aa3b, v56
	v_exp_f32_e32 v56, v56
	v_mul_f32_e32 v61, 0xbfb8aa3b, v61
	v_exp_f32_e32 v61, v61
	s_waitcnt lgkmcnt(0)
	v_lshlrev_b32_e32 v88, 16, v80
	v_add_f32_e32 v56, 1.0, v56
	v_rcp_f32_e32 v67, v56
	v_mul_f32_e32 v56, v86, v144
	v_add_f32_e32 v61, 1.0, v61
	v_mul_f32_e32 v56, 0xbfb8aa3b, v56
	v_rcp_f32_e32 v63, v61
	v_exp_f32_e32 v56, v56
	v_and_b32_e32 v89, 0xffff0000, v80
	v_and_b32_e32 v77, 0xffff0000, v58
	v_pk_fma_f32 v[62:63], v[62:63], v[88:89], v[84:85]
	v_lshlrev_b32_e32 v84, 16, v82
	v_and_b32_e32 v85, 0xffff0000, v82
	v_add_f32_e32 v56, 1.0, v56
	v_pk_fma_f32 v[66:67], v[66:67], v[84:85], v[76:77]
	v_rcp_f32_e32 v84, v56
	v_mul_f32_e32 v56, v78, v144
	v_mul_f32_e32 v58, v87, v144
	v_lshlrev_b32_e32 v86, 16, v57
	v_and_b32_e32 v87, 0xffff0000, v57
	v_mul_f32_e32 v57, v79, v144
	v_mul_f32_e32 v56, 0xbfb8aa3b, v56
	v_mul_f32_e32 v57, 0xbfb8aa3b, v57
	v_exp_f32_e32 v56, v56
	v_mul_f32_e32 v58, 0xbfb8aa3b, v58
	v_exp_f32_e32 v57, v57
	v_exp_f32_e32 v58, v58
	v_add_f32_e32 v56, 1.0, v56
	v_rcp_f32_e32 v56, v56
	v_add_f32_e32 v57, 1.0, v57
	v_add_f32_e32 v58, 1.0, v58
	v_rcp_f32_e32 v57, v57
	v_rcp_f32_e32 v85, v58
	v_lshlrev_b32_e32 v58, 16, v59
	v_and_b32_e32 v59, 0xffff0000, v59
	v_lshlrev_b32_e32 v78, 16, v83
	v_and_b32_e32 v79, 0xffff0000, v83
	v_pk_mul_f32 v[76:77], v[66:67], v[66:67]
	v_lshlrev_b32_e32 v80, 16, v81
	v_and_b32_e32 v81, 0xffff0000, v81
	v_pk_fma_f32 v[78:79], v[56:57], v[78:79], v[58:59]
	v_pk_fma_f32 v[76:77], v[62:63], v[62:63], v[76:77]
	v_pk_fma_f32 v[80:81], v[84:85], v[80:81], v[86:87]
	v_pk_mul_f32 v[56:57], v[78:79], v[78:79]
	v_add_f32_e32 v58, v76, v77
	v_pk_fma_f32 v[56:57], v[80:81], v[80:81], v[56:57]
	v_cvt_pk_bf16_f32 v59, v78, v79
	v_add_f32_e32 v56, v56, v58
	v_add_f32_e32 v61, v57, v56
	v_cvt_pk_bf16_f32 v56, v62, v63
	v_add_co_u32_e32 v62, vcc, s0, v136
	v_cvt_pk_bf16_f32 v57, v80, v81
	v_cvt_pk_bf16_f32 v58, v66, v67
	v_addc_co_u32_e32 v63, vcc, 0, v137, vcc
	global_store_dwordx4 v[62:63], v[56:59], off
	v_mul_f32_e32 v63, v68, v145
	v_mul_f32_e32 v63, 0xbfb8aa3b, v63
	v_exp_f32_e32 v63, v63
	v_mul_f32_e32 v62, v72, v145
	s_waitcnt vmcnt(7)
	v_lshlrev_b32_e32 v72, 16, v32
	v_mul_f32_e32 v62, 0xbfb8aa3b, v62
	v_add_f32_e32 v63, 1.0, v63
	v_rcp_f32_e32 v66, v63
	v_mul_f32_e32 v63, v73, v145
	v_and_b32_e32 v73, 0xffff0000, v32
	v_mul_f32_e32 v32, v69, v145
	v_mul_f32_e32 v32, 0xbfb8aa3b, v32
	v_exp_f32_e32 v32, v32
	v_mul_f32_e32 v63, 0xbfb8aa3b, v63
	v_exp_f32_e32 v62, v62
	v_exp_f32_e32 v63, v63
	v_add_f32_e32 v32, 1.0, v32
	ds_read2st64_b64 v[56:59], v154 offset0:14 offset1:15
	v_rcp_f32_e32 v67, v32
	v_mul_f32_e32 v32, v74, v145
	v_add_f32_e32 v62, 1.0, v62
	v_add_f32_e32 v63, 1.0, v63
	v_mul_f32_e32 v32, 0xbfb8aa3b, v32
	v_rcp_f32_e32 v62, v62
	v_rcp_f32_e32 v63, v63
	v_exp_f32_e32 v32, v32
	s_waitcnt lgkmcnt(0)
	v_lshlrev_b32_e32 v76, 16, v56
	v_and_b32_e32 v77, 0xffff0000, v56
	v_pk_fma_f32 v[62:63], v[62:63], v[76:77], v[72:73]
	v_lshlrev_b32_e32 v68, 16, v34
	v_and_b32_e32 v69, 0xffff0000, v34
	v_lshlrev_b32_e32 v72, 16, v58
	v_and_b32_e32 v73, 0xffff0000, v58
	v_add_f32_e32 v32, 1.0, v32
	v_pk_fma_f32 v[66:67], v[66:67], v[72:73], v[68:69]
	v_rcp_f32_e32 v72, v32
	v_mul_f32_e32 v32, v70, v145
	v_mul_f32_e32 v34, v75, v145
	v_lshlrev_b32_e32 v74, 16, v33
	v_and_b32_e32 v75, 0xffff0000, v33
	v_mul_f32_e32 v33, v71, v145
	v_mul_f32_e32 v32, 0xbfb8aa3b, v32
	v_mul_f32_e32 v33, 0xbfb8aa3b, v33
	v_exp_f32_e32 v32, v32
	v_mul_f32_e32 v34, 0xbfb8aa3b, v34
	v_exp_f32_e32 v33, v33
	v_exp_f32_e32 v34, v34
	v_add_f32_e32 v32, 1.0, v32
	v_rcp_f32_e32 v32, v32
	v_add_f32_e32 v33, 1.0, v33
	v_add_f32_e32 v34, 1.0, v34
	v_rcp_f32_e32 v33, v33
	v_rcp_f32_e32 v73, v34
	v_lshlrev_b32_e32 v34, 16, v35
	v_and_b32_e32 v35, 0xffff0000, v35
	v_lshlrev_b32_e32 v58, 16, v59
	v_and_b32_e32 v59, 0xffff0000, v59
	v_pk_mul_f32 v[68:69], v[66:67], v[66:67]
	v_lshlrev_b32_e32 v56, 16, v57
	v_and_b32_e32 v57, 0xffff0000, v57
	v_pk_fma_f32 v[58:59], v[32:33], v[58:59], v[34:35]
	v_pk_fma_f32 v[68:69], v[62:63], v[62:63], v[68:69]
	v_pk_fma_f32 v[56:57], v[72:73], v[56:57], v[74:75]
	v_pk_mul_f32 v[32:33], v[58:59], v[58:59]
	v_add_f32_e32 v34, v68, v69
	v_pk_fma_f32 v[32:33], v[56:57], v[56:57], v[32:33]
	v_cvt_pk_bf16_f32 v35, v58, v59
	v_add_f32_e32 v32, v32, v34
	v_add_f32_e32 v68, v33, v32
	v_cvt_pk_bf16_f32 v33, v56, v57
	v_add_co_u32_e32 v56, vcc, s19, v136
	v_cvt_pk_bf16_f32 v32, v62, v63
	v_cvt_pk_bf16_f32 v34, v66, v67
	v_addc_co_u32_e32 v57, vcc, 0, v137, vcc
	global_store_dwordx4 v[56:57], v[32:35], off
	v_mov_b32_e32 v56, v108
	v_mov_b32_e32 v58, v64
	v_mov_b32_e32 v32, v138
	s_nop 1
	v_permlane16_swap_b32 v32, v138
	v_mov_b32_e32 v34, v116
	v_add_f32_e32 v32, v32, v138
	v_mov_b32_e32 v33, v32
	s_nop 1
	v_permlane32_swap_b32 v32, v33
	s_nop 1
	v_permlane16_swap_b32 v34, v116
	v_mov_b32_e32 v62, v65
	v_add_f32_e32 v34, v34, v116
	v_mov_b32_e32 v35, v34
	s_nop 1
	v_permlane32_swap_b32 v35, v34
	s_nop 1
	v_permlane16_swap_b32 v108, v56
	v_mov_b32_e32 v66, v68
	v_add_f32_e32 v56, v108, v56
	v_mov_b32_e32 v57, v56
	s_nop 1
	v_permlane32_swap_b32 v57, v56
	s_nop 1
	v_permlane16_swap_b32 v58, v64
	s_mov_b32 s15, 0x10000
	v_add_f32_e32 v58, v58, v64
	v_mov_b32_e32 v59, v58
	s_nop 1
	v_permlane32_swap_b32 v58, v59
	s_nop 1
	v_permlane16_swap_b32 v65, v62
	v_mov_b32_e32 v64, v60
	v_add_f32_e32 v62, v65, v62
	v_mov_b32_e32 v63, v62
	s_nop 1
	v_permlane32_swap_b32 v63, v62
	s_nop 1
	v_permlane16_swap_b32 v60, v64
	v_mov_b32_e32 v65, v61
	v_add_f32_e32 v60, v60, v64
	v_mov_b32_e32 v64, v60
	s_nop 1
	v_permlane32_swap_b32 v60, v64
	s_nop 1
	v_permlane16_swap_b32 v65, v61
	s_mov_b32 s3, 0x18000
	v_add_f32_e32 v61, v65, v61
	v_mov_b32_e32 v65, v61
	s_nop 1
	v_permlane32_swap_b32 v65, v61
	s_nop 1
	v_permlane16_swap_b32 v68, v66
	v_cmp_eq_u32_e32 vcc, 0, v153
	v_add_f32_e32 v66, v68, v66
	v_mov_b32_e32 v67, v66
	s_nop 1
	v_permlane32_swap_b32 v67, v66
	s_and_saveexec_b64 s[0:1], vcc
	s_cbranch_execz .LBB0_1549
	v_add_f32_e32 v34, v35, v34
	v_add_f32_e32 v35, v32, v33
	v_lshl_add_u32 v32, v152, 2, s49
	v_add_f32_e32 v56, v57, v56
	v_add_u32_e32 v57, 0x1000, v32
	ds_read2_b32 v[32:33], v57 offset1:16
	v_add_f32_e32 v58, v58, v59
	v_add_f32_e32 v60, v60, v64
	v_add_f32_e32 v62, v63, v62
	v_add_f32_e32 v66, v67, v66
	s_waitcnt lgkmcnt(0)
	v_add_f32_e32 v32, v35, v32
	v_add_f32_e32 v33, v34, v33
	ds_write2_b32 v57, v32, v33 offset1:16
	ds_read2_b32 v[32:33], v57 offset0:32 offset1:48
	v_add_f32_e32 v61, v65, v61
	s_waitcnt lgkmcnt(0)
	v_add_f32_e32 v32, v56, v32
	v_add_f32_e32 v33, v58, v33
	ds_write2_b32 v57, v32, v33 offset0:32 offset1:48
	ds_read2_b32 v[32:33], v57 offset0:64 offset1:80
	s_waitcnt lgkmcnt(0)
	v_add_f32_e32 v32, v62, v32
	v_add_f32_e32 v33, v60, v33
	ds_write2_b32 v57, v32, v33 offset0:64 offset1:80
	ds_read2_b32 v[32:33], v57 offset0:96 offset1:112
	s_waitcnt lgkmcnt(0)
	v_add_f32_e32 v32, v61, v32
	v_add_f32_e32 v33, v66, v33
	ds_write2_b32 v57, v32, v33 offset0:96 offset1:112
	s_branch .LBB0_1549

.LBB0_1608:
	s_or_b64 exec, exec, s[38:39]
	v_readlane_b32 s18, v248, 44
	v_readlane_b32 s19, v248, 45
	s_mov_b64 s[38:39], -1
	s_and_b64 vcc, exec, s[18:19]
	s_waitcnt lgkmcnt(0)
	s_barrier
	s_cbranch_vccz .LBB0_1612
	v_readlane_b32 s60, v251, 4
	v_readlane_b32 s62, v251, 6
	v_readlane_b32 s63, v251, 7
	s_nop 4
	global_load_dwordx4 v[4:7], v166, s[62:63] offset:16 sc0
	global_load_dwordx4 v[8:11], v166, s[62:63] sc0
	global_load_dwordx4 v[12:15], v166, s[62:63] offset:2064 sc0
	global_load_dwordx4 v[16:19], v166, s[62:63] offset:2048 sc0
	s_lshl_b32 s12, s46, 2
	v_readlane_b32 s61, v251, 5
	v_readlane_b32 s64, v251, 8
	v_readlane_b32 s65, v251, 9
	s_andn2_b32 s12, s12, 63
	s_mov_b64 s[60:61], s[64:65]
	v_mov_b32_e32 v167, v2
	v_mov_b32_e32 v165, v2
	s_add_i32 s12, s12, 0
	s_waitcnt vmcnt(6)
	v_lshl_add_u64 v[20:21], s[60:61], 0, v[166:167]
	v_lshl_add_u64 v[22:23], s[6:7], 0, v[164:165]
	s_add_i32 s41, s12, 0x20408
	s_mov_b32 s58, 0
	s_mov_b32 s18, 0x3a800000
	s_mov_b32 s26, 0x358637bd
	v_readlane_b32 s66, v251, 10
	v_readlane_b32 s67, v251, 11
